# GEMM K loops (11 single-level ones): back edge rotated - address updates, exit test and next iteration's scalar head run before the loop-back barrier instead of after it
# baseline (speedup 1.0000x reference)
.Lpeelph1b_0:
	s_add_i32 s73, s60, 2
	s_add_u32 s61, s58, 0xfffc0080
	s_addc_u32 s62, s59, -1
	s_add_i32 s74, 0, 0x10000
	s_cmp_eq_u32 s68, s60
	s_cselect_b32 s63, s39, s62
	s_cselect_b32 s62, s43, s61
	s_cselect_b32 s61, s47, s72
	s_cselect_b32 s60, s55, s71
	s_add_i32 s76, 0, 0x14000
	v_add_u32_e32 v156, s74, v165
	v_add_u32_e32 v166, s76, v165
	ds_read_b128 v[144:147], v156
	ds_read_b128 v[148:151], v156 offset:1024
	ds_read_b128 v[152:155], v156 offset:2048
	ds_read_b128 v[156:159], v156 offset:3072
	ds_read_b128 v[160:163], v166
	ds_read_b128 v[170:173], v166 offset:1024
	ds_read_b128 v[174:177], v166 offset:2048
	ds_read_b128 v[180:183], v166 offset:3072
	v_lshl_add_u64 v[216:217], s[58:59], 0, v[142:143]
	s_add_i32 m0, s8, 0xc000
	ds_read_b128 v[184:187], v178
	ds_read_b128 v[188:191], v178 offset:1024
	ds_read_b128 v[192:195], v178 offset:2048
	ds_read_b128 v[196:199], v178 offset:3072
	ds_read_b128 v[200:203], v178 offset:4096
	ds_read_b128 v[204:207], v178 offset:5120
	ds_read_b128 v[208:211], v178 offset:6144
	ds_read_b128 v[212:215], v178 offset:7168
	global_load_lds_dwordx4 v[216:217], off
	v_lshl_add_u64 v[216:217], s[58:59], 0, v[140:141]
	s_add_i32 m0, s8, 0xe000
	s_nop 0
	global_load_lds_dwordx4 v[216:217], off
	s_waitcnt vmcnt(8)
	s_waitcnt lgkmcnt(0)
	s_barrier
	s_setprio 1
	s_waitcnt lgkmcnt(0)
	v_mfma_f32_16x16x32_bf16 v[126:129], v[144:147], v[184:187], 0
	v_mfma_f32_16x16x32_bf16 v[122:125], v[152:155], v[184:187], 0
	v_mfma_f32_16x16x32_bf16 v[110:113], v[144:147], v[192:195], 0
	v_mfma_f32_16x16x32_bf16 v[106:109], v[152:155], v[192:195], 0
	v_mfma_f32_16x16x32_bf16 v[94:97], v[144:147], v[200:203], 0
	v_mfma_f32_16x16x32_bf16 v[90:93], v[152:155], v[200:203], 0
	v_mfma_f32_16x16x32_bf16 v[78:81], v[144:147], v[208:211], 0
	v_mfma_f32_16x16x32_bf16 v[74:77], v[152:155], v[208:211], 0
	v_mfma_f32_16x16x32_bf16 v[126:129], v[148:151], v[188:191], v[126:129]
	v_mfma_f32_16x16x32_bf16 v[122:125], v[156:159], v[188:191], v[122:125]
	v_mfma_f32_16x16x32_bf16 v[110:113], v[148:151], v[196:199], v[110:113]
	v_mfma_f32_16x16x32_bf16 v[106:109], v[156:159], v[196:199], v[106:109]
	v_mfma_f32_16x16x32_bf16 v[94:97], v[148:151], v[204:207], v[94:97]
	v_mfma_f32_16x16x32_bf16 v[90:93], v[156:159], v[204:207], v[90:93]
	v_mfma_f32_16x16x32_bf16 v[78:81], v[148:151], v[212:215], v[78:81]
	v_mfma_f32_16x16x32_bf16 v[74:77], v[156:159], v[212:215], v[74:77]
	s_setprio 0
	s_setprio 1
	v_mfma_f32_16x16x32_bf16 v[118:121], v[160:163], v[184:187], 0
	v_mfma_f32_16x16x32_bf16 v[114:117], v[174:177], v[184:187], 0
	v_mfma_f32_16x16x32_bf16 v[102:105], v[160:163], v[192:195], 0
	v_mfma_f32_16x16x32_bf16 v[98:101], v[174:177], v[192:195], 0
	v_mfma_f32_16x16x32_bf16 v[86:89], v[160:163], v[200:203], 0
	v_mfma_f32_16x16x32_bf16 v[82:85], v[174:177], v[200:203], 0
	v_mfma_f32_16x16x32_bf16 v[70:73], v[160:163], v[208:211], 0
	v_mfma_f32_16x16x32_bf16 v[66:69], v[174:177], v[208:211], 0
	v_mfma_f32_16x16x32_bf16 v[118:121], v[170:173], v[188:191], v[118:121]
	v_mfma_f32_16x16x32_bf16 v[114:117], v[180:183], v[188:191], v[114:117]
	v_mfma_f32_16x16x32_bf16 v[102:105], v[170:173], v[196:199], v[102:105]
	v_mfma_f32_16x16x32_bf16 v[98:101], v[180:183], v[196:199], v[98:101]
	v_mfma_f32_16x16x32_bf16 v[86:89], v[170:173], v[204:207], v[86:89]
	v_mfma_f32_16x16x32_bf16 v[82:85], v[180:183], v[204:207], v[82:85]
	v_mfma_f32_16x16x32_bf16 v[70:73], v[170:173], v[212:215], v[70:73]
	v_mfma_f32_16x16x32_bf16 v[66:69], v[180:183], v[212:215], v[66:69]
	s_setprio 0
	s_barrier
	s_add_i32 s74, s74, s1
	v_lshl_add_u64 v[216:217], s[60:61], 0, v[130:131]
	s_mov_b32 m0, s74
	ds_read_b128 v[184:187], v178 offset:16384
	ds_read_b128 v[188:191], v178 offset:17408
	ds_read_b128 v[192:195], v178 offset:18432
	ds_read_b128 v[196:199], v178 offset:19456
	ds_read_b128 v[200:203], v178 offset:20480
	ds_read_b128 v[204:207], v178 offset:21504
	ds_read_b128 v[208:211], v178 offset:22528
	ds_read_b128 v[212:215], v178 offset:23552
	global_load_lds_dwordx4 v[216:217], off
	s_add_i32 m0, s74, 0x2000
	s_add_u32 s74, s60, 0x40000
	v_lshl_add_u64 v[218:219], s[60:61], 0, v[132:133]
	s_addc_u32 s75, s61, 0
	s_add_i32 s76, s76, s1
	global_load_lds_dwordx4 v[218:219], off
	v_lshl_add_u64 v[220:221], s[74:75], 0, v[130:131]
	s_mov_b32 m0, s76
	v_lshl_add_u64 v[222:223], s[62:63], 0, v[136:137]
	global_load_lds_dwordx4 v[220:221], off
	v_lshl_add_u64 v[220:221], s[74:75], 0, v[132:133]
	s_add_i32 m0, s76, 0x2000
	s_nop 0
	global_load_lds_dwordx4 v[220:221], off
	v_lshl_add_u64 v[220:221], s[62:63], 0, v[134:135]
	s_mov_b32 m0, s8
	s_nop 0
	global_load_lds_dwordx4 v[220:221], off
	s_mov_b32 m0, s11
	s_nop 0
	global_load_lds_dwordx4 v[222:223], off
	s_waitcnt vmcnt(8)
	s_waitcnt lgkmcnt(0)
	s_barrier
	s_setprio 1
	s_waitcnt lgkmcnt(0)
	v_mfma_f32_16x16x32_bf16 v[62:65], v[144:147], v[184:187], 0
	v_mfma_f32_16x16x32_bf16 v[58:61], v[152:155], v[184:187], 0
	v_mfma_f32_16x16x32_bf16 v[46:49], v[144:147], v[192:195], 0
	v_mfma_f32_16x16x32_bf16 v[42:45], v[152:155], v[192:195], 0
	v_mfma_f32_16x16x32_bf16 v[30:33], v[144:147], v[200:203], 0
	v_mfma_f32_16x16x32_bf16 v[26:29], v[152:155], v[200:203], 0
	v_mfma_f32_16x16x32_bf16 v[14:17], v[144:147], v[208:211], 0
	v_mfma_f32_16x16x32_bf16 v[10:13], v[152:155], v[208:211], 0
	v_mfma_f32_16x16x32_bf16 v[62:65], v[148:151], v[188:191], v[62:65]
	v_mfma_f32_16x16x32_bf16 v[58:61], v[156:159], v[188:191], v[58:61]
	v_mfma_f32_16x16x32_bf16 v[46:49], v[148:151], v[196:199], v[46:49]
	v_mfma_f32_16x16x32_bf16 v[42:45], v[156:159], v[196:199], v[42:45]
	v_mfma_f32_16x16x32_bf16 v[30:33], v[148:151], v[204:207], v[30:33]
	v_mfma_f32_16x16x32_bf16 v[26:29], v[156:159], v[204:207], v[26:29]
	v_mfma_f32_16x16x32_bf16 v[14:17], v[148:151], v[212:215], v[14:17]
	v_mfma_f32_16x16x32_bf16 v[10:13], v[156:159], v[212:215], v[10:13]
	s_setprio 0
	s_setprio 1
	v_mfma_f32_16x16x32_bf16 v[54:57], v[160:163], v[184:187], 0
	v_mfma_f32_16x16x32_bf16 v[50:53], v[174:177], v[184:187], 0
	v_mfma_f32_16x16x32_bf16 v[38:41], v[160:163], v[192:195], 0
	v_mfma_f32_16x16x32_bf16 v[34:37], v[174:177], v[192:195], 0
	v_mfma_f32_16x16x32_bf16 v[22:25], v[160:163], v[200:203], 0
	v_mfma_f32_16x16x32_bf16 v[18:21], v[174:177], v[200:203], 0
	v_mfma_f32_16x16x32_bf16 v[6:9], v[160:163], v[208:211], 0
	v_mfma_f32_16x16x32_bf16 v[2:5], v[174:177], v[208:211], 0
	v_mfma_f32_16x16x32_bf16 v[54:57], v[170:173], v[188:191], v[54:57]
	v_mfma_f32_16x16x32_bf16 v[50:53], v[180:183], v[188:191], v[50:53]
	v_mfma_f32_16x16x32_bf16 v[38:41], v[170:173], v[196:199], v[38:41]
	v_mfma_f32_16x16x32_bf16 v[34:37], v[180:183], v[196:199], v[34:37]
	v_mfma_f32_16x16x32_bf16 v[22:25], v[170:173], v[204:207], v[22:25]
	v_mfma_f32_16x16x32_bf16 v[18:21], v[180:183], v[204:207], v[18:21]
	v_mfma_f32_16x16x32_bf16 v[6:9], v[170:173], v[212:215], v[6:9]
	v_mfma_f32_16x16x32_bf16 v[2:5], v[180:183], v[212:215], v[2:5]
	s_setprio 0
	s_barrier
	s_add_i32 s74, 0, 0x18000
	s_add_i32 s75, 0, 0x1c000
	v_add_u32_e32 v156, s74, v165
	v_add_u32_e32 v166, s75, v165
	ds_read_b128 v[144:147], v156
	ds_read_b128 v[148:151], v156 offset:1024
	ds_read_b128 v[152:155], v156 offset:2048
	ds_read_b128 v[156:159], v156 offset:3072
	ds_read_b128 v[160:163], v166
	ds_read_b128 v[170:173], v166 offset:1024
	ds_read_b128 v[174:177], v166 offset:2048
	ds_read_b128 v[180:183], v166 offset:3072
	s_add_u32 s62, s62, 0x40000
	s_addc_u32 s63, s63, 0
	s_mov_b32 m0, s16
	v_lshl_add_u64 v[232:233], s[62:63], 0, v[134:135]
	ds_read_b128 v[184:187], v178 offset:32768
	ds_read_b128 v[188:191], v178 offset:33792
	ds_read_b128 v[192:195], v178 offset:34816
	ds_read_b128 v[196:199], v178 offset:35840
	ds_read_b128 v[200:203], v178 offset:36864
	ds_read_b128 v[204:207], v178 offset:37888
	ds_read_b128 v[208:211], v178 offset:38912
	ds_read_b128 v[212:215], v178 offset:39936
	global_load_lds_dwordx4 v[232:233], off
	v_lshl_add_u64 v[232:233], s[62:63], 0, v[136:137]
	s_mov_b32 m0, s25
	s_nop 0
	global_load_lds_dwordx4 v[232:233], off
	s_waitcnt vmcnt(8)
	s_waitcnt lgkmcnt(0)
	s_barrier
	s_setprio 1
	s_waitcnt lgkmcnt(0)
	v_mfma_f32_16x16x32_bf16 v[126:129], v[144:147], v[184:187], v[126:129]
	v_mfma_f32_16x16x32_bf16 v[122:125], v[152:155], v[184:187], v[122:125]
	v_mfma_f32_16x16x32_bf16 v[110:113], v[144:147], v[192:195], v[110:113]
	v_mfma_f32_16x16x32_bf16 v[106:109], v[152:155], v[192:195], v[106:109]
	v_mfma_f32_16x16x32_bf16 v[94:97], v[144:147], v[200:203], v[94:97]
	v_mfma_f32_16x16x32_bf16 v[90:93], v[152:155], v[200:203], v[90:93]
	v_mfma_f32_16x16x32_bf16 v[78:81], v[144:147], v[208:211], v[78:81]
	v_mfma_f32_16x16x32_bf16 v[74:77], v[152:155], v[208:211], v[74:77]
	v_mfma_f32_16x16x32_bf16 v[126:129], v[148:151], v[188:191], v[126:129]
	v_mfma_f32_16x16x32_bf16 v[122:125], v[156:159], v[188:191], v[122:125]
	v_mfma_f32_16x16x32_bf16 v[110:113], v[148:151], v[196:199], v[110:113]
	v_mfma_f32_16x16x32_bf16 v[106:109], v[156:159], v[196:199], v[106:109]
	v_mfma_f32_16x16x32_bf16 v[94:97], v[148:151], v[204:207], v[94:97]
	v_mfma_f32_16x16x32_bf16 v[90:93], v[156:159], v[204:207], v[90:93]
	v_mfma_f32_16x16x32_bf16 v[78:81], v[148:151], v[212:215], v[78:81]
	v_mfma_f32_16x16x32_bf16 v[74:77], v[156:159], v[212:215], v[74:77]
	s_setprio 0
	s_setprio 1
	v_mfma_f32_16x16x32_bf16 v[118:121], v[160:163], v[184:187], v[118:121]
	v_mfma_f32_16x16x32_bf16 v[114:117], v[174:177], v[184:187], v[114:117]
	v_mfma_f32_16x16x32_bf16 v[102:105], v[160:163], v[192:195], v[102:105]
	v_mfma_f32_16x16x32_bf16 v[98:101], v[174:177], v[192:195], v[98:101]
	v_mfma_f32_16x16x32_bf16 v[86:89], v[160:163], v[200:203], v[86:89]
	v_mfma_f32_16x16x32_bf16 v[82:85], v[174:177], v[200:203], v[82:85]
	v_mfma_f32_16x16x32_bf16 v[70:73], v[160:163], v[208:211], v[70:73]
	v_mfma_f32_16x16x32_bf16 v[66:69], v[174:177], v[208:211], v[66:69]
	v_mfma_f32_16x16x32_bf16 v[118:121], v[170:173], v[188:191], v[118:121]
	v_mfma_f32_16x16x32_bf16 v[114:117], v[180:183], v[188:191], v[114:117]
	v_mfma_f32_16x16x32_bf16 v[102:105], v[170:173], v[196:199], v[102:105]
	v_mfma_f32_16x16x32_bf16 v[98:101], v[180:183], v[196:199], v[98:101]
	v_mfma_f32_16x16x32_bf16 v[86:89], v[170:173], v[204:207], v[86:89]
	v_mfma_f32_16x16x32_bf16 v[82:85], v[180:183], v[204:207], v[82:85]
	v_mfma_f32_16x16x32_bf16 v[70:73], v[170:173], v[212:215], v[70:73]
	v_mfma_f32_16x16x32_bf16 v[66:69], v[180:183], v[212:215], v[66:69]
	s_setprio 0
	s_barrier
	s_add_i32 s62, s74, s1
	v_lshl_add_u64 v[216:217], v[216:217], 0, s[56:57]
	s_mov_b32 m0, s62
	ds_read_b128 v[184:187], v178 offset:49152
	ds_read_b128 v[188:191], v178 offset:50176
	ds_read_b128 v[192:195], v178 offset:51200
	ds_read_b128 v[196:199], v178 offset:52224
	ds_read_b128 v[200:203], v178 offset:53248
	ds_read_b128 v[204:207], v178 offset:54272
	ds_read_b128 v[208:211], v178 offset:55296
	ds_read_b128 v[212:215], v178 offset:56320
	global_load_lds_dwordx4 v[216:217], off
	s_add_i32 m0, s62, 0x2000
	s_add_u32 s60, s60, 0x40080
	v_lshl_add_u64 v[216:217], v[218:219], 0, s[56:57]
	s_addc_u32 s61, s61, 0
	s_add_i32 s62, s75, s1
	global_load_lds_dwordx4 v[216:217], off
	v_lshl_add_u64 v[216:217], s[60:61], 0, v[130:131]
	s_mov_b32 m0, s62
	s_nop 0
	global_load_lds_dwordx4 v[216:217], off
	v_lshl_add_u64 v[216:217], s[60:61], 0, v[132:133]
	s_add_i32 m0, s62, 0x2000
	s_nop 0
	global_load_lds_dwordx4 v[216:217], off
	v_lshl_add_u64 v[216:217], v[220:221], 0, s[56:57]
	s_mov_b32 m0, s64
	s_nop 0
	global_load_lds_dwordx4 v[216:217], off
	v_lshl_add_u64 v[216:217], v[222:223], 0, s[56:57]
	s_mov_b32 m0, s65
	s_nop 0
	global_load_lds_dwordx4 v[216:217], off
	s_waitcnt vmcnt(8)
	s_waitcnt lgkmcnt(0)
	s_barrier
	s_setprio 1
	s_waitcnt lgkmcnt(0)
	v_mfma_f32_16x16x32_bf16 v[62:65], v[144:147], v[184:187], v[62:65]
	v_mfma_f32_16x16x32_bf16 v[58:61], v[152:155], v[184:187], v[58:61]
	v_mfma_f32_16x16x32_bf16 v[46:49], v[144:147], v[192:195], v[46:49]
	v_mfma_f32_16x16x32_bf16 v[42:45], v[152:155], v[192:195], v[42:45]
	v_mfma_f32_16x16x32_bf16 v[30:33], v[144:147], v[200:203], v[30:33]
	v_mfma_f32_16x16x32_bf16 v[26:29], v[152:155], v[200:203], v[26:29]
	v_mfma_f32_16x16x32_bf16 v[14:17], v[144:147], v[208:211], v[14:17]
	v_mfma_f32_16x16x32_bf16 v[10:13], v[152:155], v[208:211], v[10:13]
	v_mfma_f32_16x16x32_bf16 v[62:65], v[148:151], v[188:191], v[62:65]
	v_mfma_f32_16x16x32_bf16 v[58:61], v[156:159], v[188:191], v[58:61]
	v_mfma_f32_16x16x32_bf16 v[46:49], v[148:151], v[196:199], v[46:49]
	v_mfma_f32_16x16x32_bf16 v[42:45], v[156:159], v[196:199], v[42:45]
	v_mfma_f32_16x16x32_bf16 v[30:33], v[148:151], v[204:207], v[30:33]
	v_mfma_f32_16x16x32_bf16 v[26:29], v[156:159], v[204:207], v[26:29]
	v_mfma_f32_16x16x32_bf16 v[14:17], v[148:151], v[212:215], v[14:17]
	v_mfma_f32_16x16x32_bf16 v[10:13], v[156:159], v[212:215], v[10:13]
	s_setprio 0
	s_setprio 1
	v_mfma_f32_16x16x32_bf16 v[54:57], v[160:163], v[184:187], v[54:57]
	v_mfma_f32_16x16x32_bf16 v[50:53], v[174:177], v[184:187], v[50:53]
	v_mfma_f32_16x16x32_bf16 v[38:41], v[160:163], v[192:195], v[38:41]
	v_mfma_f32_16x16x32_bf16 v[34:37], v[174:177], v[192:195], v[34:37]
	v_mfma_f32_16x16x32_bf16 v[22:25], v[160:163], v[200:203], v[22:25]
	v_mfma_f32_16x16x32_bf16 v[18:21], v[174:177], v[200:203], v[18:21]
	v_mfma_f32_16x16x32_bf16 v[6:9], v[160:163], v[208:211], v[6:9]
	v_mfma_f32_16x16x32_bf16 v[2:5], v[174:177], v[208:211], v[2:5]
	v_mfma_f32_16x16x32_bf16 v[54:57], v[170:173], v[188:191], v[54:57]
	v_mfma_f32_16x16x32_bf16 v[50:53], v[180:183], v[188:191], v[50:53]
	v_mfma_f32_16x16x32_bf16 v[38:41], v[170:173], v[196:199], v[38:41]
	v_mfma_f32_16x16x32_bf16 v[34:37], v[180:183], v[196:199], v[34:37]
	v_mfma_f32_16x16x32_bf16 v[22:25], v[170:173], v[204:207], v[22:25]
	v_mfma_f32_16x16x32_bf16 v[18:21], v[180:183], v[204:207], v[18:21]
	v_mfma_f32_16x16x32_bf16 v[6:9], v[170:173], v[212:215], v[6:9]
	v_mfma_f32_16x16x32_bf16 v[2:5], v[180:183], v[212:215], v[2:5]
	s_setprio 0
	s_add_u32 s71, s71, 0x100
	s_addc_u32 s72, s72, 0
	s_add_u32 s58, s58, 0x100
	s_addc_u32 s59, s59, 0
	s_cmp_ge_i32 s73, s0
	s_mov_b32 s60, s73
	s_cbranch_scc1 .Lrotph1b_pexitbar
	s_add_i32 s73, s60, 2
	s_add_u32 s61, s58, 0xfffc0080
	s_addc_u32 s62, s59, -1
	s_add_i32 s74, 0, 0x10000
	s_cmp_eq_u32 s68, s60
	s_cselect_b32 s63, s39, s62
	s_cselect_b32 s62, s43, s61
	s_cselect_b32 s61, s47, s72
	s_cselect_b32 s60, s55, s71
	s_add_i32 s76, 0, 0x14000
	s_barrier
	s_branch .Lrotph1b_body
.Lrotph1b_pexitbar:
	s_barrier
	s_branch .Lpeelexitph1b

.Lrotph1b_body:
	v_add_u32_e32 v156, s74, v165
	v_add_u32_e32 v166, s76, v165
	ds_read_b128 v[144:147], v156
	ds_read_b128 v[148:151], v156 offset:1024
	ds_read_b128 v[152:155], v156 offset:2048
	ds_read_b128 v[156:159], v156 offset:3072
	ds_read_b128 v[160:163], v166
	ds_read_b128 v[170:173], v166 offset:1024
	ds_read_b128 v[174:177], v166 offset:2048
	ds_read_b128 v[180:183], v166 offset:3072
	v_lshl_add_u64 v[216:217], s[58:59], 0, v[142:143]
	s_add_i32 m0, s8, 0xc000
	ds_read_b128 v[184:187], v178
	ds_read_b128 v[188:191], v178 offset:1024
	ds_read_b128 v[192:195], v178 offset:2048
	ds_read_b128 v[196:199], v178 offset:3072
	ds_read_b128 v[200:203], v178 offset:4096
	ds_read_b128 v[204:207], v178 offset:5120
	ds_read_b128 v[208:211], v178 offset:6144
	ds_read_b128 v[212:215], v178 offset:7168
	global_load_lds_dwordx4 v[216:217], off
	v_lshl_add_u64 v[216:217], s[58:59], 0, v[140:141]
	s_add_i32 m0, s8, 0xe000
	s_nop 0
	global_load_lds_dwordx4 v[216:217], off
	s_waitcnt vmcnt(8)
	s_waitcnt lgkmcnt(0)
	s_barrier
	s_setprio 1
	s_waitcnt lgkmcnt(0)
	v_mfma_f32_16x16x32_bf16 v[126:129], v[144:147], v[184:187], v[126:129]
	v_mfma_f32_16x16x32_bf16 v[122:125], v[152:155], v[184:187], v[122:125]
	v_mfma_f32_16x16x32_bf16 v[110:113], v[144:147], v[192:195], v[110:113]
	v_mfma_f32_16x16x32_bf16 v[106:109], v[152:155], v[192:195], v[106:109]
	v_mfma_f32_16x16x32_bf16 v[94:97], v[144:147], v[200:203], v[94:97]
	v_mfma_f32_16x16x32_bf16 v[90:93], v[152:155], v[200:203], v[90:93]
	v_mfma_f32_16x16x32_bf16 v[78:81], v[144:147], v[208:211], v[78:81]
	v_mfma_f32_16x16x32_bf16 v[74:77], v[152:155], v[208:211], v[74:77]
	v_mfma_f32_16x16x32_bf16 v[126:129], v[148:151], v[188:191], v[126:129]
	v_mfma_f32_16x16x32_bf16 v[122:125], v[156:159], v[188:191], v[122:125]
	v_mfma_f32_16x16x32_bf16 v[110:113], v[148:151], v[196:199], v[110:113]
	v_mfma_f32_16x16x32_bf16 v[106:109], v[156:159], v[196:199], v[106:109]
	v_mfma_f32_16x16x32_bf16 v[94:97], v[148:151], v[204:207], v[94:97]
	v_mfma_f32_16x16x32_bf16 v[90:93], v[156:159], v[204:207], v[90:93]
	v_mfma_f32_16x16x32_bf16 v[78:81], v[148:151], v[212:215], v[78:81]
	v_mfma_f32_16x16x32_bf16 v[74:77], v[156:159], v[212:215], v[74:77]
	s_setprio 0
	s_setprio 1
	v_mfma_f32_16x16x32_bf16 v[118:121], v[160:163], v[184:187], v[118:121]
	v_mfma_f32_16x16x32_bf16 v[114:117], v[174:177], v[184:187], v[114:117]
	v_mfma_f32_16x16x32_bf16 v[102:105], v[160:163], v[192:195], v[102:105]
	v_mfma_f32_16x16x32_bf16 v[98:101], v[174:177], v[192:195], v[98:101]
	v_mfma_f32_16x16x32_bf16 v[86:89], v[160:163], v[200:203], v[86:89]
	v_mfma_f32_16x16x32_bf16 v[82:85], v[174:177], v[200:203], v[82:85]
	v_mfma_f32_16x16x32_bf16 v[70:73], v[160:163], v[208:211], v[70:73]
	v_mfma_f32_16x16x32_bf16 v[66:69], v[174:177], v[208:211], v[66:69]
	v_mfma_f32_16x16x32_bf16 v[118:121], v[170:173], v[188:191], v[118:121]
	v_mfma_f32_16x16x32_bf16 v[114:117], v[180:183], v[188:191], v[114:117]
	v_mfma_f32_16x16x32_bf16 v[102:105], v[170:173], v[196:199], v[102:105]
	v_mfma_f32_16x16x32_bf16 v[98:101], v[180:183], v[196:199], v[98:101]
	v_mfma_f32_16x16x32_bf16 v[86:89], v[170:173], v[204:207], v[86:89]
	v_mfma_f32_16x16x32_bf16 v[82:85], v[180:183], v[204:207], v[82:85]
	v_mfma_f32_16x16x32_bf16 v[70:73], v[170:173], v[212:215], v[70:73]
	v_mfma_f32_16x16x32_bf16 v[66:69], v[180:183], v[212:215], v[66:69]
	s_setprio 0
	s_barrier
	s_add_i32 s74, s74, s1
	v_lshl_add_u64 v[216:217], s[60:61], 0, v[130:131]
	s_mov_b32 m0, s74
	ds_read_b128 v[184:187], v178 offset:16384
	ds_read_b128 v[188:191], v178 offset:17408
	ds_read_b128 v[192:195], v178 offset:18432
	ds_read_b128 v[196:199], v178 offset:19456
	ds_read_b128 v[200:203], v178 offset:20480
	ds_read_b128 v[204:207], v178 offset:21504
	ds_read_b128 v[208:211], v178 offset:22528
	ds_read_b128 v[212:215], v178 offset:23552
	global_load_lds_dwordx4 v[216:217], off
	s_add_i32 m0, s74, 0x2000
	s_add_u32 s74, s60, 0x40000
	v_lshl_add_u64 v[218:219], s[60:61], 0, v[132:133]
	s_addc_u32 s75, s61, 0
	s_add_i32 s76, s76, s1
	global_load_lds_dwordx4 v[218:219], off
	v_lshl_add_u64 v[220:221], s[74:75], 0, v[130:131]
	s_mov_b32 m0, s76
	v_lshl_add_u64 v[222:223], s[62:63], 0, v[136:137]
	global_load_lds_dwordx4 v[220:221], off
	v_lshl_add_u64 v[220:221], s[74:75], 0, v[132:133]
	s_add_i32 m0, s76, 0x2000
	s_nop 0
	global_load_lds_dwordx4 v[220:221], off
	v_lshl_add_u64 v[220:221], s[62:63], 0, v[134:135]
	s_mov_b32 m0, s8
	s_nop 0
	global_load_lds_dwordx4 v[220:221], off
	s_mov_b32 m0, s11
	s_nop 0
	global_load_lds_dwordx4 v[222:223], off
	s_waitcnt vmcnt(8)
	s_waitcnt lgkmcnt(0)
	s_barrier
	s_setprio 1
	s_waitcnt lgkmcnt(0)
	v_mfma_f32_16x16x32_bf16 v[62:65], v[144:147], v[184:187], v[62:65]
	v_mfma_f32_16x16x32_bf16 v[58:61], v[152:155], v[184:187], v[58:61]
	v_mfma_f32_16x16x32_bf16 v[46:49], v[144:147], v[192:195], v[46:49]
	v_mfma_f32_16x16x32_bf16 v[42:45], v[152:155], v[192:195], v[42:45]
	v_mfma_f32_16x16x32_bf16 v[30:33], v[144:147], v[200:203], v[30:33]
	v_mfma_f32_16x16x32_bf16 v[26:29], v[152:155], v[200:203], v[26:29]
	v_mfma_f32_16x16x32_bf16 v[14:17], v[144:147], v[208:211], v[14:17]
	v_mfma_f32_16x16x32_bf16 v[10:13], v[152:155], v[208:211], v[10:13]
	v_mfma_f32_16x16x32_bf16 v[62:65], v[148:151], v[188:191], v[62:65]
	v_mfma_f32_16x16x32_bf16 v[58:61], v[156:159], v[188:191], v[58:61]
	v_mfma_f32_16x16x32_bf16 v[46:49], v[148:151], v[196:199], v[46:49]
	v_mfma_f32_16x16x32_bf16 v[42:45], v[156:159], v[196:199], v[42:45]
	v_mfma_f32_16x16x32_bf16 v[30:33], v[148:151], v[204:207], v[30:33]
	v_mfma_f32_16x16x32_bf16 v[26:29], v[156:159], v[204:207], v[26:29]
	v_mfma_f32_16x16x32_bf16 v[14:17], v[148:151], v[212:215], v[14:17]
	v_mfma_f32_16x16x32_bf16 v[10:13], v[156:159], v[212:215], v[10:13]
	s_setprio 0
	s_setprio 1
	v_mfma_f32_16x16x32_bf16 v[54:57], v[160:163], v[184:187], v[54:57]
	v_mfma_f32_16x16x32_bf16 v[50:53], v[174:177], v[184:187], v[50:53]
	v_mfma_f32_16x16x32_bf16 v[38:41], v[160:163], v[192:195], v[38:41]
	v_mfma_f32_16x16x32_bf16 v[34:37], v[174:177], v[192:195], v[34:37]
	v_mfma_f32_16x16x32_bf16 v[22:25], v[160:163], v[200:203], v[22:25]
	v_mfma_f32_16x16x32_bf16 v[18:21], v[174:177], v[200:203], v[18:21]
	v_mfma_f32_16x16x32_bf16 v[6:9], v[160:163], v[208:211], v[6:9]
	v_mfma_f32_16x16x32_bf16 v[2:5], v[174:177], v[208:211], v[2:5]
	v_mfma_f32_16x16x32_bf16 v[54:57], v[170:173], v[188:191], v[54:57]
	v_mfma_f32_16x16x32_bf16 v[50:53], v[180:183], v[188:191], v[50:53]
	v_mfma_f32_16x16x32_bf16 v[38:41], v[170:173], v[196:199], v[38:41]
	v_mfma_f32_16x16x32_bf16 v[34:37], v[180:183], v[196:199], v[34:37]
	v_mfma_f32_16x16x32_bf16 v[22:25], v[170:173], v[204:207], v[22:25]
	v_mfma_f32_16x16x32_bf16 v[18:21], v[180:183], v[204:207], v[18:21]
	v_mfma_f32_16x16x32_bf16 v[6:9], v[170:173], v[212:215], v[6:9]
	v_mfma_f32_16x16x32_bf16 v[2:5], v[180:183], v[212:215], v[2:5]
	s_setprio 0
	s_barrier
	s_add_i32 s74, 0, 0x18000
	s_add_i32 s75, 0, 0x1c000
	v_add_u32_e32 v156, s74, v165
	v_add_u32_e32 v166, s75, v165
	ds_read_b128 v[144:147], v156
	ds_read_b128 v[148:151], v156 offset:1024
	ds_read_b128 v[152:155], v156 offset:2048
	ds_read_b128 v[156:159], v156 offset:3072
	ds_read_b128 v[160:163], v166
	ds_read_b128 v[170:173], v166 offset:1024
	ds_read_b128 v[174:177], v166 offset:2048
	ds_read_b128 v[180:183], v166 offset:3072
	s_add_u32 s62, s62, 0x40000
	s_addc_u32 s63, s63, 0
	s_mov_b32 m0, s16
	v_lshl_add_u64 v[232:233], s[62:63], 0, v[134:135]
	ds_read_b128 v[184:187], v178 offset:32768
	ds_read_b128 v[188:191], v178 offset:33792
	ds_read_b128 v[192:195], v178 offset:34816
	ds_read_b128 v[196:199], v178 offset:35840
	ds_read_b128 v[200:203], v178 offset:36864
	ds_read_b128 v[204:207], v178 offset:37888
	ds_read_b128 v[208:211], v178 offset:38912
	ds_read_b128 v[212:215], v178 offset:39936
	global_load_lds_dwordx4 v[232:233], off
	v_lshl_add_u64 v[232:233], s[62:63], 0, v[136:137]
	s_mov_b32 m0, s25
	s_nop 0
	global_load_lds_dwordx4 v[232:233], off
	s_waitcnt vmcnt(8)
	s_waitcnt lgkmcnt(0)
	s_barrier
	s_setprio 1
	s_waitcnt lgkmcnt(0)
	v_mfma_f32_16x16x32_bf16 v[126:129], v[144:147], v[184:187], v[126:129]
	v_mfma_f32_16x16x32_bf16 v[122:125], v[152:155], v[184:187], v[122:125]
	v_mfma_f32_16x16x32_bf16 v[110:113], v[144:147], v[192:195], v[110:113]
	v_mfma_f32_16x16x32_bf16 v[106:109], v[152:155], v[192:195], v[106:109]
	v_mfma_f32_16x16x32_bf16 v[94:97], v[144:147], v[200:203], v[94:97]
	v_mfma_f32_16x16x32_bf16 v[90:93], v[152:155], v[200:203], v[90:93]
	v_mfma_f32_16x16x32_bf16 v[78:81], v[144:147], v[208:211], v[78:81]
	v_mfma_f32_16x16x32_bf16 v[74:77], v[152:155], v[208:211], v[74:77]
	v_mfma_f32_16x16x32_bf16 v[126:129], v[148:151], v[188:191], v[126:129]
	v_mfma_f32_16x16x32_bf16 v[122:125], v[156:159], v[188:191], v[122:125]
	v_mfma_f32_16x16x32_bf16 v[110:113], v[148:151], v[196:199], v[110:113]
	v_mfma_f32_16x16x32_bf16 v[106:109], v[156:159], v[196:199], v[106:109]
	v_mfma_f32_16x16x32_bf16 v[94:97], v[148:151], v[204:207], v[94:97]
	v_mfma_f32_16x16x32_bf16 v[90:93], v[156:159], v[204:207], v[90:93]
	v_mfma_f32_16x16x32_bf16 v[78:81], v[148:151], v[212:215], v[78:81]
	v_mfma_f32_16x16x32_bf16 v[74:77], v[156:159], v[212:215], v[74:77]
	s_setprio 0
	s_setprio 1
	v_mfma_f32_16x16x32_bf16 v[118:121], v[160:163], v[184:187], v[118:121]
	v_mfma_f32_16x16x32_bf16 v[114:117], v[174:177], v[184:187], v[114:117]
	v_mfma_f32_16x16x32_bf16 v[102:105], v[160:163], v[192:195], v[102:105]
	v_mfma_f32_16x16x32_bf16 v[98:101], v[174:177], v[192:195], v[98:101]
	v_mfma_f32_16x16x32_bf16 v[86:89], v[160:163], v[200:203], v[86:89]
	v_mfma_f32_16x16x32_bf16 v[82:85], v[174:177], v[200:203], v[82:85]
	v_mfma_f32_16x16x32_bf16 v[70:73], v[160:163], v[208:211], v[70:73]
	v_mfma_f32_16x16x32_bf16 v[66:69], v[174:177], v[208:211], v[66:69]
	v_mfma_f32_16x16x32_bf16 v[118:121], v[170:173], v[188:191], v[118:121]
	v_mfma_f32_16x16x32_bf16 v[114:117], v[180:183], v[188:191], v[114:117]
	v_mfma_f32_16x16x32_bf16 v[102:105], v[170:173], v[196:199], v[102:105]
	v_mfma_f32_16x16x32_bf16 v[98:101], v[180:183], v[196:199], v[98:101]
	v_mfma_f32_16x16x32_bf16 v[86:89], v[170:173], v[204:207], v[86:89]
	v_mfma_f32_16x16x32_bf16 v[82:85], v[180:183], v[204:207], v[82:85]
	v_mfma_f32_16x16x32_bf16 v[70:73], v[170:173], v[212:215], v[70:73]
	v_mfma_f32_16x16x32_bf16 v[66:69], v[180:183], v[212:215], v[66:69]
	s_setprio 0
	s_barrier
	s_add_i32 s62, s74, s1
	v_lshl_add_u64 v[216:217], v[216:217], 0, s[56:57]
	s_mov_b32 m0, s62
	ds_read_b128 v[184:187], v178 offset:49152
	ds_read_b128 v[188:191], v178 offset:50176
	ds_read_b128 v[192:195], v178 offset:51200
	ds_read_b128 v[196:199], v178 offset:52224
	ds_read_b128 v[200:203], v178 offset:53248
	ds_read_b128 v[204:207], v178 offset:54272
	ds_read_b128 v[208:211], v178 offset:55296
	ds_read_b128 v[212:215], v178 offset:56320
	global_load_lds_dwordx4 v[216:217], off
	s_add_i32 m0, s62, 0x2000
	s_add_u32 s60, s60, 0x40080
	v_lshl_add_u64 v[216:217], v[218:219], 0, s[56:57]
	s_addc_u32 s61, s61, 0
	s_add_i32 s62, s75, s1
	global_load_lds_dwordx4 v[216:217], off
	v_lshl_add_u64 v[216:217], s[60:61], 0, v[130:131]
	s_mov_b32 m0, s62
	s_nop 0
	global_load_lds_dwordx4 v[216:217], off
	v_lshl_add_u64 v[216:217], s[60:61], 0, v[132:133]
	s_add_i32 m0, s62, 0x2000
	s_nop 0
	global_load_lds_dwordx4 v[216:217], off
	v_lshl_add_u64 v[216:217], v[220:221], 0, s[56:57]
	s_mov_b32 m0, s64
	s_nop 0
	global_load_lds_dwordx4 v[216:217], off
	v_lshl_add_u64 v[216:217], v[222:223], 0, s[56:57]
	s_mov_b32 m0, s65
	s_nop 0
	global_load_lds_dwordx4 v[216:217], off
	s_waitcnt vmcnt(8)
	s_waitcnt lgkmcnt(0)
	s_barrier
	s_setprio 1
	s_waitcnt lgkmcnt(0)
	v_mfma_f32_16x16x32_bf16 v[62:65], v[144:147], v[184:187], v[62:65]
	v_mfma_f32_16x16x32_bf16 v[58:61], v[152:155], v[184:187], v[58:61]
	v_mfma_f32_16x16x32_bf16 v[46:49], v[144:147], v[192:195], v[46:49]
	v_mfma_f32_16x16x32_bf16 v[42:45], v[152:155], v[192:195], v[42:45]
	v_mfma_f32_16x16x32_bf16 v[30:33], v[144:147], v[200:203], v[30:33]
	v_mfma_f32_16x16x32_bf16 v[26:29], v[152:155], v[200:203], v[26:29]
	v_mfma_f32_16x16x32_bf16 v[14:17], v[144:147], v[208:211], v[14:17]
	v_mfma_f32_16x16x32_bf16 v[10:13], v[152:155], v[208:211], v[10:13]
	v_mfma_f32_16x16x32_bf16 v[62:65], v[148:151], v[188:191], v[62:65]
	v_mfma_f32_16x16x32_bf16 v[58:61], v[156:159], v[188:191], v[58:61]
	v_mfma_f32_16x16x32_bf16 v[46:49], v[148:151], v[196:199], v[46:49]
	v_mfma_f32_16x16x32_bf16 v[42:45], v[156:159], v[196:199], v[42:45]
	v_mfma_f32_16x16x32_bf16 v[30:33], v[148:151], v[204:207], v[30:33]
	v_mfma_f32_16x16x32_bf16 v[26:29], v[156:159], v[204:207], v[26:29]
	v_mfma_f32_16x16x32_bf16 v[14:17], v[148:151], v[212:215], v[14:17]
	v_mfma_f32_16x16x32_bf16 v[10:13], v[156:159], v[212:215], v[10:13]
	s_setprio 0
	s_setprio 1
	v_mfma_f32_16x16x32_bf16 v[54:57], v[160:163], v[184:187], v[54:57]
	v_mfma_f32_16x16x32_bf16 v[50:53], v[174:177], v[184:187], v[50:53]
	v_mfma_f32_16x16x32_bf16 v[38:41], v[160:163], v[192:195], v[38:41]
	v_mfma_f32_16x16x32_bf16 v[34:37], v[174:177], v[192:195], v[34:37]
	v_mfma_f32_16x16x32_bf16 v[22:25], v[160:163], v[200:203], v[22:25]
	v_mfma_f32_16x16x32_bf16 v[18:21], v[174:177], v[200:203], v[18:21]
	v_mfma_f32_16x16x32_bf16 v[6:9], v[160:163], v[208:211], v[6:9]
	v_mfma_f32_16x16x32_bf16 v[2:5], v[174:177], v[208:211], v[2:5]
	v_mfma_f32_16x16x32_bf16 v[54:57], v[170:173], v[188:191], v[54:57]
	v_mfma_f32_16x16x32_bf16 v[50:53], v[180:183], v[188:191], v[50:53]
	v_mfma_f32_16x16x32_bf16 v[38:41], v[170:173], v[196:199], v[38:41]
	v_mfma_f32_16x16x32_bf16 v[34:37], v[180:183], v[196:199], v[34:37]
	v_mfma_f32_16x16x32_bf16 v[22:25], v[170:173], v[204:207], v[22:25]
	v_mfma_f32_16x16x32_bf16 v[18:21], v[180:183], v[204:207], v[18:21]
	v_mfma_f32_16x16x32_bf16 v[6:9], v[170:173], v[212:215], v[6:9]
	v_mfma_f32_16x16x32_bf16 v[2:5], v[180:183], v[212:215], v[2:5]
	s_setprio 0
	s_add_u32 s71, s71, 0x100
	s_addc_u32 s72, s72, 0
	s_add_u32 s58, s58, 0x100
	s_addc_u32 s59, s59, 0
	s_cmp_ge_i32 s73, s0
	s_mov_b32 s60, s73
	s_cbranch_scc1 .Lrotph1b_exitbar
	s_add_i32 s73, s60, 2
	s_add_u32 s61, s58, 0xfffc0080
	s_addc_u32 s62, s59, -1
	s_add_i32 s74, 0, 0x10000
	s_cmp_eq_u32 s68, s60
	s_cselect_b32 s63, s39, s62
	s_cselect_b32 s62, s43, s61
	s_cselect_b32 s61, s47, s72
	s_cselect_b32 s60, s55, s71
	s_add_i32 s76, 0, 0x14000
	s_barrier
	s_branch .Lrotph1b_body
.Lrotph1b_exitbar:
	s_barrier
.Lpeelexitph1b:
	s_mov_b64 s[72:73], 0xe800000
	v_mov_b32_e32 v209, v1
	s_and_b64 vcc, exec, s[34:35]
	s_cbranch_vccz .LBB0_232

.Lpeelph1f_0:
	s_add_i32 s71, s58, 2
	s_add_u32 s59, s54, 0xfffe0080
	s_addc_u32 s60, s55, -1
	s_add_i32 s72, 0, 0x10000
	s_cmp_eq_u32 s65, s58
	s_cselect_b32 s61, s39, s60
	s_cselect_b32 s60, s41, s59
	s_cselect_b32 s59, s43, s70
	s_cselect_b32 s58, s53, s69
	s_add_i32 s73, 0, 0x14000
	v_add_u32_e32 v2, s72, v198
	v_add_u32_e32 v6, s73, v198
	ds_read_b128 v[26:29], v2
	ds_read_b128 v[30:33], v2 offset:1024
	ds_read_b128 v[18:21], v2 offset:2048
	ds_read_b128 v[22:25], v2 offset:3072
	ds_read_b128 v[10:13], v6
	ds_read_b128 v[14:17], v6 offset:1024
	ds_read_b128 v[2:5], v6 offset:2048
	ds_read_b128 v[6:9], v6 offset:3072
	v_lshl_add_u64 v[170:171], s[54:55], 0, v[186:187]
	s_add_i32 m0, s8, 0xc000
	ds_read_b128 v[188:191], v200
	ds_read_b128 v[192:195], v200 offset:1024
	ds_read_b128 v[202:205], v200 offset:2048
	ds_read_b128 v[206:209], v200 offset:3072
	ds_read_b128 v[210:213], v200 offset:4096
	ds_read_b128 v[214:217], v200 offset:5120
	ds_read_b128 v[236:239], v200 offset:6144
	ds_read_b128 v[240:243], v200 offset:7168
	global_load_lds_dwordx4 v[170:171], off
	v_lshl_add_u64 v[170:171], s[54:55], 0, v[184:185]
	s_add_i32 m0, s8, 0xe000
	s_nop 0
	global_load_lds_dwordx4 v[170:171], off
	s_waitcnt vmcnt(8)
	s_waitcnt lgkmcnt(0)
	s_barrier
	s_setprio 1
	s_waitcnt lgkmcnt(0)
	v_mfma_scale_f32_16x16x128_f8f6f4 v[158:161], v[26:33], v[188:195], 0, v196, v169 op_sel_hi:[0,0,0]
	v_mfma_scale_f32_16x16x128_f8f6f4 v[154:157], v[18:25], v[188:195], 0, v196, v169 op_sel_hi:[0,0,0]
	v_mfma_scale_f32_16x16x128_f8f6f4 v[142:145], v[26:33], v[202:209], 0, v196, v169 op_sel_hi:[0,0,0]
	v_mfma_scale_f32_16x16x128_f8f6f4 v[138:141], v[18:25], v[202:209], 0, v196, v169 op_sel_hi:[0,0,0]
	v_mfma_scale_f32_16x16x128_f8f6f4 v[126:129], v[26:33], v[210:217], 0, v196, v169 op_sel_hi:[0,0,0]
	v_mfma_scale_f32_16x16x128_f8f6f4 v[122:125], v[18:25], v[210:217], 0, v196, v169 op_sel_hi:[0,0,0]
	v_mfma_scale_f32_16x16x128_f8f6f4 v[110:113], v[26:33], v[236:243], 0, v196, v169 op_sel_hi:[0,0,0]
	v_mfma_scale_f32_16x16x128_f8f6f4 v[106:109], v[18:25], v[236:243], 0, v196, v169 op_sel_hi:[0,0,0]
	s_setprio 0
	s_setprio 1
	v_mfma_scale_f32_16x16x128_f8f6f4 v[150:153], v[10:17], v[188:195], 0, v196, v169 op_sel_hi:[0,0,0]
	v_mfma_scale_f32_16x16x128_f8f6f4 v[146:149], v[2:9], v[188:195], 0, v196, v169 op_sel_hi:[0,0,0]
	v_mfma_scale_f32_16x16x128_f8f6f4 v[134:137], v[10:17], v[202:209], 0, v196, v169 op_sel_hi:[0,0,0]
	v_mfma_scale_f32_16x16x128_f8f6f4 v[130:133], v[2:9], v[202:209], 0, v196, v169 op_sel_hi:[0,0,0]
	v_mfma_scale_f32_16x16x128_f8f6f4 v[118:121], v[10:17], v[210:217], 0, v196, v169 op_sel_hi:[0,0,0]
	v_mfma_scale_f32_16x16x128_f8f6f4 v[114:117], v[2:9], v[210:217], 0, v196, v169 op_sel_hi:[0,0,0]
	v_mfma_scale_f32_16x16x128_f8f6f4 v[102:105], v[10:17], v[236:243], 0, v196, v169 op_sel_hi:[0,0,0]
	v_mfma_scale_f32_16x16x128_f8f6f4 v[98:101], v[2:9], v[236:243], 0, v196, v169 op_sel_hi:[0,0,0]
	s_setprio 0
	s_barrier
	s_add_i32 s72, s72, s1
	v_lshl_add_u64 v[188:189], s[58:59], 0, v[162:163]
	s_mov_b32 m0, s72
	ds_read_b128 v[202:205], v200 offset:16384
	ds_read_b128 v[206:209], v200 offset:17408
	ds_read_b128 v[210:213], v200 offset:18432
	ds_read_b128 v[214:217], v200 offset:19456
	ds_read_b128 v[236:239], v200 offset:20480
	ds_read_b128 v[240:243], v200 offset:21504
	ds_read_b128 v[244:247], v200 offset:22528
	ds_read_b128 v[248:251], v200 offset:23552
	global_load_lds_dwordx4 v[188:189], off
	s_add_i32 m0, s72, 0x2000
	s_add_u32 s74, s58, 0x20000
	v_lshl_add_u64 v[190:191], s[58:59], 0, v[164:165]
	s_addc_u32 s75, s59, 0
	s_add_i32 s72, s73, s1
	global_load_lds_dwordx4 v[190:191], off
	v_lshl_add_u64 v[170:171], s[74:75], 0, v[162:163]
	s_mov_b32 m0, s72
	v_lshl_add_u64 v[192:193], s[60:61], 0, v[178:179]
	global_load_lds_dwordx4 v[170:171], off
	v_lshl_add_u64 v[170:171], s[74:75], 0, v[164:165]
	s_add_i32 m0, s72, 0x2000
	v_lshl_add_u64 v[194:195], s[60:61], 0, v[180:181]
	global_load_lds_dwordx4 v[170:171], off
	s_mov_b32 m0, s8
	s_nop 0
	global_load_lds_dwordx4 v[192:193], off
	s_mov_b32 m0, s11
	s_nop 0
	global_load_lds_dwordx4 v[194:195], off
	s_waitcnt vmcnt(8)
	s_waitcnt lgkmcnt(0)
	s_barrier
	s_setprio 1
	s_waitcnt lgkmcnt(0)
	v_mfma_scale_f32_16x16x128_f8f6f4 v[94:97], v[26:33], v[202:209], 0, v196, v169 op_sel_hi:[0,0,0]
	v_mfma_scale_f32_16x16x128_f8f6f4 v[90:93], v[18:25], v[202:209], 0, v196, v169 op_sel_hi:[0,0,0]
	v_mfma_scale_f32_16x16x128_f8f6f4 v[78:81], v[26:33], v[210:217], 0, v196, v169 op_sel_hi:[0,0,0]
	v_mfma_scale_f32_16x16x128_f8f6f4 v[74:77], v[18:25], v[210:217], 0, v196, v169 op_sel_hi:[0,0,0]
	v_mfma_scale_f32_16x16x128_f8f6f4 v[62:65], v[26:33], v[236:243], 0, v196, v169 op_sel_hi:[0,0,0]
	v_mfma_scale_f32_16x16x128_f8f6f4 v[58:61], v[18:25], v[236:243], 0, v196, v169 op_sel_hi:[0,0,0]
	v_mfma_scale_f32_16x16x128_f8f6f4 v[46:49], v[26:33], v[244:251], 0, v196, v169 op_sel_hi:[0,0,0]
	v_mfma_scale_f32_16x16x128_f8f6f4 v[42:45], v[18:25], v[244:251], 0, v196, v169 op_sel_hi:[0,0,0]
	s_setprio 0
	s_setprio 1
	v_mfma_scale_f32_16x16x128_f8f6f4 v[86:89], v[10:17], v[202:209], 0, v196, v169 op_sel_hi:[0,0,0]
	v_mfma_scale_f32_16x16x128_f8f6f4 v[82:85], v[2:9], v[202:209], 0, v196, v169 op_sel_hi:[0,0,0]
	v_mfma_scale_f32_16x16x128_f8f6f4 v[70:73], v[10:17], v[210:217], 0, v196, v169 op_sel_hi:[0,0,0]
	v_mfma_scale_f32_16x16x128_f8f6f4 v[66:69], v[2:9], v[210:217], 0, v196, v169 op_sel_hi:[0,0,0]
	v_mfma_scale_f32_16x16x128_f8f6f4 v[54:57], v[10:17], v[236:243], 0, v196, v169 op_sel_hi:[0,0,0]
	v_mfma_scale_f32_16x16x128_f8f6f4 v[50:53], v[2:9], v[236:243], 0, v196, v169 op_sel_hi:[0,0,0]
	v_mfma_scale_f32_16x16x128_f8f6f4 v[38:41], v[10:17], v[244:251], 0, v196, v169 op_sel_hi:[0,0,0]
	v_mfma_scale_f32_16x16x128_f8f6f4 v[34:37], v[2:9], v[244:251], 0, v196, v169 op_sel_hi:[0,0,0]
	s_setprio 0
	s_barrier
	s_add_i32 s72, 0, 0x18000
	s_add_i32 s73, 0, 0x1c000
	v_add_u32_e32 v2, s72, v198
	v_add_u32_e32 v6, s73, v198
	ds_read_b128 v[26:29], v2
	ds_read_b128 v[30:33], v2 offset:1024
	ds_read_b128 v[18:21], v2 offset:2048
	ds_read_b128 v[22:25], v2 offset:3072
	ds_read_b128 v[10:13], v6
	ds_read_b128 v[14:17], v6 offset:1024
	ds_read_b128 v[2:5], v6 offset:2048
	ds_read_b128 v[6:9], v6 offset:3072
	s_add_u32 s60, s60, 0x20000
	s_addc_u32 s61, s61, 0
	s_mov_b32 m0, s16
	v_lshl_add_u64 v[170:171], s[60:61], 0, v[178:179]
	ds_read_b128 v[202:205], v200 offset:32768
	ds_read_b128 v[206:209], v200 offset:33792
	ds_read_b128 v[210:213], v200 offset:34816
	ds_read_b128 v[214:217], v200 offset:35840
	ds_read_b128 v[236:239], v200 offset:36864
	ds_read_b128 v[240:243], v200 offset:37888
	ds_read_b128 v[244:247], v200 offset:38912
	ds_read_b128 v[248:251], v200 offset:39936
	global_load_lds_dwordx4 v[170:171], off
	v_lshl_add_u64 v[170:171], s[60:61], 0, v[180:181]
	s_mov_b32 m0, s25
	s_nop 0
	global_load_lds_dwordx4 v[170:171], off
	s_waitcnt vmcnt(8)
	s_waitcnt lgkmcnt(0)
	s_barrier
	s_setprio 1
	s_waitcnt lgkmcnt(0)
	v_mfma_scale_f32_16x16x128_f8f6f4 v[158:161], v[26:33], v[202:209], v[158:161], v196, v169 op_sel_hi:[0,0,0]
	v_mfma_scale_f32_16x16x128_f8f6f4 v[154:157], v[18:25], v[202:209], v[154:157], v196, v169 op_sel_hi:[0,0,0]
	v_mfma_scale_f32_16x16x128_f8f6f4 v[142:145], v[26:33], v[210:217], v[142:145], v196, v169 op_sel_hi:[0,0,0]
	v_mfma_scale_f32_16x16x128_f8f6f4 v[138:141], v[18:25], v[210:217], v[138:141], v196, v169 op_sel_hi:[0,0,0]
	v_mfma_scale_f32_16x16x128_f8f6f4 v[126:129], v[26:33], v[236:243], v[126:129], v196, v169 op_sel_hi:[0,0,0]
	v_mfma_scale_f32_16x16x128_f8f6f4 v[122:125], v[18:25], v[236:243], v[122:125], v196, v169 op_sel_hi:[0,0,0]
	v_mfma_scale_f32_16x16x128_f8f6f4 v[110:113], v[26:33], v[244:251], v[110:113], v196, v169 op_sel_hi:[0,0,0]
	v_mfma_scale_f32_16x16x128_f8f6f4 v[106:109], v[18:25], v[244:251], v[106:109], v196, v169 op_sel_hi:[0,0,0]
	s_setprio 0
	s_setprio 1
	v_mfma_scale_f32_16x16x128_f8f6f4 v[150:153], v[10:17], v[202:209], v[150:153], v196, v169 op_sel_hi:[0,0,0]
	v_mfma_scale_f32_16x16x128_f8f6f4 v[146:149], v[2:9], v[202:209], v[146:149], v196, v169 op_sel_hi:[0,0,0]
	v_mfma_scale_f32_16x16x128_f8f6f4 v[134:137], v[10:17], v[210:217], v[134:137], v196, v169 op_sel_hi:[0,0,0]
	v_mfma_scale_f32_16x16x128_f8f6f4 v[130:133], v[2:9], v[210:217], v[130:133], v196, v169 op_sel_hi:[0,0,0]
	v_mfma_scale_f32_16x16x128_f8f6f4 v[118:121], v[10:17], v[236:243], v[118:121], v196, v169 op_sel_hi:[0,0,0]
	v_mfma_scale_f32_16x16x128_f8f6f4 v[114:117], v[2:9], v[236:243], v[114:117], v196, v169 op_sel_hi:[0,0,0]
	v_mfma_scale_f32_16x16x128_f8f6f4 v[102:105], v[10:17], v[244:251], v[102:105], v196, v169 op_sel_hi:[0,0,0]
	v_mfma_scale_f32_16x16x128_f8f6f4 v[98:101], v[2:9], v[244:251], v[98:101], v196, v169 op_sel_hi:[0,0,0]
	s_setprio 0
	s_barrier
	s_add_i32 s60, s72, s1
	v_lshl_add_u64 v[170:171], v[188:189], 0, s[56:57]
	s_mov_b32 m0, s60
	ds_read_b128 v[202:205], v200 offset:49152
	ds_read_b128 v[206:209], v200 offset:50176
	ds_read_b128 v[210:213], v200 offset:51200
	ds_read_b128 v[214:217], v200 offset:52224
	ds_read_b128 v[236:239], v200 offset:53248
	ds_read_b128 v[240:243], v200 offset:54272
	ds_read_b128 v[244:247], v200 offset:55296
	ds_read_b128 v[248:251], v200 offset:56320
	global_load_lds_dwordx4 v[170:171], off
	s_add_i32 m0, s60, 0x2000
	s_add_u32 s58, s58, 0x20080
	v_lshl_add_u64 v[170:171], v[190:191], 0, s[56:57]
	s_addc_u32 s59, s59, 0
	s_add_i32 s60, s73, s1
	global_load_lds_dwordx4 v[170:171], off
	v_lshl_add_u64 v[170:171], s[58:59], 0, v[162:163]
	s_mov_b32 m0, s60
	s_nop 0
	global_load_lds_dwordx4 v[170:171], off
	v_lshl_add_u64 v[170:171], s[58:59], 0, v[164:165]
	s_add_i32 m0, s60, 0x2000
	s_nop 0
	global_load_lds_dwordx4 v[170:171], off
	v_lshl_add_u64 v[170:171], v[192:193], 0, s[56:57]
	s_mov_b32 m0, s62
	s_nop 0
	global_load_lds_dwordx4 v[170:171], off
	v_lshl_add_u64 v[170:171], v[194:195], 0, s[56:57]
	s_mov_b32 m0, s63
	s_nop 0
	global_load_lds_dwordx4 v[170:171], off
	s_waitcnt vmcnt(8)
	s_waitcnt lgkmcnt(0)
	s_barrier
	s_setprio 1
	s_waitcnt lgkmcnt(0)
	v_mfma_scale_f32_16x16x128_f8f6f4 v[94:97], v[26:33], v[202:209], v[94:97], v196, v169 op_sel_hi:[0,0,0]
	v_mfma_scale_f32_16x16x128_f8f6f4 v[90:93], v[18:25], v[202:209], v[90:93], v196, v169 op_sel_hi:[0,0,0]
	v_mfma_scale_f32_16x16x128_f8f6f4 v[78:81], v[26:33], v[210:217], v[78:81], v196, v169 op_sel_hi:[0,0,0]
	v_mfma_scale_f32_16x16x128_f8f6f4 v[74:77], v[18:25], v[210:217], v[74:77], v196, v169 op_sel_hi:[0,0,0]
	v_mfma_scale_f32_16x16x128_f8f6f4 v[62:65], v[26:33], v[236:243], v[62:65], v196, v169 op_sel_hi:[0,0,0]
	v_mfma_scale_f32_16x16x128_f8f6f4 v[58:61], v[18:25], v[236:243], v[58:61], v196, v169 op_sel_hi:[0,0,0]
	v_mfma_scale_f32_16x16x128_f8f6f4 v[46:49], v[26:33], v[244:251], v[46:49], v196, v169 op_sel_hi:[0,0,0]
	v_mfma_scale_f32_16x16x128_f8f6f4 v[42:45], v[18:25], v[244:251], v[42:45], v196, v169 op_sel_hi:[0,0,0]
	s_setprio 0
	s_setprio 1
	v_mfma_scale_f32_16x16x128_f8f6f4 v[86:89], v[10:17], v[202:209], v[86:89], v196, v169 op_sel_hi:[0,0,0]
	v_mfma_scale_f32_16x16x128_f8f6f4 v[82:85], v[2:9], v[202:209], v[82:85], v196, v169 op_sel_hi:[0,0,0]
	v_mfma_scale_f32_16x16x128_f8f6f4 v[70:73], v[10:17], v[210:217], v[70:73], v196, v169 op_sel_hi:[0,0,0]
	v_mfma_scale_f32_16x16x128_f8f6f4 v[66:69], v[2:9], v[210:217], v[66:69], v196, v169 op_sel_hi:[0,0,0]
	v_mfma_scale_f32_16x16x128_f8f6f4 v[54:57], v[10:17], v[236:243], v[54:57], v196, v169 op_sel_hi:[0,0,0]
	v_mfma_scale_f32_16x16x128_f8f6f4 v[50:53], v[2:9], v[236:243], v[50:53], v196, v169 op_sel_hi:[0,0,0]
	v_mfma_scale_f32_16x16x128_f8f6f4 v[38:41], v[10:17], v[244:251], v[38:41], v196, v169 op_sel_hi:[0,0,0]
	v_mfma_scale_f32_16x16x128_f8f6f4 v[34:37], v[2:9], v[244:251], v[34:37], v196, v169 op_sel_hi:[0,0,0]
	s_setprio 0
	s_add_u32 s69, s69, 0x100
	s_addc_u32 s70, s70, 0
	s_add_u32 s54, s54, 0x100
	s_addc_u32 s55, s55, 0
	s_cmp_ge_i32 s71, s0
	s_mov_b32 s58, s71
	s_cbranch_scc1 .Lrotph1f_pexitbar
	s_add_i32 s71, s58, 2
	s_add_u32 s59, s54, 0xfffe0080
	s_addc_u32 s60, s55, -1
	s_add_i32 s72, 0, 0x10000
	s_cmp_eq_u32 s65, s58
	s_cselect_b32 s61, s39, s60
	s_cselect_b32 s60, s41, s59
	s_cselect_b32 s59, s43, s70
	s_cselect_b32 s58, s53, s69
	s_add_i32 s73, 0, 0x14000
	s_barrier
	s_branch .Lrotph1f_body

.Lrotph1f_body:
	v_add_u32_e32 v2, s72, v198
	v_add_u32_e32 v6, s73, v198
	ds_read_b128 v[26:29], v2
	ds_read_b128 v[30:33], v2 offset:1024
	ds_read_b128 v[18:21], v2 offset:2048
	ds_read_b128 v[22:25], v2 offset:3072
	ds_read_b128 v[10:13], v6
	ds_read_b128 v[14:17], v6 offset:1024
	ds_read_b128 v[2:5], v6 offset:2048
	ds_read_b128 v[6:9], v6 offset:3072
	v_lshl_add_u64 v[170:171], s[54:55], 0, v[186:187]
	s_add_i32 m0, s8, 0xc000
	ds_read_b128 v[188:191], v200
	ds_read_b128 v[192:195], v200 offset:1024
	ds_read_b128 v[202:205], v200 offset:2048
	ds_read_b128 v[206:209], v200 offset:3072
	ds_read_b128 v[210:213], v200 offset:4096
	ds_read_b128 v[214:217], v200 offset:5120
	ds_read_b128 v[236:239], v200 offset:6144
	ds_read_b128 v[240:243], v200 offset:7168
	global_load_lds_dwordx4 v[170:171], off
	v_lshl_add_u64 v[170:171], s[54:55], 0, v[184:185]
	s_add_i32 m0, s8, 0xe000
	s_nop 0
	global_load_lds_dwordx4 v[170:171], off
	s_waitcnt vmcnt(8)
	s_waitcnt lgkmcnt(0)
	s_barrier
	s_setprio 1
	s_waitcnt lgkmcnt(0)
	v_mfma_scale_f32_16x16x128_f8f6f4 v[158:161], v[26:33], v[188:195], v[158:161], v196, v169 op_sel_hi:[0,0,0]
	v_mfma_scale_f32_16x16x128_f8f6f4 v[154:157], v[18:25], v[188:195], v[154:157], v196, v169 op_sel_hi:[0,0,0]
	v_mfma_scale_f32_16x16x128_f8f6f4 v[142:145], v[26:33], v[202:209], v[142:145], v196, v169 op_sel_hi:[0,0,0]
	v_mfma_scale_f32_16x16x128_f8f6f4 v[138:141], v[18:25], v[202:209], v[138:141], v196, v169 op_sel_hi:[0,0,0]
	v_mfma_scale_f32_16x16x128_f8f6f4 v[126:129], v[26:33], v[210:217], v[126:129], v196, v169 op_sel_hi:[0,0,0]
	v_mfma_scale_f32_16x16x128_f8f6f4 v[122:125], v[18:25], v[210:217], v[122:125], v196, v169 op_sel_hi:[0,0,0]
	v_mfma_scale_f32_16x16x128_f8f6f4 v[110:113], v[26:33], v[236:243], v[110:113], v196, v169 op_sel_hi:[0,0,0]
	v_mfma_scale_f32_16x16x128_f8f6f4 v[106:109], v[18:25], v[236:243], v[106:109], v196, v169 op_sel_hi:[0,0,0]
	s_setprio 0
	s_setprio 1
	v_mfma_scale_f32_16x16x128_f8f6f4 v[150:153], v[10:17], v[188:195], v[150:153], v196, v169 op_sel_hi:[0,0,0]
	v_mfma_scale_f32_16x16x128_f8f6f4 v[146:149], v[2:9], v[188:195], v[146:149], v196, v169 op_sel_hi:[0,0,0]
	v_mfma_scale_f32_16x16x128_f8f6f4 v[134:137], v[10:17], v[202:209], v[134:137], v196, v169 op_sel_hi:[0,0,0]
	v_mfma_scale_f32_16x16x128_f8f6f4 v[130:133], v[2:9], v[202:209], v[130:133], v196, v169 op_sel_hi:[0,0,0]
	v_mfma_scale_f32_16x16x128_f8f6f4 v[118:121], v[10:17], v[210:217], v[118:121], v196, v169 op_sel_hi:[0,0,0]
	v_mfma_scale_f32_16x16x128_f8f6f4 v[114:117], v[2:9], v[210:217], v[114:117], v196, v169 op_sel_hi:[0,0,0]
	v_mfma_scale_f32_16x16x128_f8f6f4 v[102:105], v[10:17], v[236:243], v[102:105], v196, v169 op_sel_hi:[0,0,0]
	v_mfma_scale_f32_16x16x128_f8f6f4 v[98:101], v[2:9], v[236:243], v[98:101], v196, v169 op_sel_hi:[0,0,0]
	s_setprio 0
	s_barrier
	s_add_i32 s72, s72, s1
	v_lshl_add_u64 v[188:189], s[58:59], 0, v[162:163]
	s_mov_b32 m0, s72
	ds_read_b128 v[202:205], v200 offset:16384
	ds_read_b128 v[206:209], v200 offset:17408
	ds_read_b128 v[210:213], v200 offset:18432
	ds_read_b128 v[214:217], v200 offset:19456
	ds_read_b128 v[236:239], v200 offset:20480
	ds_read_b128 v[240:243], v200 offset:21504
	ds_read_b128 v[244:247], v200 offset:22528
	ds_read_b128 v[248:251], v200 offset:23552
	global_load_lds_dwordx4 v[188:189], off
	s_add_i32 m0, s72, 0x2000
	s_add_u32 s74, s58, 0x20000
	v_lshl_add_u64 v[190:191], s[58:59], 0, v[164:165]
	s_addc_u32 s75, s59, 0
	s_add_i32 s72, s73, s1
	global_load_lds_dwordx4 v[190:191], off
	v_lshl_add_u64 v[170:171], s[74:75], 0, v[162:163]
	s_mov_b32 m0, s72
	v_lshl_add_u64 v[192:193], s[60:61], 0, v[178:179]
	global_load_lds_dwordx4 v[170:171], off
	v_lshl_add_u64 v[170:171], s[74:75], 0, v[164:165]
	s_add_i32 m0, s72, 0x2000
	v_lshl_add_u64 v[194:195], s[60:61], 0, v[180:181]
	global_load_lds_dwordx4 v[170:171], off
	s_mov_b32 m0, s8
	s_nop 0
	global_load_lds_dwordx4 v[192:193], off
	s_mov_b32 m0, s11
	s_nop 0
	global_load_lds_dwordx4 v[194:195], off
	s_waitcnt vmcnt(8)
	s_waitcnt lgkmcnt(0)
	s_barrier
	s_setprio 1
	s_waitcnt lgkmcnt(0)
	v_mfma_scale_f32_16x16x128_f8f6f4 v[94:97], v[26:33], v[202:209], v[94:97], v196, v169 op_sel_hi:[0,0,0]
	v_mfma_scale_f32_16x16x128_f8f6f4 v[90:93], v[18:25], v[202:209], v[90:93], v196, v169 op_sel_hi:[0,0,0]
	v_mfma_scale_f32_16x16x128_f8f6f4 v[78:81], v[26:33], v[210:217], v[78:81], v196, v169 op_sel_hi:[0,0,0]
	v_mfma_scale_f32_16x16x128_f8f6f4 v[74:77], v[18:25], v[210:217], v[74:77], v196, v169 op_sel_hi:[0,0,0]
	v_mfma_scale_f32_16x16x128_f8f6f4 v[62:65], v[26:33], v[236:243], v[62:65], v196, v169 op_sel_hi:[0,0,0]
	v_mfma_scale_f32_16x16x128_f8f6f4 v[58:61], v[18:25], v[236:243], v[58:61], v196, v169 op_sel_hi:[0,0,0]
	v_mfma_scale_f32_16x16x128_f8f6f4 v[46:49], v[26:33], v[244:251], v[46:49], v196, v169 op_sel_hi:[0,0,0]
	v_mfma_scale_f32_16x16x128_f8f6f4 v[42:45], v[18:25], v[244:251], v[42:45], v196, v169 op_sel_hi:[0,0,0]
	s_setprio 0
	s_setprio 1
	v_mfma_scale_f32_16x16x128_f8f6f4 v[86:89], v[10:17], v[202:209], v[86:89], v196, v169 op_sel_hi:[0,0,0]
	v_mfma_scale_f32_16x16x128_f8f6f4 v[82:85], v[2:9], v[202:209], v[82:85], v196, v169 op_sel_hi:[0,0,0]
	v_mfma_scale_f32_16x16x128_f8f6f4 v[70:73], v[10:17], v[210:217], v[70:73], v196, v169 op_sel_hi:[0,0,0]
	v_mfma_scale_f32_16x16x128_f8f6f4 v[66:69], v[2:9], v[210:217], v[66:69], v196, v169 op_sel_hi:[0,0,0]
	v_mfma_scale_f32_16x16x128_f8f6f4 v[54:57], v[10:17], v[236:243], v[54:57], v196, v169 op_sel_hi:[0,0,0]
	v_mfma_scale_f32_16x16x128_f8f6f4 v[50:53], v[2:9], v[236:243], v[50:53], v196, v169 op_sel_hi:[0,0,0]
	v_mfma_scale_f32_16x16x128_f8f6f4 v[38:41], v[10:17], v[244:251], v[38:41], v196, v169 op_sel_hi:[0,0,0]
	v_mfma_scale_f32_16x16x128_f8f6f4 v[34:37], v[2:9], v[244:251], v[34:37], v196, v169 op_sel_hi:[0,0,0]
	s_setprio 0
	s_barrier
	s_add_i32 s72, 0, 0x18000
	s_add_i32 s73, 0, 0x1c000
	v_add_u32_e32 v2, s72, v198
	v_add_u32_e32 v6, s73, v198
	ds_read_b128 v[26:29], v2
	ds_read_b128 v[30:33], v2 offset:1024
	ds_read_b128 v[18:21], v2 offset:2048
	ds_read_b128 v[22:25], v2 offset:3072
	ds_read_b128 v[10:13], v6
	ds_read_b128 v[14:17], v6 offset:1024
	ds_read_b128 v[2:5], v6 offset:2048
	ds_read_b128 v[6:9], v6 offset:3072
	s_add_u32 s60, s60, 0x20000
	s_addc_u32 s61, s61, 0
	s_mov_b32 m0, s16
	v_lshl_add_u64 v[170:171], s[60:61], 0, v[178:179]
	ds_read_b128 v[202:205], v200 offset:32768
	ds_read_b128 v[206:209], v200 offset:33792
	ds_read_b128 v[210:213], v200 offset:34816
	ds_read_b128 v[214:217], v200 offset:35840
	ds_read_b128 v[236:239], v200 offset:36864
	ds_read_b128 v[240:243], v200 offset:37888
	ds_read_b128 v[244:247], v200 offset:38912
	ds_read_b128 v[248:251], v200 offset:39936
	global_load_lds_dwordx4 v[170:171], off
	v_lshl_add_u64 v[170:171], s[60:61], 0, v[180:181]
	s_mov_b32 m0, s25
	s_nop 0
	global_load_lds_dwordx4 v[170:171], off
	s_waitcnt vmcnt(8)
	s_waitcnt lgkmcnt(0)
	s_barrier
	s_setprio 1
	s_waitcnt lgkmcnt(0)
	v_mfma_scale_f32_16x16x128_f8f6f4 v[158:161], v[26:33], v[202:209], v[158:161], v196, v169 op_sel_hi:[0,0,0]
	v_mfma_scale_f32_16x16x128_f8f6f4 v[154:157], v[18:25], v[202:209], v[154:157], v196, v169 op_sel_hi:[0,0,0]
	v_mfma_scale_f32_16x16x128_f8f6f4 v[142:145], v[26:33], v[210:217], v[142:145], v196, v169 op_sel_hi:[0,0,0]
	v_mfma_scale_f32_16x16x128_f8f6f4 v[138:141], v[18:25], v[210:217], v[138:141], v196, v169 op_sel_hi:[0,0,0]
	v_mfma_scale_f32_16x16x128_f8f6f4 v[126:129], v[26:33], v[236:243], v[126:129], v196, v169 op_sel_hi:[0,0,0]
	v_mfma_scale_f32_16x16x128_f8f6f4 v[122:125], v[18:25], v[236:243], v[122:125], v196, v169 op_sel_hi:[0,0,0]
	v_mfma_scale_f32_16x16x128_f8f6f4 v[110:113], v[26:33], v[244:251], v[110:113], v196, v169 op_sel_hi:[0,0,0]
	v_mfma_scale_f32_16x16x128_f8f6f4 v[106:109], v[18:25], v[244:251], v[106:109], v196, v169 op_sel_hi:[0,0,0]
	s_setprio 0
	s_setprio 1
	v_mfma_scale_f32_16x16x128_f8f6f4 v[150:153], v[10:17], v[202:209], v[150:153], v196, v169 op_sel_hi:[0,0,0]
	v_mfma_scale_f32_16x16x128_f8f6f4 v[146:149], v[2:9], v[202:209], v[146:149], v196, v169 op_sel_hi:[0,0,0]
	v_mfma_scale_f32_16x16x128_f8f6f4 v[134:137], v[10:17], v[210:217], v[134:137], v196, v169 op_sel_hi:[0,0,0]
	v_mfma_scale_f32_16x16x128_f8f6f4 v[130:133], v[2:9], v[210:217], v[130:133], v196, v169 op_sel_hi:[0,0,0]
	v_mfma_scale_f32_16x16x128_f8f6f4 v[118:121], v[10:17], v[236:243], v[118:121], v196, v169 op_sel_hi:[0,0,0]
	v_mfma_scale_f32_16x16x128_f8f6f4 v[114:117], v[2:9], v[236:243], v[114:117], v196, v169 op_sel_hi:[0,0,0]
	v_mfma_scale_f32_16x16x128_f8f6f4 v[102:105], v[10:17], v[244:251], v[102:105], v196, v169 op_sel_hi:[0,0,0]
	v_mfma_scale_f32_16x16x128_f8f6f4 v[98:101], v[2:9], v[244:251], v[98:101], v196, v169 op_sel_hi:[0,0,0]
	s_setprio 0
	s_barrier
	s_add_i32 s60, s72, s1
	v_lshl_add_u64 v[170:171], v[188:189], 0, s[56:57]
	s_mov_b32 m0, s60
	ds_read_b128 v[202:205], v200 offset:49152
	ds_read_b128 v[206:209], v200 offset:50176
	ds_read_b128 v[210:213], v200 offset:51200
	ds_read_b128 v[214:217], v200 offset:52224
	ds_read_b128 v[236:239], v200 offset:53248
	ds_read_b128 v[240:243], v200 offset:54272
	ds_read_b128 v[244:247], v200 offset:55296
	ds_read_b128 v[248:251], v200 offset:56320
	global_load_lds_dwordx4 v[170:171], off
	s_add_i32 m0, s60, 0x2000
	s_add_u32 s58, s58, 0x20080
	v_lshl_add_u64 v[170:171], v[190:191], 0, s[56:57]
	s_addc_u32 s59, s59, 0
	s_add_i32 s60, s73, s1
	global_load_lds_dwordx4 v[170:171], off
	v_lshl_add_u64 v[170:171], s[58:59], 0, v[162:163]
	s_mov_b32 m0, s60
	s_nop 0
	global_load_lds_dwordx4 v[170:171], off
	v_lshl_add_u64 v[170:171], s[58:59], 0, v[164:165]
	s_add_i32 m0, s60, 0x2000
	s_nop 0
	global_load_lds_dwordx4 v[170:171], off
	v_lshl_add_u64 v[170:171], v[192:193], 0, s[56:57]
	s_mov_b32 m0, s62
	s_nop 0
	global_load_lds_dwordx4 v[170:171], off
	v_lshl_add_u64 v[170:171], v[194:195], 0, s[56:57]
	s_mov_b32 m0, s63
	s_nop 0
	global_load_lds_dwordx4 v[170:171], off
	s_waitcnt vmcnt(8)
	s_waitcnt lgkmcnt(0)
	s_barrier
	s_setprio 1
	s_waitcnt lgkmcnt(0)
	v_mfma_scale_f32_16x16x128_f8f6f4 v[94:97], v[26:33], v[202:209], v[94:97], v196, v169 op_sel_hi:[0,0,0]
	v_mfma_scale_f32_16x16x128_f8f6f4 v[90:93], v[18:25], v[202:209], v[90:93], v196, v169 op_sel_hi:[0,0,0]
	v_mfma_scale_f32_16x16x128_f8f6f4 v[78:81], v[26:33], v[210:217], v[78:81], v196, v169 op_sel_hi:[0,0,0]
	v_mfma_scale_f32_16x16x128_f8f6f4 v[74:77], v[18:25], v[210:217], v[74:77], v196, v169 op_sel_hi:[0,0,0]
	v_mfma_scale_f32_16x16x128_f8f6f4 v[62:65], v[26:33], v[236:243], v[62:65], v196, v169 op_sel_hi:[0,0,0]
	v_mfma_scale_f32_16x16x128_f8f6f4 v[58:61], v[18:25], v[236:243], v[58:61], v196, v169 op_sel_hi:[0,0,0]
	v_mfma_scale_f32_16x16x128_f8f6f4 v[46:49], v[26:33], v[244:251], v[46:49], v196, v169 op_sel_hi:[0,0,0]
	v_mfma_scale_f32_16x16x128_f8f6f4 v[42:45], v[18:25], v[244:251], v[42:45], v196, v169 op_sel_hi:[0,0,0]
	s_setprio 0
	s_setprio 1
	v_mfma_scale_f32_16x16x128_f8f6f4 v[86:89], v[10:17], v[202:209], v[86:89], v196, v169 op_sel_hi:[0,0,0]
	v_mfma_scale_f32_16x16x128_f8f6f4 v[82:85], v[2:9], v[202:209], v[82:85], v196, v169 op_sel_hi:[0,0,0]
	v_mfma_scale_f32_16x16x128_f8f6f4 v[70:73], v[10:17], v[210:217], v[70:73], v196, v169 op_sel_hi:[0,0,0]
	v_mfma_scale_f32_16x16x128_f8f6f4 v[66:69], v[2:9], v[210:217], v[66:69], v196, v169 op_sel_hi:[0,0,0]
	v_mfma_scale_f32_16x16x128_f8f6f4 v[54:57], v[10:17], v[236:243], v[54:57], v196, v169 op_sel_hi:[0,0,0]
	v_mfma_scale_f32_16x16x128_f8f6f4 v[50:53], v[2:9], v[236:243], v[50:53], v196, v169 op_sel_hi:[0,0,0]
	v_mfma_scale_f32_16x16x128_f8f6f4 v[38:41], v[10:17], v[244:251], v[38:41], v196, v169 op_sel_hi:[0,0,0]
	v_mfma_scale_f32_16x16x128_f8f6f4 v[34:37], v[2:9], v[244:251], v[34:37], v196, v169 op_sel_hi:[0,0,0]
	s_setprio 0
	s_add_u32 s69, s69, 0x100
	s_addc_u32 s70, s70, 0
	s_add_u32 s54, s54, 0x100
	s_addc_u32 s55, s55, 0
	s_cmp_ge_i32 s71, s0
	s_mov_b32 s58, s71
	s_cbranch_scc1 .Lrotph1f_exitbar
	s_add_i32 s71, s58, 2
	s_add_u32 s59, s54, 0xfffe0080
	s_addc_u32 s60, s55, -1
	s_add_i32 s72, 0, 0x10000
	s_cmp_eq_u32 s65, s58
	s_cselect_b32 s61, s39, s60
	s_cselect_b32 s60, s41, s59
	s_cselect_b32 s59, s43, s70
	s_cselect_b32 s58, s53, s69
	s_add_i32 s73, 0, 0x14000
	s_barrier
	s_branch .Lrotph1f_body
.Lrotph1f_exitbar:
	s_barrier
.Lpeelexitph1f:
	s_mov_b64 s[72:73], 0xe800000
	s_mov_b64 s[70:71], 0xe800800
	v_mov_b32_e32 v209, v1
	s_and_b64 vcc, exec, s[34:35]
	s_cbranch_vccz .LBB0_301

.Lpeelph3_0:
	s_add_i32 s73, s68, 2
	s_add_u32 s69, s64, 0xfffc0080
	s_addc_u32 s70, s65, -1
	s_add_i32 s74, 0, 0x10000
	s_cmp_eq_u32 s24, s68
	s_cselect_b32 s71, s59, s70
	s_cselect_b32 s70, s58, s69
	s_cselect_b32 s69, s51, s72
	s_cselect_b32 s68, s53, s66
	s_add_i32 s76, 0, 0x14000
	v_add_u32_e32 v152, s74, v220
	v_add_u32_e32 v164, s76, v220
	ds_read_b128 v[106:109], v152
	ds_read_b128 v[110:113], v152 offset:1024
	ds_read_b128 v[114:117], v152 offset:2048
	ds_read_b128 v[152:155], v152 offset:3072
	ds_read_b128 v[156:159], v164
	ds_read_b128 v[160:163], v164 offset:1024
	ds_read_b128 v[170:173], v164 offset:2048
	ds_read_b128 v[174:177], v164 offset:3072
	v_lshl_add_u64 v[164:165], s[64:65], 0, v[150:151]
	s_add_i32 m0, s14, 0xc000
	ds_read_b128 v[178:181], v222
	ds_read_b128 v[182:185], v222 offset:1024
	ds_read_b128 v[186:189], v222 offset:2048
	ds_read_b128 v[190:193], v222 offset:3072
	ds_read_b128 v[194:197], v222 offset:4096
	ds_read_b128 v[198:201], v222 offset:5120
	ds_read_b128 v[202:205], v222 offset:6144
	ds_read_b128 v[206:209], v222 offset:7168
	global_load_lds_dwordx4 v[164:165], off
	v_lshl_add_u64 v[164:165], s[64:65], 0, v[148:149]
	s_add_i32 m0, s14, 0xe000
	s_nop 0
	global_load_lds_dwordx4 v[164:165], off
	s_waitcnt vmcnt(8)
	s_waitcnt lgkmcnt(0)
	s_barrier
	s_setprio 1
	s_waitcnt lgkmcnt(0)
	v_mfma_f32_16x16x32_bf16 v[138:141], v[106:109], v[178:181], 0
	v_mfma_f32_16x16x32_bf16 v[62:65], v[114:117], v[178:181], 0
	v_mfma_f32_16x16x32_bf16 v[130:133], v[106:109], v[186:189], 0
	v_mfma_f32_16x16x32_bf16 v[54:57], v[114:117], v[186:189], 0
	v_mfma_f32_16x16x32_bf16 v[122:125], v[106:109], v[194:197], 0
	v_mfma_f32_16x16x32_bf16 v[46:49], v[114:117], v[194:197], 0
	v_mfma_f32_16x16x32_bf16 v[102:105], v[106:109], v[202:205], 0
	v_mfma_f32_16x16x32_bf16 v[38:41], v[114:117], v[202:205], 0
	v_mfma_f32_16x16x32_bf16 v[138:141], v[110:113], v[182:185], v[138:141]
	v_mfma_f32_16x16x32_bf16 v[62:65], v[152:155], v[182:185], v[62:65]
	v_mfma_f32_16x16x32_bf16 v[130:133], v[110:113], v[190:193], v[130:133]
	v_mfma_f32_16x16x32_bf16 v[54:57], v[152:155], v[190:193], v[54:57]
	v_mfma_f32_16x16x32_bf16 v[122:125], v[110:113], v[198:201], v[122:125]
	v_mfma_f32_16x16x32_bf16 v[46:49], v[152:155], v[198:201], v[46:49]
	v_mfma_f32_16x16x32_bf16 v[102:105], v[110:113], v[206:209], v[102:105]
	v_mfma_f32_16x16x32_bf16 v[38:41], v[152:155], v[206:209], v[38:41]
	s_setprio 0
	s_setprio 1
	v_mfma_f32_16x16x32_bf16 v[134:137], v[156:159], v[178:181], 0
	v_mfma_f32_16x16x32_bf16 v[58:61], v[170:173], v[178:181], 0
	v_mfma_f32_16x16x32_bf16 v[126:129], v[156:159], v[186:189], 0
	v_mfma_f32_16x16x32_bf16 v[50:53], v[170:173], v[186:189], 0
	v_mfma_f32_16x16x32_bf16 v[118:121], v[156:159], v[194:197], 0
	v_mfma_f32_16x16x32_bf16 v[42:45], v[170:173], v[194:197], 0
	v_mfma_f32_16x16x32_bf16 v[98:101], v[156:159], v[202:205], 0
	v_mfma_f32_16x16x32_bf16 v[34:37], v[170:173], v[202:205], 0
	v_mfma_f32_16x16x32_bf16 v[134:137], v[160:163], v[182:185], v[134:137]
	v_mfma_f32_16x16x32_bf16 v[58:61], v[174:177], v[182:185], v[58:61]
	v_mfma_f32_16x16x32_bf16 v[126:129], v[160:163], v[190:193], v[126:129]
	v_mfma_f32_16x16x32_bf16 v[50:53], v[174:177], v[190:193], v[50:53]
	v_mfma_f32_16x16x32_bf16 v[118:121], v[160:163], v[198:201], v[118:121]
	v_mfma_f32_16x16x32_bf16 v[42:45], v[174:177], v[198:201], v[42:45]
	v_mfma_f32_16x16x32_bf16 v[98:101], v[160:163], v[206:209], v[98:101]
	v_mfma_f32_16x16x32_bf16 v[34:37], v[174:177], v[206:209], v[34:37]
	s_setprio 0
	s_barrier
	s_add_i32 s74, s74, s13
	v_lshl_add_u64 v[164:165], s[68:69], 0, v[166:167]
	s_mov_b32 m0, s74
	ds_read_b128 v[178:181], v222 offset:16384
	ds_read_b128 v[182:185], v222 offset:17408
	ds_read_b128 v[186:189], v222 offset:18432
	ds_read_b128 v[190:193], v222 offset:19456
	ds_read_b128 v[194:197], v222 offset:20480
	ds_read_b128 v[198:201], v222 offset:21504
	ds_read_b128 v[202:205], v222 offset:22528
	ds_read_b128 v[206:209], v222 offset:23552
	global_load_lds_dwordx4 v[164:165], off
	s_add_i32 m0, s74, 0x2000
	s_add_u32 s74, s68, 0x8000
	v_lshl_add_u64 v[210:211], s[68:69], 0, v[142:143]
	s_addc_u32 s75, s69, 0
	s_add_i32 s76, s76, s13
	global_load_lds_dwordx4 v[210:211], off
	v_lshl_add_u64 v[212:213], s[74:75], 0, v[166:167]
	s_mov_b32 m0, s76
	v_lshl_add_u64 v[214:215], s[70:71], 0, v[146:147]
	global_load_lds_dwordx4 v[212:213], off
	v_lshl_add_u64 v[212:213], s[74:75], 0, v[142:143]
	s_add_i32 m0, s76, 0x2000
	s_nop 0
	global_load_lds_dwordx4 v[212:213], off
	v_lshl_add_u64 v[212:213], s[70:71], 0, v[144:145]
	s_mov_b32 m0, s14
	s_nop 0
	global_load_lds_dwordx4 v[212:213], off
	s_mov_b32 m0, s15
	s_nop 0
	global_load_lds_dwordx4 v[214:215], off
	s_waitcnt vmcnt(8)
	s_waitcnt lgkmcnt(0)
	s_barrier
	s_setprio 1
	s_waitcnt lgkmcnt(0)
	v_mfma_f32_16x16x32_bf16 v[94:97], v[106:109], v[178:181], 0
	v_mfma_f32_16x16x32_bf16 v[30:33], v[114:117], v[178:181], 0
	v_mfma_f32_16x16x32_bf16 v[86:89], v[106:109], v[186:189], 0
	v_mfma_f32_16x16x32_bf16 v[22:25], v[114:117], v[186:189], 0
	v_mfma_f32_16x16x32_bf16 v[78:81], v[106:109], v[194:197], 0
	v_mfma_f32_16x16x32_bf16 v[14:17], v[114:117], v[194:197], 0
	v_mfma_f32_16x16x32_bf16 v[70:73], v[106:109], v[202:205], 0
	v_mfma_f32_16x16x32_bf16 v[6:9], v[114:117], v[202:205], 0
	v_mfma_f32_16x16x32_bf16 v[94:97], v[110:113], v[182:185], v[94:97]
	v_mfma_f32_16x16x32_bf16 v[30:33], v[152:155], v[182:185], v[30:33]
	v_mfma_f32_16x16x32_bf16 v[86:89], v[110:113], v[190:193], v[86:89]
	v_mfma_f32_16x16x32_bf16 v[22:25], v[152:155], v[190:193], v[22:25]
	v_mfma_f32_16x16x32_bf16 v[78:81], v[110:113], v[198:201], v[78:81]
	v_mfma_f32_16x16x32_bf16 v[14:17], v[152:155], v[198:201], v[14:17]
	v_mfma_f32_16x16x32_bf16 v[70:73], v[110:113], v[206:209], v[70:73]
	v_mfma_f32_16x16x32_bf16 v[6:9], v[152:155], v[206:209], v[6:9]
	s_setprio 0
	s_setprio 1
	v_mfma_f32_16x16x32_bf16 v[90:93], v[156:159], v[178:181], 0
	v_mfma_f32_16x16x32_bf16 v[26:29], v[170:173], v[178:181], 0
	v_mfma_f32_16x16x32_bf16 v[82:85], v[156:159], v[186:189], 0
	v_mfma_f32_16x16x32_bf16 v[18:21], v[170:173], v[186:189], 0
	v_mfma_f32_16x16x32_bf16 v[74:77], v[156:159], v[194:197], 0
	v_mfma_f32_16x16x32_bf16 v[10:13], v[170:173], v[194:197], 0
	v_mfma_f32_16x16x32_bf16 v[66:69], v[156:159], v[202:205], 0
	v_mfma_f32_16x16x32_bf16 v[2:5], v[170:173], v[202:205], 0
	v_mfma_f32_16x16x32_bf16 v[90:93], v[160:163], v[182:185], v[90:93]
	v_mfma_f32_16x16x32_bf16 v[26:29], v[174:177], v[182:185], v[26:29]
	v_mfma_f32_16x16x32_bf16 v[82:85], v[160:163], v[190:193], v[82:85]
	v_mfma_f32_16x16x32_bf16 v[18:21], v[174:177], v[190:193], v[18:21]
	v_mfma_f32_16x16x32_bf16 v[74:77], v[160:163], v[198:201], v[74:77]
	v_mfma_f32_16x16x32_bf16 v[10:13], v[174:177], v[198:201], v[10:13]
	v_mfma_f32_16x16x32_bf16 v[66:69], v[160:163], v[206:209], v[66:69]
	v_mfma_f32_16x16x32_bf16 v[2:5], v[174:177], v[206:209], v[2:5]
	s_setprio 0
	s_barrier
	s_add_i32 s74, 0, 0x18000
	s_add_i32 s75, 0, 0x1c000
	v_add_u32_e32 v152, s74, v220
	v_add_u32_e32 v174, s75, v220
	ds_read_b128 v[106:109], v152
	ds_read_b128 v[110:113], v152 offset:1024
	ds_read_b128 v[114:117], v152 offset:2048
	ds_read_b128 v[152:155], v152 offset:3072
	ds_read_b128 v[156:159], v174
	ds_read_b128 v[160:163], v174 offset:1024
	ds_read_b128 v[170:173], v174 offset:2048
	ds_read_b128 v[174:177], v174 offset:3072
	s_add_u32 s70, s70, 0x40000
	s_addc_u32 s71, s71, 0
	s_mov_b32 m0, s16
	v_lshl_add_u64 v[216:217], s[70:71], 0, v[144:145]
	ds_read_b128 v[178:181], v222 offset:32768
	ds_read_b128 v[182:185], v222 offset:33792
	ds_read_b128 v[186:189], v222 offset:34816
	ds_read_b128 v[190:193], v222 offset:35840
	ds_read_b128 v[194:197], v222 offset:36864
	ds_read_b128 v[198:201], v222 offset:37888
	ds_read_b128 v[202:205], v222 offset:38912
	ds_read_b128 v[206:209], v222 offset:39936
	global_load_lds_dwordx4 v[216:217], off
	v_lshl_add_u64 v[216:217], s[70:71], 0, v[146:147]
	s_mov_b32 m0, s20
	s_nop 0
	global_load_lds_dwordx4 v[216:217], off
	s_waitcnt vmcnt(8)
	s_waitcnt lgkmcnt(0)
	s_barrier
	s_setprio 1
	s_waitcnt lgkmcnt(0)
	v_mfma_f32_16x16x32_bf16 v[138:141], v[106:109], v[178:181], v[138:141]
	v_mfma_f32_16x16x32_bf16 v[62:65], v[114:117], v[178:181], v[62:65]
	v_mfma_f32_16x16x32_bf16 v[130:133], v[106:109], v[186:189], v[130:133]
	v_mfma_f32_16x16x32_bf16 v[54:57], v[114:117], v[186:189], v[54:57]
	v_mfma_f32_16x16x32_bf16 v[122:125], v[106:109], v[194:197], v[122:125]
	v_mfma_f32_16x16x32_bf16 v[46:49], v[114:117], v[194:197], v[46:49]
	v_mfma_f32_16x16x32_bf16 v[102:105], v[106:109], v[202:205], v[102:105]
	v_mfma_f32_16x16x32_bf16 v[38:41], v[114:117], v[202:205], v[38:41]
	v_mfma_f32_16x16x32_bf16 v[138:141], v[110:113], v[182:185], v[138:141]
	v_mfma_f32_16x16x32_bf16 v[62:65], v[152:155], v[182:185], v[62:65]
	v_mfma_f32_16x16x32_bf16 v[130:133], v[110:113], v[190:193], v[130:133]
	v_mfma_f32_16x16x32_bf16 v[54:57], v[152:155], v[190:193], v[54:57]
	v_mfma_f32_16x16x32_bf16 v[122:125], v[110:113], v[198:201], v[122:125]
	v_mfma_f32_16x16x32_bf16 v[46:49], v[152:155], v[198:201], v[46:49]
	v_mfma_f32_16x16x32_bf16 v[102:105], v[110:113], v[206:209], v[102:105]
	v_mfma_f32_16x16x32_bf16 v[38:41], v[152:155], v[206:209], v[38:41]
	s_setprio 0
	s_setprio 1
	v_mfma_f32_16x16x32_bf16 v[134:137], v[156:159], v[178:181], v[134:137]
	v_mfma_f32_16x16x32_bf16 v[58:61], v[170:173], v[178:181], v[58:61]
	v_mfma_f32_16x16x32_bf16 v[126:129], v[156:159], v[186:189], v[126:129]
	v_mfma_f32_16x16x32_bf16 v[50:53], v[170:173], v[186:189], v[50:53]
	v_mfma_f32_16x16x32_bf16 v[118:121], v[156:159], v[194:197], v[118:121]
	v_mfma_f32_16x16x32_bf16 v[42:45], v[170:173], v[194:197], v[42:45]
	v_mfma_f32_16x16x32_bf16 v[98:101], v[156:159], v[202:205], v[98:101]
	v_mfma_f32_16x16x32_bf16 v[34:37], v[170:173], v[202:205], v[34:37]
	v_mfma_f32_16x16x32_bf16 v[134:137], v[160:163], v[182:185], v[134:137]
	v_mfma_f32_16x16x32_bf16 v[58:61], v[174:177], v[182:185], v[58:61]
	v_mfma_f32_16x16x32_bf16 v[126:129], v[160:163], v[190:193], v[126:129]
	v_mfma_f32_16x16x32_bf16 v[50:53], v[174:177], v[190:193], v[50:53]
	v_mfma_f32_16x16x32_bf16 v[118:121], v[160:163], v[198:201], v[118:121]
	v_mfma_f32_16x16x32_bf16 v[42:45], v[174:177], v[198:201], v[42:45]
	v_mfma_f32_16x16x32_bf16 v[98:101], v[160:163], v[206:209], v[98:101]
	v_mfma_f32_16x16x32_bf16 v[34:37], v[174:177], v[206:209], v[34:37]
	s_setprio 0
	s_barrier
	s_add_i32 s70, s74, s13
	v_lshl_add_u64 v[164:165], v[164:165], 0, s[56:57]
	s_mov_b32 m0, s70
	ds_read_b128 v[178:181], v222 offset:49152
	ds_read_b128 v[182:185], v222 offset:50176
	ds_read_b128 v[186:189], v222 offset:51200
	ds_read_b128 v[190:193], v222 offset:52224
	ds_read_b128 v[194:197], v222 offset:53248
	ds_read_b128 v[198:201], v222 offset:54272
	ds_read_b128 v[202:205], v222 offset:55296
	ds_read_b128 v[206:209], v222 offset:56320
	global_load_lds_dwordx4 v[164:165], off
	s_add_i32 m0, s70, 0x2000
	s_add_u32 s68, s68, 0x8080
	v_lshl_add_u64 v[164:165], v[210:211], 0, s[56:57]
	s_addc_u32 s69, s69, 0
	s_add_i32 s70, s75, s13
	global_load_lds_dwordx4 v[164:165], off
	v_lshl_add_u64 v[164:165], s[68:69], 0, v[166:167]
	s_mov_b32 m0, s70
	s_nop 0
	global_load_lds_dwordx4 v[164:165], off
	v_lshl_add_u64 v[164:165], s[68:69], 0, v[142:143]
	s_add_i32 m0, s70, 0x2000
	s_nop 0
	global_load_lds_dwordx4 v[164:165], off
	v_lshl_add_u64 v[164:165], v[212:213], 0, s[56:57]
	s_mov_b32 m0, s21
	s_nop 0
	global_load_lds_dwordx4 v[164:165], off
	v_lshl_add_u64 v[164:165], v[214:215], 0, s[56:57]
	s_mov_b32 m0, s22
	s_nop 0
	global_load_lds_dwordx4 v[164:165], off
	s_waitcnt vmcnt(8)
	s_waitcnt lgkmcnt(0)
	s_barrier
	s_setprio 1
	s_waitcnt lgkmcnt(0)
	v_mfma_f32_16x16x32_bf16 v[94:97], v[106:109], v[178:181], v[94:97]
	v_mfma_f32_16x16x32_bf16 v[30:33], v[114:117], v[178:181], v[30:33]
	v_mfma_f32_16x16x32_bf16 v[86:89], v[106:109], v[186:189], v[86:89]
	v_mfma_f32_16x16x32_bf16 v[22:25], v[114:117], v[186:189], v[22:25]
	v_mfma_f32_16x16x32_bf16 v[78:81], v[106:109], v[194:197], v[78:81]
	v_mfma_f32_16x16x32_bf16 v[14:17], v[114:117], v[194:197], v[14:17]
	v_mfma_f32_16x16x32_bf16 v[70:73], v[106:109], v[202:205], v[70:73]
	v_mfma_f32_16x16x32_bf16 v[6:9], v[114:117], v[202:205], v[6:9]
	v_mfma_f32_16x16x32_bf16 v[94:97], v[110:113], v[182:185], v[94:97]
	v_mfma_f32_16x16x32_bf16 v[30:33], v[152:155], v[182:185], v[30:33]
	v_mfma_f32_16x16x32_bf16 v[86:89], v[110:113], v[190:193], v[86:89]
	v_mfma_f32_16x16x32_bf16 v[22:25], v[152:155], v[190:193], v[22:25]
	v_mfma_f32_16x16x32_bf16 v[78:81], v[110:113], v[198:201], v[78:81]
	v_mfma_f32_16x16x32_bf16 v[14:17], v[152:155], v[198:201], v[14:17]
	v_mfma_f32_16x16x32_bf16 v[70:73], v[110:113], v[206:209], v[70:73]
	v_mfma_f32_16x16x32_bf16 v[6:9], v[152:155], v[206:209], v[6:9]
	s_setprio 0
	s_setprio 1
	v_mfma_f32_16x16x32_bf16 v[90:93], v[156:159], v[178:181], v[90:93]
	v_mfma_f32_16x16x32_bf16 v[26:29], v[170:173], v[178:181], v[26:29]
	v_mfma_f32_16x16x32_bf16 v[82:85], v[156:159], v[186:189], v[82:85]
	v_mfma_f32_16x16x32_bf16 v[18:21], v[170:173], v[186:189], v[18:21]
	v_mfma_f32_16x16x32_bf16 v[74:77], v[156:159], v[194:197], v[74:77]
	v_mfma_f32_16x16x32_bf16 v[10:13], v[170:173], v[194:197], v[10:13]
	v_mfma_f32_16x16x32_bf16 v[66:69], v[156:159], v[202:205], v[66:69]
	v_mfma_f32_16x16x32_bf16 v[2:5], v[170:173], v[202:205], v[2:5]
	v_mfma_f32_16x16x32_bf16 v[90:93], v[160:163], v[182:185], v[90:93]
	v_mfma_f32_16x16x32_bf16 v[26:29], v[174:177], v[182:185], v[26:29]
	v_mfma_f32_16x16x32_bf16 v[82:85], v[160:163], v[190:193], v[82:85]
	v_mfma_f32_16x16x32_bf16 v[18:21], v[174:177], v[190:193], v[18:21]
	v_mfma_f32_16x16x32_bf16 v[74:77], v[160:163], v[198:201], v[74:77]
	v_mfma_f32_16x16x32_bf16 v[10:13], v[174:177], v[198:201], v[10:13]
	v_mfma_f32_16x16x32_bf16 v[66:69], v[160:163], v[206:209], v[66:69]
	v_mfma_f32_16x16x32_bf16 v[2:5], v[174:177], v[206:209], v[2:5]
	s_setprio 0
	s_add_u32 s66, s66, 0x100
	s_addc_u32 s72, s72, 0
	s_add_u32 s64, s64, 0x100
	s_addc_u32 s65, s65, 0
	s_cmp_ge_i32 s73, s1
	s_mov_b32 s68, s73
	s_cbranch_scc1 .Lrotph3_pexitbar
	s_add_i32 s73, s68, 2
	s_add_u32 s69, s64, 0xfffc0080
	s_addc_u32 s70, s65, -1
	s_add_i32 s74, 0, 0x10000
	s_cmp_eq_u32 s24, s68
	s_cselect_b32 s71, s59, s70
	s_cselect_b32 s70, s58, s69
	s_cselect_b32 s69, s51, s72
	s_cselect_b32 s68, s53, s66
	s_add_i32 s76, 0, 0x14000
	s_barrier
	s_branch .Lrotph3_body

.Lrotph3_body:
	v_add_u32_e32 v152, s74, v220
	v_add_u32_e32 v164, s76, v220
	ds_read_b128 v[106:109], v152
	ds_read_b128 v[110:113], v152 offset:1024
	ds_read_b128 v[114:117], v152 offset:2048
	ds_read_b128 v[152:155], v152 offset:3072
	ds_read_b128 v[156:159], v164
	ds_read_b128 v[160:163], v164 offset:1024
	ds_read_b128 v[170:173], v164 offset:2048
	ds_read_b128 v[174:177], v164 offset:3072
	v_lshl_add_u64 v[164:165], s[64:65], 0, v[150:151]
	s_add_i32 m0, s14, 0xc000
	ds_read_b128 v[178:181], v222
	ds_read_b128 v[182:185], v222 offset:1024
	ds_read_b128 v[186:189], v222 offset:2048
	ds_read_b128 v[190:193], v222 offset:3072
	ds_read_b128 v[194:197], v222 offset:4096
	ds_read_b128 v[198:201], v222 offset:5120
	ds_read_b128 v[202:205], v222 offset:6144
	ds_read_b128 v[206:209], v222 offset:7168
	global_load_lds_dwordx4 v[164:165], off
	v_lshl_add_u64 v[164:165], s[64:65], 0, v[148:149]
	s_add_i32 m0, s14, 0xe000
	s_nop 0
	global_load_lds_dwordx4 v[164:165], off
	s_waitcnt vmcnt(8)
	s_waitcnt lgkmcnt(0)
	s_barrier
	s_setprio 1
	s_waitcnt lgkmcnt(0)
	v_mfma_f32_16x16x32_bf16 v[138:141], v[106:109], v[178:181], v[138:141]
	v_mfma_f32_16x16x32_bf16 v[62:65], v[114:117], v[178:181], v[62:65]
	v_mfma_f32_16x16x32_bf16 v[130:133], v[106:109], v[186:189], v[130:133]
	v_mfma_f32_16x16x32_bf16 v[54:57], v[114:117], v[186:189], v[54:57]
	v_mfma_f32_16x16x32_bf16 v[122:125], v[106:109], v[194:197], v[122:125]
	v_mfma_f32_16x16x32_bf16 v[46:49], v[114:117], v[194:197], v[46:49]
	v_mfma_f32_16x16x32_bf16 v[102:105], v[106:109], v[202:205], v[102:105]
	v_mfma_f32_16x16x32_bf16 v[38:41], v[114:117], v[202:205], v[38:41]
	v_mfma_f32_16x16x32_bf16 v[138:141], v[110:113], v[182:185], v[138:141]
	v_mfma_f32_16x16x32_bf16 v[62:65], v[152:155], v[182:185], v[62:65]
	v_mfma_f32_16x16x32_bf16 v[130:133], v[110:113], v[190:193], v[130:133]
	v_mfma_f32_16x16x32_bf16 v[54:57], v[152:155], v[190:193], v[54:57]
	v_mfma_f32_16x16x32_bf16 v[122:125], v[110:113], v[198:201], v[122:125]
	v_mfma_f32_16x16x32_bf16 v[46:49], v[152:155], v[198:201], v[46:49]
	v_mfma_f32_16x16x32_bf16 v[102:105], v[110:113], v[206:209], v[102:105]
	v_mfma_f32_16x16x32_bf16 v[38:41], v[152:155], v[206:209], v[38:41]
	s_setprio 0
	s_setprio 1
	v_mfma_f32_16x16x32_bf16 v[134:137], v[156:159], v[178:181], v[134:137]
	v_mfma_f32_16x16x32_bf16 v[58:61], v[170:173], v[178:181], v[58:61]
	v_mfma_f32_16x16x32_bf16 v[126:129], v[156:159], v[186:189], v[126:129]
	v_mfma_f32_16x16x32_bf16 v[50:53], v[170:173], v[186:189], v[50:53]
	v_mfma_f32_16x16x32_bf16 v[118:121], v[156:159], v[194:197], v[118:121]
	v_mfma_f32_16x16x32_bf16 v[42:45], v[170:173], v[194:197], v[42:45]
	v_mfma_f32_16x16x32_bf16 v[98:101], v[156:159], v[202:205], v[98:101]
	v_mfma_f32_16x16x32_bf16 v[34:37], v[170:173], v[202:205], v[34:37]
	v_mfma_f32_16x16x32_bf16 v[134:137], v[160:163], v[182:185], v[134:137]
	v_mfma_f32_16x16x32_bf16 v[58:61], v[174:177], v[182:185], v[58:61]
	v_mfma_f32_16x16x32_bf16 v[126:129], v[160:163], v[190:193], v[126:129]
	v_mfma_f32_16x16x32_bf16 v[50:53], v[174:177], v[190:193], v[50:53]
	v_mfma_f32_16x16x32_bf16 v[118:121], v[160:163], v[198:201], v[118:121]
	v_mfma_f32_16x16x32_bf16 v[42:45], v[174:177], v[198:201], v[42:45]
	v_mfma_f32_16x16x32_bf16 v[98:101], v[160:163], v[206:209], v[98:101]
	v_mfma_f32_16x16x32_bf16 v[34:37], v[174:177], v[206:209], v[34:37]
	s_setprio 0
	s_barrier
	s_add_i32 s74, s74, s13
	v_lshl_add_u64 v[164:165], s[68:69], 0, v[166:167]
	s_mov_b32 m0, s74
	ds_read_b128 v[178:181], v222 offset:16384
	ds_read_b128 v[182:185], v222 offset:17408
	ds_read_b128 v[186:189], v222 offset:18432
	ds_read_b128 v[190:193], v222 offset:19456
	ds_read_b128 v[194:197], v222 offset:20480
	ds_read_b128 v[198:201], v222 offset:21504
	ds_read_b128 v[202:205], v222 offset:22528
	ds_read_b128 v[206:209], v222 offset:23552
	global_load_lds_dwordx4 v[164:165], off
	s_add_i32 m0, s74, 0x2000
	s_add_u32 s74, s68, 0x8000
	v_lshl_add_u64 v[210:211], s[68:69], 0, v[142:143]
	s_addc_u32 s75, s69, 0
	s_add_i32 s76, s76, s13
	global_load_lds_dwordx4 v[210:211], off
	v_lshl_add_u64 v[212:213], s[74:75], 0, v[166:167]
	s_mov_b32 m0, s76
	v_lshl_add_u64 v[214:215], s[70:71], 0, v[146:147]
	global_load_lds_dwordx4 v[212:213], off
	v_lshl_add_u64 v[212:213], s[74:75], 0, v[142:143]
	s_add_i32 m0, s76, 0x2000
	s_nop 0
	global_load_lds_dwordx4 v[212:213], off
	v_lshl_add_u64 v[212:213], s[70:71], 0, v[144:145]
	s_mov_b32 m0, s14
	s_nop 0
	global_load_lds_dwordx4 v[212:213], off
	s_mov_b32 m0, s15
	s_nop 0
	global_load_lds_dwordx4 v[214:215], off
	s_waitcnt vmcnt(8)
	s_waitcnt lgkmcnt(0)
	s_barrier
	s_setprio 1
	s_waitcnt lgkmcnt(0)
	v_mfma_f32_16x16x32_bf16 v[94:97], v[106:109], v[178:181], v[94:97]
	v_mfma_f32_16x16x32_bf16 v[30:33], v[114:117], v[178:181], v[30:33]
	v_mfma_f32_16x16x32_bf16 v[86:89], v[106:109], v[186:189], v[86:89]
	v_mfma_f32_16x16x32_bf16 v[22:25], v[114:117], v[186:189], v[22:25]
	v_mfma_f32_16x16x32_bf16 v[78:81], v[106:109], v[194:197], v[78:81]
	v_mfma_f32_16x16x32_bf16 v[14:17], v[114:117], v[194:197], v[14:17]
	v_mfma_f32_16x16x32_bf16 v[70:73], v[106:109], v[202:205], v[70:73]
	v_mfma_f32_16x16x32_bf16 v[6:9], v[114:117], v[202:205], v[6:9]
	v_mfma_f32_16x16x32_bf16 v[94:97], v[110:113], v[182:185], v[94:97]
	v_mfma_f32_16x16x32_bf16 v[30:33], v[152:155], v[182:185], v[30:33]
	v_mfma_f32_16x16x32_bf16 v[86:89], v[110:113], v[190:193], v[86:89]
	v_mfma_f32_16x16x32_bf16 v[22:25], v[152:155], v[190:193], v[22:25]
	v_mfma_f32_16x16x32_bf16 v[78:81], v[110:113], v[198:201], v[78:81]
	v_mfma_f32_16x16x32_bf16 v[14:17], v[152:155], v[198:201], v[14:17]
	v_mfma_f32_16x16x32_bf16 v[70:73], v[110:113], v[206:209], v[70:73]
	v_mfma_f32_16x16x32_bf16 v[6:9], v[152:155], v[206:209], v[6:9]
	s_setprio 0
	s_setprio 1
	v_mfma_f32_16x16x32_bf16 v[90:93], v[156:159], v[178:181], v[90:93]
	v_mfma_f32_16x16x32_bf16 v[26:29], v[170:173], v[178:181], v[26:29]
	v_mfma_f32_16x16x32_bf16 v[82:85], v[156:159], v[186:189], v[82:85]
	v_mfma_f32_16x16x32_bf16 v[18:21], v[170:173], v[186:189], v[18:21]
	v_mfma_f32_16x16x32_bf16 v[74:77], v[156:159], v[194:197], v[74:77]
	v_mfma_f32_16x16x32_bf16 v[10:13], v[170:173], v[194:197], v[10:13]
	v_mfma_f32_16x16x32_bf16 v[66:69], v[156:159], v[202:205], v[66:69]
	v_mfma_f32_16x16x32_bf16 v[2:5], v[170:173], v[202:205], v[2:5]
	v_mfma_f32_16x16x32_bf16 v[90:93], v[160:163], v[182:185], v[90:93]
	v_mfma_f32_16x16x32_bf16 v[26:29], v[174:177], v[182:185], v[26:29]
	v_mfma_f32_16x16x32_bf16 v[82:85], v[160:163], v[190:193], v[82:85]
	v_mfma_f32_16x16x32_bf16 v[18:21], v[174:177], v[190:193], v[18:21]
	v_mfma_f32_16x16x32_bf16 v[74:77], v[160:163], v[198:201], v[74:77]
	v_mfma_f32_16x16x32_bf16 v[10:13], v[174:177], v[198:201], v[10:13]
	v_mfma_f32_16x16x32_bf16 v[66:69], v[160:163], v[206:209], v[66:69]
	v_mfma_f32_16x16x32_bf16 v[2:5], v[174:177], v[206:209], v[2:5]
	s_setprio 0
	s_barrier
	s_add_i32 s74, 0, 0x18000
	s_add_i32 s75, 0, 0x1c000
	v_add_u32_e32 v152, s74, v220
	v_add_u32_e32 v174, s75, v220
	ds_read_b128 v[106:109], v152
	ds_read_b128 v[110:113], v152 offset:1024
	ds_read_b128 v[114:117], v152 offset:2048
	ds_read_b128 v[152:155], v152 offset:3072
	ds_read_b128 v[156:159], v174
	ds_read_b128 v[160:163], v174 offset:1024
	ds_read_b128 v[170:173], v174 offset:2048
	ds_read_b128 v[174:177], v174 offset:3072
	s_add_u32 s70, s70, 0x40000
	s_addc_u32 s71, s71, 0
	s_mov_b32 m0, s16
	v_lshl_add_u64 v[216:217], s[70:71], 0, v[144:145]
	ds_read_b128 v[178:181], v222 offset:32768
	ds_read_b128 v[182:185], v222 offset:33792
	ds_read_b128 v[186:189], v222 offset:34816
	ds_read_b128 v[190:193], v222 offset:35840
	ds_read_b128 v[194:197], v222 offset:36864
	ds_read_b128 v[198:201], v222 offset:37888
	ds_read_b128 v[202:205], v222 offset:38912
	ds_read_b128 v[206:209], v222 offset:39936
	global_load_lds_dwordx4 v[216:217], off
	v_lshl_add_u64 v[216:217], s[70:71], 0, v[146:147]
	s_mov_b32 m0, s20
	s_nop 0
	global_load_lds_dwordx4 v[216:217], off
	s_waitcnt vmcnt(8)
	s_waitcnt lgkmcnt(0)
	s_barrier
	s_setprio 1
	s_waitcnt lgkmcnt(0)
	v_mfma_f32_16x16x32_bf16 v[138:141], v[106:109], v[178:181], v[138:141]
	v_mfma_f32_16x16x32_bf16 v[62:65], v[114:117], v[178:181], v[62:65]
	v_mfma_f32_16x16x32_bf16 v[130:133], v[106:109], v[186:189], v[130:133]
	v_mfma_f32_16x16x32_bf16 v[54:57], v[114:117], v[186:189], v[54:57]
	v_mfma_f32_16x16x32_bf16 v[122:125], v[106:109], v[194:197], v[122:125]
	v_mfma_f32_16x16x32_bf16 v[46:49], v[114:117], v[194:197], v[46:49]
	v_mfma_f32_16x16x32_bf16 v[102:105], v[106:109], v[202:205], v[102:105]
	v_mfma_f32_16x16x32_bf16 v[38:41], v[114:117], v[202:205], v[38:41]
	v_mfma_f32_16x16x32_bf16 v[138:141], v[110:113], v[182:185], v[138:141]
	v_mfma_f32_16x16x32_bf16 v[62:65], v[152:155], v[182:185], v[62:65]
	v_mfma_f32_16x16x32_bf16 v[130:133], v[110:113], v[190:193], v[130:133]
	v_mfma_f32_16x16x32_bf16 v[54:57], v[152:155], v[190:193], v[54:57]
	v_mfma_f32_16x16x32_bf16 v[122:125], v[110:113], v[198:201], v[122:125]
	v_mfma_f32_16x16x32_bf16 v[46:49], v[152:155], v[198:201], v[46:49]
	v_mfma_f32_16x16x32_bf16 v[102:105], v[110:113], v[206:209], v[102:105]
	v_mfma_f32_16x16x32_bf16 v[38:41], v[152:155], v[206:209], v[38:41]
	s_setprio 0
	s_setprio 1
	v_mfma_f32_16x16x32_bf16 v[134:137], v[156:159], v[178:181], v[134:137]
	v_mfma_f32_16x16x32_bf16 v[58:61], v[170:173], v[178:181], v[58:61]
	v_mfma_f32_16x16x32_bf16 v[126:129], v[156:159], v[186:189], v[126:129]
	v_mfma_f32_16x16x32_bf16 v[50:53], v[170:173], v[186:189], v[50:53]
	v_mfma_f32_16x16x32_bf16 v[118:121], v[156:159], v[194:197], v[118:121]
	v_mfma_f32_16x16x32_bf16 v[42:45], v[170:173], v[194:197], v[42:45]
	v_mfma_f32_16x16x32_bf16 v[98:101], v[156:159], v[202:205], v[98:101]
	v_mfma_f32_16x16x32_bf16 v[34:37], v[170:173], v[202:205], v[34:37]
	v_mfma_f32_16x16x32_bf16 v[134:137], v[160:163], v[182:185], v[134:137]
	v_mfma_f32_16x16x32_bf16 v[58:61], v[174:177], v[182:185], v[58:61]
	v_mfma_f32_16x16x32_bf16 v[126:129], v[160:163], v[190:193], v[126:129]
	v_mfma_f32_16x16x32_bf16 v[50:53], v[174:177], v[190:193], v[50:53]
	v_mfma_f32_16x16x32_bf16 v[118:121], v[160:163], v[198:201], v[118:121]
	v_mfma_f32_16x16x32_bf16 v[42:45], v[174:177], v[198:201], v[42:45]
	v_mfma_f32_16x16x32_bf16 v[98:101], v[160:163], v[206:209], v[98:101]
	v_mfma_f32_16x16x32_bf16 v[34:37], v[174:177], v[206:209], v[34:37]
	s_setprio 0
	s_barrier
	s_add_i32 s70, s74, s13
	v_lshl_add_u64 v[164:165], v[164:165], 0, s[56:57]
	s_mov_b32 m0, s70
	ds_read_b128 v[178:181], v222 offset:49152
	ds_read_b128 v[182:185], v222 offset:50176
	ds_read_b128 v[186:189], v222 offset:51200
	ds_read_b128 v[190:193], v222 offset:52224
	ds_read_b128 v[194:197], v222 offset:53248
	ds_read_b128 v[198:201], v222 offset:54272
	ds_read_b128 v[202:205], v222 offset:55296
	ds_read_b128 v[206:209], v222 offset:56320
	global_load_lds_dwordx4 v[164:165], off
	s_add_i32 m0, s70, 0x2000
	s_add_u32 s68, s68, 0x8080
	v_lshl_add_u64 v[164:165], v[210:211], 0, s[56:57]
	s_addc_u32 s69, s69, 0
	s_add_i32 s70, s75, s13
	global_load_lds_dwordx4 v[164:165], off
	v_lshl_add_u64 v[164:165], s[68:69], 0, v[166:167]
	s_mov_b32 m0, s70
	s_nop 0
	global_load_lds_dwordx4 v[164:165], off
	v_lshl_add_u64 v[164:165], s[68:69], 0, v[142:143]
	s_add_i32 m0, s70, 0x2000
	s_nop 0
	global_load_lds_dwordx4 v[164:165], off
	v_lshl_add_u64 v[164:165], v[212:213], 0, s[56:57]
	s_mov_b32 m0, s21
	s_nop 0
	global_load_lds_dwordx4 v[164:165], off
	v_lshl_add_u64 v[164:165], v[214:215], 0, s[56:57]
	s_mov_b32 m0, s22
	s_nop 0
	global_load_lds_dwordx4 v[164:165], off
	s_waitcnt vmcnt(8)
	s_waitcnt lgkmcnt(0)
	s_barrier
	s_setprio 1
	s_waitcnt lgkmcnt(0)
	v_mfma_f32_16x16x32_bf16 v[94:97], v[106:109], v[178:181], v[94:97]
	v_mfma_f32_16x16x32_bf16 v[30:33], v[114:117], v[178:181], v[30:33]
	v_mfma_f32_16x16x32_bf16 v[86:89], v[106:109], v[186:189], v[86:89]
	v_mfma_f32_16x16x32_bf16 v[22:25], v[114:117], v[186:189], v[22:25]
	v_mfma_f32_16x16x32_bf16 v[78:81], v[106:109], v[194:197], v[78:81]
	v_mfma_f32_16x16x32_bf16 v[14:17], v[114:117], v[194:197], v[14:17]
	v_mfma_f32_16x16x32_bf16 v[70:73], v[106:109], v[202:205], v[70:73]
	v_mfma_f32_16x16x32_bf16 v[6:9], v[114:117], v[202:205], v[6:9]
	v_mfma_f32_16x16x32_bf16 v[94:97], v[110:113], v[182:185], v[94:97]
	v_mfma_f32_16x16x32_bf16 v[30:33], v[152:155], v[182:185], v[30:33]
	v_mfma_f32_16x16x32_bf16 v[86:89], v[110:113], v[190:193], v[86:89]
	v_mfma_f32_16x16x32_bf16 v[22:25], v[152:155], v[190:193], v[22:25]
	v_mfma_f32_16x16x32_bf16 v[78:81], v[110:113], v[198:201], v[78:81]
	v_mfma_f32_16x16x32_bf16 v[14:17], v[152:155], v[198:201], v[14:17]
	v_mfma_f32_16x16x32_bf16 v[70:73], v[110:113], v[206:209], v[70:73]
	v_mfma_f32_16x16x32_bf16 v[6:9], v[152:155], v[206:209], v[6:9]
	s_setprio 0
	s_setprio 1
	v_mfma_f32_16x16x32_bf16 v[90:93], v[156:159], v[178:181], v[90:93]
	v_mfma_f32_16x16x32_bf16 v[26:29], v[170:173], v[178:181], v[26:29]
	v_mfma_f32_16x16x32_bf16 v[82:85], v[156:159], v[186:189], v[82:85]
	v_mfma_f32_16x16x32_bf16 v[18:21], v[170:173], v[186:189], v[18:21]
	v_mfma_f32_16x16x32_bf16 v[74:77], v[156:159], v[194:197], v[74:77]
	v_mfma_f32_16x16x32_bf16 v[10:13], v[170:173], v[194:197], v[10:13]
	v_mfma_f32_16x16x32_bf16 v[66:69], v[156:159], v[202:205], v[66:69]
	v_mfma_f32_16x16x32_bf16 v[2:5], v[170:173], v[202:205], v[2:5]
	v_mfma_f32_16x16x32_bf16 v[90:93], v[160:163], v[182:185], v[90:93]
	v_mfma_f32_16x16x32_bf16 v[26:29], v[174:177], v[182:185], v[26:29]
	v_mfma_f32_16x16x32_bf16 v[82:85], v[160:163], v[190:193], v[82:85]
	v_mfma_f32_16x16x32_bf16 v[18:21], v[174:177], v[190:193], v[18:21]
	v_mfma_f32_16x16x32_bf16 v[74:77], v[160:163], v[198:201], v[74:77]
	v_mfma_f32_16x16x32_bf16 v[10:13], v[174:177], v[198:201], v[10:13]
	v_mfma_f32_16x16x32_bf16 v[66:69], v[160:163], v[206:209], v[66:69]
	v_mfma_f32_16x16x32_bf16 v[2:5], v[174:177], v[206:209], v[2:5]
	s_setprio 0
	s_add_u32 s66, s66, 0x100
	s_addc_u32 s72, s72, 0
	s_add_u32 s64, s64, 0x100
	s_addc_u32 s65, s65, 0
	s_cmp_ge_i32 s73, s1
	s_mov_b32 s68, s73
	s_cbranch_scc1 .Lrotph3_exitbar
	s_add_i32 s73, s68, 2
	s_add_u32 s69, s64, 0xfffc0080
	s_addc_u32 s70, s65, -1
	s_add_i32 s74, 0, 0x10000
	s_cmp_eq_u32 s24, s68
	s_cselect_b32 s71, s59, s70
	s_cselect_b32 s70, s58, s69
	s_cselect_b32 s69, s51, s72
	s_cselect_b32 s68, s53, s66
	s_add_i32 s76, 0, 0x14000
	s_barrier
	s_branch .Lrotph3_body
.Lrotph3_exitbar:
	s_barrier
.Lpeelexitph3:
	s_branch .LBB0_471

.Lpeelph6_0:
	s_add_i32 s84, s68, 2
	s_add_u32 s69, s74, 0xfffc0080
	s_addc_u32 s70, s75, -1
	s_add_i32 s88, 0, 0x10000
	s_cmp_eq_u32 s72, s68
	s_cselect_b32 s71, s29, s70
	s_cselect_b32 s70, s43, s69
	s_cselect_b32 s69, s55, s79
	s_cselect_b32 s68, s59, s77
	s_add_i32 s92, 0, 0x14000
	v_add_u32_e32 v78, s88, v204
	v_add_u32_e32 v170, s92, v204
	ds_read_b128 v[58:61], v78
	ds_read_b128 v[62:65], v78 offset:1024
	ds_read_b128 v[74:77], v78 offset:2048
	ds_read_b128 v[78:81], v78 offset:3072
	ds_read_b128 v[146:149], v170
	ds_read_b128 v[150:153], v170 offset:1024
	ds_read_b128 v[154:157], v170 offset:2048
	ds_read_b128 v[170:173], v170 offset:3072
	v_lshl_add_u64 v[202:203], s[74:75], 0, v[180:181]
	s_add_i32 m0, s15, 0xc000
	ds_read_b128 v[174:177], v208
	ds_read_b128 v[182:185], v208 offset:1024
	ds_read_b128 v[186:189], v208 offset:2048
	ds_read_b128 v[190:193], v208 offset:3072
	ds_read_b128 v[194:197], v208 offset:4096
	ds_read_b128 v[198:201], v208 offset:5120
	ds_read_b128 v[210:213], v208 offset:6144
	ds_read_b128 v[214:217], v208 offset:7168
	global_load_lds_dwordx4 v[202:203], off
	v_lshl_add_u64 v[202:203], s[74:75], 0, v[178:179]
	s_add_i32 m0, s15, 0xe000
	s_nop 0
	global_load_lds_dwordx4 v[202:203], off
	s_waitcnt vmcnt(8)
	s_waitcnt lgkmcnt(0)
	s_barrier
	s_setprio 1
	s_waitcnt lgkmcnt(0)
	v_mfma_f32_16x16x32_bf16 v[142:145], v[58:61], v[174:177], 0
	v_mfma_f32_16x16x32_bf16 v[138:141], v[74:77], v[174:177], 0
	v_mfma_f32_16x16x32_bf16 v[126:129], v[58:61], v[186:189], 0
	v_mfma_f32_16x16x32_bf16 v[122:125], v[74:77], v[186:189], 0
	v_mfma_f32_16x16x32_bf16 v[110:113], v[58:61], v[194:197], 0
	v_mfma_f32_16x16x32_bf16 v[106:109], v[74:77], v[194:197], 0
	v_mfma_f32_16x16x32_bf16 v[94:97], v[58:61], v[210:213], 0
	v_mfma_f32_16x16x32_bf16 v[90:93], v[74:77], v[210:213], 0
	v_mfma_f32_16x16x32_bf16 v[142:145], v[62:65], v[182:185], v[142:145]
	v_mfma_f32_16x16x32_bf16 v[138:141], v[78:81], v[182:185], v[138:141]
	v_mfma_f32_16x16x32_bf16 v[126:129], v[62:65], v[190:193], v[126:129]
	v_mfma_f32_16x16x32_bf16 v[122:125], v[78:81], v[190:193], v[122:125]
	v_mfma_f32_16x16x32_bf16 v[110:113], v[62:65], v[198:201], v[110:113]
	v_mfma_f32_16x16x32_bf16 v[106:109], v[78:81], v[198:201], v[106:109]
	v_mfma_f32_16x16x32_bf16 v[94:97], v[62:65], v[214:217], v[94:97]
	v_mfma_f32_16x16x32_bf16 v[90:93], v[78:81], v[214:217], v[90:93]
	s_setprio 0
	s_setprio 1
	v_mfma_f32_16x16x32_bf16 v[134:137], v[146:149], v[174:177], 0
	v_mfma_f32_16x16x32_bf16 v[130:133], v[154:157], v[174:177], 0
	v_mfma_f32_16x16x32_bf16 v[118:121], v[146:149], v[186:189], 0
	v_mfma_f32_16x16x32_bf16 v[114:117], v[154:157], v[186:189], 0
	v_mfma_f32_16x16x32_bf16 v[102:105], v[146:149], v[194:197], 0
	v_mfma_f32_16x16x32_bf16 v[98:101], v[154:157], v[194:197], 0
	v_mfma_f32_16x16x32_bf16 v[86:89], v[146:149], v[210:213], 0
	v_mfma_f32_16x16x32_bf16 v[82:85], v[154:157], v[210:213], 0
	v_mfma_f32_16x16x32_bf16 v[134:137], v[150:153], v[182:185], v[134:137]
	v_mfma_f32_16x16x32_bf16 v[130:133], v[170:173], v[182:185], v[130:133]
	v_mfma_f32_16x16x32_bf16 v[118:121], v[150:153], v[190:193], v[118:121]
	v_mfma_f32_16x16x32_bf16 v[114:117], v[170:173], v[190:193], v[114:117]
	v_mfma_f32_16x16x32_bf16 v[102:105], v[150:153], v[198:201], v[102:105]
	v_mfma_f32_16x16x32_bf16 v[98:101], v[170:173], v[198:201], v[98:101]
	v_mfma_f32_16x16x32_bf16 v[86:89], v[150:153], v[214:217], v[86:89]
	v_mfma_f32_16x16x32_bf16 v[82:85], v[170:173], v[214:217], v[82:85]
	s_setprio 0
	s_barrier
	s_add_i32 s88, s88, s14
	v_lshl_add_u64 v[202:203], s[68:69], 0, v[166:167]
	s_mov_b32 m0, s88
	ds_read_b128 v[174:177], v208 offset:16384
	ds_read_b128 v[182:185], v208 offset:17408
	ds_read_b128 v[186:189], v208 offset:18432
	ds_read_b128 v[190:193], v208 offset:19456
	ds_read_b128 v[194:197], v208 offset:20480
	ds_read_b128 v[198:201], v208 offset:21504
	ds_read_b128 v[210:213], v208 offset:22528
	ds_read_b128 v[214:217], v208 offset:23552
	global_load_lds_dwordx4 v[202:203], off
	s_add_i32 m0, s88, 0x2000
	s_add_u32 s90, s68, 0x40000
	v_lshl_add_u64 v[218:219], s[68:69], 0, v[158:159]
	s_addc_u32 s91, s69, 0
	s_add_i32 s88, s92, s14
	global_load_lds_dwordx4 v[218:219], off
	v_lshl_add_u64 v[220:221], s[90:91], 0, v[166:167]
	s_mov_b32 m0, s88
	v_lshl_add_u64 v[222:223], s[70:71], 0, v[162:163]
	global_load_lds_dwordx4 v[220:221], off
	v_lshl_add_u64 v[220:221], s[90:91], 0, v[158:159]
	s_add_i32 m0, s88, 0x2000
	s_nop 0
	global_load_lds_dwordx4 v[220:221], off
	v_lshl_add_u64 v[220:221], s[70:71], 0, v[160:161]
	s_mov_b32 m0, s15
	s_nop 0
	global_load_lds_dwordx4 v[220:221], off
	s_mov_b32 m0, s16
	s_nop 0
	global_load_lds_dwordx4 v[222:223], off
	s_waitcnt vmcnt(8)
	s_waitcnt lgkmcnt(0)
	s_barrier
	s_setprio 1
	s_waitcnt lgkmcnt(0)
	v_mfma_f32_16x16x32_bf16 v[70:73], v[58:61], v[174:177], 0
	v_mfma_f32_16x16x32_bf16 v[66:69], v[74:77], v[174:177], 0
	v_mfma_f32_16x16x32_bf16 v[46:49], v[58:61], v[186:189], 0
	v_mfma_f32_16x16x32_bf16 v[42:45], v[74:77], v[186:189], 0
	v_mfma_f32_16x16x32_bf16 v[30:33], v[58:61], v[194:197], 0
	v_mfma_f32_16x16x32_bf16 v[26:29], v[74:77], v[194:197], 0
	v_mfma_f32_16x16x32_bf16 v[14:17], v[58:61], v[210:213], 0
	v_mfma_f32_16x16x32_bf16 v[10:13], v[74:77], v[210:213], 0
	v_mfma_f32_16x16x32_bf16 v[70:73], v[62:65], v[182:185], v[70:73]
	v_mfma_f32_16x16x32_bf16 v[66:69], v[78:81], v[182:185], v[66:69]
	v_mfma_f32_16x16x32_bf16 v[46:49], v[62:65], v[190:193], v[46:49]
	v_mfma_f32_16x16x32_bf16 v[42:45], v[78:81], v[190:193], v[42:45]
	v_mfma_f32_16x16x32_bf16 v[30:33], v[62:65], v[198:201], v[30:33]
	v_mfma_f32_16x16x32_bf16 v[26:29], v[78:81], v[198:201], v[26:29]
	v_mfma_f32_16x16x32_bf16 v[14:17], v[62:65], v[214:217], v[14:17]
	v_mfma_f32_16x16x32_bf16 v[10:13], v[78:81], v[214:217], v[10:13]
	s_setprio 0
	s_setprio 1
	v_mfma_f32_16x16x32_bf16 v[54:57], v[146:149], v[174:177], 0
	v_mfma_f32_16x16x32_bf16 v[50:53], v[154:157], v[174:177], 0
	v_mfma_f32_16x16x32_bf16 v[38:41], v[146:149], v[186:189], 0
	v_mfma_f32_16x16x32_bf16 v[34:37], v[154:157], v[186:189], 0
	v_mfma_f32_16x16x32_bf16 v[22:25], v[146:149], v[194:197], 0
	v_mfma_f32_16x16x32_bf16 v[18:21], v[154:157], v[194:197], 0
	v_mfma_f32_16x16x32_bf16 v[6:9], v[146:149], v[210:213], 0
	v_mfma_f32_16x16x32_bf16 v[2:5], v[154:157], v[210:213], 0
	v_mfma_f32_16x16x32_bf16 v[54:57], v[150:153], v[182:185], v[54:57]
	v_mfma_f32_16x16x32_bf16 v[50:53], v[170:173], v[182:185], v[50:53]
	v_mfma_f32_16x16x32_bf16 v[38:41], v[150:153], v[190:193], v[38:41]
	v_mfma_f32_16x16x32_bf16 v[34:37], v[170:173], v[190:193], v[34:37]
	v_mfma_f32_16x16x32_bf16 v[22:25], v[150:153], v[198:201], v[22:25]
	v_mfma_f32_16x16x32_bf16 v[18:21], v[170:173], v[198:201], v[18:21]
	v_mfma_f32_16x16x32_bf16 v[6:9], v[150:153], v[214:217], v[6:9]
	v_mfma_f32_16x16x32_bf16 v[2:5], v[170:173], v[214:217], v[2:5]
	s_setprio 0
	s_barrier
	s_add_i32 s88, 0, 0x18000
	s_add_i32 s90, 0, 0x1c000
	v_add_u32_e32 v78, s88, v204
	v_add_u32_e32 v170, s90, v204
	ds_read_b128 v[58:61], v78
	ds_read_b128 v[62:65], v78 offset:1024
	ds_read_b128 v[74:77], v78 offset:2048
	ds_read_b128 v[78:81], v78 offset:3072
	ds_read_b128 v[146:149], v170
	ds_read_b128 v[150:153], v170 offset:1024
	ds_read_b128 v[154:157], v170 offset:2048
	ds_read_b128 v[170:173], v170 offset:3072
	s_add_u32 s70, s70, 0x40000
	s_addc_u32 s71, s71, 0
	s_mov_b32 m0, s20
	v_lshl_add_u64 v[232:233], s[70:71], 0, v[160:161]
	ds_read_b128 v[174:177], v208 offset:32768
	ds_read_b128 v[182:185], v208 offset:33792
	ds_read_b128 v[186:189], v208 offset:34816
	ds_read_b128 v[190:193], v208 offset:35840
	ds_read_b128 v[194:197], v208 offset:36864
	ds_read_b128 v[198:201], v208 offset:37888
	ds_read_b128 v[210:213], v208 offset:38912
	ds_read_b128 v[214:217], v208 offset:39936
	global_load_lds_dwordx4 v[232:233], off
	v_lshl_add_u64 v[232:233], s[70:71], 0, v[162:163]
	s_mov_b32 m0, s21
	s_nop 0
	global_load_lds_dwordx4 v[232:233], off
	s_waitcnt vmcnt(8)
	s_waitcnt lgkmcnt(0)
	s_barrier
	s_setprio 1
	s_waitcnt lgkmcnt(0)
	v_mfma_f32_16x16x32_bf16 v[142:145], v[58:61], v[174:177], v[142:145]
	v_mfma_f32_16x16x32_bf16 v[138:141], v[74:77], v[174:177], v[138:141]
	v_mfma_f32_16x16x32_bf16 v[126:129], v[58:61], v[186:189], v[126:129]
	v_mfma_f32_16x16x32_bf16 v[122:125], v[74:77], v[186:189], v[122:125]
	v_mfma_f32_16x16x32_bf16 v[110:113], v[58:61], v[194:197], v[110:113]
	v_mfma_f32_16x16x32_bf16 v[106:109], v[74:77], v[194:197], v[106:109]
	v_mfma_f32_16x16x32_bf16 v[94:97], v[58:61], v[210:213], v[94:97]
	v_mfma_f32_16x16x32_bf16 v[90:93], v[74:77], v[210:213], v[90:93]
	v_mfma_f32_16x16x32_bf16 v[142:145], v[62:65], v[182:185], v[142:145]
	v_mfma_f32_16x16x32_bf16 v[138:141], v[78:81], v[182:185], v[138:141]
	v_mfma_f32_16x16x32_bf16 v[126:129], v[62:65], v[190:193], v[126:129]
	v_mfma_f32_16x16x32_bf16 v[122:125], v[78:81], v[190:193], v[122:125]
	v_mfma_f32_16x16x32_bf16 v[110:113], v[62:65], v[198:201], v[110:113]
	v_mfma_f32_16x16x32_bf16 v[106:109], v[78:81], v[198:201], v[106:109]
	v_mfma_f32_16x16x32_bf16 v[94:97], v[62:65], v[214:217], v[94:97]
	v_mfma_f32_16x16x32_bf16 v[90:93], v[78:81], v[214:217], v[90:93]
	s_setprio 0
	s_setprio 1
	v_mfma_f32_16x16x32_bf16 v[134:137], v[146:149], v[174:177], v[134:137]
	v_mfma_f32_16x16x32_bf16 v[130:133], v[154:157], v[174:177], v[130:133]
	v_mfma_f32_16x16x32_bf16 v[118:121], v[146:149], v[186:189], v[118:121]
	v_mfma_f32_16x16x32_bf16 v[114:117], v[154:157], v[186:189], v[114:117]
	v_mfma_f32_16x16x32_bf16 v[102:105], v[146:149], v[194:197], v[102:105]
	v_mfma_f32_16x16x32_bf16 v[98:101], v[154:157], v[194:197], v[98:101]
	v_mfma_f32_16x16x32_bf16 v[86:89], v[146:149], v[210:213], v[86:89]
	v_mfma_f32_16x16x32_bf16 v[82:85], v[154:157], v[210:213], v[82:85]
	v_mfma_f32_16x16x32_bf16 v[134:137], v[150:153], v[182:185], v[134:137]
	v_mfma_f32_16x16x32_bf16 v[130:133], v[170:173], v[182:185], v[130:133]
	v_mfma_f32_16x16x32_bf16 v[118:121], v[150:153], v[190:193], v[118:121]
	v_mfma_f32_16x16x32_bf16 v[114:117], v[170:173], v[190:193], v[114:117]
	v_mfma_f32_16x16x32_bf16 v[102:105], v[150:153], v[198:201], v[102:105]
	v_mfma_f32_16x16x32_bf16 v[98:101], v[170:173], v[198:201], v[98:101]
	v_mfma_f32_16x16x32_bf16 v[86:89], v[150:153], v[214:217], v[86:89]
	v_mfma_f32_16x16x32_bf16 v[82:85], v[170:173], v[214:217], v[82:85]
	s_setprio 0
	s_barrier
	s_add_i32 s70, s88, s14
	v_lshl_add_u64 v[202:203], v[202:203], 0, s[56:57]
	s_mov_b32 m0, s70
	ds_read_b128 v[174:177], v208 offset:49152
	ds_read_b128 v[182:185], v208 offset:50176
	ds_read_b128 v[186:189], v208 offset:51200
	ds_read_b128 v[190:193], v208 offset:52224
	ds_read_b128 v[194:197], v208 offset:53248
	ds_read_b128 v[198:201], v208 offset:54272
	ds_read_b128 v[210:213], v208 offset:55296
	ds_read_b128 v[214:217], v208 offset:56320
	global_load_lds_dwordx4 v[202:203], off
	s_add_i32 m0, s70, 0x2000
	s_add_u32 s68, s68, 0x40080
	v_lshl_add_u64 v[202:203], v[218:219], 0, s[56:57]
	s_addc_u32 s69, s69, 0
	s_add_i32 s70, s90, s14
	global_load_lds_dwordx4 v[202:203], off
	v_lshl_add_u64 v[202:203], s[68:69], 0, v[166:167]
	s_mov_b32 m0, s70
	s_nop 0
	global_load_lds_dwordx4 v[202:203], off
	v_lshl_add_u64 v[202:203], s[68:69], 0, v[158:159]
	s_add_i32 m0, s70, 0x2000
	s_nop 0
	global_load_lds_dwordx4 v[202:203], off
	v_lshl_add_u64 v[202:203], v[220:221], 0, s[56:57]
	s_mov_b32 m0, s24
	s_nop 0
	global_load_lds_dwordx4 v[202:203], off
	v_lshl_add_u64 v[202:203], v[222:223], 0, s[56:57]
	s_mov_b32 m0, s25
	s_nop 0
	global_load_lds_dwordx4 v[202:203], off
	s_waitcnt vmcnt(8)
	s_waitcnt lgkmcnt(0)
	s_barrier
	s_setprio 1
	s_waitcnt lgkmcnt(0)
	v_mfma_f32_16x16x32_bf16 v[70:73], v[58:61], v[174:177], v[70:73]
	v_mfma_f32_16x16x32_bf16 v[66:69], v[74:77], v[174:177], v[66:69]
	v_mfma_f32_16x16x32_bf16 v[46:49], v[58:61], v[186:189], v[46:49]
	v_mfma_f32_16x16x32_bf16 v[42:45], v[74:77], v[186:189], v[42:45]
	v_mfma_f32_16x16x32_bf16 v[30:33], v[58:61], v[194:197], v[30:33]
	v_mfma_f32_16x16x32_bf16 v[26:29], v[74:77], v[194:197], v[26:29]
	v_mfma_f32_16x16x32_bf16 v[14:17], v[58:61], v[210:213], v[14:17]
	v_mfma_f32_16x16x32_bf16 v[10:13], v[74:77], v[210:213], v[10:13]
	v_mfma_f32_16x16x32_bf16 v[70:73], v[62:65], v[182:185], v[70:73]
	v_mfma_f32_16x16x32_bf16 v[66:69], v[78:81], v[182:185], v[66:69]
	v_mfma_f32_16x16x32_bf16 v[46:49], v[62:65], v[190:193], v[46:49]
	v_mfma_f32_16x16x32_bf16 v[42:45], v[78:81], v[190:193], v[42:45]
	v_mfma_f32_16x16x32_bf16 v[30:33], v[62:65], v[198:201], v[30:33]
	v_mfma_f32_16x16x32_bf16 v[26:29], v[78:81], v[198:201], v[26:29]
	v_mfma_f32_16x16x32_bf16 v[14:17], v[62:65], v[214:217], v[14:17]
	v_mfma_f32_16x16x32_bf16 v[10:13], v[78:81], v[214:217], v[10:13]
	s_setprio 0
	s_setprio 1
	v_mfma_f32_16x16x32_bf16 v[54:57], v[146:149], v[174:177], v[54:57]
	v_mfma_f32_16x16x32_bf16 v[50:53], v[154:157], v[174:177], v[50:53]
	v_mfma_f32_16x16x32_bf16 v[38:41], v[146:149], v[186:189], v[38:41]
	v_mfma_f32_16x16x32_bf16 v[34:37], v[154:157], v[186:189], v[34:37]
	v_mfma_f32_16x16x32_bf16 v[22:25], v[146:149], v[194:197], v[22:25]
	v_mfma_f32_16x16x32_bf16 v[18:21], v[154:157], v[194:197], v[18:21]
	v_mfma_f32_16x16x32_bf16 v[6:9], v[146:149], v[210:213], v[6:9]
	v_mfma_f32_16x16x32_bf16 v[2:5], v[154:157], v[210:213], v[2:5]
	v_mfma_f32_16x16x32_bf16 v[54:57], v[150:153], v[182:185], v[54:57]
	v_mfma_f32_16x16x32_bf16 v[50:53], v[170:173], v[182:185], v[50:53]
	v_mfma_f32_16x16x32_bf16 v[38:41], v[150:153], v[190:193], v[38:41]
	v_mfma_f32_16x16x32_bf16 v[34:37], v[170:173], v[190:193], v[34:37]
	v_mfma_f32_16x16x32_bf16 v[22:25], v[150:153], v[198:201], v[22:25]
	v_mfma_f32_16x16x32_bf16 v[18:21], v[170:173], v[198:201], v[18:21]
	v_mfma_f32_16x16x32_bf16 v[6:9], v[150:153], v[214:217], v[6:9]
	v_mfma_f32_16x16x32_bf16 v[2:5], v[170:173], v[214:217], v[2:5]
	s_setprio 0
	s_add_u32 s77, s77, 0x100
	s_addc_u32 s79, s79, 0
	s_add_u32 s74, s74, 0x100
	s_addc_u32 s75, s75, 0
	s_cmp_ge_i32 s84, s1
	s_mov_b32 s68, s84
	s_cbranch_scc1 .Lrotph6_pexitbar
	s_add_i32 s84, s68, 2
	s_add_u32 s69, s74, 0xfffc0080
	s_addc_u32 s70, s75, -1
	s_add_i32 s88, 0, 0x10000
	s_cmp_eq_u32 s72, s68
	s_cselect_b32 s71, s29, s70
	s_cselect_b32 s70, s43, s69
	s_cselect_b32 s69, s55, s79
	s_cselect_b32 s68, s59, s77
	s_add_i32 s92, 0, 0x14000
	s_barrier
	s_branch .Lrotph6_body

.Lrotph6_body:
	v_add_u32_e32 v78, s88, v204
	v_add_u32_e32 v170, s92, v204
	ds_read_b128 v[58:61], v78
	ds_read_b128 v[62:65], v78 offset:1024
	ds_read_b128 v[74:77], v78 offset:2048
	ds_read_b128 v[78:81], v78 offset:3072
	ds_read_b128 v[146:149], v170
	ds_read_b128 v[150:153], v170 offset:1024
	ds_read_b128 v[154:157], v170 offset:2048
	ds_read_b128 v[170:173], v170 offset:3072
	v_lshl_add_u64 v[202:203], s[74:75], 0, v[180:181]
	s_add_i32 m0, s15, 0xc000
	ds_read_b128 v[174:177], v208
	ds_read_b128 v[182:185], v208 offset:1024
	ds_read_b128 v[186:189], v208 offset:2048
	ds_read_b128 v[190:193], v208 offset:3072
	ds_read_b128 v[194:197], v208 offset:4096
	ds_read_b128 v[198:201], v208 offset:5120
	ds_read_b128 v[210:213], v208 offset:6144
	ds_read_b128 v[214:217], v208 offset:7168
	global_load_lds_dwordx4 v[202:203], off
	v_lshl_add_u64 v[202:203], s[74:75], 0, v[178:179]
	s_add_i32 m0, s15, 0xe000
	s_nop 0
	global_load_lds_dwordx4 v[202:203], off
	s_waitcnt vmcnt(8)
	s_waitcnt lgkmcnt(0)
	s_barrier
	s_setprio 1
	s_waitcnt lgkmcnt(0)
	v_mfma_f32_16x16x32_bf16 v[142:145], v[58:61], v[174:177], v[142:145]
	v_mfma_f32_16x16x32_bf16 v[138:141], v[74:77], v[174:177], v[138:141]
	v_mfma_f32_16x16x32_bf16 v[126:129], v[58:61], v[186:189], v[126:129]
	v_mfma_f32_16x16x32_bf16 v[122:125], v[74:77], v[186:189], v[122:125]
	v_mfma_f32_16x16x32_bf16 v[110:113], v[58:61], v[194:197], v[110:113]
	v_mfma_f32_16x16x32_bf16 v[106:109], v[74:77], v[194:197], v[106:109]
	v_mfma_f32_16x16x32_bf16 v[94:97], v[58:61], v[210:213], v[94:97]
	v_mfma_f32_16x16x32_bf16 v[90:93], v[74:77], v[210:213], v[90:93]
	v_mfma_f32_16x16x32_bf16 v[142:145], v[62:65], v[182:185], v[142:145]
	v_mfma_f32_16x16x32_bf16 v[138:141], v[78:81], v[182:185], v[138:141]
	v_mfma_f32_16x16x32_bf16 v[126:129], v[62:65], v[190:193], v[126:129]
	v_mfma_f32_16x16x32_bf16 v[122:125], v[78:81], v[190:193], v[122:125]
	v_mfma_f32_16x16x32_bf16 v[110:113], v[62:65], v[198:201], v[110:113]
	v_mfma_f32_16x16x32_bf16 v[106:109], v[78:81], v[198:201], v[106:109]
	v_mfma_f32_16x16x32_bf16 v[94:97], v[62:65], v[214:217], v[94:97]
	v_mfma_f32_16x16x32_bf16 v[90:93], v[78:81], v[214:217], v[90:93]
	s_setprio 0
	s_setprio 1
	v_mfma_f32_16x16x32_bf16 v[134:137], v[146:149], v[174:177], v[134:137]
	v_mfma_f32_16x16x32_bf16 v[130:133], v[154:157], v[174:177], v[130:133]
	v_mfma_f32_16x16x32_bf16 v[118:121], v[146:149], v[186:189], v[118:121]
	v_mfma_f32_16x16x32_bf16 v[114:117], v[154:157], v[186:189], v[114:117]
	v_mfma_f32_16x16x32_bf16 v[102:105], v[146:149], v[194:197], v[102:105]
	v_mfma_f32_16x16x32_bf16 v[98:101], v[154:157], v[194:197], v[98:101]
	v_mfma_f32_16x16x32_bf16 v[86:89], v[146:149], v[210:213], v[86:89]
	v_mfma_f32_16x16x32_bf16 v[82:85], v[154:157], v[210:213], v[82:85]
	v_mfma_f32_16x16x32_bf16 v[134:137], v[150:153], v[182:185], v[134:137]
	v_mfma_f32_16x16x32_bf16 v[130:133], v[170:173], v[182:185], v[130:133]
	v_mfma_f32_16x16x32_bf16 v[118:121], v[150:153], v[190:193], v[118:121]
	v_mfma_f32_16x16x32_bf16 v[114:117], v[170:173], v[190:193], v[114:117]
	v_mfma_f32_16x16x32_bf16 v[102:105], v[150:153], v[198:201], v[102:105]
	v_mfma_f32_16x16x32_bf16 v[98:101], v[170:173], v[198:201], v[98:101]
	v_mfma_f32_16x16x32_bf16 v[86:89], v[150:153], v[214:217], v[86:89]
	v_mfma_f32_16x16x32_bf16 v[82:85], v[170:173], v[214:217], v[82:85]
	s_setprio 0
	s_barrier
	s_add_i32 s88, s88, s14
	v_lshl_add_u64 v[202:203], s[68:69], 0, v[166:167]
	s_mov_b32 m0, s88
	ds_read_b128 v[174:177], v208 offset:16384
	ds_read_b128 v[182:185], v208 offset:17408
	ds_read_b128 v[186:189], v208 offset:18432
	ds_read_b128 v[190:193], v208 offset:19456
	ds_read_b128 v[194:197], v208 offset:20480
	ds_read_b128 v[198:201], v208 offset:21504
	ds_read_b128 v[210:213], v208 offset:22528
	ds_read_b128 v[214:217], v208 offset:23552
	global_load_lds_dwordx4 v[202:203], off
	s_add_i32 m0, s88, 0x2000
	s_add_u32 s90, s68, 0x40000
	v_lshl_add_u64 v[218:219], s[68:69], 0, v[158:159]
	s_addc_u32 s91, s69, 0
	s_add_i32 s88, s92, s14
	global_load_lds_dwordx4 v[218:219], off
	v_lshl_add_u64 v[220:221], s[90:91], 0, v[166:167]
	s_mov_b32 m0, s88
	v_lshl_add_u64 v[222:223], s[70:71], 0, v[162:163]
	global_load_lds_dwordx4 v[220:221], off
	v_lshl_add_u64 v[220:221], s[90:91], 0, v[158:159]
	s_add_i32 m0, s88, 0x2000
	s_nop 0
	global_load_lds_dwordx4 v[220:221], off
	v_lshl_add_u64 v[220:221], s[70:71], 0, v[160:161]
	s_mov_b32 m0, s15
	s_nop 0
	global_load_lds_dwordx4 v[220:221], off
	s_mov_b32 m0, s16
	s_nop 0
	global_load_lds_dwordx4 v[222:223], off
	s_waitcnt vmcnt(8)
	s_waitcnt lgkmcnt(0)
	s_barrier
	s_setprio 1
	s_waitcnt lgkmcnt(0)
	v_mfma_f32_16x16x32_bf16 v[70:73], v[58:61], v[174:177], v[70:73]
	v_mfma_f32_16x16x32_bf16 v[66:69], v[74:77], v[174:177], v[66:69]
	v_mfma_f32_16x16x32_bf16 v[46:49], v[58:61], v[186:189], v[46:49]
	v_mfma_f32_16x16x32_bf16 v[42:45], v[74:77], v[186:189], v[42:45]
	v_mfma_f32_16x16x32_bf16 v[30:33], v[58:61], v[194:197], v[30:33]
	v_mfma_f32_16x16x32_bf16 v[26:29], v[74:77], v[194:197], v[26:29]
	v_mfma_f32_16x16x32_bf16 v[14:17], v[58:61], v[210:213], v[14:17]
	v_mfma_f32_16x16x32_bf16 v[10:13], v[74:77], v[210:213], v[10:13]
	v_mfma_f32_16x16x32_bf16 v[70:73], v[62:65], v[182:185], v[70:73]
	v_mfma_f32_16x16x32_bf16 v[66:69], v[78:81], v[182:185], v[66:69]
	v_mfma_f32_16x16x32_bf16 v[46:49], v[62:65], v[190:193], v[46:49]
	v_mfma_f32_16x16x32_bf16 v[42:45], v[78:81], v[190:193], v[42:45]
	v_mfma_f32_16x16x32_bf16 v[30:33], v[62:65], v[198:201], v[30:33]
	v_mfma_f32_16x16x32_bf16 v[26:29], v[78:81], v[198:201], v[26:29]
	v_mfma_f32_16x16x32_bf16 v[14:17], v[62:65], v[214:217], v[14:17]
	v_mfma_f32_16x16x32_bf16 v[10:13], v[78:81], v[214:217], v[10:13]
	s_setprio 0
	s_setprio 1
	v_mfma_f32_16x16x32_bf16 v[54:57], v[146:149], v[174:177], v[54:57]
	v_mfma_f32_16x16x32_bf16 v[50:53], v[154:157], v[174:177], v[50:53]
	v_mfma_f32_16x16x32_bf16 v[38:41], v[146:149], v[186:189], v[38:41]
	v_mfma_f32_16x16x32_bf16 v[34:37], v[154:157], v[186:189], v[34:37]
	v_mfma_f32_16x16x32_bf16 v[22:25], v[146:149], v[194:197], v[22:25]
	v_mfma_f32_16x16x32_bf16 v[18:21], v[154:157], v[194:197], v[18:21]
	v_mfma_f32_16x16x32_bf16 v[6:9], v[146:149], v[210:213], v[6:9]
	v_mfma_f32_16x16x32_bf16 v[2:5], v[154:157], v[210:213], v[2:5]
	v_mfma_f32_16x16x32_bf16 v[54:57], v[150:153], v[182:185], v[54:57]
	v_mfma_f32_16x16x32_bf16 v[50:53], v[170:173], v[182:185], v[50:53]
	v_mfma_f32_16x16x32_bf16 v[38:41], v[150:153], v[190:193], v[38:41]
	v_mfma_f32_16x16x32_bf16 v[34:37], v[170:173], v[190:193], v[34:37]
	v_mfma_f32_16x16x32_bf16 v[22:25], v[150:153], v[198:201], v[22:25]
	v_mfma_f32_16x16x32_bf16 v[18:21], v[170:173], v[198:201], v[18:21]
	v_mfma_f32_16x16x32_bf16 v[6:9], v[150:153], v[214:217], v[6:9]
	v_mfma_f32_16x16x32_bf16 v[2:5], v[170:173], v[214:217], v[2:5]
	s_setprio 0
	s_barrier
	s_add_i32 s88, 0, 0x18000
	s_add_i32 s90, 0, 0x1c000
	v_add_u32_e32 v78, s88, v204
	v_add_u32_e32 v170, s90, v204
	ds_read_b128 v[58:61], v78
	ds_read_b128 v[62:65], v78 offset:1024
	ds_read_b128 v[74:77], v78 offset:2048
	ds_read_b128 v[78:81], v78 offset:3072
	ds_read_b128 v[146:149], v170
	ds_read_b128 v[150:153], v170 offset:1024
	ds_read_b128 v[154:157], v170 offset:2048
	ds_read_b128 v[170:173], v170 offset:3072
	s_add_u32 s70, s70, 0x40000
	s_addc_u32 s71, s71, 0
	s_mov_b32 m0, s20
	v_lshl_add_u64 v[232:233], s[70:71], 0, v[160:161]
	ds_read_b128 v[174:177], v208 offset:32768
	ds_read_b128 v[182:185], v208 offset:33792
	ds_read_b128 v[186:189], v208 offset:34816
	ds_read_b128 v[190:193], v208 offset:35840
	ds_read_b128 v[194:197], v208 offset:36864
	ds_read_b128 v[198:201], v208 offset:37888
	ds_read_b128 v[210:213], v208 offset:38912
	ds_read_b128 v[214:217], v208 offset:39936
	global_load_lds_dwordx4 v[232:233], off
	v_lshl_add_u64 v[232:233], s[70:71], 0, v[162:163]
	s_mov_b32 m0, s21
	s_nop 0
	global_load_lds_dwordx4 v[232:233], off
	s_waitcnt vmcnt(8)
	s_waitcnt lgkmcnt(0)
	s_barrier
	s_setprio 1
	s_waitcnt lgkmcnt(0)
	v_mfma_f32_16x16x32_bf16 v[142:145], v[58:61], v[174:177], v[142:145]
	v_mfma_f32_16x16x32_bf16 v[138:141], v[74:77], v[174:177], v[138:141]
	v_mfma_f32_16x16x32_bf16 v[126:129], v[58:61], v[186:189], v[126:129]
	v_mfma_f32_16x16x32_bf16 v[122:125], v[74:77], v[186:189], v[122:125]
	v_mfma_f32_16x16x32_bf16 v[110:113], v[58:61], v[194:197], v[110:113]
	v_mfma_f32_16x16x32_bf16 v[106:109], v[74:77], v[194:197], v[106:109]
	v_mfma_f32_16x16x32_bf16 v[94:97], v[58:61], v[210:213], v[94:97]
	v_mfma_f32_16x16x32_bf16 v[90:93], v[74:77], v[210:213], v[90:93]
	v_mfma_f32_16x16x32_bf16 v[142:145], v[62:65], v[182:185], v[142:145]
	v_mfma_f32_16x16x32_bf16 v[138:141], v[78:81], v[182:185], v[138:141]
	v_mfma_f32_16x16x32_bf16 v[126:129], v[62:65], v[190:193], v[126:129]
	v_mfma_f32_16x16x32_bf16 v[122:125], v[78:81], v[190:193], v[122:125]
	v_mfma_f32_16x16x32_bf16 v[110:113], v[62:65], v[198:201], v[110:113]
	v_mfma_f32_16x16x32_bf16 v[106:109], v[78:81], v[198:201], v[106:109]
	v_mfma_f32_16x16x32_bf16 v[94:97], v[62:65], v[214:217], v[94:97]
	v_mfma_f32_16x16x32_bf16 v[90:93], v[78:81], v[214:217], v[90:93]
	s_setprio 0
	s_setprio 1
	v_mfma_f32_16x16x32_bf16 v[134:137], v[146:149], v[174:177], v[134:137]
	v_mfma_f32_16x16x32_bf16 v[130:133], v[154:157], v[174:177], v[130:133]
	v_mfma_f32_16x16x32_bf16 v[118:121], v[146:149], v[186:189], v[118:121]
	v_mfma_f32_16x16x32_bf16 v[114:117], v[154:157], v[186:189], v[114:117]
	v_mfma_f32_16x16x32_bf16 v[102:105], v[146:149], v[194:197], v[102:105]
	v_mfma_f32_16x16x32_bf16 v[98:101], v[154:157], v[194:197], v[98:101]
	v_mfma_f32_16x16x32_bf16 v[86:89], v[146:149], v[210:213], v[86:89]
	v_mfma_f32_16x16x32_bf16 v[82:85], v[154:157], v[210:213], v[82:85]
	v_mfma_f32_16x16x32_bf16 v[134:137], v[150:153], v[182:185], v[134:137]
	v_mfma_f32_16x16x32_bf16 v[130:133], v[170:173], v[182:185], v[130:133]
	v_mfma_f32_16x16x32_bf16 v[118:121], v[150:153], v[190:193], v[118:121]
	v_mfma_f32_16x16x32_bf16 v[114:117], v[170:173], v[190:193], v[114:117]
	v_mfma_f32_16x16x32_bf16 v[102:105], v[150:153], v[198:201], v[102:105]
	v_mfma_f32_16x16x32_bf16 v[98:101], v[170:173], v[198:201], v[98:101]
	v_mfma_f32_16x16x32_bf16 v[86:89], v[150:153], v[214:217], v[86:89]
	v_mfma_f32_16x16x32_bf16 v[82:85], v[170:173], v[214:217], v[82:85]
	s_setprio 0
	s_barrier
	s_add_i32 s70, s88, s14
	v_lshl_add_u64 v[202:203], v[202:203], 0, s[56:57]
	s_mov_b32 m0, s70
	ds_read_b128 v[174:177], v208 offset:49152
	ds_read_b128 v[182:185], v208 offset:50176
	ds_read_b128 v[186:189], v208 offset:51200
	ds_read_b128 v[190:193], v208 offset:52224
	ds_read_b128 v[194:197], v208 offset:53248
	ds_read_b128 v[198:201], v208 offset:54272
	ds_read_b128 v[210:213], v208 offset:55296
	ds_read_b128 v[214:217], v208 offset:56320
	global_load_lds_dwordx4 v[202:203], off
	s_add_i32 m0, s70, 0x2000
	s_add_u32 s68, s68, 0x40080
	v_lshl_add_u64 v[202:203], v[218:219], 0, s[56:57]
	s_addc_u32 s69, s69, 0
	s_add_i32 s70, s90, s14
	global_load_lds_dwordx4 v[202:203], off
	v_lshl_add_u64 v[202:203], s[68:69], 0, v[166:167]
	s_mov_b32 m0, s70
	s_nop 0
	global_load_lds_dwordx4 v[202:203], off
	v_lshl_add_u64 v[202:203], s[68:69], 0, v[158:159]
	s_add_i32 m0, s70, 0x2000
	s_nop 0
	global_load_lds_dwordx4 v[202:203], off
	v_lshl_add_u64 v[202:203], v[220:221], 0, s[56:57]
	s_mov_b32 m0, s24
	s_nop 0
	global_load_lds_dwordx4 v[202:203], off
	v_lshl_add_u64 v[202:203], v[222:223], 0, s[56:57]
	s_mov_b32 m0, s25
	s_nop 0
	global_load_lds_dwordx4 v[202:203], off
	s_waitcnt vmcnt(8)
	s_waitcnt lgkmcnt(0)
	s_barrier
	s_setprio 1
	s_waitcnt lgkmcnt(0)
	v_mfma_f32_16x16x32_bf16 v[70:73], v[58:61], v[174:177], v[70:73]
	v_mfma_f32_16x16x32_bf16 v[66:69], v[74:77], v[174:177], v[66:69]
	v_mfma_f32_16x16x32_bf16 v[46:49], v[58:61], v[186:189], v[46:49]
	v_mfma_f32_16x16x32_bf16 v[42:45], v[74:77], v[186:189], v[42:45]
	v_mfma_f32_16x16x32_bf16 v[30:33], v[58:61], v[194:197], v[30:33]
	v_mfma_f32_16x16x32_bf16 v[26:29], v[74:77], v[194:197], v[26:29]
	v_mfma_f32_16x16x32_bf16 v[14:17], v[58:61], v[210:213], v[14:17]
	v_mfma_f32_16x16x32_bf16 v[10:13], v[74:77], v[210:213], v[10:13]
	v_mfma_f32_16x16x32_bf16 v[70:73], v[62:65], v[182:185], v[70:73]
	v_mfma_f32_16x16x32_bf16 v[66:69], v[78:81], v[182:185], v[66:69]
	v_mfma_f32_16x16x32_bf16 v[46:49], v[62:65], v[190:193], v[46:49]
	v_mfma_f32_16x16x32_bf16 v[42:45], v[78:81], v[190:193], v[42:45]
	v_mfma_f32_16x16x32_bf16 v[30:33], v[62:65], v[198:201], v[30:33]
	v_mfma_f32_16x16x32_bf16 v[26:29], v[78:81], v[198:201], v[26:29]
	v_mfma_f32_16x16x32_bf16 v[14:17], v[62:65], v[214:217], v[14:17]
	v_mfma_f32_16x16x32_bf16 v[10:13], v[78:81], v[214:217], v[10:13]
	s_setprio 0
	s_setprio 1
	v_mfma_f32_16x16x32_bf16 v[54:57], v[146:149], v[174:177], v[54:57]
	v_mfma_f32_16x16x32_bf16 v[50:53], v[154:157], v[174:177], v[50:53]
	v_mfma_f32_16x16x32_bf16 v[38:41], v[146:149], v[186:189], v[38:41]
	v_mfma_f32_16x16x32_bf16 v[34:37], v[154:157], v[186:189], v[34:37]
	v_mfma_f32_16x16x32_bf16 v[22:25], v[146:149], v[194:197], v[22:25]
	v_mfma_f32_16x16x32_bf16 v[18:21], v[154:157], v[194:197], v[18:21]
	v_mfma_f32_16x16x32_bf16 v[6:9], v[146:149], v[210:213], v[6:9]
	v_mfma_f32_16x16x32_bf16 v[2:5], v[154:157], v[210:213], v[2:5]
	v_mfma_f32_16x16x32_bf16 v[54:57], v[150:153], v[182:185], v[54:57]
	v_mfma_f32_16x16x32_bf16 v[50:53], v[170:173], v[182:185], v[50:53]
	v_mfma_f32_16x16x32_bf16 v[38:41], v[150:153], v[190:193], v[38:41]
	v_mfma_f32_16x16x32_bf16 v[34:37], v[170:173], v[190:193], v[34:37]
	v_mfma_f32_16x16x32_bf16 v[22:25], v[150:153], v[198:201], v[22:25]
	v_mfma_f32_16x16x32_bf16 v[18:21], v[170:173], v[198:201], v[18:21]
	v_mfma_f32_16x16x32_bf16 v[6:9], v[150:153], v[214:217], v[6:9]
	v_mfma_f32_16x16x32_bf16 v[2:5], v[170:173], v[214:217], v[2:5]
	s_setprio 0
	s_add_u32 s77, s77, 0x100
	s_addc_u32 s79, s79, 0
	s_add_u32 s74, s74, 0x100
	s_addc_u32 s75, s75, 0
	s_cmp_ge_i32 s84, s1
	s_mov_b32 s68, s84
	s_cbranch_scc1 .Lrotph6_exitbar
	s_add_i32 s84, s68, 2
	s_add_u32 s69, s74, 0xfffc0080
	s_addc_u32 s70, s75, -1
	s_add_i32 s88, 0, 0x10000
	s_cmp_eq_u32 s72, s68
	s_cselect_b32 s71, s29, s70
	s_cselect_b32 s70, s43, s69
	s_cselect_b32 s69, s55, s79
	s_cselect_b32 s68, s59, s77
	s_add_i32 s92, 0, 0x14000
	s_barrier
	s_branch .Lrotph6_body
.Lrotph6_exitbar:
	s_barrier
.Lpeelexitph6:
	s_movk_i32 s79, 0x1ff
	s_mov_b32 s84, 0xf800000
	s_mov_b32 s88, 0xe800000
	s_and_b64 vcc, exec, s[48:49]
	s_cbranch_vccz .LBB0_667

.Lpeelph7b_0:
	s_add_i32 s69, s58, 2
	s_add_u32 s59, s54, 0xfffc0080
	s_addc_u32 s60, s55, -1
	s_add_i32 s70, 0, 0x10000
	s_cmp_eq_u32 s53, s58
	s_cselect_b32 s61, s43, s60
	s_cselect_b32 s60, s45, s59
	v_add_u32_e32 v146, s70, v151
	s_cselect_b32 s59, s64, s68
	s_cselect_b32 s58, s65, s66
	s_add_i32 s72, 0, 0x14000
	ds_read_b128 v[142:145], v146
	ds_read_b128 v[156:159], v146 offset:1024
	ds_read_b128 v[160:163], v146 offset:2048
	ds_read_b128 v[170:173], v146 offset:3072
	v_add_u32_e32 v146, s72, v151
	ds_read_b128 v[174:177], v146
	ds_read_b128 v[178:181], v146 offset:1024
	ds_read_b128 v[182:185], v146 offset:2048
	ds_read_b128 v[186:189], v146 offset:3072
	v_lshl_add_u64 v[146:147], s[54:55], 0, v[140:141]
	s_add_i32 m0, s16, 0xc000
	ds_read_b128 v[190:193], v154
	ds_read_b128 v[194:197], v154 offset:1024
	ds_read_b128 v[198:201], v154 offset:2048
	ds_read_b128 v[202:205], v154 offset:3072
	ds_read_b128 v[206:209], v154 offset:4096
	ds_read_b128 v[210:213], v154 offset:5120
	ds_read_b128 v[214:217], v154 offset:6144
	ds_read_b128 v[218:221], v154 offset:7168
	global_load_lds_dwordx4 v[146:147], off
	v_lshl_add_u64 v[146:147], s[54:55], 0, v[138:139]
	s_add_i32 m0, s16, 0xe000
	s_nop 0
	global_load_lds_dwordx4 v[146:147], off
	s_waitcnt vmcnt(8)
	s_waitcnt lgkmcnt(0)
	s_barrier
	s_setprio 1
	s_waitcnt lgkmcnt(0)
	v_mfma_f32_16x16x32_bf16 v[126:129], v[142:145], v[190:193], 0
	v_mfma_f32_16x16x32_bf16 v[118:121], v[160:163], v[190:193], 0
	v_mfma_f32_16x16x32_bf16 v[110:113], v[142:145], v[198:201], 0
	v_mfma_f32_16x16x32_bf16 v[102:105], v[160:163], v[198:201], 0
	v_mfma_f32_16x16x32_bf16 v[94:97], v[142:145], v[206:209], 0
	v_mfma_f32_16x16x32_bf16 v[86:89], v[160:163], v[206:209], 0
	v_mfma_f32_16x16x32_bf16 v[78:81], v[142:145], v[214:217], 0
	v_mfma_f32_16x16x32_bf16 v[70:73], v[160:163], v[214:217], 0
	v_mfma_f32_16x16x32_bf16 v[126:129], v[156:159], v[194:197], v[126:129]
	v_mfma_f32_16x16x32_bf16 v[118:121], v[170:173], v[194:197], v[118:121]
	v_mfma_f32_16x16x32_bf16 v[110:113], v[156:159], v[202:205], v[110:113]
	v_mfma_f32_16x16x32_bf16 v[102:105], v[170:173], v[202:205], v[102:105]
	v_mfma_f32_16x16x32_bf16 v[94:97], v[156:159], v[210:213], v[94:97]
	v_mfma_f32_16x16x32_bf16 v[86:89], v[170:173], v[210:213], v[86:89]
	v_mfma_f32_16x16x32_bf16 v[78:81], v[156:159], v[218:221], v[78:81]
	v_mfma_f32_16x16x32_bf16 v[70:73], v[170:173], v[218:221], v[70:73]
	s_setprio 0
	s_setprio 1
	v_mfma_f32_16x16x32_bf16 v[122:125], v[174:177], v[190:193], 0
	v_mfma_f32_16x16x32_bf16 v[114:117], v[182:185], v[190:193], 0
	v_mfma_f32_16x16x32_bf16 v[106:109], v[174:177], v[198:201], 0
	v_mfma_f32_16x16x32_bf16 v[98:101], v[182:185], v[198:201], 0
	v_mfma_f32_16x16x32_bf16 v[90:93], v[174:177], v[206:209], 0
	v_mfma_f32_16x16x32_bf16 v[82:85], v[182:185], v[206:209], 0
	v_mfma_f32_16x16x32_bf16 v[74:77], v[174:177], v[214:217], 0
	v_mfma_f32_16x16x32_bf16 v[66:69], v[182:185], v[214:217], 0
	v_mfma_f32_16x16x32_bf16 v[122:125], v[178:181], v[194:197], v[122:125]
	v_mfma_f32_16x16x32_bf16 v[114:117], v[186:189], v[194:197], v[114:117]
	v_mfma_f32_16x16x32_bf16 v[106:109], v[178:181], v[202:205], v[106:109]
	v_mfma_f32_16x16x32_bf16 v[98:101], v[186:189], v[202:205], v[98:101]
	v_mfma_f32_16x16x32_bf16 v[90:93], v[178:181], v[210:213], v[90:93]
	v_mfma_f32_16x16x32_bf16 v[82:85], v[186:189], v[210:213], v[82:85]
	v_mfma_f32_16x16x32_bf16 v[74:77], v[178:181], v[218:221], v[74:77]
	v_mfma_f32_16x16x32_bf16 v[66:69], v[186:189], v[218:221], v[66:69]
	s_setprio 0
	s_barrier
	s_add_i32 s70, s70, s14
	v_lshl_add_u64 v[146:147], s[58:59], 0, v[166:167]
	s_mov_b32 m0, s70
	ds_read_b128 v[190:193], v154 offset:16384
	ds_read_b128 v[194:197], v154 offset:17408
	ds_read_b128 v[198:201], v154 offset:18432
	ds_read_b128 v[202:205], v154 offset:19456
	ds_read_b128 v[206:209], v154 offset:20480
	ds_read_b128 v[210:213], v154 offset:21504
	ds_read_b128 v[214:217], v154 offset:22528
	ds_read_b128 v[218:221], v154 offset:23552
	global_load_lds_dwordx4 v[146:147], off
	s_add_i32 m0, s70, 0x2000
	s_add_u32 s70, s58, 0x40000
	v_lshl_add_u64 v[164:165], s[58:59], 0, v[134:135]
	s_addc_u32 s71, s59, 0
	s_add_i32 s72, s72, s14
	global_load_lds_dwordx4 v[164:165], off
	v_lshl_add_u64 v[222:223], s[70:71], 0, v[166:167]
	s_mov_b32 m0, s72
	v_lshl_add_u64 v[232:233], s[60:61], 0, v[130:131]
	global_load_lds_dwordx4 v[222:223], off
	v_lshl_add_u64 v[222:223], s[70:71], 0, v[134:135]
	s_add_i32 m0, s72, 0x2000
	s_nop 0
	global_load_lds_dwordx4 v[222:223], off
	v_lshl_add_u64 v[222:223], s[60:61], 0, v[132:133]
	s_mov_b32 m0, s16
	s_nop 0
	global_load_lds_dwordx4 v[222:223], off
	s_mov_b32 m0, s20
	s_nop 0
	global_load_lds_dwordx4 v[232:233], off
	s_waitcnt vmcnt(8)
	s_waitcnt lgkmcnt(0)
	s_barrier
	s_setprio 1
	s_waitcnt lgkmcnt(0)
	v_mfma_f32_16x16x32_bf16 v[62:65], v[142:145], v[190:193], 0
	v_mfma_f32_16x16x32_bf16 v[54:57], v[160:163], v[190:193], 0
	v_mfma_f32_16x16x32_bf16 v[46:49], v[142:145], v[198:201], 0
	v_mfma_f32_16x16x32_bf16 v[38:41], v[160:163], v[198:201], 0
	v_mfma_f32_16x16x32_bf16 v[30:33], v[142:145], v[206:209], 0
	v_mfma_f32_16x16x32_bf16 v[22:25], v[160:163], v[206:209], 0
	v_mfma_f32_16x16x32_bf16 v[14:17], v[142:145], v[214:217], 0
	v_mfma_f32_16x16x32_bf16 v[6:9], v[160:163], v[214:217], 0
	v_mfma_f32_16x16x32_bf16 v[62:65], v[156:159], v[194:197], v[62:65]
	v_mfma_f32_16x16x32_bf16 v[54:57], v[170:173], v[194:197], v[54:57]
	v_mfma_f32_16x16x32_bf16 v[46:49], v[156:159], v[202:205], v[46:49]
	v_mfma_f32_16x16x32_bf16 v[38:41], v[170:173], v[202:205], v[38:41]
	v_mfma_f32_16x16x32_bf16 v[30:33], v[156:159], v[210:213], v[30:33]
	v_mfma_f32_16x16x32_bf16 v[22:25], v[170:173], v[210:213], v[22:25]
	v_mfma_f32_16x16x32_bf16 v[14:17], v[156:159], v[218:221], v[14:17]
	v_mfma_f32_16x16x32_bf16 v[6:9], v[170:173], v[218:221], v[6:9]
	s_setprio 0
	s_setprio 1
	v_mfma_f32_16x16x32_bf16 v[58:61], v[174:177], v[190:193], 0
	v_mfma_f32_16x16x32_bf16 v[50:53], v[182:185], v[190:193], 0
	v_mfma_f32_16x16x32_bf16 v[42:45], v[174:177], v[198:201], 0
	v_mfma_f32_16x16x32_bf16 v[34:37], v[182:185], v[198:201], 0
	v_mfma_f32_16x16x32_bf16 v[26:29], v[174:177], v[206:209], 0
	v_mfma_f32_16x16x32_bf16 v[18:21], v[182:185], v[206:209], 0
	v_mfma_f32_16x16x32_bf16 v[10:13], v[174:177], v[214:217], 0
	v_mfma_f32_16x16x32_bf16 v[2:5], v[182:185], v[214:217], 0
	v_mfma_f32_16x16x32_bf16 v[58:61], v[178:181], v[194:197], v[58:61]
	v_mfma_f32_16x16x32_bf16 v[50:53], v[186:189], v[194:197], v[50:53]
	v_mfma_f32_16x16x32_bf16 v[42:45], v[178:181], v[202:205], v[42:45]
	v_mfma_f32_16x16x32_bf16 v[34:37], v[186:189], v[202:205], v[34:37]
	v_mfma_f32_16x16x32_bf16 v[26:29], v[178:181], v[210:213], v[26:29]
	v_mfma_f32_16x16x32_bf16 v[18:21], v[186:189], v[210:213], v[18:21]
	v_mfma_f32_16x16x32_bf16 v[10:13], v[178:181], v[218:221], v[10:13]
	v_mfma_f32_16x16x32_bf16 v[2:5], v[186:189], v[218:221], v[2:5]
	s_setprio 0
	s_barrier
	s_add_i32 s70, 0, 0x18000
	v_add_u32_e32 v148, s70, v151
	s_add_i32 s71, 0, 0x1c000
	ds_read_b128 v[142:145], v148
	ds_read_b128 v[156:159], v148 offset:1024
	ds_read_b128 v[160:163], v148 offset:2048
	ds_read_b128 v[170:173], v148 offset:3072
	v_add_u32_e32 v148, s71, v151
	ds_read_b128 v[174:177], v148
	ds_read_b128 v[178:181], v148 offset:1024
	ds_read_b128 v[182:185], v148 offset:2048
	ds_read_b128 v[186:189], v148 offset:3072
	s_add_u32 s60, s60, 0x40000
	s_addc_u32 s61, s61, 0
	s_mov_b32 m0, s21
	v_lshl_add_u64 v[234:235], s[60:61], 0, v[132:133]
	ds_read_b128 v[190:193], v154 offset:32768
	ds_read_b128 v[194:197], v154 offset:33792
	ds_read_b128 v[198:201], v154 offset:34816
	ds_read_b128 v[202:205], v154 offset:35840
	ds_read_b128 v[206:209], v154 offset:36864
	ds_read_b128 v[210:213], v154 offset:37888
	ds_read_b128 v[214:217], v154 offset:38912
	ds_read_b128 v[218:221], v154 offset:39936
	global_load_lds_dwordx4 v[234:235], off
	v_lshl_add_u64 v[234:235], s[60:61], 0, v[130:131]
	s_mov_b32 m0, s22
	s_nop 0
	global_load_lds_dwordx4 v[234:235], off
	s_waitcnt vmcnt(8)
	s_waitcnt lgkmcnt(0)
	s_barrier
	s_setprio 1
	s_waitcnt lgkmcnt(0)
	v_mfma_f32_16x16x32_bf16 v[126:129], v[142:145], v[190:193], v[126:129]
	v_mfma_f32_16x16x32_bf16 v[118:121], v[160:163], v[190:193], v[118:121]
	v_mfma_f32_16x16x32_bf16 v[110:113], v[142:145], v[198:201], v[110:113]
	v_mfma_f32_16x16x32_bf16 v[102:105], v[160:163], v[198:201], v[102:105]
	v_mfma_f32_16x16x32_bf16 v[94:97], v[142:145], v[206:209], v[94:97]
	v_mfma_f32_16x16x32_bf16 v[86:89], v[160:163], v[206:209], v[86:89]
	v_mfma_f32_16x16x32_bf16 v[78:81], v[142:145], v[214:217], v[78:81]
	v_mfma_f32_16x16x32_bf16 v[70:73], v[160:163], v[214:217], v[70:73]
	v_mfma_f32_16x16x32_bf16 v[126:129], v[156:159], v[194:197], v[126:129]
	v_mfma_f32_16x16x32_bf16 v[118:121], v[170:173], v[194:197], v[118:121]
	v_mfma_f32_16x16x32_bf16 v[110:113], v[156:159], v[202:205], v[110:113]
	v_mfma_f32_16x16x32_bf16 v[102:105], v[170:173], v[202:205], v[102:105]
	v_mfma_f32_16x16x32_bf16 v[94:97], v[156:159], v[210:213], v[94:97]
	v_mfma_f32_16x16x32_bf16 v[86:89], v[170:173], v[210:213], v[86:89]
	v_mfma_f32_16x16x32_bf16 v[78:81], v[156:159], v[218:221], v[78:81]
	v_mfma_f32_16x16x32_bf16 v[70:73], v[170:173], v[218:221], v[70:73]
	s_setprio 0
	s_setprio 1
	v_mfma_f32_16x16x32_bf16 v[122:125], v[174:177], v[190:193], v[122:125]
	v_mfma_f32_16x16x32_bf16 v[114:117], v[182:185], v[190:193], v[114:117]
	v_mfma_f32_16x16x32_bf16 v[106:109], v[174:177], v[198:201], v[106:109]
	v_mfma_f32_16x16x32_bf16 v[98:101], v[182:185], v[198:201], v[98:101]
	v_mfma_f32_16x16x32_bf16 v[90:93], v[174:177], v[206:209], v[90:93]
	v_mfma_f32_16x16x32_bf16 v[82:85], v[182:185], v[206:209], v[82:85]
	v_mfma_f32_16x16x32_bf16 v[74:77], v[174:177], v[214:217], v[74:77]
	v_mfma_f32_16x16x32_bf16 v[66:69], v[182:185], v[214:217], v[66:69]
	v_mfma_f32_16x16x32_bf16 v[122:125], v[178:181], v[194:197], v[122:125]
	v_mfma_f32_16x16x32_bf16 v[114:117], v[186:189], v[194:197], v[114:117]
	v_mfma_f32_16x16x32_bf16 v[106:109], v[178:181], v[202:205], v[106:109]
	v_mfma_f32_16x16x32_bf16 v[98:101], v[186:189], v[202:205], v[98:101]
	v_mfma_f32_16x16x32_bf16 v[90:93], v[178:181], v[210:213], v[90:93]
	v_mfma_f32_16x16x32_bf16 v[82:85], v[186:189], v[210:213], v[82:85]
	v_mfma_f32_16x16x32_bf16 v[74:77], v[178:181], v[218:221], v[74:77]
	v_mfma_f32_16x16x32_bf16 v[66:69], v[186:189], v[218:221], v[66:69]
	s_setprio 0
	s_barrier
	s_add_i32 s60, s70, s14
	v_lshl_add_u64 v[146:147], v[146:147], 0, s[56:57]
	s_mov_b32 m0, s60
	ds_read_b128 v[190:193], v154 offset:49152
	ds_read_b128 v[194:197], v154 offset:50176
	ds_read_b128 v[198:201], v154 offset:51200
	ds_read_b128 v[202:205], v154 offset:52224
	ds_read_b128 v[206:209], v154 offset:53248
	ds_read_b128 v[210:213], v154 offset:54272
	ds_read_b128 v[214:217], v154 offset:55296
	ds_read_b128 v[218:221], v154 offset:56320
	global_load_lds_dwordx4 v[146:147], off
	s_add_i32 m0, s60, 0x2000
	s_add_u32 s58, s58, 0x40080
	v_lshl_add_u64 v[146:147], v[164:165], 0, s[56:57]
	s_addc_u32 s59, s59, 0
	s_add_i32 s60, s71, s14
	global_load_lds_dwordx4 v[146:147], off
	v_lshl_add_u64 v[146:147], s[58:59], 0, v[166:167]
	s_mov_b32 m0, s60
	s_nop 0
	global_load_lds_dwordx4 v[146:147], off
	v_lshl_add_u64 v[146:147], s[58:59], 0, v[134:135]
	s_add_i32 m0, s60, 0x2000
	s_nop 0
	global_load_lds_dwordx4 v[146:147], off
	v_lshl_add_u64 v[146:147], v[222:223], 0, s[56:57]
	s_mov_b32 m0, s23
	s_nop 0
	global_load_lds_dwordx4 v[146:147], off
	v_lshl_add_u64 v[146:147], v[232:233], 0, s[56:57]
	s_mov_b32 m0, s24
	s_nop 0
	global_load_lds_dwordx4 v[146:147], off
	s_waitcnt vmcnt(8)
	s_waitcnt lgkmcnt(0)
	s_barrier
	s_setprio 1
	s_waitcnt lgkmcnt(0)
	v_mfma_f32_16x16x32_bf16 v[62:65], v[142:145], v[190:193], v[62:65]
	v_mfma_f32_16x16x32_bf16 v[54:57], v[160:163], v[190:193], v[54:57]
	v_mfma_f32_16x16x32_bf16 v[46:49], v[142:145], v[198:201], v[46:49]
	v_mfma_f32_16x16x32_bf16 v[38:41], v[160:163], v[198:201], v[38:41]
	v_mfma_f32_16x16x32_bf16 v[30:33], v[142:145], v[206:209], v[30:33]
	v_mfma_f32_16x16x32_bf16 v[22:25], v[160:163], v[206:209], v[22:25]
	v_mfma_f32_16x16x32_bf16 v[14:17], v[142:145], v[214:217], v[14:17]
	v_mfma_f32_16x16x32_bf16 v[6:9], v[160:163], v[214:217], v[6:9]
	v_mfma_f32_16x16x32_bf16 v[62:65], v[156:159], v[194:197], v[62:65]
	v_mfma_f32_16x16x32_bf16 v[54:57], v[170:173], v[194:197], v[54:57]
	v_mfma_f32_16x16x32_bf16 v[46:49], v[156:159], v[202:205], v[46:49]
	v_mfma_f32_16x16x32_bf16 v[38:41], v[170:173], v[202:205], v[38:41]
	v_mfma_f32_16x16x32_bf16 v[30:33], v[156:159], v[210:213], v[30:33]
	v_mfma_f32_16x16x32_bf16 v[22:25], v[170:173], v[210:213], v[22:25]
	v_mfma_f32_16x16x32_bf16 v[14:17], v[156:159], v[218:221], v[14:17]
	v_mfma_f32_16x16x32_bf16 v[6:9], v[170:173], v[218:221], v[6:9]
	s_setprio 0
	s_setprio 1
	v_mfma_f32_16x16x32_bf16 v[58:61], v[174:177], v[190:193], v[58:61]
	v_mfma_f32_16x16x32_bf16 v[50:53], v[182:185], v[190:193], v[50:53]
	v_mfma_f32_16x16x32_bf16 v[42:45], v[174:177], v[198:201], v[42:45]
	v_mfma_f32_16x16x32_bf16 v[34:37], v[182:185], v[198:201], v[34:37]
	v_mfma_f32_16x16x32_bf16 v[26:29], v[174:177], v[206:209], v[26:29]
	v_mfma_f32_16x16x32_bf16 v[18:21], v[182:185], v[206:209], v[18:21]
	v_mfma_f32_16x16x32_bf16 v[10:13], v[174:177], v[214:217], v[10:13]
	v_mfma_f32_16x16x32_bf16 v[2:5], v[182:185], v[214:217], v[2:5]
	v_mfma_f32_16x16x32_bf16 v[58:61], v[178:181], v[194:197], v[58:61]
	v_mfma_f32_16x16x32_bf16 v[50:53], v[186:189], v[194:197], v[50:53]
	v_mfma_f32_16x16x32_bf16 v[42:45], v[178:181], v[202:205], v[42:45]
	v_mfma_f32_16x16x32_bf16 v[34:37], v[186:189], v[202:205], v[34:37]
	v_mfma_f32_16x16x32_bf16 v[26:29], v[178:181], v[210:213], v[26:29]
	v_mfma_f32_16x16x32_bf16 v[18:21], v[186:189], v[210:213], v[18:21]
	v_mfma_f32_16x16x32_bf16 v[10:13], v[178:181], v[218:221], v[10:13]
	v_mfma_f32_16x16x32_bf16 v[2:5], v[186:189], v[218:221], v[2:5]
	s_setprio 0
	s_add_u32 s66, s66, 0x100
	s_addc_u32 s68, s68, 0
	s_add_u32 s54, s54, 0x100
	s_addc_u32 s55, s55, 0
	s_cmp_ge_i32 s69, s13
	s_mov_b32 s58, s69
	s_cbranch_scc1 .Lrotph7b_pexitbar
	s_add_i32 s69, s58, 2
	s_add_u32 s59, s54, 0xfffc0080
	s_addc_u32 s60, s55, -1
	s_add_i32 s70, 0, 0x10000
	s_cmp_eq_u32 s53, s58
	s_cselect_b32 s61, s43, s60
	s_cselect_b32 s60, s45, s59
	s_barrier
	s_branch .Lrotph7b_body

.Lrotph7b_body:
	v_add_u32_e32 v146, s70, v151
	s_cselect_b32 s59, s64, s68
	s_cselect_b32 s58, s65, s66
	s_add_i32 s72, 0, 0x14000
	ds_read_b128 v[142:145], v146
	ds_read_b128 v[156:159], v146 offset:1024
	ds_read_b128 v[160:163], v146 offset:2048
	ds_read_b128 v[170:173], v146 offset:3072
	v_add_u32_e32 v146, s72, v151
	ds_read_b128 v[174:177], v146
	ds_read_b128 v[178:181], v146 offset:1024
	ds_read_b128 v[182:185], v146 offset:2048
	ds_read_b128 v[186:189], v146 offset:3072
	v_lshl_add_u64 v[146:147], s[54:55], 0, v[140:141]
	s_add_i32 m0, s16, 0xc000
	ds_read_b128 v[190:193], v154
	ds_read_b128 v[194:197], v154 offset:1024
	ds_read_b128 v[198:201], v154 offset:2048
	ds_read_b128 v[202:205], v154 offset:3072
	ds_read_b128 v[206:209], v154 offset:4096
	ds_read_b128 v[210:213], v154 offset:5120
	ds_read_b128 v[214:217], v154 offset:6144
	ds_read_b128 v[218:221], v154 offset:7168
	global_load_lds_dwordx4 v[146:147], off
	v_lshl_add_u64 v[146:147], s[54:55], 0, v[138:139]
	s_add_i32 m0, s16, 0xe000
	s_nop 0
	global_load_lds_dwordx4 v[146:147], off
	s_waitcnt vmcnt(8)
	s_waitcnt lgkmcnt(0)
	s_barrier
	s_setprio 1
	s_waitcnt lgkmcnt(0)
	v_mfma_f32_16x16x32_bf16 v[126:129], v[142:145], v[190:193], v[126:129]
	v_mfma_f32_16x16x32_bf16 v[118:121], v[160:163], v[190:193], v[118:121]
	v_mfma_f32_16x16x32_bf16 v[110:113], v[142:145], v[198:201], v[110:113]
	v_mfma_f32_16x16x32_bf16 v[102:105], v[160:163], v[198:201], v[102:105]
	v_mfma_f32_16x16x32_bf16 v[94:97], v[142:145], v[206:209], v[94:97]
	v_mfma_f32_16x16x32_bf16 v[86:89], v[160:163], v[206:209], v[86:89]
	v_mfma_f32_16x16x32_bf16 v[78:81], v[142:145], v[214:217], v[78:81]
	v_mfma_f32_16x16x32_bf16 v[70:73], v[160:163], v[214:217], v[70:73]
	v_mfma_f32_16x16x32_bf16 v[126:129], v[156:159], v[194:197], v[126:129]
	v_mfma_f32_16x16x32_bf16 v[118:121], v[170:173], v[194:197], v[118:121]
	v_mfma_f32_16x16x32_bf16 v[110:113], v[156:159], v[202:205], v[110:113]
	v_mfma_f32_16x16x32_bf16 v[102:105], v[170:173], v[202:205], v[102:105]
	v_mfma_f32_16x16x32_bf16 v[94:97], v[156:159], v[210:213], v[94:97]
	v_mfma_f32_16x16x32_bf16 v[86:89], v[170:173], v[210:213], v[86:89]
	v_mfma_f32_16x16x32_bf16 v[78:81], v[156:159], v[218:221], v[78:81]
	v_mfma_f32_16x16x32_bf16 v[70:73], v[170:173], v[218:221], v[70:73]
	s_setprio 0
	s_setprio 1
	v_mfma_f32_16x16x32_bf16 v[122:125], v[174:177], v[190:193], v[122:125]
	v_mfma_f32_16x16x32_bf16 v[114:117], v[182:185], v[190:193], v[114:117]
	v_mfma_f32_16x16x32_bf16 v[106:109], v[174:177], v[198:201], v[106:109]
	v_mfma_f32_16x16x32_bf16 v[98:101], v[182:185], v[198:201], v[98:101]
	v_mfma_f32_16x16x32_bf16 v[90:93], v[174:177], v[206:209], v[90:93]
	v_mfma_f32_16x16x32_bf16 v[82:85], v[182:185], v[206:209], v[82:85]
	v_mfma_f32_16x16x32_bf16 v[74:77], v[174:177], v[214:217], v[74:77]
	v_mfma_f32_16x16x32_bf16 v[66:69], v[182:185], v[214:217], v[66:69]
	v_mfma_f32_16x16x32_bf16 v[122:125], v[178:181], v[194:197], v[122:125]
	v_mfma_f32_16x16x32_bf16 v[114:117], v[186:189], v[194:197], v[114:117]
	v_mfma_f32_16x16x32_bf16 v[106:109], v[178:181], v[202:205], v[106:109]
	v_mfma_f32_16x16x32_bf16 v[98:101], v[186:189], v[202:205], v[98:101]
	v_mfma_f32_16x16x32_bf16 v[90:93], v[178:181], v[210:213], v[90:93]
	v_mfma_f32_16x16x32_bf16 v[82:85], v[186:189], v[210:213], v[82:85]
	v_mfma_f32_16x16x32_bf16 v[74:77], v[178:181], v[218:221], v[74:77]
	v_mfma_f32_16x16x32_bf16 v[66:69], v[186:189], v[218:221], v[66:69]
	s_setprio 0
	s_barrier
	s_add_i32 s70, s70, s14
	v_lshl_add_u64 v[146:147], s[58:59], 0, v[166:167]
	s_mov_b32 m0, s70
	ds_read_b128 v[190:193], v154 offset:16384
	ds_read_b128 v[194:197], v154 offset:17408
	ds_read_b128 v[198:201], v154 offset:18432
	ds_read_b128 v[202:205], v154 offset:19456
	ds_read_b128 v[206:209], v154 offset:20480
	ds_read_b128 v[210:213], v154 offset:21504
	ds_read_b128 v[214:217], v154 offset:22528
	ds_read_b128 v[218:221], v154 offset:23552
	global_load_lds_dwordx4 v[146:147], off
	s_add_i32 m0, s70, 0x2000
	s_add_u32 s70, s58, 0x40000
	v_lshl_add_u64 v[164:165], s[58:59], 0, v[134:135]
	s_addc_u32 s71, s59, 0
	s_add_i32 s72, s72, s14
	global_load_lds_dwordx4 v[164:165], off
	v_lshl_add_u64 v[222:223], s[70:71], 0, v[166:167]
	s_mov_b32 m0, s72
	v_lshl_add_u64 v[232:233], s[60:61], 0, v[130:131]
	global_load_lds_dwordx4 v[222:223], off
	v_lshl_add_u64 v[222:223], s[70:71], 0, v[134:135]
	s_add_i32 m0, s72, 0x2000
	s_nop 0
	global_load_lds_dwordx4 v[222:223], off
	v_lshl_add_u64 v[222:223], s[60:61], 0, v[132:133]
	s_mov_b32 m0, s16
	s_nop 0
	global_load_lds_dwordx4 v[222:223], off
	s_mov_b32 m0, s20
	s_nop 0
	global_load_lds_dwordx4 v[232:233], off
	s_waitcnt vmcnt(8)
	s_waitcnt lgkmcnt(0)
	s_barrier
	s_setprio 1
	s_waitcnt lgkmcnt(0)
	v_mfma_f32_16x16x32_bf16 v[62:65], v[142:145], v[190:193], v[62:65]
	v_mfma_f32_16x16x32_bf16 v[54:57], v[160:163], v[190:193], v[54:57]
	v_mfma_f32_16x16x32_bf16 v[46:49], v[142:145], v[198:201], v[46:49]
	v_mfma_f32_16x16x32_bf16 v[38:41], v[160:163], v[198:201], v[38:41]
	v_mfma_f32_16x16x32_bf16 v[30:33], v[142:145], v[206:209], v[30:33]
	v_mfma_f32_16x16x32_bf16 v[22:25], v[160:163], v[206:209], v[22:25]
	v_mfma_f32_16x16x32_bf16 v[14:17], v[142:145], v[214:217], v[14:17]
	v_mfma_f32_16x16x32_bf16 v[6:9], v[160:163], v[214:217], v[6:9]
	v_mfma_f32_16x16x32_bf16 v[62:65], v[156:159], v[194:197], v[62:65]
	v_mfma_f32_16x16x32_bf16 v[54:57], v[170:173], v[194:197], v[54:57]
	v_mfma_f32_16x16x32_bf16 v[46:49], v[156:159], v[202:205], v[46:49]
	v_mfma_f32_16x16x32_bf16 v[38:41], v[170:173], v[202:205], v[38:41]
	v_mfma_f32_16x16x32_bf16 v[30:33], v[156:159], v[210:213], v[30:33]
	v_mfma_f32_16x16x32_bf16 v[22:25], v[170:173], v[210:213], v[22:25]
	v_mfma_f32_16x16x32_bf16 v[14:17], v[156:159], v[218:221], v[14:17]
	v_mfma_f32_16x16x32_bf16 v[6:9], v[170:173], v[218:221], v[6:9]
	s_setprio 0
	s_setprio 1
	v_mfma_f32_16x16x32_bf16 v[58:61], v[174:177], v[190:193], v[58:61]
	v_mfma_f32_16x16x32_bf16 v[50:53], v[182:185], v[190:193], v[50:53]
	v_mfma_f32_16x16x32_bf16 v[42:45], v[174:177], v[198:201], v[42:45]
	v_mfma_f32_16x16x32_bf16 v[34:37], v[182:185], v[198:201], v[34:37]
	v_mfma_f32_16x16x32_bf16 v[26:29], v[174:177], v[206:209], v[26:29]
	v_mfma_f32_16x16x32_bf16 v[18:21], v[182:185], v[206:209], v[18:21]
	v_mfma_f32_16x16x32_bf16 v[10:13], v[174:177], v[214:217], v[10:13]
	v_mfma_f32_16x16x32_bf16 v[2:5], v[182:185], v[214:217], v[2:5]
	v_mfma_f32_16x16x32_bf16 v[58:61], v[178:181], v[194:197], v[58:61]
	v_mfma_f32_16x16x32_bf16 v[50:53], v[186:189], v[194:197], v[50:53]
	v_mfma_f32_16x16x32_bf16 v[42:45], v[178:181], v[202:205], v[42:45]
	v_mfma_f32_16x16x32_bf16 v[34:37], v[186:189], v[202:205], v[34:37]
	v_mfma_f32_16x16x32_bf16 v[26:29], v[178:181], v[210:213], v[26:29]
	v_mfma_f32_16x16x32_bf16 v[18:21], v[186:189], v[210:213], v[18:21]
	v_mfma_f32_16x16x32_bf16 v[10:13], v[178:181], v[218:221], v[10:13]
	v_mfma_f32_16x16x32_bf16 v[2:5], v[186:189], v[218:221], v[2:5]
	s_setprio 0
	s_barrier
	s_add_i32 s70, 0, 0x18000
	v_add_u32_e32 v148, s70, v151
	s_add_i32 s71, 0, 0x1c000
	ds_read_b128 v[142:145], v148
	ds_read_b128 v[156:159], v148 offset:1024
	ds_read_b128 v[160:163], v148 offset:2048
	ds_read_b128 v[170:173], v148 offset:3072
	v_add_u32_e32 v148, s71, v151
	ds_read_b128 v[174:177], v148
	ds_read_b128 v[178:181], v148 offset:1024
	ds_read_b128 v[182:185], v148 offset:2048
	ds_read_b128 v[186:189], v148 offset:3072
	s_add_u32 s60, s60, 0x40000
	s_addc_u32 s61, s61, 0
	s_mov_b32 m0, s21
	v_lshl_add_u64 v[234:235], s[60:61], 0, v[132:133]
	ds_read_b128 v[190:193], v154 offset:32768
	ds_read_b128 v[194:197], v154 offset:33792
	ds_read_b128 v[198:201], v154 offset:34816
	ds_read_b128 v[202:205], v154 offset:35840
	ds_read_b128 v[206:209], v154 offset:36864
	ds_read_b128 v[210:213], v154 offset:37888
	ds_read_b128 v[214:217], v154 offset:38912
	ds_read_b128 v[218:221], v154 offset:39936
	global_load_lds_dwordx4 v[234:235], off
	v_lshl_add_u64 v[234:235], s[60:61], 0, v[130:131]
	s_mov_b32 m0, s22
	s_nop 0
	global_load_lds_dwordx4 v[234:235], off
	s_waitcnt vmcnt(8)
	s_waitcnt lgkmcnt(0)
	s_barrier
	s_setprio 1
	s_waitcnt lgkmcnt(0)
	v_mfma_f32_16x16x32_bf16 v[126:129], v[142:145], v[190:193], v[126:129]
	v_mfma_f32_16x16x32_bf16 v[118:121], v[160:163], v[190:193], v[118:121]
	v_mfma_f32_16x16x32_bf16 v[110:113], v[142:145], v[198:201], v[110:113]
	v_mfma_f32_16x16x32_bf16 v[102:105], v[160:163], v[198:201], v[102:105]
	v_mfma_f32_16x16x32_bf16 v[94:97], v[142:145], v[206:209], v[94:97]
	v_mfma_f32_16x16x32_bf16 v[86:89], v[160:163], v[206:209], v[86:89]
	v_mfma_f32_16x16x32_bf16 v[78:81], v[142:145], v[214:217], v[78:81]
	v_mfma_f32_16x16x32_bf16 v[70:73], v[160:163], v[214:217], v[70:73]
	v_mfma_f32_16x16x32_bf16 v[126:129], v[156:159], v[194:197], v[126:129]
	v_mfma_f32_16x16x32_bf16 v[118:121], v[170:173], v[194:197], v[118:121]
	v_mfma_f32_16x16x32_bf16 v[110:113], v[156:159], v[202:205], v[110:113]
	v_mfma_f32_16x16x32_bf16 v[102:105], v[170:173], v[202:205], v[102:105]
	v_mfma_f32_16x16x32_bf16 v[94:97], v[156:159], v[210:213], v[94:97]
	v_mfma_f32_16x16x32_bf16 v[86:89], v[170:173], v[210:213], v[86:89]
	v_mfma_f32_16x16x32_bf16 v[78:81], v[156:159], v[218:221], v[78:81]
	v_mfma_f32_16x16x32_bf16 v[70:73], v[170:173], v[218:221], v[70:73]
	s_setprio 0
	s_setprio 1
	v_mfma_f32_16x16x32_bf16 v[122:125], v[174:177], v[190:193], v[122:125]
	v_mfma_f32_16x16x32_bf16 v[114:117], v[182:185], v[190:193], v[114:117]
	v_mfma_f32_16x16x32_bf16 v[106:109], v[174:177], v[198:201], v[106:109]
	v_mfma_f32_16x16x32_bf16 v[98:101], v[182:185], v[198:201], v[98:101]
	v_mfma_f32_16x16x32_bf16 v[90:93], v[174:177], v[206:209], v[90:93]
	v_mfma_f32_16x16x32_bf16 v[82:85], v[182:185], v[206:209], v[82:85]
	v_mfma_f32_16x16x32_bf16 v[74:77], v[174:177], v[214:217], v[74:77]
	v_mfma_f32_16x16x32_bf16 v[66:69], v[182:185], v[214:217], v[66:69]
	v_mfma_f32_16x16x32_bf16 v[122:125], v[178:181], v[194:197], v[122:125]
	v_mfma_f32_16x16x32_bf16 v[114:117], v[186:189], v[194:197], v[114:117]
	v_mfma_f32_16x16x32_bf16 v[106:109], v[178:181], v[202:205], v[106:109]
	v_mfma_f32_16x16x32_bf16 v[98:101], v[186:189], v[202:205], v[98:101]
	v_mfma_f32_16x16x32_bf16 v[90:93], v[178:181], v[210:213], v[90:93]
	v_mfma_f32_16x16x32_bf16 v[82:85], v[186:189], v[210:213], v[82:85]
	v_mfma_f32_16x16x32_bf16 v[74:77], v[178:181], v[218:221], v[74:77]
	v_mfma_f32_16x16x32_bf16 v[66:69], v[186:189], v[218:221], v[66:69]
	s_setprio 0
	s_barrier
	s_add_i32 s60, s70, s14
	v_lshl_add_u64 v[146:147], v[146:147], 0, s[56:57]
	s_mov_b32 m0, s60
	ds_read_b128 v[190:193], v154 offset:49152
	ds_read_b128 v[194:197], v154 offset:50176
	ds_read_b128 v[198:201], v154 offset:51200
	ds_read_b128 v[202:205], v154 offset:52224
	ds_read_b128 v[206:209], v154 offset:53248
	ds_read_b128 v[210:213], v154 offset:54272
	ds_read_b128 v[214:217], v154 offset:55296
	ds_read_b128 v[218:221], v154 offset:56320
	global_load_lds_dwordx4 v[146:147], off
	s_add_i32 m0, s60, 0x2000
	s_add_u32 s58, s58, 0x40080
	v_lshl_add_u64 v[146:147], v[164:165], 0, s[56:57]
	s_addc_u32 s59, s59, 0
	s_add_i32 s60, s71, s14
	global_load_lds_dwordx4 v[146:147], off
	v_lshl_add_u64 v[146:147], s[58:59], 0, v[166:167]
	s_mov_b32 m0, s60
	s_nop 0
	global_load_lds_dwordx4 v[146:147], off
	v_lshl_add_u64 v[146:147], s[58:59], 0, v[134:135]
	s_add_i32 m0, s60, 0x2000
	s_nop 0
	global_load_lds_dwordx4 v[146:147], off
	v_lshl_add_u64 v[146:147], v[222:223], 0, s[56:57]
	s_mov_b32 m0, s23
	s_nop 0
	global_load_lds_dwordx4 v[146:147], off
	v_lshl_add_u64 v[146:147], v[232:233], 0, s[56:57]
	s_mov_b32 m0, s24
	s_nop 0
	global_load_lds_dwordx4 v[146:147], off
	s_waitcnt vmcnt(8)
	s_waitcnt lgkmcnt(0)
	s_barrier
	s_setprio 1
	s_waitcnt lgkmcnt(0)
	v_mfma_f32_16x16x32_bf16 v[62:65], v[142:145], v[190:193], v[62:65]
	v_mfma_f32_16x16x32_bf16 v[54:57], v[160:163], v[190:193], v[54:57]
	v_mfma_f32_16x16x32_bf16 v[46:49], v[142:145], v[198:201], v[46:49]
	v_mfma_f32_16x16x32_bf16 v[38:41], v[160:163], v[198:201], v[38:41]
	v_mfma_f32_16x16x32_bf16 v[30:33], v[142:145], v[206:209], v[30:33]
	v_mfma_f32_16x16x32_bf16 v[22:25], v[160:163], v[206:209], v[22:25]
	v_mfma_f32_16x16x32_bf16 v[14:17], v[142:145], v[214:217], v[14:17]
	v_mfma_f32_16x16x32_bf16 v[6:9], v[160:163], v[214:217], v[6:9]
	v_mfma_f32_16x16x32_bf16 v[62:65], v[156:159], v[194:197], v[62:65]
	v_mfma_f32_16x16x32_bf16 v[54:57], v[170:173], v[194:197], v[54:57]
	v_mfma_f32_16x16x32_bf16 v[46:49], v[156:159], v[202:205], v[46:49]
	v_mfma_f32_16x16x32_bf16 v[38:41], v[170:173], v[202:205], v[38:41]
	v_mfma_f32_16x16x32_bf16 v[30:33], v[156:159], v[210:213], v[30:33]
	v_mfma_f32_16x16x32_bf16 v[22:25], v[170:173], v[210:213], v[22:25]
	v_mfma_f32_16x16x32_bf16 v[14:17], v[156:159], v[218:221], v[14:17]
	v_mfma_f32_16x16x32_bf16 v[6:9], v[170:173], v[218:221], v[6:9]
	s_setprio 0
	s_setprio 1
	v_mfma_f32_16x16x32_bf16 v[58:61], v[174:177], v[190:193], v[58:61]
	v_mfma_f32_16x16x32_bf16 v[50:53], v[182:185], v[190:193], v[50:53]
	v_mfma_f32_16x16x32_bf16 v[42:45], v[174:177], v[198:201], v[42:45]
	v_mfma_f32_16x16x32_bf16 v[34:37], v[182:185], v[198:201], v[34:37]
	v_mfma_f32_16x16x32_bf16 v[26:29], v[174:177], v[206:209], v[26:29]
	v_mfma_f32_16x16x32_bf16 v[18:21], v[182:185], v[206:209], v[18:21]
	v_mfma_f32_16x16x32_bf16 v[10:13], v[174:177], v[214:217], v[10:13]
	v_mfma_f32_16x16x32_bf16 v[2:5], v[182:185], v[214:217], v[2:5]
	v_mfma_f32_16x16x32_bf16 v[58:61], v[178:181], v[194:197], v[58:61]
	v_mfma_f32_16x16x32_bf16 v[50:53], v[186:189], v[194:197], v[50:53]
	v_mfma_f32_16x16x32_bf16 v[42:45], v[178:181], v[202:205], v[42:45]
	v_mfma_f32_16x16x32_bf16 v[34:37], v[186:189], v[202:205], v[34:37]
	v_mfma_f32_16x16x32_bf16 v[26:29], v[178:181], v[210:213], v[26:29]
	v_mfma_f32_16x16x32_bf16 v[18:21], v[186:189], v[210:213], v[18:21]
	v_mfma_f32_16x16x32_bf16 v[10:13], v[178:181], v[218:221], v[10:13]
	v_mfma_f32_16x16x32_bf16 v[2:5], v[186:189], v[218:221], v[2:5]
	s_setprio 0
	s_add_u32 s66, s66, 0x100
	s_addc_u32 s68, s68, 0
	s_add_u32 s54, s54, 0x100
	s_addc_u32 s55, s55, 0
	s_cmp_ge_i32 s69, s13
	s_mov_b32 s58, s69
	s_cbranch_scc1 .Lrotph7b_exitbar
	s_add_i32 s69, s58, 2
	s_add_u32 s59, s54, 0xfffc0080
	s_addc_u32 s60, s55, -1
	s_add_i32 s70, 0, 0x10000
	s_cmp_eq_u32 s53, s58
	s_cselect_b32 s61, s43, s60
	s_cselect_b32 s60, s45, s59
	s_barrier
	s_branch .Lrotph7b_body
.Lrotph7b_exitbar:
	s_barrier
.Lpeelexitph7b:
	s_mov_b64 s[72:73], 0xe800000
	s_mov_b64 s[70:71], 0xe800800
	v_mov_b32_e32 v209, v1
	s_and_b64 vcc, exec, s[36:37]
	s_cbranch_vccz .LBB0_820

.Lpeelph7f_0:
	s_add_i32 s66, s54, 2
	s_add_u32 s55, s52, 0xfffe0080
	s_addc_u32 s58, s53, -1
	s_add_i32 s68, 0, 0x10000
	s_cmp_eq_u32 s51, s54
	s_cselect_b32 s59, s41, s58
	s_cselect_b32 s58, s43, s55
	s_cselect_b32 s55, s62, s65
	s_cselect_b32 s54, s63, s64
	s_add_i32 s69, 0, 0x14000
	v_add_u32_e32 v2, s68, v196
	v_add_u32_e32 v6, s69, v196
	ds_read_b128 v[26:29], v2
	ds_read_b128 v[30:33], v2 offset:1024
	ds_read_b128 v[18:21], v2 offset:2048
	ds_read_b128 v[22:25], v2 offset:3072
	ds_read_b128 v[10:13], v6
	ds_read_b128 v[14:17], v6 offset:1024
	ds_read_b128 v[2:5], v6 offset:2048
	ds_read_b128 v[6:9], v6 offset:3072
	v_lshl_add_u64 v[170:171], s[52:53], 0, v[184:185]
	s_add_i32 m0, s16, 0xc000
	ds_read_b128 v[186:189], v198
	ds_read_b128 v[190:193], v198 offset:1024
	ds_read_b128 v[200:203], v198 offset:2048
	ds_read_b128 v[204:207], v198 offset:3072
	ds_read_b128 v[208:211], v198 offset:4096
	ds_read_b128 v[212:215], v198 offset:5120
	ds_read_b128 v[216:219], v198 offset:6144
	ds_read_b128 v[220:223], v198 offset:7168
	global_load_lds_dwordx4 v[170:171], off
	v_lshl_add_u64 v[170:171], s[52:53], 0, v[182:183]
	s_add_i32 m0, s16, 0xe000
	s_nop 0
	global_load_lds_dwordx4 v[170:171], off
	s_waitcnt vmcnt(8)
	s_waitcnt lgkmcnt(0)
	s_barrier
	s_setprio 1
	s_waitcnt lgkmcnt(0)
	v_mfma_scale_f32_16x16x128_f8f6f4 v[158:161], v[26:33], v[186:193], 0, v194, v169 op_sel_hi:[0,0,0]
	v_mfma_scale_f32_16x16x128_f8f6f4 v[150:153], v[18:25], v[186:193], 0, v194, v169 op_sel_hi:[0,0,0]
	v_mfma_scale_f32_16x16x128_f8f6f4 v[142:145], v[26:33], v[200:207], 0, v194, v169 op_sel_hi:[0,0,0]
	v_mfma_scale_f32_16x16x128_f8f6f4 v[134:137], v[18:25], v[200:207], 0, v194, v169 op_sel_hi:[0,0,0]
	v_mfma_scale_f32_16x16x128_f8f6f4 v[126:129], v[26:33], v[208:215], 0, v194, v169 op_sel_hi:[0,0,0]
	v_mfma_scale_f32_16x16x128_f8f6f4 v[118:121], v[18:25], v[208:215], 0, v194, v169 op_sel_hi:[0,0,0]
	v_mfma_scale_f32_16x16x128_f8f6f4 v[110:113], v[26:33], v[216:223], 0, v194, v169 op_sel_hi:[0,0,0]
	v_mfma_scale_f32_16x16x128_f8f6f4 v[102:105], v[18:25], v[216:223], 0, v194, v169 op_sel_hi:[0,0,0]
	s_setprio 0
	s_setprio 1
	v_mfma_scale_f32_16x16x128_f8f6f4 v[154:157], v[10:17], v[186:193], 0, v194, v169 op_sel_hi:[0,0,0]
	v_mfma_scale_f32_16x16x128_f8f6f4 v[146:149], v[2:9], v[186:193], 0, v194, v169 op_sel_hi:[0,0,0]
	v_mfma_scale_f32_16x16x128_f8f6f4 v[138:141], v[10:17], v[200:207], 0, v194, v169 op_sel_hi:[0,0,0]
	v_mfma_scale_f32_16x16x128_f8f6f4 v[130:133], v[2:9], v[200:207], 0, v194, v169 op_sel_hi:[0,0,0]
	v_mfma_scale_f32_16x16x128_f8f6f4 v[122:125], v[10:17], v[208:215], 0, v194, v169 op_sel_hi:[0,0,0]
	v_mfma_scale_f32_16x16x128_f8f6f4 v[114:117], v[2:9], v[208:215], 0, v194, v169 op_sel_hi:[0,0,0]
	v_mfma_scale_f32_16x16x128_f8f6f4 v[106:109], v[10:17], v[216:223], 0, v194, v169 op_sel_hi:[0,0,0]
	v_mfma_scale_f32_16x16x128_f8f6f4 v[98:101], v[2:9], v[216:223], 0, v194, v169 op_sel_hi:[0,0,0]
	s_setprio 0
	s_barrier
	s_add_i32 s68, s68, s14
	v_lshl_add_u64 v[186:187], s[54:55], 0, v[166:167]
	s_mov_b32 m0, s68
	ds_read_b128 v[200:203], v198 offset:16384
	ds_read_b128 v[204:207], v198 offset:17408
	ds_read_b128 v[208:211], v198 offset:18432
	ds_read_b128 v[212:215], v198 offset:19456
	ds_read_b128 v[216:219], v198 offset:20480
	ds_read_b128 v[220:223], v198 offset:21504
	ds_read_b128 v[236:239], v198 offset:22528
	ds_read_b128 v[240:243], v198 offset:23552
	global_load_lds_dwordx4 v[186:187], off
	s_add_i32 m0, s68, 0x2000
	s_add_u32 s70, s54, 0x20000
	v_lshl_add_u64 v[188:189], s[54:55], 0, v[178:179]
	s_addc_u32 s71, s55, 0
	s_add_i32 s68, s69, s14
	global_load_lds_dwordx4 v[188:189], off
	v_lshl_add_u64 v[170:171], s[70:71], 0, v[166:167]
	s_mov_b32 m0, s68
	v_lshl_add_u64 v[190:191], s[58:59], 0, v[164:165]
	global_load_lds_dwordx4 v[170:171], off
	v_lshl_add_u64 v[170:171], s[70:71], 0, v[178:179]
	s_add_i32 m0, s68, 0x2000
	v_lshl_add_u64 v[192:193], s[58:59], 0, v[162:163]
	global_load_lds_dwordx4 v[170:171], off
	s_mov_b32 m0, s16
	s_nop 0
	global_load_lds_dwordx4 v[190:191], off
	s_mov_b32 m0, s20
	s_nop 0
	global_load_lds_dwordx4 v[192:193], off
	s_waitcnt vmcnt(8)
	s_waitcnt lgkmcnt(0)
	s_barrier
	s_setprio 1
	s_waitcnt lgkmcnt(0)
	v_mfma_scale_f32_16x16x128_f8f6f4 v[94:97], v[26:33], v[200:207], 0, v194, v169 op_sel_hi:[0,0,0]
	v_mfma_scale_f32_16x16x128_f8f6f4 v[86:89], v[18:25], v[200:207], 0, v194, v169 op_sel_hi:[0,0,0]
	v_mfma_scale_f32_16x16x128_f8f6f4 v[78:81], v[26:33], v[208:215], 0, v194, v169 op_sel_hi:[0,0,0]
	v_mfma_scale_f32_16x16x128_f8f6f4 v[70:73], v[18:25], v[208:215], 0, v194, v169 op_sel_hi:[0,0,0]
	v_mfma_scale_f32_16x16x128_f8f6f4 v[62:65], v[26:33], v[216:223], 0, v194, v169 op_sel_hi:[0,0,0]
	v_mfma_scale_f32_16x16x128_f8f6f4 v[54:57], v[18:25], v[216:223], 0, v194, v169 op_sel_hi:[0,0,0]
	v_mfma_scale_f32_16x16x128_f8f6f4 v[46:49], v[26:33], v[236:243], 0, v194, v169 op_sel_hi:[0,0,0]
	v_mfma_scale_f32_16x16x128_f8f6f4 v[38:41], v[18:25], v[236:243], 0, v194, v169 op_sel_hi:[0,0,0]
	s_setprio 0
	s_setprio 1
	v_mfma_scale_f32_16x16x128_f8f6f4 v[90:93], v[10:17], v[200:207], 0, v194, v169 op_sel_hi:[0,0,0]
	v_mfma_scale_f32_16x16x128_f8f6f4 v[82:85], v[2:9], v[200:207], 0, v194, v169 op_sel_hi:[0,0,0]
	v_mfma_scale_f32_16x16x128_f8f6f4 v[74:77], v[10:17], v[208:215], 0, v194, v169 op_sel_hi:[0,0,0]
	v_mfma_scale_f32_16x16x128_f8f6f4 v[66:69], v[2:9], v[208:215], 0, v194, v169 op_sel_hi:[0,0,0]
	v_mfma_scale_f32_16x16x128_f8f6f4 v[58:61], v[10:17], v[216:223], 0, v194, v169 op_sel_hi:[0,0,0]
	v_mfma_scale_f32_16x16x128_f8f6f4 v[50:53], v[2:9], v[216:223], 0, v194, v169 op_sel_hi:[0,0,0]
	v_mfma_scale_f32_16x16x128_f8f6f4 v[42:45], v[10:17], v[236:243], 0, v194, v169 op_sel_hi:[0,0,0]
	v_mfma_scale_f32_16x16x128_f8f6f4 v[34:37], v[2:9], v[236:243], 0, v194, v169 op_sel_hi:[0,0,0]
	s_setprio 0
	s_barrier
	s_add_i32 s68, 0, 0x18000
	s_add_i32 s69, 0, 0x1c000
	v_add_u32_e32 v2, s68, v196
	v_add_u32_e32 v6, s69, v196
	ds_read_b128 v[26:29], v2
	ds_read_b128 v[30:33], v2 offset:1024
	ds_read_b128 v[18:21], v2 offset:2048
	ds_read_b128 v[22:25], v2 offset:3072
	ds_read_b128 v[10:13], v6
	ds_read_b128 v[14:17], v6 offset:1024
	ds_read_b128 v[2:5], v6 offset:2048
	ds_read_b128 v[6:9], v6 offset:3072
	s_add_u32 s58, s58, 0x20000
	s_addc_u32 s59, s59, 0
	s_mov_b32 m0, s21
	v_lshl_add_u64 v[170:171], s[58:59], 0, v[164:165]
	ds_read_b128 v[200:203], v198 offset:32768
	ds_read_b128 v[204:207], v198 offset:33792
	ds_read_b128 v[208:211], v198 offset:34816
	ds_read_b128 v[212:215], v198 offset:35840
	ds_read_b128 v[216:219], v198 offset:36864
	ds_read_b128 v[220:223], v198 offset:37888
	ds_read_b128 v[236:239], v198 offset:38912
	ds_read_b128 v[240:243], v198 offset:39936
	global_load_lds_dwordx4 v[170:171], off
	v_lshl_add_u64 v[170:171], s[58:59], 0, v[162:163]
	s_mov_b32 m0, s22
	s_nop 0
	global_load_lds_dwordx4 v[170:171], off
	s_waitcnt vmcnt(8)
	s_waitcnt lgkmcnt(0)
	s_barrier
	s_setprio 1
	s_waitcnt lgkmcnt(0)
	v_mfma_scale_f32_16x16x128_f8f6f4 v[158:161], v[26:33], v[200:207], v[158:161], v194, v169 op_sel_hi:[0,0,0]
	v_mfma_scale_f32_16x16x128_f8f6f4 v[150:153], v[18:25], v[200:207], v[150:153], v194, v169 op_sel_hi:[0,0,0]
	v_mfma_scale_f32_16x16x128_f8f6f4 v[142:145], v[26:33], v[208:215], v[142:145], v194, v169 op_sel_hi:[0,0,0]
	v_mfma_scale_f32_16x16x128_f8f6f4 v[134:137], v[18:25], v[208:215], v[134:137], v194, v169 op_sel_hi:[0,0,0]
	v_mfma_scale_f32_16x16x128_f8f6f4 v[126:129], v[26:33], v[216:223], v[126:129], v194, v169 op_sel_hi:[0,0,0]
	v_mfma_scale_f32_16x16x128_f8f6f4 v[118:121], v[18:25], v[216:223], v[118:121], v194, v169 op_sel_hi:[0,0,0]
	v_mfma_scale_f32_16x16x128_f8f6f4 v[110:113], v[26:33], v[236:243], v[110:113], v194, v169 op_sel_hi:[0,0,0]
	v_mfma_scale_f32_16x16x128_f8f6f4 v[102:105], v[18:25], v[236:243], v[102:105], v194, v169 op_sel_hi:[0,0,0]
	s_setprio 0
	s_setprio 1
	v_mfma_scale_f32_16x16x128_f8f6f4 v[154:157], v[10:17], v[200:207], v[154:157], v194, v169 op_sel_hi:[0,0,0]
	v_mfma_scale_f32_16x16x128_f8f6f4 v[146:149], v[2:9], v[200:207], v[146:149], v194, v169 op_sel_hi:[0,0,0]
	v_mfma_scale_f32_16x16x128_f8f6f4 v[138:141], v[10:17], v[208:215], v[138:141], v194, v169 op_sel_hi:[0,0,0]
	v_mfma_scale_f32_16x16x128_f8f6f4 v[130:133], v[2:9], v[208:215], v[130:133], v194, v169 op_sel_hi:[0,0,0]
	v_mfma_scale_f32_16x16x128_f8f6f4 v[122:125], v[10:17], v[216:223], v[122:125], v194, v169 op_sel_hi:[0,0,0]
	v_mfma_scale_f32_16x16x128_f8f6f4 v[114:117], v[2:9], v[216:223], v[114:117], v194, v169 op_sel_hi:[0,0,0]
	v_mfma_scale_f32_16x16x128_f8f6f4 v[106:109], v[10:17], v[236:243], v[106:109], v194, v169 op_sel_hi:[0,0,0]
	v_mfma_scale_f32_16x16x128_f8f6f4 v[98:101], v[2:9], v[236:243], v[98:101], v194, v169 op_sel_hi:[0,0,0]
	s_setprio 0
	s_barrier
	s_add_i32 s58, s68, s14
	v_lshl_add_u64 v[170:171], v[186:187], 0, s[56:57]
	s_mov_b32 m0, s58
	ds_read_b128 v[200:203], v198 offset:49152
	ds_read_b128 v[204:207], v198 offset:50176
	ds_read_b128 v[208:211], v198 offset:51200
	ds_read_b128 v[212:215], v198 offset:52224
	ds_read_b128 v[216:219], v198 offset:53248
	ds_read_b128 v[220:223], v198 offset:54272
	ds_read_b128 v[236:239], v198 offset:55296
	ds_read_b128 v[240:243], v198 offset:56320
	global_load_lds_dwordx4 v[170:171], off
	s_add_i32 m0, s58, 0x2000
	s_add_u32 s54, s54, 0x20080
	v_lshl_add_u64 v[170:171], v[188:189], 0, s[56:57]
	s_addc_u32 s55, s55, 0
	s_add_i32 s58, s69, s14
	global_load_lds_dwordx4 v[170:171], off
	v_lshl_add_u64 v[170:171], s[54:55], 0, v[166:167]
	s_mov_b32 m0, s58
	s_nop 0
	global_load_lds_dwordx4 v[170:171], off
	v_lshl_add_u64 v[170:171], s[54:55], 0, v[178:179]
	s_add_i32 m0, s58, 0x2000
	s_nop 0
	global_load_lds_dwordx4 v[170:171], off
	v_lshl_add_u64 v[170:171], v[190:191], 0, s[56:57]
	s_mov_b32 m0, s23
	s_nop 0
	global_load_lds_dwordx4 v[170:171], off
	v_lshl_add_u64 v[170:171], v[192:193], 0, s[56:57]
	s_mov_b32 m0, s24
	s_nop 0
	global_load_lds_dwordx4 v[170:171], off
	s_waitcnt vmcnt(8)
	s_waitcnt lgkmcnt(0)
	s_barrier
	s_setprio 1
	s_waitcnt lgkmcnt(0)
	v_mfma_scale_f32_16x16x128_f8f6f4 v[94:97], v[26:33], v[200:207], v[94:97], v194, v169 op_sel_hi:[0,0,0]
	v_mfma_scale_f32_16x16x128_f8f6f4 v[86:89], v[18:25], v[200:207], v[86:89], v194, v169 op_sel_hi:[0,0,0]
	v_mfma_scale_f32_16x16x128_f8f6f4 v[78:81], v[26:33], v[208:215], v[78:81], v194, v169 op_sel_hi:[0,0,0]
	v_mfma_scale_f32_16x16x128_f8f6f4 v[70:73], v[18:25], v[208:215], v[70:73], v194, v169 op_sel_hi:[0,0,0]
	v_mfma_scale_f32_16x16x128_f8f6f4 v[62:65], v[26:33], v[216:223], v[62:65], v194, v169 op_sel_hi:[0,0,0]
	v_mfma_scale_f32_16x16x128_f8f6f4 v[54:57], v[18:25], v[216:223], v[54:57], v194, v169 op_sel_hi:[0,0,0]
	v_mfma_scale_f32_16x16x128_f8f6f4 v[46:49], v[26:33], v[236:243], v[46:49], v194, v169 op_sel_hi:[0,0,0]
	v_mfma_scale_f32_16x16x128_f8f6f4 v[38:41], v[18:25], v[236:243], v[38:41], v194, v169 op_sel_hi:[0,0,0]
	s_setprio 0
	s_setprio 1
	v_mfma_scale_f32_16x16x128_f8f6f4 v[90:93], v[10:17], v[200:207], v[90:93], v194, v169 op_sel_hi:[0,0,0]
	v_mfma_scale_f32_16x16x128_f8f6f4 v[82:85], v[2:9], v[200:207], v[82:85], v194, v169 op_sel_hi:[0,0,0]
	v_mfma_scale_f32_16x16x128_f8f6f4 v[74:77], v[10:17], v[208:215], v[74:77], v194, v169 op_sel_hi:[0,0,0]
	v_mfma_scale_f32_16x16x128_f8f6f4 v[66:69], v[2:9], v[208:215], v[66:69], v194, v169 op_sel_hi:[0,0,0]
	v_mfma_scale_f32_16x16x128_f8f6f4 v[58:61], v[10:17], v[216:223], v[58:61], v194, v169 op_sel_hi:[0,0,0]
	v_mfma_scale_f32_16x16x128_f8f6f4 v[50:53], v[2:9], v[216:223], v[50:53], v194, v169 op_sel_hi:[0,0,0]
	v_mfma_scale_f32_16x16x128_f8f6f4 v[42:45], v[10:17], v[236:243], v[42:45], v194, v169 op_sel_hi:[0,0,0]
	v_mfma_scale_f32_16x16x128_f8f6f4 v[34:37], v[2:9], v[236:243], v[34:37], v194, v169 op_sel_hi:[0,0,0]
	s_setprio 0
	s_add_u32 s64, s64, 0x100
	s_addc_u32 s65, s65, 0
	s_add_u32 s52, s52, 0x100
	s_addc_u32 s53, s53, 0
	s_cmp_ge_i32 s66, s13
	s_mov_b32 s54, s66
	s_cbranch_scc1 .Lrotph7f_pexitbar
	s_add_i32 s66, s54, 2
	s_add_u32 s55, s52, 0xfffe0080
	s_addc_u32 s58, s53, -1
	s_add_i32 s68, 0, 0x10000
	s_cmp_eq_u32 s51, s54
	s_cselect_b32 s59, s41, s58
	s_cselect_b32 s58, s43, s55
	s_cselect_b32 s55, s62, s65
	s_cselect_b32 s54, s63, s64
	s_add_i32 s69, 0, 0x14000
	s_barrier
	s_branch .Lrotph7f_body

.Lrotph7f_body:
	v_add_u32_e32 v2, s68, v196
	v_add_u32_e32 v6, s69, v196
	ds_read_b128 v[26:29], v2
	ds_read_b128 v[30:33], v2 offset:1024
	ds_read_b128 v[18:21], v2 offset:2048
	ds_read_b128 v[22:25], v2 offset:3072
	ds_read_b128 v[10:13], v6
	ds_read_b128 v[14:17], v6 offset:1024
	ds_read_b128 v[2:5], v6 offset:2048
	ds_read_b128 v[6:9], v6 offset:3072
	v_lshl_add_u64 v[170:171], s[52:53], 0, v[184:185]
	s_add_i32 m0, s16, 0xc000
	ds_read_b128 v[186:189], v198
	ds_read_b128 v[190:193], v198 offset:1024
	ds_read_b128 v[200:203], v198 offset:2048
	ds_read_b128 v[204:207], v198 offset:3072
	ds_read_b128 v[208:211], v198 offset:4096
	ds_read_b128 v[212:215], v198 offset:5120
	ds_read_b128 v[216:219], v198 offset:6144
	ds_read_b128 v[220:223], v198 offset:7168
	global_load_lds_dwordx4 v[170:171], off
	v_lshl_add_u64 v[170:171], s[52:53], 0, v[182:183]
	s_add_i32 m0, s16, 0xe000
	s_nop 0
	global_load_lds_dwordx4 v[170:171], off
	s_waitcnt vmcnt(8)
	s_waitcnt lgkmcnt(0)
	s_barrier
	s_setprio 1
	s_waitcnt lgkmcnt(0)
	v_mfma_scale_f32_16x16x128_f8f6f4 v[158:161], v[26:33], v[186:193], v[158:161], v194, v169 op_sel_hi:[0,0,0]
	v_mfma_scale_f32_16x16x128_f8f6f4 v[150:153], v[18:25], v[186:193], v[150:153], v194, v169 op_sel_hi:[0,0,0]
	v_mfma_scale_f32_16x16x128_f8f6f4 v[142:145], v[26:33], v[200:207], v[142:145], v194, v169 op_sel_hi:[0,0,0]
	v_mfma_scale_f32_16x16x128_f8f6f4 v[134:137], v[18:25], v[200:207], v[134:137], v194, v169 op_sel_hi:[0,0,0]
	v_mfma_scale_f32_16x16x128_f8f6f4 v[126:129], v[26:33], v[208:215], v[126:129], v194, v169 op_sel_hi:[0,0,0]
	v_mfma_scale_f32_16x16x128_f8f6f4 v[118:121], v[18:25], v[208:215], v[118:121], v194, v169 op_sel_hi:[0,0,0]
	v_mfma_scale_f32_16x16x128_f8f6f4 v[110:113], v[26:33], v[216:223], v[110:113], v194, v169 op_sel_hi:[0,0,0]
	v_mfma_scale_f32_16x16x128_f8f6f4 v[102:105], v[18:25], v[216:223], v[102:105], v194, v169 op_sel_hi:[0,0,0]
	s_setprio 0
	s_setprio 1
	v_mfma_scale_f32_16x16x128_f8f6f4 v[154:157], v[10:17], v[186:193], v[154:157], v194, v169 op_sel_hi:[0,0,0]
	v_mfma_scale_f32_16x16x128_f8f6f4 v[146:149], v[2:9], v[186:193], v[146:149], v194, v169 op_sel_hi:[0,0,0]
	v_mfma_scale_f32_16x16x128_f8f6f4 v[138:141], v[10:17], v[200:207], v[138:141], v194, v169 op_sel_hi:[0,0,0]
	v_mfma_scale_f32_16x16x128_f8f6f4 v[130:133], v[2:9], v[200:207], v[130:133], v194, v169 op_sel_hi:[0,0,0]
	v_mfma_scale_f32_16x16x128_f8f6f4 v[122:125], v[10:17], v[208:215], v[122:125], v194, v169 op_sel_hi:[0,0,0]
	v_mfma_scale_f32_16x16x128_f8f6f4 v[114:117], v[2:9], v[208:215], v[114:117], v194, v169 op_sel_hi:[0,0,0]
	v_mfma_scale_f32_16x16x128_f8f6f4 v[106:109], v[10:17], v[216:223], v[106:109], v194, v169 op_sel_hi:[0,0,0]
	v_mfma_scale_f32_16x16x128_f8f6f4 v[98:101], v[2:9], v[216:223], v[98:101], v194, v169 op_sel_hi:[0,0,0]
	s_setprio 0
	s_barrier
	s_add_i32 s68, s68, s14
	v_lshl_add_u64 v[186:187], s[54:55], 0, v[166:167]
	s_mov_b32 m0, s68
	ds_read_b128 v[200:203], v198 offset:16384
	ds_read_b128 v[204:207], v198 offset:17408
	ds_read_b128 v[208:211], v198 offset:18432
	ds_read_b128 v[212:215], v198 offset:19456
	ds_read_b128 v[216:219], v198 offset:20480
	ds_read_b128 v[220:223], v198 offset:21504
	ds_read_b128 v[236:239], v198 offset:22528
	ds_read_b128 v[240:243], v198 offset:23552
	global_load_lds_dwordx4 v[186:187], off
	s_add_i32 m0, s68, 0x2000
	s_add_u32 s70, s54, 0x20000
	v_lshl_add_u64 v[188:189], s[54:55], 0, v[178:179]
	s_addc_u32 s71, s55, 0
	s_add_i32 s68, s69, s14
	global_load_lds_dwordx4 v[188:189], off
	v_lshl_add_u64 v[170:171], s[70:71], 0, v[166:167]
	s_mov_b32 m0, s68
	v_lshl_add_u64 v[190:191], s[58:59], 0, v[164:165]
	global_load_lds_dwordx4 v[170:171], off
	v_lshl_add_u64 v[170:171], s[70:71], 0, v[178:179]
	s_add_i32 m0, s68, 0x2000
	v_lshl_add_u64 v[192:193], s[58:59], 0, v[162:163]
	global_load_lds_dwordx4 v[170:171], off
	s_mov_b32 m0, s16
	s_nop 0
	global_load_lds_dwordx4 v[190:191], off
	s_mov_b32 m0, s20
	s_nop 0
	global_load_lds_dwordx4 v[192:193], off
	s_waitcnt vmcnt(8)
	s_waitcnt lgkmcnt(0)
	s_barrier
	s_setprio 1
	s_waitcnt lgkmcnt(0)
	v_mfma_scale_f32_16x16x128_f8f6f4 v[94:97], v[26:33], v[200:207], v[94:97], v194, v169 op_sel_hi:[0,0,0]
	v_mfma_scale_f32_16x16x128_f8f6f4 v[86:89], v[18:25], v[200:207], v[86:89], v194, v169 op_sel_hi:[0,0,0]
	v_mfma_scale_f32_16x16x128_f8f6f4 v[78:81], v[26:33], v[208:215], v[78:81], v194, v169 op_sel_hi:[0,0,0]
	v_mfma_scale_f32_16x16x128_f8f6f4 v[70:73], v[18:25], v[208:215], v[70:73], v194, v169 op_sel_hi:[0,0,0]
	v_mfma_scale_f32_16x16x128_f8f6f4 v[62:65], v[26:33], v[216:223], v[62:65], v194, v169 op_sel_hi:[0,0,0]
	v_mfma_scale_f32_16x16x128_f8f6f4 v[54:57], v[18:25], v[216:223], v[54:57], v194, v169 op_sel_hi:[0,0,0]
	v_mfma_scale_f32_16x16x128_f8f6f4 v[46:49], v[26:33], v[236:243], v[46:49], v194, v169 op_sel_hi:[0,0,0]
	v_mfma_scale_f32_16x16x128_f8f6f4 v[38:41], v[18:25], v[236:243], v[38:41], v194, v169 op_sel_hi:[0,0,0]
	s_setprio 0
	s_setprio 1
	v_mfma_scale_f32_16x16x128_f8f6f4 v[90:93], v[10:17], v[200:207], v[90:93], v194, v169 op_sel_hi:[0,0,0]
	v_mfma_scale_f32_16x16x128_f8f6f4 v[82:85], v[2:9], v[200:207], v[82:85], v194, v169 op_sel_hi:[0,0,0]
	v_mfma_scale_f32_16x16x128_f8f6f4 v[74:77], v[10:17], v[208:215], v[74:77], v194, v169 op_sel_hi:[0,0,0]
	v_mfma_scale_f32_16x16x128_f8f6f4 v[66:69], v[2:9], v[208:215], v[66:69], v194, v169 op_sel_hi:[0,0,0]
	v_mfma_scale_f32_16x16x128_f8f6f4 v[58:61], v[10:17], v[216:223], v[58:61], v194, v169 op_sel_hi:[0,0,0]
	v_mfma_scale_f32_16x16x128_f8f6f4 v[50:53], v[2:9], v[216:223], v[50:53], v194, v169 op_sel_hi:[0,0,0]
	v_mfma_scale_f32_16x16x128_f8f6f4 v[42:45], v[10:17], v[236:243], v[42:45], v194, v169 op_sel_hi:[0,0,0]
	v_mfma_scale_f32_16x16x128_f8f6f4 v[34:37], v[2:9], v[236:243], v[34:37], v194, v169 op_sel_hi:[0,0,0]
	s_setprio 0
	s_barrier
	s_add_i32 s68, 0, 0x18000
	s_add_i32 s69, 0, 0x1c000
	v_add_u32_e32 v2, s68, v196
	v_add_u32_e32 v6, s69, v196
	ds_read_b128 v[26:29], v2
	ds_read_b128 v[30:33], v2 offset:1024
	ds_read_b128 v[18:21], v2 offset:2048
	ds_read_b128 v[22:25], v2 offset:3072
	ds_read_b128 v[10:13], v6
	ds_read_b128 v[14:17], v6 offset:1024
	ds_read_b128 v[2:5], v6 offset:2048
	ds_read_b128 v[6:9], v6 offset:3072
	s_add_u32 s58, s58, 0x20000
	s_addc_u32 s59, s59, 0
	s_mov_b32 m0, s21
	v_lshl_add_u64 v[170:171], s[58:59], 0, v[164:165]
	ds_read_b128 v[200:203], v198 offset:32768
	ds_read_b128 v[204:207], v198 offset:33792
	ds_read_b128 v[208:211], v198 offset:34816
	ds_read_b128 v[212:215], v198 offset:35840
	ds_read_b128 v[216:219], v198 offset:36864
	ds_read_b128 v[220:223], v198 offset:37888
	ds_read_b128 v[236:239], v198 offset:38912
	ds_read_b128 v[240:243], v198 offset:39936
	global_load_lds_dwordx4 v[170:171], off
	v_lshl_add_u64 v[170:171], s[58:59], 0, v[162:163]
	s_mov_b32 m0, s22
	s_nop 0
	global_load_lds_dwordx4 v[170:171], off
	s_waitcnt vmcnt(8)
	s_waitcnt lgkmcnt(0)
	s_barrier
	s_setprio 1
	s_waitcnt lgkmcnt(0)
	v_mfma_scale_f32_16x16x128_f8f6f4 v[158:161], v[26:33], v[200:207], v[158:161], v194, v169 op_sel_hi:[0,0,0]
	v_mfma_scale_f32_16x16x128_f8f6f4 v[150:153], v[18:25], v[200:207], v[150:153], v194, v169 op_sel_hi:[0,0,0]
	v_mfma_scale_f32_16x16x128_f8f6f4 v[142:145], v[26:33], v[208:215], v[142:145], v194, v169 op_sel_hi:[0,0,0]
	v_mfma_scale_f32_16x16x128_f8f6f4 v[134:137], v[18:25], v[208:215], v[134:137], v194, v169 op_sel_hi:[0,0,0]
	v_mfma_scale_f32_16x16x128_f8f6f4 v[126:129], v[26:33], v[216:223], v[126:129], v194, v169 op_sel_hi:[0,0,0]
	v_mfma_scale_f32_16x16x128_f8f6f4 v[118:121], v[18:25], v[216:223], v[118:121], v194, v169 op_sel_hi:[0,0,0]
	v_mfma_scale_f32_16x16x128_f8f6f4 v[110:113], v[26:33], v[236:243], v[110:113], v194, v169 op_sel_hi:[0,0,0]
	v_mfma_scale_f32_16x16x128_f8f6f4 v[102:105], v[18:25], v[236:243], v[102:105], v194, v169 op_sel_hi:[0,0,0]
	s_setprio 0
	s_setprio 1
	v_mfma_scale_f32_16x16x128_f8f6f4 v[154:157], v[10:17], v[200:207], v[154:157], v194, v169 op_sel_hi:[0,0,0]
	v_mfma_scale_f32_16x16x128_f8f6f4 v[146:149], v[2:9], v[200:207], v[146:149], v194, v169 op_sel_hi:[0,0,0]
	v_mfma_scale_f32_16x16x128_f8f6f4 v[138:141], v[10:17], v[208:215], v[138:141], v194, v169 op_sel_hi:[0,0,0]
	v_mfma_scale_f32_16x16x128_f8f6f4 v[130:133], v[2:9], v[208:215], v[130:133], v194, v169 op_sel_hi:[0,0,0]
	v_mfma_scale_f32_16x16x128_f8f6f4 v[122:125], v[10:17], v[216:223], v[122:125], v194, v169 op_sel_hi:[0,0,0]
	v_mfma_scale_f32_16x16x128_f8f6f4 v[114:117], v[2:9], v[216:223], v[114:117], v194, v169 op_sel_hi:[0,0,0]
	v_mfma_scale_f32_16x16x128_f8f6f4 v[106:109], v[10:17], v[236:243], v[106:109], v194, v169 op_sel_hi:[0,0,0]
	v_mfma_scale_f32_16x16x128_f8f6f4 v[98:101], v[2:9], v[236:243], v[98:101], v194, v169 op_sel_hi:[0,0,0]
	s_setprio 0
	s_barrier
	s_add_i32 s58, s68, s14
	v_lshl_add_u64 v[170:171], v[186:187], 0, s[56:57]
	s_mov_b32 m0, s58
	ds_read_b128 v[200:203], v198 offset:49152
	ds_read_b128 v[204:207], v198 offset:50176
	ds_read_b128 v[208:211], v198 offset:51200
	ds_read_b128 v[212:215], v198 offset:52224
	ds_read_b128 v[216:219], v198 offset:53248
	ds_read_b128 v[220:223], v198 offset:54272
	ds_read_b128 v[236:239], v198 offset:55296
	ds_read_b128 v[240:243], v198 offset:56320
	global_load_lds_dwordx4 v[170:171], off
	s_add_i32 m0, s58, 0x2000
	s_add_u32 s54, s54, 0x20080
	v_lshl_add_u64 v[170:171], v[188:189], 0, s[56:57]
	s_addc_u32 s55, s55, 0
	s_add_i32 s58, s69, s14
	global_load_lds_dwordx4 v[170:171], off
	v_lshl_add_u64 v[170:171], s[54:55], 0, v[166:167]
	s_mov_b32 m0, s58
	s_nop 0
	global_load_lds_dwordx4 v[170:171], off
	v_lshl_add_u64 v[170:171], s[54:55], 0, v[178:179]
	s_add_i32 m0, s58, 0x2000
	s_nop 0
	global_load_lds_dwordx4 v[170:171], off
	v_lshl_add_u64 v[170:171], v[190:191], 0, s[56:57]
	s_mov_b32 m0, s23
	s_nop 0
	global_load_lds_dwordx4 v[170:171], off
	v_lshl_add_u64 v[170:171], v[192:193], 0, s[56:57]
	s_mov_b32 m0, s24
	s_nop 0
	global_load_lds_dwordx4 v[170:171], off
	s_waitcnt vmcnt(8)
	s_waitcnt lgkmcnt(0)
	s_barrier
	s_setprio 1
	s_waitcnt lgkmcnt(0)
	v_mfma_scale_f32_16x16x128_f8f6f4 v[94:97], v[26:33], v[200:207], v[94:97], v194, v169 op_sel_hi:[0,0,0]
	v_mfma_scale_f32_16x16x128_f8f6f4 v[86:89], v[18:25], v[200:207], v[86:89], v194, v169 op_sel_hi:[0,0,0]
	v_mfma_scale_f32_16x16x128_f8f6f4 v[78:81], v[26:33], v[208:215], v[78:81], v194, v169 op_sel_hi:[0,0,0]
	v_mfma_scale_f32_16x16x128_f8f6f4 v[70:73], v[18:25], v[208:215], v[70:73], v194, v169 op_sel_hi:[0,0,0]
	v_mfma_scale_f32_16x16x128_f8f6f4 v[62:65], v[26:33], v[216:223], v[62:65], v194, v169 op_sel_hi:[0,0,0]
	v_mfma_scale_f32_16x16x128_f8f6f4 v[54:57], v[18:25], v[216:223], v[54:57], v194, v169 op_sel_hi:[0,0,0]
	v_mfma_scale_f32_16x16x128_f8f6f4 v[46:49], v[26:33], v[236:243], v[46:49], v194, v169 op_sel_hi:[0,0,0]
	v_mfma_scale_f32_16x16x128_f8f6f4 v[38:41], v[18:25], v[236:243], v[38:41], v194, v169 op_sel_hi:[0,0,0]
	s_setprio 0
	s_setprio 1
	v_mfma_scale_f32_16x16x128_f8f6f4 v[90:93], v[10:17], v[200:207], v[90:93], v194, v169 op_sel_hi:[0,0,0]
	v_mfma_scale_f32_16x16x128_f8f6f4 v[82:85], v[2:9], v[200:207], v[82:85], v194, v169 op_sel_hi:[0,0,0]
	v_mfma_scale_f32_16x16x128_f8f6f4 v[74:77], v[10:17], v[208:215], v[74:77], v194, v169 op_sel_hi:[0,0,0]
	v_mfma_scale_f32_16x16x128_f8f6f4 v[66:69], v[2:9], v[208:215], v[66:69], v194, v169 op_sel_hi:[0,0,0]
	v_mfma_scale_f32_16x16x128_f8f6f4 v[58:61], v[10:17], v[216:223], v[58:61], v194, v169 op_sel_hi:[0,0,0]
	v_mfma_scale_f32_16x16x128_f8f6f4 v[50:53], v[2:9], v[216:223], v[50:53], v194, v169 op_sel_hi:[0,0,0]
	v_mfma_scale_f32_16x16x128_f8f6f4 v[42:45], v[10:17], v[236:243], v[42:45], v194, v169 op_sel_hi:[0,0,0]
	v_mfma_scale_f32_16x16x128_f8f6f4 v[34:37], v[2:9], v[236:243], v[34:37], v194, v169 op_sel_hi:[0,0,0]
	s_setprio 0
	s_add_u32 s64, s64, 0x100
	s_addc_u32 s65, s65, 0
	s_add_u32 s52, s52, 0x100
	s_addc_u32 s53, s53, 0
	s_cmp_ge_i32 s66, s13
	s_mov_b32 s54, s66
	s_cbranch_scc1 .Lrotph7f_exitbar
	s_add_i32 s66, s54, 2
	s_add_u32 s55, s52, 0xfffe0080
	s_addc_u32 s58, s53, -1
	s_add_i32 s68, 0, 0x10000
	s_cmp_eq_u32 s51, s54
	s_cselect_b32 s59, s41, s58
	s_cselect_b32 s58, s43, s55
	s_cselect_b32 s55, s62, s65
	s_cselect_b32 s54, s63, s64
	s_add_i32 s69, 0, 0x14000
	s_barrier
	s_branch .Lrotph7f_body
.Lrotph7f_exitbar:
	s_barrier
.Lpeelexitph7f:
	s_mov_b64 s[70:71], 0xe800800
	v_mov_b32_e32 v209, v1
	s_and_b64 vcc, exec, s[36:37]
	s_cbranch_vccz .LBB0_845

.Lpeelph8_0:
	s_add_i32 s75, s62, 2
	s_add_u32 s60, s58, 0x100
	s_addc_u32 s61, s59, 0
	s_add_i32 s76, 0, 0x10000
	s_cmp_eq_u32 s68, s62
	s_cselect_b32 s65, s53, s61
	s_cselect_b32 s64, s52, s60
	s_cselect_b32 s63, s55, s74
	s_cselect_b32 s62, s54, s73
	s_add_i32 s77, 0, 0x14000
	v_add_u32_e32 v2, s76, v200
	v_add_u32_e32 v6, s77, v200
	ds_read_b128 v[26:29], v2
	ds_read_b128 v[30:33], v2 offset:1024
	ds_read_b128 v[18:21], v2 offset:2048
	ds_read_b128 v[22:25], v2 offset:3072
	ds_read_b128 v[10:13], v6
	ds_read_b128 v[14:17], v6 offset:1024
	s_waitcnt lgkmcnt(0)
	ds_read_b128 v[2:5], v6 offset:2048
	ds_read_b128 v[6:9], v6 offset:3072
	v_lshl_add_u64 v[170:171], s[58:59], 0, v[184:185]
	s_add_i32 m0, s15, 0xc000
	ds_read_b128 v[186:189], v204
	ds_read_b128 v[190:193], v204 offset:1024
	ds_read_b128 v[206:209], v204 offset:2048
	ds_read_b128 v[210:213], v204 offset:3072
	ds_read_b128 v[214:217], v204 offset:4096
	ds_read_b128 v[218:221], v204 offset:5120
	ds_read_b128 v[236:239], v204 offset:6144
	ds_read_b128 v[240:243], v204 offset:7168
	global_load_lds_dwordx4 v[170:171], off
	v_lshl_add_u64 v[170:171], s[58:59], 0, v[182:183]
	s_add_i32 m0, s15, 0xe000
	s_nop 0
	global_load_lds_dwordx4 v[170:171], off
	s_waitcnt vmcnt(8)
	s_waitcnt lgkmcnt(0)
	s_barrier
	s_setprio 1
	s_waitcnt lgkmcnt(0)
	v_mfma_scale_f32_16x16x128_f8f6f4 v[158:161], v[26:33], v[186:193], 0, v198, v169 op_sel_hi:[0,0,0]
	v_mfma_scale_f32_16x16x128_f8f6f4 v[154:157], v[18:25], v[186:193], 0, v198, v169 op_sel_hi:[0,0,0]
	v_mfma_scale_f32_16x16x128_f8f6f4 v[142:145], v[26:33], v[206:213], 0, v198, v169 op_sel_hi:[0,0,0]
	v_mfma_scale_f32_16x16x128_f8f6f4 v[138:141], v[18:25], v[206:213], 0, v198, v169 op_sel_hi:[0,0,0]
	v_mfma_scale_f32_16x16x128_f8f6f4 v[126:129], v[26:33], v[214:221], 0, v198, v169 op_sel_hi:[0,0,0]
	v_mfma_scale_f32_16x16x128_f8f6f4 v[122:125], v[18:25], v[214:221], 0, v198, v169 op_sel_hi:[0,0,0]
	v_mfma_scale_f32_16x16x128_f8f6f4 v[110:113], v[26:33], v[236:243], 0, v198, v169 op_sel_hi:[0,0,0]
	v_mfma_scale_f32_16x16x128_f8f6f4 v[106:109], v[18:25], v[236:243], 0, v198, v169 op_sel_hi:[0,0,0]
	s_setprio 0
	s_setprio 1
	v_mfma_scale_f32_16x16x128_f8f6f4 v[150:153], v[10:17], v[186:193], 0, v198, v169 op_sel_hi:[0,0,0]
	v_mfma_scale_f32_16x16x128_f8f6f4 v[146:149], v[2:9], v[186:193], 0, v198, v169 op_sel_hi:[0,0,0]
	v_mfma_scale_f32_16x16x128_f8f6f4 v[134:137], v[10:17], v[206:213], 0, v198, v169 op_sel_hi:[0,0,0]
	v_mfma_scale_f32_16x16x128_f8f6f4 v[130:133], v[2:9], v[206:213], 0, v198, v169 op_sel_hi:[0,0,0]
	v_mfma_scale_f32_16x16x128_f8f6f4 v[118:121], v[10:17], v[214:221], 0, v198, v169 op_sel_hi:[0,0,0]
	v_mfma_scale_f32_16x16x128_f8f6f4 v[114:117], v[2:9], v[214:221], 0, v198, v169 op_sel_hi:[0,0,0]
	v_mfma_scale_f32_16x16x128_f8f6f4 v[102:105], v[10:17], v[236:243], 0, v198, v169 op_sel_hi:[0,0,0]
	v_mfma_scale_f32_16x16x128_f8f6f4 v[98:101], v[2:9], v[236:243], 0, v198, v169 op_sel_hi:[0,0,0]
	s_setprio 0
	s_barrier
	s_add_i32 s58, s76, s14
	v_lshl_add_u64 v[186:187], s[62:63], 0, v[166:167]
	s_mov_b32 m0, s58
	ds_read_b128 v[206:209], v204 offset:16384
	ds_read_b128 v[210:213], v204 offset:17408
	ds_read_b128 v[214:217], v204 offset:18432
	ds_read_b128 v[218:221], v204 offset:19456
	ds_read_b128 v[236:239], v204 offset:20480
	ds_read_b128 v[240:243], v204 offset:21504
	ds_read_b128 v[244:247], v204 offset:22528
	ds_read_b128 v[248:251], v204 offset:23552
	global_load_lds_dwordx4 v[186:187], off
	s_add_i32 m0, s58, 0x2000
	s_add_u32 s58, s62, 0x70000
	v_lshl_add_u64 v[188:189], s[62:63], 0, v[162:163]
	s_addc_u32 s59, s63, 0
	s_add_i32 s76, s77, s14
	global_load_lds_dwordx4 v[188:189], off
	v_lshl_add_u64 v[170:171], s[58:59], 0, v[166:167]
	s_mov_b32 m0, s76
	v_lshl_add_u64 v[190:191], s[64:65], 0, v[164:165]
	global_load_lds_dwordx4 v[170:171], off
	v_lshl_add_u64 v[170:171], s[58:59], 0, v[162:163]
	s_add_i32 m0, s76, 0x2000
	v_lshl_add_u64 v[192:193], s[64:65], 0, v[178:179]
	global_load_lds_dwordx4 v[170:171], off
	s_mov_b32 m0, s15
	s_nop 0
	global_load_lds_dwordx4 v[190:191], off
	s_mov_b32 m0, s16
	s_nop 0
	global_load_lds_dwordx4 v[192:193], off
	s_waitcnt vmcnt(8)
	s_waitcnt lgkmcnt(0)
	s_barrier
	s_setprio 1
	s_waitcnt lgkmcnt(0)
	v_mfma_scale_f32_16x16x128_f8f6f4 v[94:97], v[26:33], v[206:213], 0, v198, v169 op_sel_hi:[0,0,0]
	v_mfma_scale_f32_16x16x128_f8f6f4 v[90:93], v[18:25], v[206:213], 0, v198, v169 op_sel_hi:[0,0,0]
	v_mfma_scale_f32_16x16x128_f8f6f4 v[78:81], v[26:33], v[214:221], 0, v198, v169 op_sel_hi:[0,0,0]
	v_mfma_scale_f32_16x16x128_f8f6f4 v[74:77], v[18:25], v[214:221], 0, v198, v169 op_sel_hi:[0,0,0]
	v_mfma_scale_f32_16x16x128_f8f6f4 v[62:65], v[26:33], v[236:243], 0, v198, v169 op_sel_hi:[0,0,0]
	v_mfma_scale_f32_16x16x128_f8f6f4 v[58:61], v[18:25], v[236:243], 0, v198, v169 op_sel_hi:[0,0,0]
	v_mfma_scale_f32_16x16x128_f8f6f4 v[46:49], v[26:33], v[244:251], 0, v198, v169 op_sel_hi:[0,0,0]
	v_mfma_scale_f32_16x16x128_f8f6f4 v[42:45], v[18:25], v[244:251], 0, v198, v169 op_sel_hi:[0,0,0]
	s_setprio 0
	s_setprio 1
	v_mfma_scale_f32_16x16x128_f8f6f4 v[86:89], v[10:17], v[206:213], 0, v198, v169 op_sel_hi:[0,0,0]
	v_mfma_scale_f32_16x16x128_f8f6f4 v[82:85], v[2:9], v[206:213], 0, v198, v169 op_sel_hi:[0,0,0]
	v_mfma_scale_f32_16x16x128_f8f6f4 v[70:73], v[10:17], v[214:221], 0, v198, v169 op_sel_hi:[0,0,0]
	v_mfma_scale_f32_16x16x128_f8f6f4 v[66:69], v[2:9], v[214:221], 0, v198, v169 op_sel_hi:[0,0,0]
	v_mfma_scale_f32_16x16x128_f8f6f4 v[54:57], v[10:17], v[236:243], 0, v198, v169 op_sel_hi:[0,0,0]
	v_mfma_scale_f32_16x16x128_f8f6f4 v[50:53], v[2:9], v[236:243], 0, v198, v169 op_sel_hi:[0,0,0]
	v_mfma_scale_f32_16x16x128_f8f6f4 v[38:41], v[10:17], v[244:251], 0, v198, v169 op_sel_hi:[0,0,0]
	v_mfma_scale_f32_16x16x128_f8f6f4 v[34:37], v[2:9], v[244:251], 0, v198, v169 op_sel_hi:[0,0,0]
	s_setprio 0
	s_barrier
	s_add_i32 s76, 0, 0x18000
	s_add_i32 s77, 0, 0x1c000
	v_add_u32_e32 v2, s76, v200
	v_add_u32_e32 v6, s77, v200
	ds_read_b128 v[26:29], v2
	ds_read_b128 v[30:33], v2 offset:1024
	ds_read_b128 v[18:21], v2 offset:2048
	ds_read_b128 v[22:25], v2 offset:3072
	ds_read_b128 v[10:13], v6
	ds_read_b128 v[14:17], v6 offset:1024
	ds_read_b128 v[2:5], v6 offset:2048
	ds_read_b128 v[6:9], v6 offset:3072
	s_add_u32 s58, s64, 0x70000
	s_addc_u32 s59, s65, 0
	s_mov_b32 m0, s20
	v_lshl_add_u64 v[170:171], s[58:59], 0, v[164:165]
	ds_read_b128 v[206:209], v204 offset:32768
	ds_read_b128 v[210:213], v204 offset:33792
	ds_read_b128 v[214:217], v204 offset:34816
	ds_read_b128 v[218:221], v204 offset:35840
	ds_read_b128 v[236:239], v204 offset:36864
	ds_read_b128 v[240:243], v204 offset:37888
	ds_read_b128 v[244:247], v204 offset:38912
	ds_read_b128 v[248:251], v204 offset:39936
	global_load_lds_dwordx4 v[170:171], off
	v_lshl_add_u64 v[170:171], s[58:59], 0, v[178:179]
	s_mov_b32 m0, s21
	s_nop 0
	global_load_lds_dwordx4 v[170:171], off
	s_waitcnt vmcnt(8)
	s_waitcnt lgkmcnt(0)
	s_barrier
	s_setprio 1
	s_waitcnt lgkmcnt(0)
	v_mfma_scale_f32_16x16x128_f8f6f4 v[158:161], v[26:33], v[206:213], v[158:161], v198, v169 op_sel_hi:[0,0,0]
	v_mfma_scale_f32_16x16x128_f8f6f4 v[154:157], v[18:25], v[206:213], v[154:157], v198, v169 op_sel_hi:[0,0,0]
	v_mfma_scale_f32_16x16x128_f8f6f4 v[142:145], v[26:33], v[214:221], v[142:145], v198, v169 op_sel_hi:[0,0,0]
	v_mfma_scale_f32_16x16x128_f8f6f4 v[138:141], v[18:25], v[214:221], v[138:141], v198, v169 op_sel_hi:[0,0,0]
	v_mfma_scale_f32_16x16x128_f8f6f4 v[126:129], v[26:33], v[236:243], v[126:129], v198, v169 op_sel_hi:[0,0,0]
	v_mfma_scale_f32_16x16x128_f8f6f4 v[122:125], v[18:25], v[236:243], v[122:125], v198, v169 op_sel_hi:[0,0,0]
	v_mfma_scale_f32_16x16x128_f8f6f4 v[110:113], v[26:33], v[244:251], v[110:113], v198, v169 op_sel_hi:[0,0,0]
	v_mfma_scale_f32_16x16x128_f8f6f4 v[106:109], v[18:25], v[244:251], v[106:109], v198, v169 op_sel_hi:[0,0,0]
	s_setprio 0
	s_setprio 1
	v_mfma_scale_f32_16x16x128_f8f6f4 v[150:153], v[10:17], v[206:213], v[150:153], v198, v169 op_sel_hi:[0,0,0]
	v_mfma_scale_f32_16x16x128_f8f6f4 v[146:149], v[2:9], v[206:213], v[146:149], v198, v169 op_sel_hi:[0,0,0]
	v_mfma_scale_f32_16x16x128_f8f6f4 v[134:137], v[10:17], v[214:221], v[134:137], v198, v169 op_sel_hi:[0,0,0]
	v_mfma_scale_f32_16x16x128_f8f6f4 v[130:133], v[2:9], v[214:221], v[130:133], v198, v169 op_sel_hi:[0,0,0]
	v_mfma_scale_f32_16x16x128_f8f6f4 v[118:121], v[10:17], v[236:243], v[118:121], v198, v169 op_sel_hi:[0,0,0]
	v_mfma_scale_f32_16x16x128_f8f6f4 v[114:117], v[2:9], v[236:243], v[114:117], v198, v169 op_sel_hi:[0,0,0]
	v_mfma_scale_f32_16x16x128_f8f6f4 v[102:105], v[10:17], v[244:251], v[102:105], v198, v169 op_sel_hi:[0,0,0]
	v_mfma_scale_f32_16x16x128_f8f6f4 v[98:101], v[2:9], v[244:251], v[98:101], v198, v169 op_sel_hi:[0,0,0]
	s_setprio 0
	s_barrier
	s_add_i32 s58, s76, s14
	v_lshl_add_u64 v[170:171], v[186:187], 0, s[56:57]
	s_mov_b32 m0, s58
	ds_read_b128 v[206:209], v204 offset:49152
	ds_read_b128 v[210:213], v204 offset:50176
	ds_read_b128 v[214:217], v204 offset:51200
	ds_read_b128 v[218:221], v204 offset:52224
	ds_read_b128 v[236:239], v204 offset:53248
	ds_read_b128 v[240:243], v204 offset:54272
	ds_read_b128 v[244:247], v204 offset:55296
	ds_read_b128 v[248:251], v204 offset:56320
	global_load_lds_dwordx4 v[170:171], off
	s_add_i32 m0, s58, 0x2000
	s_add_u32 s58, s62, 0x70080
	v_lshl_add_u64 v[170:171], v[188:189], 0, s[56:57]
	s_addc_u32 s59, s63, 0
	s_add_i32 s62, s77, s14
	global_load_lds_dwordx4 v[170:171], off
	v_lshl_add_u64 v[170:171], s[58:59], 0, v[166:167]
	s_mov_b32 m0, s62
	s_nop 0
	global_load_lds_dwordx4 v[170:171], off
	v_lshl_add_u64 v[170:171], s[58:59], 0, v[162:163]
	s_add_i32 m0, s62, 0x2000
	s_nop 0
	global_load_lds_dwordx4 v[170:171], off
	v_lshl_add_u64 v[170:171], v[190:191], 0, s[56:57]
	s_mov_b32 m0, s24
	s_nop 0
	global_load_lds_dwordx4 v[170:171], off
	v_lshl_add_u64 v[170:171], v[192:193], 0, s[56:57]
	s_mov_b32 m0, s25
	s_nop 0
	global_load_lds_dwordx4 v[170:171], off
	s_waitcnt vmcnt(8)
	s_waitcnt lgkmcnt(0)
	s_barrier
	s_setprio 1
	s_waitcnt lgkmcnt(0)
	v_mfma_scale_f32_16x16x128_f8f6f4 v[94:97], v[26:33], v[206:213], v[94:97], v198, v169 op_sel_hi:[0,0,0]
	v_mfma_scale_f32_16x16x128_f8f6f4 v[90:93], v[18:25], v[206:213], v[90:93], v198, v169 op_sel_hi:[0,0,0]
	v_mfma_scale_f32_16x16x128_f8f6f4 v[78:81], v[26:33], v[214:221], v[78:81], v198, v169 op_sel_hi:[0,0,0]
	v_mfma_scale_f32_16x16x128_f8f6f4 v[74:77], v[18:25], v[214:221], v[74:77], v198, v169 op_sel_hi:[0,0,0]
	v_mfma_scale_f32_16x16x128_f8f6f4 v[62:65], v[26:33], v[236:243], v[62:65], v198, v169 op_sel_hi:[0,0,0]
	v_mfma_scale_f32_16x16x128_f8f6f4 v[58:61], v[18:25], v[236:243], v[58:61], v198, v169 op_sel_hi:[0,0,0]
	v_mfma_scale_f32_16x16x128_f8f6f4 v[46:49], v[26:33], v[244:251], v[46:49], v198, v169 op_sel_hi:[0,0,0]
	v_mfma_scale_f32_16x16x128_f8f6f4 v[42:45], v[18:25], v[244:251], v[42:45], v198, v169 op_sel_hi:[0,0,0]
	s_setprio 0
	s_setprio 1
	v_mfma_scale_f32_16x16x128_f8f6f4 v[86:89], v[10:17], v[206:213], v[86:89], v198, v169 op_sel_hi:[0,0,0]
	v_mfma_scale_f32_16x16x128_f8f6f4 v[82:85], v[2:9], v[206:213], v[82:85], v198, v169 op_sel_hi:[0,0,0]
	v_mfma_scale_f32_16x16x128_f8f6f4 v[70:73], v[10:17], v[214:221], v[70:73], v198, v169 op_sel_hi:[0,0,0]
	v_mfma_scale_f32_16x16x128_f8f6f4 v[66:69], v[2:9], v[214:221], v[66:69], v198, v169 op_sel_hi:[0,0,0]
	v_mfma_scale_f32_16x16x128_f8f6f4 v[54:57], v[10:17], v[236:243], v[54:57], v198, v169 op_sel_hi:[0,0,0]
	v_mfma_scale_f32_16x16x128_f8f6f4 v[50:53], v[2:9], v[236:243], v[50:53], v198, v169 op_sel_hi:[0,0,0]
	v_mfma_scale_f32_16x16x128_f8f6f4 v[38:41], v[10:17], v[244:251], v[38:41], v198, v169 op_sel_hi:[0,0,0]
	v_mfma_scale_f32_16x16x128_f8f6f4 v[34:37], v[2:9], v[244:251], v[34:37], v198, v169 op_sel_hi:[0,0,0]
	s_setprio 0
	s_add_u32 s73, s73, 0x100
	s_addc_u32 s74, s74, 0
	s_cmp_ge_i32 s75, s1
	s_mov_b64 s[58:59], s[60:61]
	s_mov_b32 s62, s75
	s_cbranch_scc1 .Lrotph8_pexitbar
	s_add_i32 s75, s62, 2
	s_add_u32 s60, s58, 0x100
	s_addc_u32 s61, s59, 0
	s_add_i32 s76, 0, 0x10000
	s_cmp_eq_u32 s68, s62
	s_cselect_b32 s65, s53, s61
	s_cselect_b32 s64, s52, s60
	s_cselect_b32 s63, s55, s74
	s_cselect_b32 s62, s54, s73
	s_add_i32 s77, 0, 0x14000
	s_barrier
	s_branch .Lrotph8_body

.Lrotph8_body:
	v_add_u32_e32 v2, s76, v200
	v_add_u32_e32 v6, s77, v200
	ds_read_b128 v[26:29], v2
	ds_read_b128 v[30:33], v2 offset:1024
	ds_read_b128 v[18:21], v2 offset:2048
	ds_read_b128 v[22:25], v2 offset:3072
	ds_read_b128 v[10:13], v6
	ds_read_b128 v[14:17], v6 offset:1024
	s_waitcnt lgkmcnt(0)
	ds_read_b128 v[2:5], v6 offset:2048
	ds_read_b128 v[6:9], v6 offset:3072
	v_lshl_add_u64 v[170:171], s[58:59], 0, v[184:185]
	s_add_i32 m0, s15, 0xc000
	ds_read_b128 v[186:189], v204
	ds_read_b128 v[190:193], v204 offset:1024
	ds_read_b128 v[206:209], v204 offset:2048
	ds_read_b128 v[210:213], v204 offset:3072
	ds_read_b128 v[214:217], v204 offset:4096
	ds_read_b128 v[218:221], v204 offset:5120
	ds_read_b128 v[236:239], v204 offset:6144
	ds_read_b128 v[240:243], v204 offset:7168
	global_load_lds_dwordx4 v[170:171], off
	v_lshl_add_u64 v[170:171], s[58:59], 0, v[182:183]
	s_add_i32 m0, s15, 0xe000
	s_nop 0
	global_load_lds_dwordx4 v[170:171], off
	s_waitcnt vmcnt(8)
	s_waitcnt lgkmcnt(0)
	s_barrier
	s_setprio 1
	s_waitcnt lgkmcnt(0)
	v_mfma_scale_f32_16x16x128_f8f6f4 v[158:161], v[26:33], v[186:193], v[158:161], v198, v169 op_sel_hi:[0,0,0]
	v_mfma_scale_f32_16x16x128_f8f6f4 v[154:157], v[18:25], v[186:193], v[154:157], v198, v169 op_sel_hi:[0,0,0]
	v_mfma_scale_f32_16x16x128_f8f6f4 v[142:145], v[26:33], v[206:213], v[142:145], v198, v169 op_sel_hi:[0,0,0]
	v_mfma_scale_f32_16x16x128_f8f6f4 v[138:141], v[18:25], v[206:213], v[138:141], v198, v169 op_sel_hi:[0,0,0]
	v_mfma_scale_f32_16x16x128_f8f6f4 v[126:129], v[26:33], v[214:221], v[126:129], v198, v169 op_sel_hi:[0,0,0]
	v_mfma_scale_f32_16x16x128_f8f6f4 v[122:125], v[18:25], v[214:221], v[122:125], v198, v169 op_sel_hi:[0,0,0]
	v_mfma_scale_f32_16x16x128_f8f6f4 v[110:113], v[26:33], v[236:243], v[110:113], v198, v169 op_sel_hi:[0,0,0]
	v_mfma_scale_f32_16x16x128_f8f6f4 v[106:109], v[18:25], v[236:243], v[106:109], v198, v169 op_sel_hi:[0,0,0]
	s_setprio 0
	s_setprio 1
	v_mfma_scale_f32_16x16x128_f8f6f4 v[150:153], v[10:17], v[186:193], v[150:153], v198, v169 op_sel_hi:[0,0,0]
	v_mfma_scale_f32_16x16x128_f8f6f4 v[146:149], v[2:9], v[186:193], v[146:149], v198, v169 op_sel_hi:[0,0,0]
	v_mfma_scale_f32_16x16x128_f8f6f4 v[134:137], v[10:17], v[206:213], v[134:137], v198, v169 op_sel_hi:[0,0,0]
	v_mfma_scale_f32_16x16x128_f8f6f4 v[130:133], v[2:9], v[206:213], v[130:133], v198, v169 op_sel_hi:[0,0,0]
	v_mfma_scale_f32_16x16x128_f8f6f4 v[118:121], v[10:17], v[214:221], v[118:121], v198, v169 op_sel_hi:[0,0,0]
	v_mfma_scale_f32_16x16x128_f8f6f4 v[114:117], v[2:9], v[214:221], v[114:117], v198, v169 op_sel_hi:[0,0,0]
	v_mfma_scale_f32_16x16x128_f8f6f4 v[102:105], v[10:17], v[236:243], v[102:105], v198, v169 op_sel_hi:[0,0,0]
	v_mfma_scale_f32_16x16x128_f8f6f4 v[98:101], v[2:9], v[236:243], v[98:101], v198, v169 op_sel_hi:[0,0,0]
	s_setprio 0
	s_barrier
	s_add_i32 s58, s76, s14
	v_lshl_add_u64 v[186:187], s[62:63], 0, v[166:167]
	s_mov_b32 m0, s58
	ds_read_b128 v[206:209], v204 offset:16384
	ds_read_b128 v[210:213], v204 offset:17408
	ds_read_b128 v[214:217], v204 offset:18432
	ds_read_b128 v[218:221], v204 offset:19456
	ds_read_b128 v[236:239], v204 offset:20480
	ds_read_b128 v[240:243], v204 offset:21504
	ds_read_b128 v[244:247], v204 offset:22528
	ds_read_b128 v[248:251], v204 offset:23552
	global_load_lds_dwordx4 v[186:187], off
	s_add_i32 m0, s58, 0x2000
	s_add_u32 s58, s62, 0x70000
	v_lshl_add_u64 v[188:189], s[62:63], 0, v[162:163]
	s_addc_u32 s59, s63, 0
	s_add_i32 s76, s77, s14
	global_load_lds_dwordx4 v[188:189], off
	v_lshl_add_u64 v[170:171], s[58:59], 0, v[166:167]
	s_mov_b32 m0, s76
	v_lshl_add_u64 v[190:191], s[64:65], 0, v[164:165]
	global_load_lds_dwordx4 v[170:171], off
	v_lshl_add_u64 v[170:171], s[58:59], 0, v[162:163]
	s_add_i32 m0, s76, 0x2000
	v_lshl_add_u64 v[192:193], s[64:65], 0, v[178:179]
	global_load_lds_dwordx4 v[170:171], off
	s_mov_b32 m0, s15
	s_nop 0
	global_load_lds_dwordx4 v[190:191], off
	s_mov_b32 m0, s16
	s_nop 0
	global_load_lds_dwordx4 v[192:193], off
	s_waitcnt vmcnt(8)
	s_waitcnt lgkmcnt(0)
	s_barrier
	s_setprio 1
	s_waitcnt lgkmcnt(0)
	v_mfma_scale_f32_16x16x128_f8f6f4 v[94:97], v[26:33], v[206:213], v[94:97], v198, v169 op_sel_hi:[0,0,0]
	v_mfma_scale_f32_16x16x128_f8f6f4 v[90:93], v[18:25], v[206:213], v[90:93], v198, v169 op_sel_hi:[0,0,0]
	v_mfma_scale_f32_16x16x128_f8f6f4 v[78:81], v[26:33], v[214:221], v[78:81], v198, v169 op_sel_hi:[0,0,0]
	v_mfma_scale_f32_16x16x128_f8f6f4 v[74:77], v[18:25], v[214:221], v[74:77], v198, v169 op_sel_hi:[0,0,0]
	v_mfma_scale_f32_16x16x128_f8f6f4 v[62:65], v[26:33], v[236:243], v[62:65], v198, v169 op_sel_hi:[0,0,0]
	v_mfma_scale_f32_16x16x128_f8f6f4 v[58:61], v[18:25], v[236:243], v[58:61], v198, v169 op_sel_hi:[0,0,0]
	v_mfma_scale_f32_16x16x128_f8f6f4 v[46:49], v[26:33], v[244:251], v[46:49], v198, v169 op_sel_hi:[0,0,0]
	v_mfma_scale_f32_16x16x128_f8f6f4 v[42:45], v[18:25], v[244:251], v[42:45], v198, v169 op_sel_hi:[0,0,0]
	s_setprio 0
	s_setprio 1
	v_mfma_scale_f32_16x16x128_f8f6f4 v[86:89], v[10:17], v[206:213], v[86:89], v198, v169 op_sel_hi:[0,0,0]
	v_mfma_scale_f32_16x16x128_f8f6f4 v[82:85], v[2:9], v[206:213], v[82:85], v198, v169 op_sel_hi:[0,0,0]
	v_mfma_scale_f32_16x16x128_f8f6f4 v[70:73], v[10:17], v[214:221], v[70:73], v198, v169 op_sel_hi:[0,0,0]
	v_mfma_scale_f32_16x16x128_f8f6f4 v[66:69], v[2:9], v[214:221], v[66:69], v198, v169 op_sel_hi:[0,0,0]
	v_mfma_scale_f32_16x16x128_f8f6f4 v[54:57], v[10:17], v[236:243], v[54:57], v198, v169 op_sel_hi:[0,0,0]
	v_mfma_scale_f32_16x16x128_f8f6f4 v[50:53], v[2:9], v[236:243], v[50:53], v198, v169 op_sel_hi:[0,0,0]
	v_mfma_scale_f32_16x16x128_f8f6f4 v[38:41], v[10:17], v[244:251], v[38:41], v198, v169 op_sel_hi:[0,0,0]
	v_mfma_scale_f32_16x16x128_f8f6f4 v[34:37], v[2:9], v[244:251], v[34:37], v198, v169 op_sel_hi:[0,0,0]
	s_setprio 0
	s_barrier
	s_add_i32 s76, 0, 0x18000
	s_add_i32 s77, 0, 0x1c000
	v_add_u32_e32 v2, s76, v200
	v_add_u32_e32 v6, s77, v200
	ds_read_b128 v[26:29], v2
	ds_read_b128 v[30:33], v2 offset:1024
	ds_read_b128 v[18:21], v2 offset:2048
	ds_read_b128 v[22:25], v2 offset:3072
	ds_read_b128 v[10:13], v6
	ds_read_b128 v[14:17], v6 offset:1024
	ds_read_b128 v[2:5], v6 offset:2048
	ds_read_b128 v[6:9], v6 offset:3072
	s_add_u32 s58, s64, 0x70000
	s_addc_u32 s59, s65, 0
	s_mov_b32 m0, s20
	v_lshl_add_u64 v[170:171], s[58:59], 0, v[164:165]
	ds_read_b128 v[206:209], v204 offset:32768
	ds_read_b128 v[210:213], v204 offset:33792
	ds_read_b128 v[214:217], v204 offset:34816
	ds_read_b128 v[218:221], v204 offset:35840
	ds_read_b128 v[236:239], v204 offset:36864
	ds_read_b128 v[240:243], v204 offset:37888
	ds_read_b128 v[244:247], v204 offset:38912
	ds_read_b128 v[248:251], v204 offset:39936
	global_load_lds_dwordx4 v[170:171], off
	v_lshl_add_u64 v[170:171], s[58:59], 0, v[178:179]
	s_mov_b32 m0, s21
	s_nop 0
	global_load_lds_dwordx4 v[170:171], off
	s_waitcnt vmcnt(8)
	s_waitcnt lgkmcnt(0)
	s_barrier
	s_setprio 1
	s_waitcnt lgkmcnt(0)
	v_mfma_scale_f32_16x16x128_f8f6f4 v[158:161], v[26:33], v[206:213], v[158:161], v198, v169 op_sel_hi:[0,0,0]
	v_mfma_scale_f32_16x16x128_f8f6f4 v[154:157], v[18:25], v[206:213], v[154:157], v198, v169 op_sel_hi:[0,0,0]
	v_mfma_scale_f32_16x16x128_f8f6f4 v[142:145], v[26:33], v[214:221], v[142:145], v198, v169 op_sel_hi:[0,0,0]
	v_mfma_scale_f32_16x16x128_f8f6f4 v[138:141], v[18:25], v[214:221], v[138:141], v198, v169 op_sel_hi:[0,0,0]
	v_mfma_scale_f32_16x16x128_f8f6f4 v[126:129], v[26:33], v[236:243], v[126:129], v198, v169 op_sel_hi:[0,0,0]
	v_mfma_scale_f32_16x16x128_f8f6f4 v[122:125], v[18:25], v[236:243], v[122:125], v198, v169 op_sel_hi:[0,0,0]
	v_mfma_scale_f32_16x16x128_f8f6f4 v[110:113], v[26:33], v[244:251], v[110:113], v198, v169 op_sel_hi:[0,0,0]
	v_mfma_scale_f32_16x16x128_f8f6f4 v[106:109], v[18:25], v[244:251], v[106:109], v198, v169 op_sel_hi:[0,0,0]
	s_setprio 0
	s_setprio 1
	v_mfma_scale_f32_16x16x128_f8f6f4 v[150:153], v[10:17], v[206:213], v[150:153], v198, v169 op_sel_hi:[0,0,0]
	v_mfma_scale_f32_16x16x128_f8f6f4 v[146:149], v[2:9], v[206:213], v[146:149], v198, v169 op_sel_hi:[0,0,0]
	v_mfma_scale_f32_16x16x128_f8f6f4 v[134:137], v[10:17], v[214:221], v[134:137], v198, v169 op_sel_hi:[0,0,0]
	v_mfma_scale_f32_16x16x128_f8f6f4 v[130:133], v[2:9], v[214:221], v[130:133], v198, v169 op_sel_hi:[0,0,0]
	v_mfma_scale_f32_16x16x128_f8f6f4 v[118:121], v[10:17], v[236:243], v[118:121], v198, v169 op_sel_hi:[0,0,0]
	v_mfma_scale_f32_16x16x128_f8f6f4 v[114:117], v[2:9], v[236:243], v[114:117], v198, v169 op_sel_hi:[0,0,0]
	v_mfma_scale_f32_16x16x128_f8f6f4 v[102:105], v[10:17], v[244:251], v[102:105], v198, v169 op_sel_hi:[0,0,0]
	v_mfma_scale_f32_16x16x128_f8f6f4 v[98:101], v[2:9], v[244:251], v[98:101], v198, v169 op_sel_hi:[0,0,0]
	s_setprio 0
	s_barrier
	s_add_i32 s58, s76, s14
	v_lshl_add_u64 v[170:171], v[186:187], 0, s[56:57]
	s_mov_b32 m0, s58
	ds_read_b128 v[206:209], v204 offset:49152
	ds_read_b128 v[210:213], v204 offset:50176
	ds_read_b128 v[214:217], v204 offset:51200
	ds_read_b128 v[218:221], v204 offset:52224
	ds_read_b128 v[236:239], v204 offset:53248
	ds_read_b128 v[240:243], v204 offset:54272
	ds_read_b128 v[244:247], v204 offset:55296
	ds_read_b128 v[248:251], v204 offset:56320
	global_load_lds_dwordx4 v[170:171], off
	s_add_i32 m0, s58, 0x2000
	s_add_u32 s58, s62, 0x70080
	v_lshl_add_u64 v[170:171], v[188:189], 0, s[56:57]
	s_addc_u32 s59, s63, 0
	s_add_i32 s62, s77, s14
	global_load_lds_dwordx4 v[170:171], off
	v_lshl_add_u64 v[170:171], s[58:59], 0, v[166:167]
	s_mov_b32 m0, s62
	s_nop 0
	global_load_lds_dwordx4 v[170:171], off
	v_lshl_add_u64 v[170:171], s[58:59], 0, v[162:163]
	s_add_i32 m0, s62, 0x2000
	s_nop 0
	global_load_lds_dwordx4 v[170:171], off
	v_lshl_add_u64 v[170:171], v[190:191], 0, s[56:57]
	s_mov_b32 m0, s24
	s_nop 0
	global_load_lds_dwordx4 v[170:171], off
	v_lshl_add_u64 v[170:171], v[192:193], 0, s[56:57]
	s_mov_b32 m0, s25
	s_nop 0
	global_load_lds_dwordx4 v[170:171], off
	s_waitcnt vmcnt(8)
	s_waitcnt lgkmcnt(0)
	s_barrier
	s_setprio 1
	s_waitcnt lgkmcnt(0)
	v_mfma_scale_f32_16x16x128_f8f6f4 v[94:97], v[26:33], v[206:213], v[94:97], v198, v169 op_sel_hi:[0,0,0]
	v_mfma_scale_f32_16x16x128_f8f6f4 v[90:93], v[18:25], v[206:213], v[90:93], v198, v169 op_sel_hi:[0,0,0]
	v_mfma_scale_f32_16x16x128_f8f6f4 v[78:81], v[26:33], v[214:221], v[78:81], v198, v169 op_sel_hi:[0,0,0]
	v_mfma_scale_f32_16x16x128_f8f6f4 v[74:77], v[18:25], v[214:221], v[74:77], v198, v169 op_sel_hi:[0,0,0]
	v_mfma_scale_f32_16x16x128_f8f6f4 v[62:65], v[26:33], v[236:243], v[62:65], v198, v169 op_sel_hi:[0,0,0]
	v_mfma_scale_f32_16x16x128_f8f6f4 v[58:61], v[18:25], v[236:243], v[58:61], v198, v169 op_sel_hi:[0,0,0]
	v_mfma_scale_f32_16x16x128_f8f6f4 v[46:49], v[26:33], v[244:251], v[46:49], v198, v169 op_sel_hi:[0,0,0]
	v_mfma_scale_f32_16x16x128_f8f6f4 v[42:45], v[18:25], v[244:251], v[42:45], v198, v169 op_sel_hi:[0,0,0]
	s_setprio 0
	s_setprio 1
	v_mfma_scale_f32_16x16x128_f8f6f4 v[86:89], v[10:17], v[206:213], v[86:89], v198, v169 op_sel_hi:[0,0,0]
	v_mfma_scale_f32_16x16x128_f8f6f4 v[82:85], v[2:9], v[206:213], v[82:85], v198, v169 op_sel_hi:[0,0,0]
	v_mfma_scale_f32_16x16x128_f8f6f4 v[70:73], v[10:17], v[214:221], v[70:73], v198, v169 op_sel_hi:[0,0,0]
	v_mfma_scale_f32_16x16x128_f8f6f4 v[66:69], v[2:9], v[214:221], v[66:69], v198, v169 op_sel_hi:[0,0,0]
	v_mfma_scale_f32_16x16x128_f8f6f4 v[54:57], v[10:17], v[236:243], v[54:57], v198, v169 op_sel_hi:[0,0,0]
	v_mfma_scale_f32_16x16x128_f8f6f4 v[50:53], v[2:9], v[236:243], v[50:53], v198, v169 op_sel_hi:[0,0,0]
	v_mfma_scale_f32_16x16x128_f8f6f4 v[38:41], v[10:17], v[244:251], v[38:41], v198, v169 op_sel_hi:[0,0,0]
	v_mfma_scale_f32_16x16x128_f8f6f4 v[34:37], v[2:9], v[244:251], v[34:37], v198, v169 op_sel_hi:[0,0,0]
	s_setprio 0
	s_add_u32 s73, s73, 0x100
	s_addc_u32 s74, s74, 0
	s_cmp_ge_i32 s75, s1
	s_mov_b64 s[58:59], s[60:61]
	s_mov_b32 s62, s75
	s_cbranch_scc1 .Lrotph8_exitbar
	s_add_i32 s75, s62, 2
	s_add_u32 s60, s58, 0x100
	s_addc_u32 s61, s59, 0
	s_add_i32 s76, 0, 0x10000
	s_cmp_eq_u32 s68, s62
	s_cselect_b32 s65, s53, s61
	s_cselect_b32 s64, s52, s60
	s_cselect_b32 s63, s55, s74
	s_cselect_b32 s62, s54, s73
	s_add_i32 s77, 0, 0x14000
	s_barrier
	s_branch .Lrotph8_body
.Lrotph8_exitbar:
	s_barrier
.Lpeelexitph8:
	v_mov_b32_e32 v209, v1
	s_and_b64 vcc, exec, s[46:47]
	s_cbranch_vccz .LBB0_927

.Lpeelph9_0:
	s_add_i32 s27, s37, 2
	s_add_u32 s40, s38, 0xfffe0080
	s_addc_u32 s41, s39, -1
	s_add_i32 s65, 0, 0x10000
	s_cmp_eq_u32 s95, s37
	s_cselect_b32 s69, s0, s41
	s_cselect_b32 s68, s1, s40
	s_cselect_b32 s41, s8, s19
	s_cselect_b32 s40, s11, s16
	s_add_i32 s37, 0, 0x14000
	v_add_u32_e32 v2, s65, v221
	v_add_u32_e32 v6, s37, v221
	ds_read_b128 v[26:29], v2
	ds_read_b128 v[30:33], v2 offset:1024
	ds_read_b128 v[18:21], v2 offset:2048
	ds_read_b128 v[22:25], v2 offset:3072
	ds_read_b128 v[10:13], v6
	ds_read_b128 v[14:17], v6 offset:1024
	ds_read_b128 v[2:5], v6 offset:2048
	ds_read_b128 v[6:9], v6 offset:3072
	v_lshl_add_u64 v[170:171], s[38:39], 0, v[192:193]
	s_add_i32 m0, s21, 0xc000
	ds_read_b128 v[194:197], v222
	ds_read_b128 v[198:201], v222 offset:1024
	ds_read_b128 v[202:205], v222 offset:2048
	ds_read_b128 v[206:209], v222 offset:3072
	ds_read_b128 v[210:213], v222 offset:4096
	ds_read_b128 v[214:217], v222 offset:5120
	ds_read_b128 v[236:239], v222 offset:6144
	ds_read_b128 v[240:243], v222 offset:7168
	global_load_lds_dwordx4 v[170:171], off
	v_lshl_add_u64 v[170:171], s[38:39], 0, v[190:191]
	s_add_i32 m0, s21, 0xe000
	s_nop 0
	global_load_lds_dwordx4 v[170:171], off
	s_waitcnt vmcnt(8)
	s_waitcnt lgkmcnt(0)
	s_barrier
	s_setprio 1
	s_waitcnt lgkmcnt(0)
	v_mfma_scale_f32_16x16x128_f8f6f4 v[94:97], v[26:33], v[194:201], 0, v183, v169 op_sel_hi:[0,0,0]
	v_mfma_scale_f32_16x16x128_f8f6f4 v[90:93], v[18:25], v[194:201], 0, v183, v169 op_sel_hi:[0,0,0]
	v_mfma_scale_f32_16x16x128_f8f6f4 v[86:89], v[26:33], v[202:209], 0, v183, v169 op_sel_hi:[0,0,0]
	v_mfma_scale_f32_16x16x128_f8f6f4 v[82:85], v[18:25], v[202:209], 0, v183, v169 op_sel_hi:[0,0,0]
	v_mfma_scale_f32_16x16x128_f8f6f4 v[78:81], v[26:33], v[210:217], 0, v183, v169 op_sel_hi:[0,0,0]
	v_mfma_scale_f32_16x16x128_f8f6f4 v[74:77], v[18:25], v[210:217], 0, v183, v169 op_sel_hi:[0,0,0]
	v_mfma_scale_f32_16x16x128_f8f6f4 v[70:73], v[26:33], v[236:243], 0, v183, v169 op_sel_hi:[0,0,0]
	v_mfma_scale_f32_16x16x128_f8f6f4 v[66:69], v[18:25], v[236:243], 0, v183, v169 op_sel_hi:[0,0,0]
	s_setprio 0
	s_setprio 1
	v_mfma_scale_f32_16x16x128_f8f6f4 v[158:161], v[10:17], v[194:201], 0, v183, v169 op_sel_hi:[0,0,0]
	v_mfma_scale_f32_16x16x128_f8f6f4 v[154:157], v[2:9], v[194:201], 0, v183, v169 op_sel_hi:[0,0,0]
	v_mfma_scale_f32_16x16x128_f8f6f4 v[150:153], v[10:17], v[202:209], 0, v183, v169 op_sel_hi:[0,0,0]
	v_mfma_scale_f32_16x16x128_f8f6f4 v[146:149], v[2:9], v[202:209], 0, v183, v169 op_sel_hi:[0,0,0]
	v_mfma_scale_f32_16x16x128_f8f6f4 v[142:145], v[10:17], v[210:217], 0, v183, v169 op_sel_hi:[0,0,0]
	v_mfma_scale_f32_16x16x128_f8f6f4 v[138:141], v[2:9], v[210:217], 0, v183, v169 op_sel_hi:[0,0,0]
	v_mfma_scale_f32_16x16x128_f8f6f4 v[134:137], v[10:17], v[236:243], 0, v183, v169 op_sel_hi:[0,0,0]
	v_mfma_scale_f32_16x16x128_f8f6f4 v[130:133], v[2:9], v[236:243], 0, v183, v169 op_sel_hi:[0,0,0]
	s_setprio 0
	s_barrier
	s_add_i32 s65, s65, s20
	v_lshl_add_u64 v[194:195], s[40:41], 0, v[162:163]
	s_mov_b32 m0, s65
	ds_read_b128 v[202:205], v222 offset:16384
	ds_read_b128 v[206:209], v222 offset:17408
	ds_read_b128 v[210:213], v222 offset:18432
	ds_read_b128 v[214:217], v222 offset:19456
	ds_read_b128 v[236:239], v222 offset:20480
	ds_read_b128 v[240:243], v222 offset:21504
	ds_read_b128 v[244:247], v222 offset:22528
	ds_read_b128 v[248:251], v222 offset:23552
	global_load_lds_dwordx4 v[194:195], off
	s_add_i32 m0, s65, 0x2000
	s_add_u32 s70, s40, 0x20000
	v_lshl_add_u64 v[196:197], s[40:41], 0, v[164:165]
	s_addc_u32 s71, s41, 0
	s_add_i32 s37, s37, s20
	global_load_lds_dwordx4 v[196:197], off
	v_lshl_add_u64 v[170:171], s[70:71], 0, v[162:163]
	s_mov_b32 m0, s37
	v_lshl_add_u64 v[198:199], s[68:69], 0, v[178:179]
	global_load_lds_dwordx4 v[170:171], off
	v_lshl_add_u64 v[170:171], s[70:71], 0, v[164:165]
	s_add_i32 m0, s37, 0x2000
	v_lshl_add_u64 v[200:201], s[68:69], 0, v[180:181]
	global_load_lds_dwordx4 v[170:171], off
	s_mov_b32 m0, s21
	s_nop 0
	global_load_lds_dwordx4 v[198:199], off
	s_mov_b32 m0, s22
	s_nop 0
	global_load_lds_dwordx4 v[200:201], off
	s_waitcnt vmcnt(8)
	s_waitcnt lgkmcnt(0)
	s_barrier
	s_setprio 1
	s_waitcnt lgkmcnt(0)
	v_mfma_scale_f32_16x16x128_f8f6f4 v[62:65], v[26:33], v[202:209], 0, v183, v169 op_sel_hi:[0,0,0]
	v_mfma_scale_f32_16x16x128_f8f6f4 v[58:61], v[18:25], v[202:209], 0, v183, v169 op_sel_hi:[0,0,0]
	v_mfma_scale_f32_16x16x128_f8f6f4 v[54:57], v[26:33], v[210:217], 0, v183, v169 op_sel_hi:[0,0,0]
	v_mfma_scale_f32_16x16x128_f8f6f4 v[50:53], v[18:25], v[210:217], 0, v183, v169 op_sel_hi:[0,0,0]
	v_mfma_scale_f32_16x16x128_f8f6f4 v[46:49], v[26:33], v[236:243], 0, v183, v169 op_sel_hi:[0,0,0]
	v_mfma_scale_f32_16x16x128_f8f6f4 v[42:45], v[18:25], v[236:243], 0, v183, v169 op_sel_hi:[0,0,0]
	v_mfma_scale_f32_16x16x128_f8f6f4 v[38:41], v[26:33], v[244:251], 0, v183, v169 op_sel_hi:[0,0,0]
	v_mfma_scale_f32_16x16x128_f8f6f4 v[34:37], v[18:25], v[244:251], 0, v183, v169 op_sel_hi:[0,0,0]
	s_setprio 0
	s_setprio 1
	v_mfma_scale_f32_16x16x128_f8f6f4 v[126:129], v[10:17], v[202:209], 0, v183, v169 op_sel_hi:[0,0,0]
	v_mfma_scale_f32_16x16x128_f8f6f4 v[122:125], v[2:9], v[202:209], 0, v183, v169 op_sel_hi:[0,0,0]
	v_mfma_scale_f32_16x16x128_f8f6f4 v[118:121], v[10:17], v[210:217], 0, v183, v169 op_sel_hi:[0,0,0]
	v_mfma_scale_f32_16x16x128_f8f6f4 v[114:117], v[2:9], v[210:217], 0, v183, v169 op_sel_hi:[0,0,0]
	v_mfma_scale_f32_16x16x128_f8f6f4 v[110:113], v[10:17], v[236:243], 0, v183, v169 op_sel_hi:[0,0,0]
	v_mfma_scale_f32_16x16x128_f8f6f4 v[106:109], v[2:9], v[236:243], 0, v183, v169 op_sel_hi:[0,0,0]
	v_mfma_scale_f32_16x16x128_f8f6f4 v[102:105], v[10:17], v[244:251], 0, v183, v169 op_sel_hi:[0,0,0]
	v_mfma_scale_f32_16x16x128_f8f6f4 v[98:101], v[2:9], v[244:251], 0, v183, v169 op_sel_hi:[0,0,0]
	s_setprio 0
	s_barrier
	s_add_i32 s37, 0, 0x18000
	s_add_i32 s65, 0, 0x1c000
	v_add_u32_e32 v2, s37, v221
	v_add_u32_e32 v6, s65, v221
	ds_read_b128 v[26:29], v2
	ds_read_b128 v[30:33], v2 offset:1024
	ds_read_b128 v[18:21], v2 offset:2048
	ds_read_b128 v[22:25], v2 offset:3072
	ds_read_b128 v[10:13], v6
	ds_read_b128 v[14:17], v6 offset:1024
	ds_read_b128 v[2:5], v6 offset:2048
	ds_read_b128 v[6:9], v6 offset:3072
	s_add_u32 s68, s68, 0x20000
	s_addc_u32 s69, s69, 0
	s_mov_b32 m0, s23
	v_lshl_add_u64 v[170:171], s[68:69], 0, v[178:179]
	ds_read_b128 v[202:205], v222 offset:32768
	ds_read_b128 v[206:209], v222 offset:33792
	ds_read_b128 v[210:213], v222 offset:34816
	ds_read_b128 v[214:217], v222 offset:35840
	ds_read_b128 v[236:239], v222 offset:36864
	ds_read_b128 v[240:243], v222 offset:37888
	ds_read_b128 v[244:247], v222 offset:38912
	ds_read_b128 v[248:251], v222 offset:39936
	global_load_lds_dwordx4 v[170:171], off
	v_lshl_add_u64 v[170:171], s[68:69], 0, v[180:181]
	s_mov_b32 m0, s12
	s_nop 0
	global_load_lds_dwordx4 v[170:171], off
	s_waitcnt vmcnt(8)
	s_waitcnt lgkmcnt(0)
	s_barrier
	s_setprio 1
	s_waitcnt lgkmcnt(0)
	v_mfma_scale_f32_16x16x128_f8f6f4 v[94:97], v[26:33], v[202:209], v[94:97], v183, v169 op_sel_hi:[0,0,0]
	v_mfma_scale_f32_16x16x128_f8f6f4 v[90:93], v[18:25], v[202:209], v[90:93], v183, v169 op_sel_hi:[0,0,0]
	v_mfma_scale_f32_16x16x128_f8f6f4 v[86:89], v[26:33], v[210:217], v[86:89], v183, v169 op_sel_hi:[0,0,0]
	v_mfma_scale_f32_16x16x128_f8f6f4 v[82:85], v[18:25], v[210:217], v[82:85], v183, v169 op_sel_hi:[0,0,0]
	v_mfma_scale_f32_16x16x128_f8f6f4 v[78:81], v[26:33], v[236:243], v[78:81], v183, v169 op_sel_hi:[0,0,0]
	v_mfma_scale_f32_16x16x128_f8f6f4 v[74:77], v[18:25], v[236:243], v[74:77], v183, v169 op_sel_hi:[0,0,0]
	v_mfma_scale_f32_16x16x128_f8f6f4 v[70:73], v[26:33], v[244:251], v[70:73], v183, v169 op_sel_hi:[0,0,0]
	v_mfma_scale_f32_16x16x128_f8f6f4 v[66:69], v[18:25], v[244:251], v[66:69], v183, v169 op_sel_hi:[0,0,0]
	s_setprio 0
	s_setprio 1
	v_mfma_scale_f32_16x16x128_f8f6f4 v[158:161], v[10:17], v[202:209], v[158:161], v183, v169 op_sel_hi:[0,0,0]
	v_mfma_scale_f32_16x16x128_f8f6f4 v[154:157], v[2:9], v[202:209], v[154:157], v183, v169 op_sel_hi:[0,0,0]
	v_mfma_scale_f32_16x16x128_f8f6f4 v[150:153], v[10:17], v[210:217], v[150:153], v183, v169 op_sel_hi:[0,0,0]
	v_mfma_scale_f32_16x16x128_f8f6f4 v[146:149], v[2:9], v[210:217], v[146:149], v183, v169 op_sel_hi:[0,0,0]
	v_mfma_scale_f32_16x16x128_f8f6f4 v[142:145], v[10:17], v[236:243], v[142:145], v183, v169 op_sel_hi:[0,0,0]
	v_mfma_scale_f32_16x16x128_f8f6f4 v[138:141], v[2:9], v[236:243], v[138:141], v183, v169 op_sel_hi:[0,0,0]
	v_mfma_scale_f32_16x16x128_f8f6f4 v[134:137], v[10:17], v[244:251], v[134:137], v183, v169 op_sel_hi:[0,0,0]
	v_mfma_scale_f32_16x16x128_f8f6f4 v[130:133], v[2:9], v[244:251], v[130:133], v183, v169 op_sel_hi:[0,0,0]
	s_setprio 0
	s_barrier
	s_add_i32 s37, s37, s20
	v_lshl_add_u64 v[170:171], v[194:195], 0, s[56:57]
	s_mov_b32 m0, s37
	ds_read_b128 v[202:205], v222 offset:49152
	ds_read_b128 v[206:209], v222 offset:50176
	ds_read_b128 v[210:213], v222 offset:51200
	ds_read_b128 v[214:217], v222 offset:52224
	ds_read_b128 v[236:239], v222 offset:53248
	ds_read_b128 v[240:243], v222 offset:54272
	ds_read_b128 v[244:247], v222 offset:55296
	ds_read_b128 v[248:251], v222 offset:56320
	global_load_lds_dwordx4 v[170:171], off
	s_add_i32 m0, s37, 0x2000
	s_add_u32 s40, s40, 0x20080
	v_lshl_add_u64 v[170:171], v[196:197], 0, s[56:57]
	s_addc_u32 s41, s41, 0
	s_add_i32 s37, s65, s20
	global_load_lds_dwordx4 v[170:171], off
	v_lshl_add_u64 v[170:171], s[40:41], 0, v[162:163]
	s_mov_b32 m0, s37
	s_nop 0
	global_load_lds_dwordx4 v[170:171], off
	v_lshl_add_u64 v[170:171], s[40:41], 0, v[164:165]
	s_add_i32 m0, s37, 0x2000
	s_nop 0
	global_load_lds_dwordx4 v[170:171], off
	v_lshl_add_u64 v[170:171], v[198:199], 0, s[56:57]
	s_mov_b32 m0, s92
	s_nop 0
	global_load_lds_dwordx4 v[170:171], off
	v_lshl_add_u64 v[170:171], v[200:201], 0, s[56:57]
	s_mov_b32 m0, s93
	s_nop 0
	global_load_lds_dwordx4 v[170:171], off
	s_waitcnt vmcnt(8)
	s_waitcnt lgkmcnt(0)
	s_barrier
	s_setprio 1
	s_waitcnt lgkmcnt(0)
	v_mfma_scale_f32_16x16x128_f8f6f4 v[62:65], v[26:33], v[202:209], v[62:65], v183, v169 op_sel_hi:[0,0,0]
	v_mfma_scale_f32_16x16x128_f8f6f4 v[58:61], v[18:25], v[202:209], v[58:61], v183, v169 op_sel_hi:[0,0,0]
	v_mfma_scale_f32_16x16x128_f8f6f4 v[54:57], v[26:33], v[210:217], v[54:57], v183, v169 op_sel_hi:[0,0,0]
	v_mfma_scale_f32_16x16x128_f8f6f4 v[50:53], v[18:25], v[210:217], v[50:53], v183, v169 op_sel_hi:[0,0,0]
	v_mfma_scale_f32_16x16x128_f8f6f4 v[46:49], v[26:33], v[236:243], v[46:49], v183, v169 op_sel_hi:[0,0,0]
	v_mfma_scale_f32_16x16x128_f8f6f4 v[42:45], v[18:25], v[236:243], v[42:45], v183, v169 op_sel_hi:[0,0,0]
	v_mfma_scale_f32_16x16x128_f8f6f4 v[38:41], v[26:33], v[244:251], v[38:41], v183, v169 op_sel_hi:[0,0,0]
	v_mfma_scale_f32_16x16x128_f8f6f4 v[34:37], v[18:25], v[244:251], v[34:37], v183, v169 op_sel_hi:[0,0,0]
	s_setprio 0
	s_setprio 1
	v_mfma_scale_f32_16x16x128_f8f6f4 v[126:129], v[10:17], v[202:209], v[126:129], v183, v169 op_sel_hi:[0,0,0]
	v_mfma_scale_f32_16x16x128_f8f6f4 v[122:125], v[2:9], v[202:209], v[122:125], v183, v169 op_sel_hi:[0,0,0]
	v_mfma_scale_f32_16x16x128_f8f6f4 v[118:121], v[10:17], v[210:217], v[118:121], v183, v169 op_sel_hi:[0,0,0]
	v_mfma_scale_f32_16x16x128_f8f6f4 v[114:117], v[2:9], v[210:217], v[114:117], v183, v169 op_sel_hi:[0,0,0]
	v_mfma_scale_f32_16x16x128_f8f6f4 v[110:113], v[10:17], v[236:243], v[110:113], v183, v169 op_sel_hi:[0,0,0]
	v_mfma_scale_f32_16x16x128_f8f6f4 v[106:109], v[2:9], v[236:243], v[106:109], v183, v169 op_sel_hi:[0,0,0]
	v_mfma_scale_f32_16x16x128_f8f6f4 v[102:105], v[10:17], v[244:251], v[102:105], v183, v169 op_sel_hi:[0,0,0]
	v_mfma_scale_f32_16x16x128_f8f6f4 v[98:101], v[2:9], v[244:251], v[98:101], v183, v169 op_sel_hi:[0,0,0]
	s_setprio 0
	s_add_u32 s16, s16, 0x100
	s_addc_u32 s19, s19, 0
	s_add_u32 s38, s38, 0x100
	s_addc_u32 s39, s39, 0
	s_cmp_ge_i32 s27, s74
	s_mov_b32 s37, s27
	s_cbranch_scc1 .Lrotph9_pexitbar
	s_add_i32 s27, s37, 2
	s_add_u32 s40, s38, 0xfffe0080
	s_addc_u32 s41, s39, -1
	s_add_i32 s65, 0, 0x10000
	s_cmp_eq_u32 s95, s37
	s_cselect_b32 s69, s0, s41
	s_cselect_b32 s68, s1, s40
	s_cselect_b32 s41, s8, s19
	s_cselect_b32 s40, s11, s16
	s_add_i32 s37, 0, 0x14000
	s_barrier
	s_branch .Lrotph9_body

.Lrotph9_body:
	v_add_u32_e32 v2, s65, v221
	v_add_u32_e32 v6, s37, v221
	ds_read_b128 v[26:29], v2
	ds_read_b128 v[30:33], v2 offset:1024
	ds_read_b128 v[18:21], v2 offset:2048
	ds_read_b128 v[22:25], v2 offset:3072
	ds_read_b128 v[10:13], v6
	ds_read_b128 v[14:17], v6 offset:1024
	ds_read_b128 v[2:5], v6 offset:2048
	ds_read_b128 v[6:9], v6 offset:3072
	v_lshl_add_u64 v[170:171], s[38:39], 0, v[192:193]
	s_add_i32 m0, s21, 0xc000
	ds_read_b128 v[194:197], v222
	ds_read_b128 v[198:201], v222 offset:1024
	ds_read_b128 v[202:205], v222 offset:2048
	ds_read_b128 v[206:209], v222 offset:3072
	ds_read_b128 v[210:213], v222 offset:4096
	ds_read_b128 v[214:217], v222 offset:5120
	ds_read_b128 v[236:239], v222 offset:6144
	ds_read_b128 v[240:243], v222 offset:7168
	global_load_lds_dwordx4 v[170:171], off
	v_lshl_add_u64 v[170:171], s[38:39], 0, v[190:191]
	s_add_i32 m0, s21, 0xe000
	s_nop 0
	global_load_lds_dwordx4 v[170:171], off
	s_waitcnt vmcnt(8)
	s_waitcnt lgkmcnt(0)
	s_barrier
	s_setprio 1
	s_waitcnt lgkmcnt(0)
	v_mfma_scale_f32_16x16x128_f8f6f4 v[94:97], v[26:33], v[194:201], v[94:97], v183, v169 op_sel_hi:[0,0,0]
	v_mfma_scale_f32_16x16x128_f8f6f4 v[90:93], v[18:25], v[194:201], v[90:93], v183, v169 op_sel_hi:[0,0,0]
	v_mfma_scale_f32_16x16x128_f8f6f4 v[86:89], v[26:33], v[202:209], v[86:89], v183, v169 op_sel_hi:[0,0,0]
	v_mfma_scale_f32_16x16x128_f8f6f4 v[82:85], v[18:25], v[202:209], v[82:85], v183, v169 op_sel_hi:[0,0,0]
	v_mfma_scale_f32_16x16x128_f8f6f4 v[78:81], v[26:33], v[210:217], v[78:81], v183, v169 op_sel_hi:[0,0,0]
	v_mfma_scale_f32_16x16x128_f8f6f4 v[74:77], v[18:25], v[210:217], v[74:77], v183, v169 op_sel_hi:[0,0,0]
	v_mfma_scale_f32_16x16x128_f8f6f4 v[70:73], v[26:33], v[236:243], v[70:73], v183, v169 op_sel_hi:[0,0,0]
	v_mfma_scale_f32_16x16x128_f8f6f4 v[66:69], v[18:25], v[236:243], v[66:69], v183, v169 op_sel_hi:[0,0,0]
	s_setprio 0
	s_setprio 1
	v_mfma_scale_f32_16x16x128_f8f6f4 v[158:161], v[10:17], v[194:201], v[158:161], v183, v169 op_sel_hi:[0,0,0]
	v_mfma_scale_f32_16x16x128_f8f6f4 v[154:157], v[2:9], v[194:201], v[154:157], v183, v169 op_sel_hi:[0,0,0]
	v_mfma_scale_f32_16x16x128_f8f6f4 v[150:153], v[10:17], v[202:209], v[150:153], v183, v169 op_sel_hi:[0,0,0]
	v_mfma_scale_f32_16x16x128_f8f6f4 v[146:149], v[2:9], v[202:209], v[146:149], v183, v169 op_sel_hi:[0,0,0]
	v_mfma_scale_f32_16x16x128_f8f6f4 v[142:145], v[10:17], v[210:217], v[142:145], v183, v169 op_sel_hi:[0,0,0]
	v_mfma_scale_f32_16x16x128_f8f6f4 v[138:141], v[2:9], v[210:217], v[138:141], v183, v169 op_sel_hi:[0,0,0]
	v_mfma_scale_f32_16x16x128_f8f6f4 v[134:137], v[10:17], v[236:243], v[134:137], v183, v169 op_sel_hi:[0,0,0]
	v_mfma_scale_f32_16x16x128_f8f6f4 v[130:133], v[2:9], v[236:243], v[130:133], v183, v169 op_sel_hi:[0,0,0]
	s_setprio 0
	s_barrier
	s_add_i32 s65, s65, s20
	v_lshl_add_u64 v[194:195], s[40:41], 0, v[162:163]
	s_mov_b32 m0, s65
	ds_read_b128 v[202:205], v222 offset:16384
	ds_read_b128 v[206:209], v222 offset:17408
	ds_read_b128 v[210:213], v222 offset:18432
	ds_read_b128 v[214:217], v222 offset:19456
	ds_read_b128 v[236:239], v222 offset:20480
	ds_read_b128 v[240:243], v222 offset:21504
	ds_read_b128 v[244:247], v222 offset:22528
	ds_read_b128 v[248:251], v222 offset:23552
	global_load_lds_dwordx4 v[194:195], off
	s_add_i32 m0, s65, 0x2000
	s_add_u32 s70, s40, 0x20000
	v_lshl_add_u64 v[196:197], s[40:41], 0, v[164:165]
	s_addc_u32 s71, s41, 0
	s_add_i32 s37, s37, s20
	global_load_lds_dwordx4 v[196:197], off
	v_lshl_add_u64 v[170:171], s[70:71], 0, v[162:163]
	s_mov_b32 m0, s37
	v_lshl_add_u64 v[198:199], s[68:69], 0, v[178:179]
	global_load_lds_dwordx4 v[170:171], off
	v_lshl_add_u64 v[170:171], s[70:71], 0, v[164:165]
	s_add_i32 m0, s37, 0x2000
	v_lshl_add_u64 v[200:201], s[68:69], 0, v[180:181]
	global_load_lds_dwordx4 v[170:171], off
	s_mov_b32 m0, s21
	s_nop 0
	global_load_lds_dwordx4 v[198:199], off
	s_mov_b32 m0, s22
	s_nop 0
	global_load_lds_dwordx4 v[200:201], off
	s_waitcnt vmcnt(8)
	s_waitcnt lgkmcnt(0)
	s_barrier
	s_setprio 1
	s_waitcnt lgkmcnt(0)
	v_mfma_scale_f32_16x16x128_f8f6f4 v[62:65], v[26:33], v[202:209], v[62:65], v183, v169 op_sel_hi:[0,0,0]
	v_mfma_scale_f32_16x16x128_f8f6f4 v[58:61], v[18:25], v[202:209], v[58:61], v183, v169 op_sel_hi:[0,0,0]
	v_mfma_scale_f32_16x16x128_f8f6f4 v[54:57], v[26:33], v[210:217], v[54:57], v183, v169 op_sel_hi:[0,0,0]
	v_mfma_scale_f32_16x16x128_f8f6f4 v[50:53], v[18:25], v[210:217], v[50:53], v183, v169 op_sel_hi:[0,0,0]
	v_mfma_scale_f32_16x16x128_f8f6f4 v[46:49], v[26:33], v[236:243], v[46:49], v183, v169 op_sel_hi:[0,0,0]
	v_mfma_scale_f32_16x16x128_f8f6f4 v[42:45], v[18:25], v[236:243], v[42:45], v183, v169 op_sel_hi:[0,0,0]
	v_mfma_scale_f32_16x16x128_f8f6f4 v[38:41], v[26:33], v[244:251], v[38:41], v183, v169 op_sel_hi:[0,0,0]
	v_mfma_scale_f32_16x16x128_f8f6f4 v[34:37], v[18:25], v[244:251], v[34:37], v183, v169 op_sel_hi:[0,0,0]
	s_setprio 0
	s_setprio 1
	v_mfma_scale_f32_16x16x128_f8f6f4 v[126:129], v[10:17], v[202:209], v[126:129], v183, v169 op_sel_hi:[0,0,0]
	v_mfma_scale_f32_16x16x128_f8f6f4 v[122:125], v[2:9], v[202:209], v[122:125], v183, v169 op_sel_hi:[0,0,0]
	v_mfma_scale_f32_16x16x128_f8f6f4 v[118:121], v[10:17], v[210:217], v[118:121], v183, v169 op_sel_hi:[0,0,0]
	v_mfma_scale_f32_16x16x128_f8f6f4 v[114:117], v[2:9], v[210:217], v[114:117], v183, v169 op_sel_hi:[0,0,0]
	v_mfma_scale_f32_16x16x128_f8f6f4 v[110:113], v[10:17], v[236:243], v[110:113], v183, v169 op_sel_hi:[0,0,0]
	v_mfma_scale_f32_16x16x128_f8f6f4 v[106:109], v[2:9], v[236:243], v[106:109], v183, v169 op_sel_hi:[0,0,0]
	v_mfma_scale_f32_16x16x128_f8f6f4 v[102:105], v[10:17], v[244:251], v[102:105], v183, v169 op_sel_hi:[0,0,0]
	v_mfma_scale_f32_16x16x128_f8f6f4 v[98:101], v[2:9], v[244:251], v[98:101], v183, v169 op_sel_hi:[0,0,0]
	s_setprio 0
	s_barrier
	s_add_i32 s37, 0, 0x18000
	s_add_i32 s65, 0, 0x1c000
	v_add_u32_e32 v2, s37, v221
	v_add_u32_e32 v6, s65, v221
	ds_read_b128 v[26:29], v2
	ds_read_b128 v[30:33], v2 offset:1024
	ds_read_b128 v[18:21], v2 offset:2048
	ds_read_b128 v[22:25], v2 offset:3072
	ds_read_b128 v[10:13], v6
	ds_read_b128 v[14:17], v6 offset:1024
	ds_read_b128 v[2:5], v6 offset:2048
	ds_read_b128 v[6:9], v6 offset:3072
	s_add_u32 s68, s68, 0x20000
	s_addc_u32 s69, s69, 0
	s_mov_b32 m0, s23
	v_lshl_add_u64 v[170:171], s[68:69], 0, v[178:179]
	ds_read_b128 v[202:205], v222 offset:32768
	ds_read_b128 v[206:209], v222 offset:33792
	ds_read_b128 v[210:213], v222 offset:34816
	ds_read_b128 v[214:217], v222 offset:35840
	ds_read_b128 v[236:239], v222 offset:36864
	ds_read_b128 v[240:243], v222 offset:37888
	ds_read_b128 v[244:247], v222 offset:38912
	ds_read_b128 v[248:251], v222 offset:39936
	global_load_lds_dwordx4 v[170:171], off
	v_lshl_add_u64 v[170:171], s[68:69], 0, v[180:181]
	s_mov_b32 m0, s12
	s_nop 0
	global_load_lds_dwordx4 v[170:171], off
	s_waitcnt vmcnt(8)
	s_waitcnt lgkmcnt(0)
	s_barrier
	s_setprio 1
	s_waitcnt lgkmcnt(0)
	v_mfma_scale_f32_16x16x128_f8f6f4 v[94:97], v[26:33], v[202:209], v[94:97], v183, v169 op_sel_hi:[0,0,0]
	v_mfma_scale_f32_16x16x128_f8f6f4 v[90:93], v[18:25], v[202:209], v[90:93], v183, v169 op_sel_hi:[0,0,0]
	v_mfma_scale_f32_16x16x128_f8f6f4 v[86:89], v[26:33], v[210:217], v[86:89], v183, v169 op_sel_hi:[0,0,0]
	v_mfma_scale_f32_16x16x128_f8f6f4 v[82:85], v[18:25], v[210:217], v[82:85], v183, v169 op_sel_hi:[0,0,0]
	v_mfma_scale_f32_16x16x128_f8f6f4 v[78:81], v[26:33], v[236:243], v[78:81], v183, v169 op_sel_hi:[0,0,0]
	v_mfma_scale_f32_16x16x128_f8f6f4 v[74:77], v[18:25], v[236:243], v[74:77], v183, v169 op_sel_hi:[0,0,0]
	v_mfma_scale_f32_16x16x128_f8f6f4 v[70:73], v[26:33], v[244:251], v[70:73], v183, v169 op_sel_hi:[0,0,0]
	v_mfma_scale_f32_16x16x128_f8f6f4 v[66:69], v[18:25], v[244:251], v[66:69], v183, v169 op_sel_hi:[0,0,0]
	s_setprio 0
	s_setprio 1
	v_mfma_scale_f32_16x16x128_f8f6f4 v[158:161], v[10:17], v[202:209], v[158:161], v183, v169 op_sel_hi:[0,0,0]
	v_mfma_scale_f32_16x16x128_f8f6f4 v[154:157], v[2:9], v[202:209], v[154:157], v183, v169 op_sel_hi:[0,0,0]
	v_mfma_scale_f32_16x16x128_f8f6f4 v[150:153], v[10:17], v[210:217], v[150:153], v183, v169 op_sel_hi:[0,0,0]
	v_mfma_scale_f32_16x16x128_f8f6f4 v[146:149], v[2:9], v[210:217], v[146:149], v183, v169 op_sel_hi:[0,0,0]
	v_mfma_scale_f32_16x16x128_f8f6f4 v[142:145], v[10:17], v[236:243], v[142:145], v183, v169 op_sel_hi:[0,0,0]
	v_mfma_scale_f32_16x16x128_f8f6f4 v[138:141], v[2:9], v[236:243], v[138:141], v183, v169 op_sel_hi:[0,0,0]
	v_mfma_scale_f32_16x16x128_f8f6f4 v[134:137], v[10:17], v[244:251], v[134:137], v183, v169 op_sel_hi:[0,0,0]
	v_mfma_scale_f32_16x16x128_f8f6f4 v[130:133], v[2:9], v[244:251], v[130:133], v183, v169 op_sel_hi:[0,0,0]
	s_setprio 0
	s_barrier
	s_add_i32 s37, s37, s20
	v_lshl_add_u64 v[170:171], v[194:195], 0, s[56:57]
	s_mov_b32 m0, s37
	ds_read_b128 v[202:205], v222 offset:49152
	ds_read_b128 v[206:209], v222 offset:50176
	ds_read_b128 v[210:213], v222 offset:51200
	ds_read_b128 v[214:217], v222 offset:52224
	ds_read_b128 v[236:239], v222 offset:53248
	ds_read_b128 v[240:243], v222 offset:54272
	ds_read_b128 v[244:247], v222 offset:55296
	ds_read_b128 v[248:251], v222 offset:56320
	global_load_lds_dwordx4 v[170:171], off
	s_add_i32 m0, s37, 0x2000
	s_add_u32 s40, s40, 0x20080
	v_lshl_add_u64 v[170:171], v[196:197], 0, s[56:57]
	s_addc_u32 s41, s41, 0
	s_add_i32 s37, s65, s20
	global_load_lds_dwordx4 v[170:171], off
	v_lshl_add_u64 v[170:171], s[40:41], 0, v[162:163]
	s_mov_b32 m0, s37
	s_nop 0
	global_load_lds_dwordx4 v[170:171], off
	v_lshl_add_u64 v[170:171], s[40:41], 0, v[164:165]
	s_add_i32 m0, s37, 0x2000
	s_nop 0
	global_load_lds_dwordx4 v[170:171], off
	v_lshl_add_u64 v[170:171], v[198:199], 0, s[56:57]
	s_mov_b32 m0, s92
	s_nop 0
	global_load_lds_dwordx4 v[170:171], off
	v_lshl_add_u64 v[170:171], v[200:201], 0, s[56:57]
	s_mov_b32 m0, s93
	s_nop 0
	global_load_lds_dwordx4 v[170:171], off
	s_waitcnt vmcnt(8)
	s_waitcnt lgkmcnt(0)
	s_barrier
	s_setprio 1
	s_waitcnt lgkmcnt(0)
	v_mfma_scale_f32_16x16x128_f8f6f4 v[62:65], v[26:33], v[202:209], v[62:65], v183, v169 op_sel_hi:[0,0,0]
	v_mfma_scale_f32_16x16x128_f8f6f4 v[58:61], v[18:25], v[202:209], v[58:61], v183, v169 op_sel_hi:[0,0,0]
	v_mfma_scale_f32_16x16x128_f8f6f4 v[54:57], v[26:33], v[210:217], v[54:57], v183, v169 op_sel_hi:[0,0,0]
	v_mfma_scale_f32_16x16x128_f8f6f4 v[50:53], v[18:25], v[210:217], v[50:53], v183, v169 op_sel_hi:[0,0,0]
	v_mfma_scale_f32_16x16x128_f8f6f4 v[46:49], v[26:33], v[236:243], v[46:49], v183, v169 op_sel_hi:[0,0,0]
	v_mfma_scale_f32_16x16x128_f8f6f4 v[42:45], v[18:25], v[236:243], v[42:45], v183, v169 op_sel_hi:[0,0,0]
	v_mfma_scale_f32_16x16x128_f8f6f4 v[38:41], v[26:33], v[244:251], v[38:41], v183, v169 op_sel_hi:[0,0,0]
	v_mfma_scale_f32_16x16x128_f8f6f4 v[34:37], v[18:25], v[244:251], v[34:37], v183, v169 op_sel_hi:[0,0,0]
	s_setprio 0
	s_setprio 1
	v_mfma_scale_f32_16x16x128_f8f6f4 v[126:129], v[10:17], v[202:209], v[126:129], v183, v169 op_sel_hi:[0,0,0]
	v_mfma_scale_f32_16x16x128_f8f6f4 v[122:125], v[2:9], v[202:209], v[122:125], v183, v169 op_sel_hi:[0,0,0]
	v_mfma_scale_f32_16x16x128_f8f6f4 v[118:121], v[10:17], v[210:217], v[118:121], v183, v169 op_sel_hi:[0,0,0]
	v_mfma_scale_f32_16x16x128_f8f6f4 v[114:117], v[2:9], v[210:217], v[114:117], v183, v169 op_sel_hi:[0,0,0]
	v_mfma_scale_f32_16x16x128_f8f6f4 v[110:113], v[10:17], v[236:243], v[110:113], v183, v169 op_sel_hi:[0,0,0]
	v_mfma_scale_f32_16x16x128_f8f6f4 v[106:109], v[2:9], v[236:243], v[106:109], v183, v169 op_sel_hi:[0,0,0]
	v_mfma_scale_f32_16x16x128_f8f6f4 v[102:105], v[10:17], v[244:251], v[102:105], v183, v169 op_sel_hi:[0,0,0]
	v_mfma_scale_f32_16x16x128_f8f6f4 v[98:101], v[2:9], v[244:251], v[98:101], v183, v169 op_sel_hi:[0,0,0]
	s_setprio 0
	s_add_u32 s16, s16, 0x100
	s_addc_u32 s19, s19, 0
	s_add_u32 s38, s38, 0x100
	s_addc_u32 s39, s39, 0
	s_cmp_ge_i32 s27, s74
	s_mov_b32 s37, s27
	s_cbranch_scc1 .Lrotph9_exitbar
	s_add_i32 s27, s37, 2
	s_add_u32 s40, s38, 0xfffe0080
	s_addc_u32 s41, s39, -1
	s_add_i32 s65, 0, 0x10000
	s_cmp_eq_u32 s95, s37
	s_cselect_b32 s69, s0, s41
	s_cselect_b32 s68, s1, s40
	s_cselect_b32 s41, s8, s19
	s_cselect_b32 s40, s11, s16
	s_add_i32 s37, 0, 0x14000
	s_barrier
	s_branch .Lrotph9_body
.Lrotph9_exitbar:
	s_barrier
.Lpeelexitph9:
	s_mov_b64 s[70:71], 0xe800800
	v_mov_b32_e32 v209, v1
	s_and_b64 vcc, exec, s[52:53]
	s_cbranch_vccz .LBB0_1019

.Lpeelph12_0:
	s_add_i32 s66, s54, 2
	s_add_u32 s55, s52, 0xfffc0080
	s_addc_u32 s58, s53, -1
	s_add_i32 s68, 0, 0x10000
	s_cmp_eq_u32 s60, s54
	s_cselect_b32 s59, s41, s58
	s_cselect_b32 s58, s43, s55
	v_add_u32_e32 v144, s68, v147
	s_cselect_b32 s55, s62, s65
	s_cselect_b32 s54, s63, s64
	s_add_i32 s70, 0, 0x14000
	ds_read_b128 v[140:143], v144
	ds_read_b128 v[150:153], v144 offset:1024
	ds_read_b128 v[154:157], v144 offset:2048
	ds_read_b128 v[158:161], v144 offset:3072
	v_add_u32_e32 v144, s70, v147
	ds_read_b128 v[162:165], v144
	ds_read_b128 v[170:173], v144 offset:1024
	ds_read_b128 v[174:177], v144 offset:2048
	ds_read_b128 v[178:181], v144 offset:3072
	v_lshl_add_u64 v[144:145], s[52:53], 0, v[138:139]
	s_add_i32 m0, s16, 0xc000
	ds_read_b128 v[182:185], v149
	ds_read_b128 v[186:189], v149 offset:1024
	ds_read_b128 v[190:193], v149 offset:2048
	ds_read_b128 v[194:197], v149 offset:3072
	ds_read_b128 v[198:201], v149 offset:4096
	ds_read_b128 v[202:205], v149 offset:5120
	ds_read_b128 v[206:209], v149 offset:6144
	ds_read_b128 v[210:213], v149 offset:7168
	global_load_lds_dwordx4 v[144:145], off
	v_lshl_add_u64 v[144:145], s[52:53], 0, v[136:137]
	s_add_i32 m0, s16, 0xe000
	s_nop 0
	global_load_lds_dwordx4 v[144:145], off
	s_waitcnt vmcnt(8)
	s_waitcnt lgkmcnt(0)
	s_barrier
	s_setprio 1
	s_waitcnt lgkmcnt(0)
	v_mfma_f32_16x16x32_bf16 v[126:129], v[140:143], v[182:185], 0
	v_mfma_f32_16x16x32_bf16 v[122:125], v[154:157], v[182:185], 0
	v_mfma_f32_16x16x32_bf16 v[110:113], v[140:143], v[190:193], 0
	v_mfma_f32_16x16x32_bf16 v[106:109], v[154:157], v[190:193], 0
	v_mfma_f32_16x16x32_bf16 v[94:97], v[140:143], v[198:201], 0
	v_mfma_f32_16x16x32_bf16 v[90:93], v[154:157], v[198:201], 0
	v_mfma_f32_16x16x32_bf16 v[78:81], v[140:143], v[206:209], 0
	v_mfma_f32_16x16x32_bf16 v[74:77], v[154:157], v[206:209], 0
	v_mfma_f32_16x16x32_bf16 v[126:129], v[150:153], v[186:189], v[126:129]
	v_mfma_f32_16x16x32_bf16 v[122:125], v[158:161], v[186:189], v[122:125]
	v_mfma_f32_16x16x32_bf16 v[110:113], v[150:153], v[194:197], v[110:113]
	v_mfma_f32_16x16x32_bf16 v[106:109], v[158:161], v[194:197], v[106:109]
	v_mfma_f32_16x16x32_bf16 v[94:97], v[150:153], v[202:205], v[94:97]
	v_mfma_f32_16x16x32_bf16 v[90:93], v[158:161], v[202:205], v[90:93]
	v_mfma_f32_16x16x32_bf16 v[78:81], v[150:153], v[210:213], v[78:81]
	v_mfma_f32_16x16x32_bf16 v[74:77], v[158:161], v[210:213], v[74:77]
	s_setprio 0
	s_setprio 1
	v_mfma_f32_16x16x32_bf16 v[118:121], v[162:165], v[182:185], 0
	v_mfma_f32_16x16x32_bf16 v[114:117], v[174:177], v[182:185], 0
	v_mfma_f32_16x16x32_bf16 v[102:105], v[162:165], v[190:193], 0
	v_mfma_f32_16x16x32_bf16 v[98:101], v[174:177], v[190:193], 0
	v_mfma_f32_16x16x32_bf16 v[86:89], v[162:165], v[198:201], 0
	v_mfma_f32_16x16x32_bf16 v[82:85], v[174:177], v[198:201], 0
	v_mfma_f32_16x16x32_bf16 v[70:73], v[162:165], v[206:209], 0
	v_mfma_f32_16x16x32_bf16 v[66:69], v[174:177], v[206:209], 0
	v_mfma_f32_16x16x32_bf16 v[118:121], v[170:173], v[186:189], v[118:121]
	v_mfma_f32_16x16x32_bf16 v[114:117], v[178:181], v[186:189], v[114:117]
	v_mfma_f32_16x16x32_bf16 v[102:105], v[170:173], v[194:197], v[102:105]
	v_mfma_f32_16x16x32_bf16 v[98:101], v[178:181], v[194:197], v[98:101]
	v_mfma_f32_16x16x32_bf16 v[86:89], v[170:173], v[202:205], v[86:89]
	v_mfma_f32_16x16x32_bf16 v[82:85], v[178:181], v[202:205], v[82:85]
	v_mfma_f32_16x16x32_bf16 v[70:73], v[170:173], v[210:213], v[70:73]
	v_mfma_f32_16x16x32_bf16 v[66:69], v[178:181], v[210:213], v[66:69]
	s_setprio 0
	s_barrier
	s_add_i32 s68, s68, s15
	v_lshl_add_u64 v[144:145], s[54:55], 0, v[166:167]
	s_mov_b32 m0, s68
	ds_read_b128 v[182:185], v149 offset:16384
	ds_read_b128 v[186:189], v149 offset:17408
	ds_read_b128 v[190:193], v149 offset:18432
	ds_read_b128 v[194:197], v149 offset:19456
	ds_read_b128 v[198:201], v149 offset:20480
	ds_read_b128 v[202:205], v149 offset:21504
	ds_read_b128 v[206:209], v149 offset:22528
	ds_read_b128 v[210:213], v149 offset:23552
	global_load_lds_dwordx4 v[144:145], off
	s_add_i32 m0, s68, 0x2000
	s_add_u32 s68, s54, 0x40000
	v_lshl_add_u64 v[214:215], s[54:55], 0, v[130:131]
	s_addc_u32 s69, s55, 0
	s_add_i32 s70, s70, s15
	global_load_lds_dwordx4 v[214:215], off
	v_lshl_add_u64 v[216:217], s[68:69], 0, v[166:167]
	s_mov_b32 m0, s70
	v_lshl_add_u64 v[218:219], s[58:59], 0, v[134:135]
	global_load_lds_dwordx4 v[216:217], off
	v_lshl_add_u64 v[216:217], s[68:69], 0, v[130:131]
	s_add_i32 m0, s70, 0x2000
	s_nop 0
	global_load_lds_dwordx4 v[216:217], off
	v_lshl_add_u64 v[216:217], s[58:59], 0, v[132:133]
	s_mov_b32 m0, s16
	s_nop 0
	global_load_lds_dwordx4 v[216:217], off
	s_mov_b32 m0, s20
	s_nop 0
	global_load_lds_dwordx4 v[218:219], off
	s_waitcnt vmcnt(8)
	s_waitcnt lgkmcnt(0)
	s_barrier
	s_setprio 1
	s_waitcnt lgkmcnt(0)
	v_mfma_f32_16x16x32_bf16 v[62:65], v[140:143], v[182:185], 0
	v_mfma_f32_16x16x32_bf16 v[58:61], v[154:157], v[182:185], 0
	v_mfma_f32_16x16x32_bf16 v[46:49], v[140:143], v[190:193], 0
	v_mfma_f32_16x16x32_bf16 v[42:45], v[154:157], v[190:193], 0
	v_mfma_f32_16x16x32_bf16 v[30:33], v[140:143], v[198:201], 0
	v_mfma_f32_16x16x32_bf16 v[26:29], v[154:157], v[198:201], 0
	v_mfma_f32_16x16x32_bf16 v[14:17], v[140:143], v[206:209], 0
	v_mfma_f32_16x16x32_bf16 v[10:13], v[154:157], v[206:209], 0
	v_mfma_f32_16x16x32_bf16 v[62:65], v[150:153], v[186:189], v[62:65]
	v_mfma_f32_16x16x32_bf16 v[58:61], v[158:161], v[186:189], v[58:61]
	v_mfma_f32_16x16x32_bf16 v[46:49], v[150:153], v[194:197], v[46:49]
	v_mfma_f32_16x16x32_bf16 v[42:45], v[158:161], v[194:197], v[42:45]
	v_mfma_f32_16x16x32_bf16 v[30:33], v[150:153], v[202:205], v[30:33]
	v_mfma_f32_16x16x32_bf16 v[26:29], v[158:161], v[202:205], v[26:29]
	v_mfma_f32_16x16x32_bf16 v[14:17], v[150:153], v[210:213], v[14:17]
	v_mfma_f32_16x16x32_bf16 v[10:13], v[158:161], v[210:213], v[10:13]
	s_setprio 0
	s_setprio 1
	v_mfma_f32_16x16x32_bf16 v[54:57], v[162:165], v[182:185], 0
	v_mfma_f32_16x16x32_bf16 v[50:53], v[174:177], v[182:185], 0
	v_mfma_f32_16x16x32_bf16 v[38:41], v[162:165], v[190:193], 0
	v_mfma_f32_16x16x32_bf16 v[34:37], v[174:177], v[190:193], 0
	v_mfma_f32_16x16x32_bf16 v[22:25], v[162:165], v[198:201], 0
	v_mfma_f32_16x16x32_bf16 v[18:21], v[174:177], v[198:201], 0
	v_mfma_f32_16x16x32_bf16 v[6:9], v[162:165], v[206:209], 0
	v_mfma_f32_16x16x32_bf16 v[2:5], v[174:177], v[206:209], 0
	v_mfma_f32_16x16x32_bf16 v[54:57], v[170:173], v[186:189], v[54:57]
	v_mfma_f32_16x16x32_bf16 v[50:53], v[178:181], v[186:189], v[50:53]
	v_mfma_f32_16x16x32_bf16 v[38:41], v[170:173], v[194:197], v[38:41]
	v_mfma_f32_16x16x32_bf16 v[34:37], v[178:181], v[194:197], v[34:37]
	v_mfma_f32_16x16x32_bf16 v[22:25], v[170:173], v[202:205], v[22:25]
	v_mfma_f32_16x16x32_bf16 v[18:21], v[178:181], v[202:205], v[18:21]
	v_mfma_f32_16x16x32_bf16 v[6:9], v[170:173], v[210:213], v[6:9]
	v_mfma_f32_16x16x32_bf16 v[2:5], v[178:181], v[210:213], v[2:5]
	s_setprio 0
	s_barrier
	s_add_i32 s68, 0, 0x18000
	s_add_i32 s69, 0, 0x1c000
	v_add_u32_e32 v158, s68, v147
	v_add_u32_e32 v169, s69, v147
	ds_read_b128 v[140:143], v158
	ds_read_b128 v[150:153], v158 offset:1024
	ds_read_b128 v[154:157], v158 offset:2048
	ds_read_b128 v[158:161], v158 offset:3072
	ds_read_b128 v[162:165], v169
	ds_read_b128 v[170:173], v169 offset:1024
	ds_read_b128 v[174:177], v169 offset:2048
	ds_read_b128 v[178:181], v169 offset:3072
	s_add_u32 s58, s58, 0x40000
	s_addc_u32 s59, s59, 0
	s_mov_b32 m0, s21
	v_lshl_add_u64 v[220:221], s[58:59], 0, v[132:133]
	ds_read_b128 v[182:185], v149 offset:32768
	ds_read_b128 v[186:189], v149 offset:33792
	ds_read_b128 v[190:193], v149 offset:34816
	ds_read_b128 v[194:197], v149 offset:35840
	ds_read_b128 v[198:201], v149 offset:36864
	ds_read_b128 v[202:205], v149 offset:37888
	ds_read_b128 v[206:209], v149 offset:38912
	ds_read_b128 v[210:213], v149 offset:39936
	global_load_lds_dwordx4 v[220:221], off
	v_lshl_add_u64 v[220:221], s[58:59], 0, v[134:135]
	s_mov_b32 m0, s22
	s_nop 0
	global_load_lds_dwordx4 v[220:221], off
	s_waitcnt vmcnt(8)
	s_waitcnt lgkmcnt(0)
	s_barrier
	s_setprio 1
	s_waitcnt lgkmcnt(0)
	v_mfma_f32_16x16x32_bf16 v[126:129], v[140:143], v[182:185], v[126:129]
	v_mfma_f32_16x16x32_bf16 v[122:125], v[154:157], v[182:185], v[122:125]
	v_mfma_f32_16x16x32_bf16 v[110:113], v[140:143], v[190:193], v[110:113]
	v_mfma_f32_16x16x32_bf16 v[106:109], v[154:157], v[190:193], v[106:109]
	v_mfma_f32_16x16x32_bf16 v[94:97], v[140:143], v[198:201], v[94:97]
	v_mfma_f32_16x16x32_bf16 v[90:93], v[154:157], v[198:201], v[90:93]
	v_mfma_f32_16x16x32_bf16 v[78:81], v[140:143], v[206:209], v[78:81]
	v_mfma_f32_16x16x32_bf16 v[74:77], v[154:157], v[206:209], v[74:77]
	v_mfma_f32_16x16x32_bf16 v[126:129], v[150:153], v[186:189], v[126:129]
	v_mfma_f32_16x16x32_bf16 v[122:125], v[158:161], v[186:189], v[122:125]
	v_mfma_f32_16x16x32_bf16 v[110:113], v[150:153], v[194:197], v[110:113]
	v_mfma_f32_16x16x32_bf16 v[106:109], v[158:161], v[194:197], v[106:109]
	v_mfma_f32_16x16x32_bf16 v[94:97], v[150:153], v[202:205], v[94:97]
	v_mfma_f32_16x16x32_bf16 v[90:93], v[158:161], v[202:205], v[90:93]
	v_mfma_f32_16x16x32_bf16 v[78:81], v[150:153], v[210:213], v[78:81]
	v_mfma_f32_16x16x32_bf16 v[74:77], v[158:161], v[210:213], v[74:77]
	s_setprio 0
	s_setprio 1
	v_mfma_f32_16x16x32_bf16 v[118:121], v[162:165], v[182:185], v[118:121]
	v_mfma_f32_16x16x32_bf16 v[114:117], v[174:177], v[182:185], v[114:117]
	v_mfma_f32_16x16x32_bf16 v[102:105], v[162:165], v[190:193], v[102:105]
	v_mfma_f32_16x16x32_bf16 v[98:101], v[174:177], v[190:193], v[98:101]
	v_mfma_f32_16x16x32_bf16 v[86:89], v[162:165], v[198:201], v[86:89]
	v_mfma_f32_16x16x32_bf16 v[82:85], v[174:177], v[198:201], v[82:85]
	v_mfma_f32_16x16x32_bf16 v[70:73], v[162:165], v[206:209], v[70:73]
	v_mfma_f32_16x16x32_bf16 v[66:69], v[174:177], v[206:209], v[66:69]
	v_mfma_f32_16x16x32_bf16 v[118:121], v[170:173], v[186:189], v[118:121]
	v_mfma_f32_16x16x32_bf16 v[114:117], v[178:181], v[186:189], v[114:117]
	v_mfma_f32_16x16x32_bf16 v[102:105], v[170:173], v[194:197], v[102:105]
	v_mfma_f32_16x16x32_bf16 v[98:101], v[178:181], v[194:197], v[98:101]
	v_mfma_f32_16x16x32_bf16 v[86:89], v[170:173], v[202:205], v[86:89]
	v_mfma_f32_16x16x32_bf16 v[82:85], v[178:181], v[202:205], v[82:85]
	v_mfma_f32_16x16x32_bf16 v[70:73], v[170:173], v[210:213], v[70:73]
	v_mfma_f32_16x16x32_bf16 v[66:69], v[178:181], v[210:213], v[66:69]
	s_setprio 0
	s_barrier
	s_add_i32 s58, s68, s15
	v_lshl_add_u64 v[144:145], v[144:145], 0, s[56:57]
	s_mov_b32 m0, s58
	ds_read_b128 v[182:185], v149 offset:49152
	ds_read_b128 v[186:189], v149 offset:50176
	ds_read_b128 v[190:193], v149 offset:51200
	ds_read_b128 v[194:197], v149 offset:52224
	ds_read_b128 v[198:201], v149 offset:53248
	ds_read_b128 v[202:205], v149 offset:54272
	ds_read_b128 v[206:209], v149 offset:55296
	ds_read_b128 v[210:213], v149 offset:56320
	global_load_lds_dwordx4 v[144:145], off
	s_add_i32 m0, s58, 0x2000
	s_add_u32 s54, s54, 0x40080
	v_lshl_add_u64 v[144:145], v[214:215], 0, s[56:57]
	s_addc_u32 s55, s55, 0
	s_add_i32 s58, s69, s15
	global_load_lds_dwordx4 v[144:145], off
	v_lshl_add_u64 v[144:145], s[54:55], 0, v[166:167]
	s_mov_b32 m0, s58
	s_nop 0
	global_load_lds_dwordx4 v[144:145], off
	v_lshl_add_u64 v[144:145], s[54:55], 0, v[130:131]
	s_add_i32 m0, s58, 0x2000
	s_nop 0
	global_load_lds_dwordx4 v[144:145], off
	v_lshl_add_u64 v[144:145], v[216:217], 0, s[56:57]
	s_mov_b32 m0, s23
	s_nop 0
	global_load_lds_dwordx4 v[144:145], off
	v_lshl_add_u64 v[144:145], v[218:219], 0, s[56:57]
	s_mov_b32 m0, s24
	s_nop 0
	global_load_lds_dwordx4 v[144:145], off
	s_waitcnt vmcnt(8)
	s_waitcnt lgkmcnt(0)
	s_barrier
	s_setprio 1
	s_waitcnt lgkmcnt(0)
	v_mfma_f32_16x16x32_bf16 v[62:65], v[140:143], v[182:185], v[62:65]
	v_mfma_f32_16x16x32_bf16 v[58:61], v[154:157], v[182:185], v[58:61]
	v_mfma_f32_16x16x32_bf16 v[46:49], v[140:143], v[190:193], v[46:49]
	v_mfma_f32_16x16x32_bf16 v[42:45], v[154:157], v[190:193], v[42:45]
	v_mfma_f32_16x16x32_bf16 v[30:33], v[140:143], v[198:201], v[30:33]
	v_mfma_f32_16x16x32_bf16 v[26:29], v[154:157], v[198:201], v[26:29]
	v_mfma_f32_16x16x32_bf16 v[14:17], v[140:143], v[206:209], v[14:17]
	v_mfma_f32_16x16x32_bf16 v[10:13], v[154:157], v[206:209], v[10:13]
	v_mfma_f32_16x16x32_bf16 v[62:65], v[150:153], v[186:189], v[62:65]
	v_mfma_f32_16x16x32_bf16 v[58:61], v[158:161], v[186:189], v[58:61]
	v_mfma_f32_16x16x32_bf16 v[46:49], v[150:153], v[194:197], v[46:49]
	v_mfma_f32_16x16x32_bf16 v[42:45], v[158:161], v[194:197], v[42:45]
	v_mfma_f32_16x16x32_bf16 v[30:33], v[150:153], v[202:205], v[30:33]
	v_mfma_f32_16x16x32_bf16 v[26:29], v[158:161], v[202:205], v[26:29]
	v_mfma_f32_16x16x32_bf16 v[14:17], v[150:153], v[210:213], v[14:17]
	v_mfma_f32_16x16x32_bf16 v[10:13], v[158:161], v[210:213], v[10:13]
	s_setprio 0
	s_setprio 1
	v_mfma_f32_16x16x32_bf16 v[54:57], v[162:165], v[182:185], v[54:57]
	v_mfma_f32_16x16x32_bf16 v[50:53], v[174:177], v[182:185], v[50:53]
	v_mfma_f32_16x16x32_bf16 v[38:41], v[162:165], v[190:193], v[38:41]
	v_mfma_f32_16x16x32_bf16 v[34:37], v[174:177], v[190:193], v[34:37]
	v_mfma_f32_16x16x32_bf16 v[22:25], v[162:165], v[198:201], v[22:25]
	v_mfma_f32_16x16x32_bf16 v[18:21], v[174:177], v[198:201], v[18:21]
	v_mfma_f32_16x16x32_bf16 v[6:9], v[162:165], v[206:209], v[6:9]
	v_mfma_f32_16x16x32_bf16 v[2:5], v[174:177], v[206:209], v[2:5]
	v_mfma_f32_16x16x32_bf16 v[54:57], v[170:173], v[186:189], v[54:57]
	v_mfma_f32_16x16x32_bf16 v[50:53], v[178:181], v[186:189], v[50:53]
	v_mfma_f32_16x16x32_bf16 v[38:41], v[170:173], v[194:197], v[38:41]
	v_mfma_f32_16x16x32_bf16 v[34:37], v[178:181], v[194:197], v[34:37]
	v_mfma_f32_16x16x32_bf16 v[22:25], v[170:173], v[202:205], v[22:25]
	v_mfma_f32_16x16x32_bf16 v[18:21], v[178:181], v[202:205], v[18:21]
	v_mfma_f32_16x16x32_bf16 v[6:9], v[170:173], v[210:213], v[6:9]
	v_mfma_f32_16x16x32_bf16 v[2:5], v[178:181], v[210:213], v[2:5]
	s_setprio 0
	s_add_u32 s64, s64, 0x100
	s_addc_u32 s65, s65, 0
	s_add_u32 s52, s52, 0x100
	s_addc_u32 s53, s53, 0
	s_cmp_ge_i32 s66, s1
	s_mov_b32 s54, s66
	s_cbranch_scc1 .Lrotph12_pexitbar
	s_add_i32 s66, s54, 2
	s_add_u32 s55, s52, 0xfffc0080
	s_addc_u32 s58, s53, -1
	s_add_i32 s68, 0, 0x10000
	s_cmp_eq_u32 s60, s54
	s_cselect_b32 s59, s41, s58
	s_cselect_b32 s58, s43, s55
	s_barrier
	s_branch .Lrotph12_body

.Lrotph12_body:
	v_add_u32_e32 v144, s68, v147
	s_cselect_b32 s55, s62, s65
	s_cselect_b32 s54, s63, s64
	s_add_i32 s70, 0, 0x14000
	ds_read_b128 v[140:143], v144
	ds_read_b128 v[150:153], v144 offset:1024
	ds_read_b128 v[154:157], v144 offset:2048
	ds_read_b128 v[158:161], v144 offset:3072
	v_add_u32_e32 v144, s70, v147
	ds_read_b128 v[162:165], v144
	ds_read_b128 v[170:173], v144 offset:1024
	ds_read_b128 v[174:177], v144 offset:2048
	ds_read_b128 v[178:181], v144 offset:3072
	v_lshl_add_u64 v[144:145], s[52:53], 0, v[138:139]
	s_add_i32 m0, s16, 0xc000
	ds_read_b128 v[182:185], v149
	ds_read_b128 v[186:189], v149 offset:1024
	ds_read_b128 v[190:193], v149 offset:2048
	ds_read_b128 v[194:197], v149 offset:3072
	ds_read_b128 v[198:201], v149 offset:4096
	ds_read_b128 v[202:205], v149 offset:5120
	ds_read_b128 v[206:209], v149 offset:6144
	ds_read_b128 v[210:213], v149 offset:7168
	global_load_lds_dwordx4 v[144:145], off
	v_lshl_add_u64 v[144:145], s[52:53], 0, v[136:137]
	s_add_i32 m0, s16, 0xe000
	s_nop 0
	global_load_lds_dwordx4 v[144:145], off
	s_waitcnt vmcnt(8)
	s_waitcnt lgkmcnt(0)
	s_barrier
	s_setprio 1
	s_waitcnt lgkmcnt(0)
	v_mfma_f32_16x16x32_bf16 v[126:129], v[140:143], v[182:185], v[126:129]
	v_mfma_f32_16x16x32_bf16 v[122:125], v[154:157], v[182:185], v[122:125]
	v_mfma_f32_16x16x32_bf16 v[110:113], v[140:143], v[190:193], v[110:113]
	v_mfma_f32_16x16x32_bf16 v[106:109], v[154:157], v[190:193], v[106:109]
	v_mfma_f32_16x16x32_bf16 v[94:97], v[140:143], v[198:201], v[94:97]
	v_mfma_f32_16x16x32_bf16 v[90:93], v[154:157], v[198:201], v[90:93]
	v_mfma_f32_16x16x32_bf16 v[78:81], v[140:143], v[206:209], v[78:81]
	v_mfma_f32_16x16x32_bf16 v[74:77], v[154:157], v[206:209], v[74:77]
	v_mfma_f32_16x16x32_bf16 v[126:129], v[150:153], v[186:189], v[126:129]
	v_mfma_f32_16x16x32_bf16 v[122:125], v[158:161], v[186:189], v[122:125]
	v_mfma_f32_16x16x32_bf16 v[110:113], v[150:153], v[194:197], v[110:113]
	v_mfma_f32_16x16x32_bf16 v[106:109], v[158:161], v[194:197], v[106:109]
	v_mfma_f32_16x16x32_bf16 v[94:97], v[150:153], v[202:205], v[94:97]
	v_mfma_f32_16x16x32_bf16 v[90:93], v[158:161], v[202:205], v[90:93]
	v_mfma_f32_16x16x32_bf16 v[78:81], v[150:153], v[210:213], v[78:81]
	v_mfma_f32_16x16x32_bf16 v[74:77], v[158:161], v[210:213], v[74:77]
	s_setprio 0
	s_setprio 1
	v_mfma_f32_16x16x32_bf16 v[118:121], v[162:165], v[182:185], v[118:121]
	v_mfma_f32_16x16x32_bf16 v[114:117], v[174:177], v[182:185], v[114:117]
	v_mfma_f32_16x16x32_bf16 v[102:105], v[162:165], v[190:193], v[102:105]
	v_mfma_f32_16x16x32_bf16 v[98:101], v[174:177], v[190:193], v[98:101]
	v_mfma_f32_16x16x32_bf16 v[86:89], v[162:165], v[198:201], v[86:89]
	v_mfma_f32_16x16x32_bf16 v[82:85], v[174:177], v[198:201], v[82:85]
	v_mfma_f32_16x16x32_bf16 v[70:73], v[162:165], v[206:209], v[70:73]
	v_mfma_f32_16x16x32_bf16 v[66:69], v[174:177], v[206:209], v[66:69]
	v_mfma_f32_16x16x32_bf16 v[118:121], v[170:173], v[186:189], v[118:121]
	v_mfma_f32_16x16x32_bf16 v[114:117], v[178:181], v[186:189], v[114:117]
	v_mfma_f32_16x16x32_bf16 v[102:105], v[170:173], v[194:197], v[102:105]
	v_mfma_f32_16x16x32_bf16 v[98:101], v[178:181], v[194:197], v[98:101]
	v_mfma_f32_16x16x32_bf16 v[86:89], v[170:173], v[202:205], v[86:89]
	v_mfma_f32_16x16x32_bf16 v[82:85], v[178:181], v[202:205], v[82:85]
	v_mfma_f32_16x16x32_bf16 v[70:73], v[170:173], v[210:213], v[70:73]
	v_mfma_f32_16x16x32_bf16 v[66:69], v[178:181], v[210:213], v[66:69]
	s_setprio 0
	s_barrier
	s_add_i32 s68, s68, s15
	v_lshl_add_u64 v[144:145], s[54:55], 0, v[166:167]
	s_mov_b32 m0, s68
	ds_read_b128 v[182:185], v149 offset:16384
	ds_read_b128 v[186:189], v149 offset:17408
	ds_read_b128 v[190:193], v149 offset:18432
	ds_read_b128 v[194:197], v149 offset:19456
	ds_read_b128 v[198:201], v149 offset:20480
	ds_read_b128 v[202:205], v149 offset:21504
	ds_read_b128 v[206:209], v149 offset:22528
	ds_read_b128 v[210:213], v149 offset:23552
	global_load_lds_dwordx4 v[144:145], off
	s_add_i32 m0, s68, 0x2000
	s_add_u32 s68, s54, 0x40000
	v_lshl_add_u64 v[214:215], s[54:55], 0, v[130:131]
	s_addc_u32 s69, s55, 0
	s_add_i32 s70, s70, s15
	global_load_lds_dwordx4 v[214:215], off
	v_lshl_add_u64 v[216:217], s[68:69], 0, v[166:167]
	s_mov_b32 m0, s70
	v_lshl_add_u64 v[218:219], s[58:59], 0, v[134:135]
	global_load_lds_dwordx4 v[216:217], off
	v_lshl_add_u64 v[216:217], s[68:69], 0, v[130:131]
	s_add_i32 m0, s70, 0x2000
	s_nop 0
	global_load_lds_dwordx4 v[216:217], off
	v_lshl_add_u64 v[216:217], s[58:59], 0, v[132:133]
	s_mov_b32 m0, s16
	s_nop 0
	global_load_lds_dwordx4 v[216:217], off
	s_mov_b32 m0, s20
	s_nop 0
	global_load_lds_dwordx4 v[218:219], off
	s_waitcnt vmcnt(8)
	s_waitcnt lgkmcnt(0)
	s_barrier
	s_setprio 1
	s_waitcnt lgkmcnt(0)
	v_mfma_f32_16x16x32_bf16 v[62:65], v[140:143], v[182:185], v[62:65]
	v_mfma_f32_16x16x32_bf16 v[58:61], v[154:157], v[182:185], v[58:61]
	v_mfma_f32_16x16x32_bf16 v[46:49], v[140:143], v[190:193], v[46:49]
	v_mfma_f32_16x16x32_bf16 v[42:45], v[154:157], v[190:193], v[42:45]
	v_mfma_f32_16x16x32_bf16 v[30:33], v[140:143], v[198:201], v[30:33]
	v_mfma_f32_16x16x32_bf16 v[26:29], v[154:157], v[198:201], v[26:29]
	v_mfma_f32_16x16x32_bf16 v[14:17], v[140:143], v[206:209], v[14:17]
	v_mfma_f32_16x16x32_bf16 v[10:13], v[154:157], v[206:209], v[10:13]
	v_mfma_f32_16x16x32_bf16 v[62:65], v[150:153], v[186:189], v[62:65]
	v_mfma_f32_16x16x32_bf16 v[58:61], v[158:161], v[186:189], v[58:61]
	v_mfma_f32_16x16x32_bf16 v[46:49], v[150:153], v[194:197], v[46:49]
	v_mfma_f32_16x16x32_bf16 v[42:45], v[158:161], v[194:197], v[42:45]
	v_mfma_f32_16x16x32_bf16 v[30:33], v[150:153], v[202:205], v[30:33]
	v_mfma_f32_16x16x32_bf16 v[26:29], v[158:161], v[202:205], v[26:29]
	v_mfma_f32_16x16x32_bf16 v[14:17], v[150:153], v[210:213], v[14:17]
	v_mfma_f32_16x16x32_bf16 v[10:13], v[158:161], v[210:213], v[10:13]
	s_setprio 0
	s_setprio 1
	v_mfma_f32_16x16x32_bf16 v[54:57], v[162:165], v[182:185], v[54:57]
	v_mfma_f32_16x16x32_bf16 v[50:53], v[174:177], v[182:185], v[50:53]
	v_mfma_f32_16x16x32_bf16 v[38:41], v[162:165], v[190:193], v[38:41]
	v_mfma_f32_16x16x32_bf16 v[34:37], v[174:177], v[190:193], v[34:37]
	v_mfma_f32_16x16x32_bf16 v[22:25], v[162:165], v[198:201], v[22:25]
	v_mfma_f32_16x16x32_bf16 v[18:21], v[174:177], v[198:201], v[18:21]
	v_mfma_f32_16x16x32_bf16 v[6:9], v[162:165], v[206:209], v[6:9]
	v_mfma_f32_16x16x32_bf16 v[2:5], v[174:177], v[206:209], v[2:5]
	v_mfma_f32_16x16x32_bf16 v[54:57], v[170:173], v[186:189], v[54:57]
	v_mfma_f32_16x16x32_bf16 v[50:53], v[178:181], v[186:189], v[50:53]
	v_mfma_f32_16x16x32_bf16 v[38:41], v[170:173], v[194:197], v[38:41]
	v_mfma_f32_16x16x32_bf16 v[34:37], v[178:181], v[194:197], v[34:37]
	v_mfma_f32_16x16x32_bf16 v[22:25], v[170:173], v[202:205], v[22:25]
	v_mfma_f32_16x16x32_bf16 v[18:21], v[178:181], v[202:205], v[18:21]
	v_mfma_f32_16x16x32_bf16 v[6:9], v[170:173], v[210:213], v[6:9]
	v_mfma_f32_16x16x32_bf16 v[2:5], v[178:181], v[210:213], v[2:5]
	s_setprio 0
	s_barrier
	s_add_i32 s68, 0, 0x18000
	s_add_i32 s69, 0, 0x1c000
	v_add_u32_e32 v158, s68, v147
	v_add_u32_e32 v169, s69, v147
	ds_read_b128 v[140:143], v158
	ds_read_b128 v[150:153], v158 offset:1024
	ds_read_b128 v[154:157], v158 offset:2048
	ds_read_b128 v[158:161], v158 offset:3072
	ds_read_b128 v[162:165], v169
	ds_read_b128 v[170:173], v169 offset:1024
	ds_read_b128 v[174:177], v169 offset:2048
	ds_read_b128 v[178:181], v169 offset:3072
	s_add_u32 s58, s58, 0x40000
	s_addc_u32 s59, s59, 0
	s_mov_b32 m0, s21
	v_lshl_add_u64 v[220:221], s[58:59], 0, v[132:133]
	ds_read_b128 v[182:185], v149 offset:32768
	ds_read_b128 v[186:189], v149 offset:33792
	ds_read_b128 v[190:193], v149 offset:34816
	ds_read_b128 v[194:197], v149 offset:35840
	ds_read_b128 v[198:201], v149 offset:36864
	ds_read_b128 v[202:205], v149 offset:37888
	ds_read_b128 v[206:209], v149 offset:38912
	ds_read_b128 v[210:213], v149 offset:39936
	global_load_lds_dwordx4 v[220:221], off
	v_lshl_add_u64 v[220:221], s[58:59], 0, v[134:135]
	s_mov_b32 m0, s22
	s_nop 0
	global_load_lds_dwordx4 v[220:221], off
	s_waitcnt vmcnt(8)
	s_waitcnt lgkmcnt(0)
	s_barrier
	s_setprio 1
	s_waitcnt lgkmcnt(0)
	v_mfma_f32_16x16x32_bf16 v[126:129], v[140:143], v[182:185], v[126:129]
	v_mfma_f32_16x16x32_bf16 v[122:125], v[154:157], v[182:185], v[122:125]
	v_mfma_f32_16x16x32_bf16 v[110:113], v[140:143], v[190:193], v[110:113]
	v_mfma_f32_16x16x32_bf16 v[106:109], v[154:157], v[190:193], v[106:109]
	v_mfma_f32_16x16x32_bf16 v[94:97], v[140:143], v[198:201], v[94:97]
	v_mfma_f32_16x16x32_bf16 v[90:93], v[154:157], v[198:201], v[90:93]
	v_mfma_f32_16x16x32_bf16 v[78:81], v[140:143], v[206:209], v[78:81]
	v_mfma_f32_16x16x32_bf16 v[74:77], v[154:157], v[206:209], v[74:77]
	v_mfma_f32_16x16x32_bf16 v[126:129], v[150:153], v[186:189], v[126:129]
	v_mfma_f32_16x16x32_bf16 v[122:125], v[158:161], v[186:189], v[122:125]
	v_mfma_f32_16x16x32_bf16 v[110:113], v[150:153], v[194:197], v[110:113]
	v_mfma_f32_16x16x32_bf16 v[106:109], v[158:161], v[194:197], v[106:109]
	v_mfma_f32_16x16x32_bf16 v[94:97], v[150:153], v[202:205], v[94:97]
	v_mfma_f32_16x16x32_bf16 v[90:93], v[158:161], v[202:205], v[90:93]
	v_mfma_f32_16x16x32_bf16 v[78:81], v[150:153], v[210:213], v[78:81]
	v_mfma_f32_16x16x32_bf16 v[74:77], v[158:161], v[210:213], v[74:77]
	s_setprio 0
	s_setprio 1
	v_mfma_f32_16x16x32_bf16 v[118:121], v[162:165], v[182:185], v[118:121]
	v_mfma_f32_16x16x32_bf16 v[114:117], v[174:177], v[182:185], v[114:117]
	v_mfma_f32_16x16x32_bf16 v[102:105], v[162:165], v[190:193], v[102:105]
	v_mfma_f32_16x16x32_bf16 v[98:101], v[174:177], v[190:193], v[98:101]
	v_mfma_f32_16x16x32_bf16 v[86:89], v[162:165], v[198:201], v[86:89]
	v_mfma_f32_16x16x32_bf16 v[82:85], v[174:177], v[198:201], v[82:85]
	v_mfma_f32_16x16x32_bf16 v[70:73], v[162:165], v[206:209], v[70:73]
	v_mfma_f32_16x16x32_bf16 v[66:69], v[174:177], v[206:209], v[66:69]
	v_mfma_f32_16x16x32_bf16 v[118:121], v[170:173], v[186:189], v[118:121]
	v_mfma_f32_16x16x32_bf16 v[114:117], v[178:181], v[186:189], v[114:117]
	v_mfma_f32_16x16x32_bf16 v[102:105], v[170:173], v[194:197], v[102:105]
	v_mfma_f32_16x16x32_bf16 v[98:101], v[178:181], v[194:197], v[98:101]
	v_mfma_f32_16x16x32_bf16 v[86:89], v[170:173], v[202:205], v[86:89]
	v_mfma_f32_16x16x32_bf16 v[82:85], v[178:181], v[202:205], v[82:85]
	v_mfma_f32_16x16x32_bf16 v[70:73], v[170:173], v[210:213], v[70:73]
	v_mfma_f32_16x16x32_bf16 v[66:69], v[178:181], v[210:213], v[66:69]
	s_setprio 0
	s_barrier
	s_add_i32 s58, s68, s15
	v_lshl_add_u64 v[144:145], v[144:145], 0, s[56:57]
	s_mov_b32 m0, s58
	ds_read_b128 v[182:185], v149 offset:49152
	ds_read_b128 v[186:189], v149 offset:50176
	ds_read_b128 v[190:193], v149 offset:51200
	ds_read_b128 v[194:197], v149 offset:52224
	ds_read_b128 v[198:201], v149 offset:53248
	ds_read_b128 v[202:205], v149 offset:54272
	ds_read_b128 v[206:209], v149 offset:55296
	ds_read_b128 v[210:213], v149 offset:56320
	global_load_lds_dwordx4 v[144:145], off
	s_add_i32 m0, s58, 0x2000
	s_add_u32 s54, s54, 0x40080
	v_lshl_add_u64 v[144:145], v[214:215], 0, s[56:57]
	s_addc_u32 s55, s55, 0
	s_add_i32 s58, s69, s15
	global_load_lds_dwordx4 v[144:145], off
	v_lshl_add_u64 v[144:145], s[54:55], 0, v[166:167]
	s_mov_b32 m0, s58
	s_nop 0
	global_load_lds_dwordx4 v[144:145], off
	v_lshl_add_u64 v[144:145], s[54:55], 0, v[130:131]
	s_add_i32 m0, s58, 0x2000
	s_nop 0
	global_load_lds_dwordx4 v[144:145], off
	v_lshl_add_u64 v[144:145], v[216:217], 0, s[56:57]
	s_mov_b32 m0, s23
	s_nop 0
	global_load_lds_dwordx4 v[144:145], off
	v_lshl_add_u64 v[144:145], v[218:219], 0, s[56:57]
	s_mov_b32 m0, s24
	s_nop 0
	global_load_lds_dwordx4 v[144:145], off
	s_waitcnt vmcnt(8)
	s_waitcnt lgkmcnt(0)
	s_barrier
	s_setprio 1
	s_waitcnt lgkmcnt(0)
	v_mfma_f32_16x16x32_bf16 v[62:65], v[140:143], v[182:185], v[62:65]
	v_mfma_f32_16x16x32_bf16 v[58:61], v[154:157], v[182:185], v[58:61]
	v_mfma_f32_16x16x32_bf16 v[46:49], v[140:143], v[190:193], v[46:49]
	v_mfma_f32_16x16x32_bf16 v[42:45], v[154:157], v[190:193], v[42:45]
	v_mfma_f32_16x16x32_bf16 v[30:33], v[140:143], v[198:201], v[30:33]
	v_mfma_f32_16x16x32_bf16 v[26:29], v[154:157], v[198:201], v[26:29]
	v_mfma_f32_16x16x32_bf16 v[14:17], v[140:143], v[206:209], v[14:17]
	v_mfma_f32_16x16x32_bf16 v[10:13], v[154:157], v[206:209], v[10:13]
	v_mfma_f32_16x16x32_bf16 v[62:65], v[150:153], v[186:189], v[62:65]
	v_mfma_f32_16x16x32_bf16 v[58:61], v[158:161], v[186:189], v[58:61]
	v_mfma_f32_16x16x32_bf16 v[46:49], v[150:153], v[194:197], v[46:49]
	v_mfma_f32_16x16x32_bf16 v[42:45], v[158:161], v[194:197], v[42:45]
	v_mfma_f32_16x16x32_bf16 v[30:33], v[150:153], v[202:205], v[30:33]
	v_mfma_f32_16x16x32_bf16 v[26:29], v[158:161], v[202:205], v[26:29]
	v_mfma_f32_16x16x32_bf16 v[14:17], v[150:153], v[210:213], v[14:17]
	v_mfma_f32_16x16x32_bf16 v[10:13], v[158:161], v[210:213], v[10:13]
	s_setprio 0
	s_setprio 1
	v_mfma_f32_16x16x32_bf16 v[54:57], v[162:165], v[182:185], v[54:57]
	v_mfma_f32_16x16x32_bf16 v[50:53], v[174:177], v[182:185], v[50:53]
	v_mfma_f32_16x16x32_bf16 v[38:41], v[162:165], v[190:193], v[38:41]
	v_mfma_f32_16x16x32_bf16 v[34:37], v[174:177], v[190:193], v[34:37]
	v_mfma_f32_16x16x32_bf16 v[22:25], v[162:165], v[198:201], v[22:25]
	v_mfma_f32_16x16x32_bf16 v[18:21], v[174:177], v[198:201], v[18:21]
	v_mfma_f32_16x16x32_bf16 v[6:9], v[162:165], v[206:209], v[6:9]
	v_mfma_f32_16x16x32_bf16 v[2:5], v[174:177], v[206:209], v[2:5]
	v_mfma_f32_16x16x32_bf16 v[54:57], v[170:173], v[186:189], v[54:57]
	v_mfma_f32_16x16x32_bf16 v[50:53], v[178:181], v[186:189], v[50:53]
	v_mfma_f32_16x16x32_bf16 v[38:41], v[170:173], v[194:197], v[38:41]
	v_mfma_f32_16x16x32_bf16 v[34:37], v[178:181], v[194:197], v[34:37]
	v_mfma_f32_16x16x32_bf16 v[22:25], v[170:173], v[202:205], v[22:25]
	v_mfma_f32_16x16x32_bf16 v[18:21], v[178:181], v[202:205], v[18:21]
	v_mfma_f32_16x16x32_bf16 v[6:9], v[170:173], v[210:213], v[6:9]
	v_mfma_f32_16x16x32_bf16 v[2:5], v[178:181], v[210:213], v[2:5]
	s_setprio 0
	s_add_u32 s64, s64, 0x100
	s_addc_u32 s65, s65, 0
	s_add_u32 s52, s52, 0x100
	s_addc_u32 s53, s53, 0
	s_cmp_ge_i32 s66, s1
	s_mov_b32 s54, s66
	s_cbranch_scc1 .Lrotph12_exitbar
	s_add_i32 s66, s54, 2
	s_add_u32 s55, s52, 0xfffc0080
	s_addc_u32 s58, s53, -1
	s_add_i32 s68, 0, 0x10000
	s_cmp_eq_u32 s60, s54
	s_cselect_b32 s59, s41, s58
	s_cselect_b32 s58, s43, s55
	s_barrier
	s_branch .Lrotph12_body
.Lrotph12_exitbar:
	s_barrier
.Lpeelexitph12:
	s_mov_b64 s[70:71], 0xe800800
	v_mov_b32_e32 v209, v1
	s_and_b64 vcc, exec, s[34:35]
	s_cbranch_vccz .LBB0_1441

.Lpeelph16_0:
	s_add_i32 s91, s64, 2
	s_add_u32 s62, s60, 0x100
	s_addc_u32 s63, s61, 0
	s_add_i32 s92, 0, 0x10000
	s_cmp_eq_u32 s74, s64
	s_cselect_b32 s69, s53, s63
	s_cselect_b32 s68, s52, s62
	s_cselect_b32 s65, s55, s59
	s_cselect_b32 s64, s54, s51
	s_add_i32 s93, 0, 0x14000
	v_add_u32_e32 v2, s92, v196
	v_add_u32_e32 v6, s93, v196
	ds_read_b128 v[26:29], v2
	ds_read_b128 v[30:33], v2 offset:1024
	ds_read_b128 v[18:21], v2 offset:2048
	ds_read_b128 v[22:25], v2 offset:3072
	ds_read_b128 v[10:13], v6
	ds_read_b128 v[14:17], v6 offset:1024
	ds_read_b128 v[2:5], v6 offset:2048
	ds_read_b128 v[6:9], v6 offset:3072
	v_lshl_add_u64 v[216:217], s[60:61], 0, v[184:185]
	s_add_i32 m0, s21, 0xc000
	ds_read_b128 v[170:173], v198
	ds_read_b128 v[174:177], v198 offset:1024
	ds_read_b128 v[186:189], v198 offset:2048
	ds_read_b128 v[190:193], v198 offset:3072
	ds_read_b128 v[200:203], v198 offset:4096
	ds_read_b128 v[204:207], v198 offset:5120
	ds_read_b128 v[208:211], v198 offset:6144
	ds_read_b128 v[212:215], v198 offset:7168
	global_load_lds_dwordx4 v[216:217], off
	v_lshl_add_u64 v[216:217], s[60:61], 0, v[182:183]
	s_add_i32 m0, s21, 0xe000
	s_nop 0
	global_load_lds_dwordx4 v[216:217], off
	s_waitcnt vmcnt(8)
	s_waitcnt lgkmcnt(0)
	s_barrier
	s_setprio 1
	s_waitcnt lgkmcnt(0)
	v_mfma_scale_f32_16x16x128_f8f6f4 v[154:157], v[26:33], v[170:177], 0, v194, v169 op_sel_hi:[0,0,0]
	v_mfma_scale_f32_16x16x128_f8f6f4 v[158:161], v[18:25], v[170:177], 0, v194, v169 op_sel_hi:[0,0,0]
	v_mfma_scale_f32_16x16x128_f8f6f4 v[138:141], v[26:33], v[186:193], 0, v194, v169 op_sel_hi:[0,0,0]
	v_mfma_scale_f32_16x16x128_f8f6f4 v[142:145], v[18:25], v[186:193], 0, v194, v169 op_sel_hi:[0,0,0]
	v_mfma_scale_f32_16x16x128_f8f6f4 v[122:125], v[26:33], v[200:207], 0, v194, v169 op_sel_hi:[0,0,0]
	v_mfma_scale_f32_16x16x128_f8f6f4 v[126:129], v[18:25], v[200:207], 0, v194, v169 op_sel_hi:[0,0,0]
	v_mfma_scale_f32_16x16x128_f8f6f4 v[106:109], v[26:33], v[208:215], 0, v194, v169 op_sel_hi:[0,0,0]
	v_mfma_scale_f32_16x16x128_f8f6f4 v[110:113], v[18:25], v[208:215], 0, v194, v169 op_sel_hi:[0,0,0]
	s_setprio 0
	s_setprio 1
	v_mfma_scale_f32_16x16x128_f8f6f4 v[146:149], v[10:17], v[170:177], 0, v194, v169 op_sel_hi:[0,0,0]
	v_mfma_scale_f32_16x16x128_f8f6f4 v[150:153], v[2:9], v[170:177], 0, v194, v169 op_sel_hi:[0,0,0]
	v_mfma_scale_f32_16x16x128_f8f6f4 v[130:133], v[10:17], v[186:193], 0, v194, v169 op_sel_hi:[0,0,0]
	v_mfma_scale_f32_16x16x128_f8f6f4 v[134:137], v[2:9], v[186:193], 0, v194, v169 op_sel_hi:[0,0,0]
	v_mfma_scale_f32_16x16x128_f8f6f4 v[114:117], v[10:17], v[200:207], 0, v194, v169 op_sel_hi:[0,0,0]
	v_mfma_scale_f32_16x16x128_f8f6f4 v[118:121], v[2:9], v[200:207], 0, v194, v169 op_sel_hi:[0,0,0]
	v_mfma_scale_f32_16x16x128_f8f6f4 v[98:101], v[10:17], v[208:215], 0, v194, v169 op_sel_hi:[0,0,0]
	v_mfma_scale_f32_16x16x128_f8f6f4 v[102:105], v[2:9], v[208:215], 0, v194, v169 op_sel_hi:[0,0,0]
	s_setprio 0
	s_barrier
	s_add_i32 s60, s92, s20
	v_lshl_add_u64 v[186:187], s[64:65], 0, v[164:165]
	s_mov_b32 m0, s60
	ds_read_b128 v[170:173], v198 offset:16384
	ds_read_b128 v[174:177], v198 offset:17408
	ds_read_b128 v[200:203], v198 offset:18432
	ds_read_b128 v[204:207], v198 offset:19456
	ds_read_b128 v[208:211], v198 offset:20480
	ds_read_b128 v[212:215], v198 offset:21504
	ds_read_b128 v[216:219], v198 offset:22528
	ds_read_b128 v[220:223], v198 offset:23552
	global_load_lds_dwordx4 v[186:187], off
	s_add_i32 m0, s60, 0x2000
	s_add_u32 s60, s64, 0x70000
	v_lshl_add_u64 v[188:189], s[64:65], 0, v[180:181]
	s_addc_u32 s61, s65, 0
	s_add_i32 s92, s93, s20
	global_load_lds_dwordx4 v[188:189], off
	v_lshl_add_u64 v[190:191], s[60:61], 0, v[164:165]
	s_mov_b32 m0, s92
	v_lshl_add_u64 v[192:193], s[68:69], 0, v[178:179]
	global_load_lds_dwordx4 v[190:191], off
	v_lshl_add_u64 v[190:191], s[60:61], 0, v[180:181]
	s_add_i32 m0, s92, 0x2000
	s_nop 0
	global_load_lds_dwordx4 v[190:191], off
	v_lshl_add_u64 v[190:191], s[68:69], 0, v[162:163]
	s_mov_b32 m0, s21
	s_nop 0
	global_load_lds_dwordx4 v[190:191], off
	s_mov_b32 m0, s22
	s_nop 0
	global_load_lds_dwordx4 v[192:193], off
	s_waitcnt vmcnt(8)
	s_waitcnt lgkmcnt(0)
	s_barrier
	s_setprio 1
	s_waitcnt lgkmcnt(0)
	v_mfma_scale_f32_16x16x128_f8f6f4 v[90:93], v[26:33], v[170:177], 0, v194, v169 op_sel_hi:[0,0,0]
	v_mfma_scale_f32_16x16x128_f8f6f4 v[94:97], v[18:25], v[170:177], 0, v194, v169 op_sel_hi:[0,0,0]
	v_mfma_scale_f32_16x16x128_f8f6f4 v[74:77], v[26:33], v[200:207], 0, v194, v169 op_sel_hi:[0,0,0]
	v_mfma_scale_f32_16x16x128_f8f6f4 v[78:81], v[18:25], v[200:207], 0, v194, v169 op_sel_hi:[0,0,0]
	v_mfma_scale_f32_16x16x128_f8f6f4 v[58:61], v[26:33], v[208:215], 0, v194, v169 op_sel_hi:[0,0,0]
	v_mfma_scale_f32_16x16x128_f8f6f4 v[62:65], v[18:25], v[208:215], 0, v194, v169 op_sel_hi:[0,0,0]
	v_mfma_scale_f32_16x16x128_f8f6f4 v[42:45], v[26:33], v[216:223], 0, v194, v169 op_sel_hi:[0,0,0]
	v_mfma_scale_f32_16x16x128_f8f6f4 v[46:49], v[18:25], v[216:223], 0, v194, v169 op_sel_hi:[0,0,0]
	s_setprio 0
	s_setprio 1
	v_mfma_scale_f32_16x16x128_f8f6f4 v[82:85], v[10:17], v[170:177], 0, v194, v169 op_sel_hi:[0,0,0]
	v_mfma_scale_f32_16x16x128_f8f6f4 v[86:89], v[2:9], v[170:177], 0, v194, v169 op_sel_hi:[0,0,0]
	v_mfma_scale_f32_16x16x128_f8f6f4 v[66:69], v[10:17], v[200:207], 0, v194, v169 op_sel_hi:[0,0,0]
	v_mfma_scale_f32_16x16x128_f8f6f4 v[70:73], v[2:9], v[200:207], 0, v194, v169 op_sel_hi:[0,0,0]
	v_mfma_scale_f32_16x16x128_f8f6f4 v[50:53], v[10:17], v[208:215], 0, v194, v169 op_sel_hi:[0,0,0]
	v_mfma_scale_f32_16x16x128_f8f6f4 v[54:57], v[2:9], v[208:215], 0, v194, v169 op_sel_hi:[0,0,0]
	v_mfma_scale_f32_16x16x128_f8f6f4 v[34:37], v[10:17], v[216:223], 0, v194, v169 op_sel_hi:[0,0,0]
	v_mfma_scale_f32_16x16x128_f8f6f4 v[38:41], v[2:9], v[216:223], 0, v194, v169 op_sel_hi:[0,0,0]
	s_setprio 0
	s_barrier
	s_add_i32 s92, 0, 0x18000
	s_add_i32 s93, 0, 0x1c000
	v_add_u32_e32 v2, s92, v196
	v_add_u32_e32 v6, s93, v196
	ds_read_b128 v[26:29], v2
	ds_read_b128 v[30:33], v2 offset:1024
	ds_read_b128 v[18:21], v2 offset:2048
	ds_read_b128 v[22:25], v2 offset:3072
	ds_read_b128 v[10:13], v6
	ds_read_b128 v[14:17], v6 offset:1024
	ds_read_b128 v[2:5], v6 offset:2048
	ds_read_b128 v[6:9], v6 offset:3072
	s_add_u32 s60, s68, 0x70000
	s_addc_u32 s61, s69, 0
	s_mov_b32 m0, s23
	v_lshl_add_u64 v[232:233], s[60:61], 0, v[162:163]
	ds_read_b128 v[170:173], v198 offset:32768
	ds_read_b128 v[174:177], v198 offset:33792
	ds_read_b128 v[200:203], v198 offset:34816
	ds_read_b128 v[204:207], v198 offset:35840
	ds_read_b128 v[208:211], v198 offset:36864
	ds_read_b128 v[212:215], v198 offset:37888
	ds_read_b128 v[216:219], v198 offset:38912
	ds_read_b128 v[220:223], v198 offset:39936
	global_load_lds_dwordx4 v[232:233], off
	v_lshl_add_u64 v[232:233], s[60:61], 0, v[178:179]
	s_mov_b32 m0, s70
	s_nop 0
	global_load_lds_dwordx4 v[232:233], off
	s_waitcnt vmcnt(8)
	s_waitcnt lgkmcnt(0)
	s_barrier
	s_setprio 1
	s_waitcnt lgkmcnt(0)
	v_mfma_scale_f32_16x16x128_f8f6f4 v[154:157], v[26:33], v[170:177], v[154:157], v194, v169 op_sel_hi:[0,0,0]
	v_mfma_scale_f32_16x16x128_f8f6f4 v[158:161], v[18:25], v[170:177], v[158:161], v194, v169 op_sel_hi:[0,0,0]
	v_mfma_scale_f32_16x16x128_f8f6f4 v[138:141], v[26:33], v[200:207], v[138:141], v194, v169 op_sel_hi:[0,0,0]
	v_mfma_scale_f32_16x16x128_f8f6f4 v[142:145], v[18:25], v[200:207], v[142:145], v194, v169 op_sel_hi:[0,0,0]
	v_mfma_scale_f32_16x16x128_f8f6f4 v[122:125], v[26:33], v[208:215], v[122:125], v194, v169 op_sel_hi:[0,0,0]
	v_mfma_scale_f32_16x16x128_f8f6f4 v[126:129], v[18:25], v[208:215], v[126:129], v194, v169 op_sel_hi:[0,0,0]
	v_mfma_scale_f32_16x16x128_f8f6f4 v[106:109], v[26:33], v[216:223], v[106:109], v194, v169 op_sel_hi:[0,0,0]
	v_mfma_scale_f32_16x16x128_f8f6f4 v[110:113], v[18:25], v[216:223], v[110:113], v194, v169 op_sel_hi:[0,0,0]
	s_setprio 0
	s_setprio 1
	v_mfma_scale_f32_16x16x128_f8f6f4 v[146:149], v[10:17], v[170:177], v[146:149], v194, v169 op_sel_hi:[0,0,0]
	v_mfma_scale_f32_16x16x128_f8f6f4 v[150:153], v[2:9], v[170:177], v[150:153], v194, v169 op_sel_hi:[0,0,0]
	v_mfma_scale_f32_16x16x128_f8f6f4 v[130:133], v[10:17], v[200:207], v[130:133], v194, v169 op_sel_hi:[0,0,0]
	v_mfma_scale_f32_16x16x128_f8f6f4 v[134:137], v[2:9], v[200:207], v[134:137], v194, v169 op_sel_hi:[0,0,0]
	v_mfma_scale_f32_16x16x128_f8f6f4 v[114:117], v[10:17], v[208:215], v[114:117], v194, v169 op_sel_hi:[0,0,0]
	v_mfma_scale_f32_16x16x128_f8f6f4 v[118:121], v[2:9], v[208:215], v[118:121], v194, v169 op_sel_hi:[0,0,0]
	v_mfma_scale_f32_16x16x128_f8f6f4 v[98:101], v[10:17], v[216:223], v[98:101], v194, v169 op_sel_hi:[0,0,0]
	v_mfma_scale_f32_16x16x128_f8f6f4 v[102:105], v[2:9], v[216:223], v[102:105], v194, v169 op_sel_hi:[0,0,0]
	s_setprio 0
	s_barrier
	s_add_i32 s60, s92, s20
	v_lshl_add_u64 v[186:187], v[186:187], 0, s[56:57]
	s_mov_b32 m0, s60
	ds_read_b128 v[170:173], v198 offset:49152
	ds_read_b128 v[174:177], v198 offset:50176
	ds_read_b128 v[200:203], v198 offset:51200
	ds_read_b128 v[204:207], v198 offset:52224
	ds_read_b128 v[208:211], v198 offset:53248
	ds_read_b128 v[212:215], v198 offset:54272
	ds_read_b128 v[216:219], v198 offset:55296
	ds_read_b128 v[220:223], v198 offset:56320
	global_load_lds_dwordx4 v[186:187], off
	s_add_i32 m0, s60, 0x2000
	s_add_u32 s60, s64, 0x70080
	v_lshl_add_u64 v[186:187], v[188:189], 0, s[56:57]
	s_addc_u32 s61, s65, 0
	s_add_i32 s64, s93, s20
	global_load_lds_dwordx4 v[186:187], off
	v_lshl_add_u64 v[186:187], s[60:61], 0, v[164:165]
	s_mov_b32 m0, s64
	s_nop 0
	global_load_lds_dwordx4 v[186:187], off
	v_lshl_add_u64 v[186:187], s[60:61], 0, v[180:181]
	s_add_i32 m0, s64, 0x2000
	s_nop 0
	global_load_lds_dwordx4 v[186:187], off
	v_lshl_add_u64 v[186:187], v[190:191], 0, s[56:57]
	s_mov_b32 m0, s71
	s_nop 0
	global_load_lds_dwordx4 v[186:187], off
	v_lshl_add_u64 v[186:187], v[192:193], 0, s[56:57]
	s_mov_b32 m0, s72
	s_nop 0
	global_load_lds_dwordx4 v[186:187], off
	s_waitcnt vmcnt(8)
	s_waitcnt lgkmcnt(0)
	s_barrier
	s_setprio 1
	s_waitcnt lgkmcnt(0)
	v_mfma_scale_f32_16x16x128_f8f6f4 v[90:93], v[26:33], v[170:177], v[90:93], v194, v169 op_sel_hi:[0,0,0]
	v_mfma_scale_f32_16x16x128_f8f6f4 v[94:97], v[18:25], v[170:177], v[94:97], v194, v169 op_sel_hi:[0,0,0]
	v_mfma_scale_f32_16x16x128_f8f6f4 v[74:77], v[26:33], v[200:207], v[74:77], v194, v169 op_sel_hi:[0,0,0]
	v_mfma_scale_f32_16x16x128_f8f6f4 v[78:81], v[18:25], v[200:207], v[78:81], v194, v169 op_sel_hi:[0,0,0]
	v_mfma_scale_f32_16x16x128_f8f6f4 v[58:61], v[26:33], v[208:215], v[58:61], v194, v169 op_sel_hi:[0,0,0]
	v_mfma_scale_f32_16x16x128_f8f6f4 v[62:65], v[18:25], v[208:215], v[62:65], v194, v169 op_sel_hi:[0,0,0]
	v_mfma_scale_f32_16x16x128_f8f6f4 v[42:45], v[26:33], v[216:223], v[42:45], v194, v169 op_sel_hi:[0,0,0]
	v_mfma_scale_f32_16x16x128_f8f6f4 v[46:49], v[18:25], v[216:223], v[46:49], v194, v169 op_sel_hi:[0,0,0]
	s_setprio 0
	s_setprio 1
	v_mfma_scale_f32_16x16x128_f8f6f4 v[82:85], v[10:17], v[170:177], v[82:85], v194, v169 op_sel_hi:[0,0,0]
	v_mfma_scale_f32_16x16x128_f8f6f4 v[86:89], v[2:9], v[170:177], v[86:89], v194, v169 op_sel_hi:[0,0,0]
	v_mfma_scale_f32_16x16x128_f8f6f4 v[66:69], v[10:17], v[200:207], v[66:69], v194, v169 op_sel_hi:[0,0,0]
	v_mfma_scale_f32_16x16x128_f8f6f4 v[70:73], v[2:9], v[200:207], v[70:73], v194, v169 op_sel_hi:[0,0,0]
	v_mfma_scale_f32_16x16x128_f8f6f4 v[50:53], v[10:17], v[208:215], v[50:53], v194, v169 op_sel_hi:[0,0,0]
	v_mfma_scale_f32_16x16x128_f8f6f4 v[54:57], v[2:9], v[208:215], v[54:57], v194, v169 op_sel_hi:[0,0,0]
	v_mfma_scale_f32_16x16x128_f8f6f4 v[34:37], v[10:17], v[216:223], v[34:37], v194, v169 op_sel_hi:[0,0,0]
	v_mfma_scale_f32_16x16x128_f8f6f4 v[38:41], v[2:9], v[216:223], v[38:41], v194, v169 op_sel_hi:[0,0,0]
	s_setprio 0
	s_add_u32 s51, s51, 0x100
	s_addc_u32 s59, s59, 0
	s_cmp_ge_i32 s91, s8
	s_mov_b64 s[60:61], s[62:63]
	s_mov_b32 s64, s91
	s_cbranch_scc1 .Lrotph16_pexitbar
	s_add_i32 s91, s64, 2
	s_add_u32 s62, s60, 0x100
	s_addc_u32 s63, s61, 0
	s_add_i32 s92, 0, 0x10000
	s_cmp_eq_u32 s74, s64
	s_cselect_b32 s69, s53, s63
	s_cselect_b32 s68, s52, s62
	s_cselect_b32 s65, s55, s59
	s_cselect_b32 s64, s54, s51
	s_add_i32 s93, 0, 0x14000
	s_barrier
	s_branch .Lrotph16_body

.Lrotph16_body:
	v_add_u32_e32 v2, s92, v196
	v_add_u32_e32 v6, s93, v196
	ds_read_b128 v[26:29], v2
	ds_read_b128 v[30:33], v2 offset:1024
	ds_read_b128 v[18:21], v2 offset:2048
	ds_read_b128 v[22:25], v2 offset:3072
	ds_read_b128 v[10:13], v6
	ds_read_b128 v[14:17], v6 offset:1024
	ds_read_b128 v[2:5], v6 offset:2048
	ds_read_b128 v[6:9], v6 offset:3072
	v_lshl_add_u64 v[216:217], s[60:61], 0, v[184:185]
	s_add_i32 m0, s21, 0xc000
	ds_read_b128 v[170:173], v198
	ds_read_b128 v[174:177], v198 offset:1024
	ds_read_b128 v[186:189], v198 offset:2048
	ds_read_b128 v[190:193], v198 offset:3072
	ds_read_b128 v[200:203], v198 offset:4096
	ds_read_b128 v[204:207], v198 offset:5120
	ds_read_b128 v[208:211], v198 offset:6144
	ds_read_b128 v[212:215], v198 offset:7168
	global_load_lds_dwordx4 v[216:217], off
	v_lshl_add_u64 v[216:217], s[60:61], 0, v[182:183]
	s_add_i32 m0, s21, 0xe000
	s_nop 0
	global_load_lds_dwordx4 v[216:217], off
	s_waitcnt vmcnt(8)
	s_waitcnt lgkmcnt(0)
	s_barrier
	s_setprio 1
	s_waitcnt lgkmcnt(0)
	v_mfma_scale_f32_16x16x128_f8f6f4 v[154:157], v[26:33], v[170:177], v[154:157], v194, v169 op_sel_hi:[0,0,0]
	v_mfma_scale_f32_16x16x128_f8f6f4 v[158:161], v[18:25], v[170:177], v[158:161], v194, v169 op_sel_hi:[0,0,0]
	v_mfma_scale_f32_16x16x128_f8f6f4 v[138:141], v[26:33], v[186:193], v[138:141], v194, v169 op_sel_hi:[0,0,0]
	v_mfma_scale_f32_16x16x128_f8f6f4 v[142:145], v[18:25], v[186:193], v[142:145], v194, v169 op_sel_hi:[0,0,0]
	v_mfma_scale_f32_16x16x128_f8f6f4 v[122:125], v[26:33], v[200:207], v[122:125], v194, v169 op_sel_hi:[0,0,0]
	v_mfma_scale_f32_16x16x128_f8f6f4 v[126:129], v[18:25], v[200:207], v[126:129], v194, v169 op_sel_hi:[0,0,0]
	v_mfma_scale_f32_16x16x128_f8f6f4 v[106:109], v[26:33], v[208:215], v[106:109], v194, v169 op_sel_hi:[0,0,0]
	v_mfma_scale_f32_16x16x128_f8f6f4 v[110:113], v[18:25], v[208:215], v[110:113], v194, v169 op_sel_hi:[0,0,0]
	s_setprio 0
	s_setprio 1
	v_mfma_scale_f32_16x16x128_f8f6f4 v[146:149], v[10:17], v[170:177], v[146:149], v194, v169 op_sel_hi:[0,0,0]
	v_mfma_scale_f32_16x16x128_f8f6f4 v[150:153], v[2:9], v[170:177], v[150:153], v194, v169 op_sel_hi:[0,0,0]
	v_mfma_scale_f32_16x16x128_f8f6f4 v[130:133], v[10:17], v[186:193], v[130:133], v194, v169 op_sel_hi:[0,0,0]
	v_mfma_scale_f32_16x16x128_f8f6f4 v[134:137], v[2:9], v[186:193], v[134:137], v194, v169 op_sel_hi:[0,0,0]
	v_mfma_scale_f32_16x16x128_f8f6f4 v[114:117], v[10:17], v[200:207], v[114:117], v194, v169 op_sel_hi:[0,0,0]
	v_mfma_scale_f32_16x16x128_f8f6f4 v[118:121], v[2:9], v[200:207], v[118:121], v194, v169 op_sel_hi:[0,0,0]
	v_mfma_scale_f32_16x16x128_f8f6f4 v[98:101], v[10:17], v[208:215], v[98:101], v194, v169 op_sel_hi:[0,0,0]
	v_mfma_scale_f32_16x16x128_f8f6f4 v[102:105], v[2:9], v[208:215], v[102:105], v194, v169 op_sel_hi:[0,0,0]
	s_setprio 0
	s_barrier
	s_add_i32 s60, s92, s20
	v_lshl_add_u64 v[186:187], s[64:65], 0, v[164:165]
	s_mov_b32 m0, s60
	ds_read_b128 v[170:173], v198 offset:16384
	ds_read_b128 v[174:177], v198 offset:17408
	ds_read_b128 v[200:203], v198 offset:18432
	ds_read_b128 v[204:207], v198 offset:19456
	ds_read_b128 v[208:211], v198 offset:20480
	ds_read_b128 v[212:215], v198 offset:21504
	ds_read_b128 v[216:219], v198 offset:22528
	ds_read_b128 v[220:223], v198 offset:23552
	global_load_lds_dwordx4 v[186:187], off
	s_add_i32 m0, s60, 0x2000
	s_add_u32 s60, s64, 0x70000
	v_lshl_add_u64 v[188:189], s[64:65], 0, v[180:181]
	s_addc_u32 s61, s65, 0
	s_add_i32 s92, s93, s20
	global_load_lds_dwordx4 v[188:189], off
	v_lshl_add_u64 v[190:191], s[60:61], 0, v[164:165]
	s_mov_b32 m0, s92
	v_lshl_add_u64 v[192:193], s[68:69], 0, v[178:179]
	global_load_lds_dwordx4 v[190:191], off
	v_lshl_add_u64 v[190:191], s[60:61], 0, v[180:181]
	s_add_i32 m0, s92, 0x2000
	s_nop 0
	global_load_lds_dwordx4 v[190:191], off
	v_lshl_add_u64 v[190:191], s[68:69], 0, v[162:163]
	s_mov_b32 m0, s21
	s_nop 0
	global_load_lds_dwordx4 v[190:191], off
	s_mov_b32 m0, s22
	s_nop 0
	global_load_lds_dwordx4 v[192:193], off
	s_waitcnt vmcnt(8)
	s_waitcnt lgkmcnt(0)
	s_barrier
	s_setprio 1
	s_waitcnt lgkmcnt(0)
	v_mfma_scale_f32_16x16x128_f8f6f4 v[90:93], v[26:33], v[170:177], v[90:93], v194, v169 op_sel_hi:[0,0,0]
	v_mfma_scale_f32_16x16x128_f8f6f4 v[94:97], v[18:25], v[170:177], v[94:97], v194, v169 op_sel_hi:[0,0,0]
	v_mfma_scale_f32_16x16x128_f8f6f4 v[74:77], v[26:33], v[200:207], v[74:77], v194, v169 op_sel_hi:[0,0,0]
	v_mfma_scale_f32_16x16x128_f8f6f4 v[78:81], v[18:25], v[200:207], v[78:81], v194, v169 op_sel_hi:[0,0,0]
	v_mfma_scale_f32_16x16x128_f8f6f4 v[58:61], v[26:33], v[208:215], v[58:61], v194, v169 op_sel_hi:[0,0,0]
	v_mfma_scale_f32_16x16x128_f8f6f4 v[62:65], v[18:25], v[208:215], v[62:65], v194, v169 op_sel_hi:[0,0,0]
	v_mfma_scale_f32_16x16x128_f8f6f4 v[42:45], v[26:33], v[216:223], v[42:45], v194, v169 op_sel_hi:[0,0,0]
	v_mfma_scale_f32_16x16x128_f8f6f4 v[46:49], v[18:25], v[216:223], v[46:49], v194, v169 op_sel_hi:[0,0,0]
	s_setprio 0
	s_setprio 1
	v_mfma_scale_f32_16x16x128_f8f6f4 v[82:85], v[10:17], v[170:177], v[82:85], v194, v169 op_sel_hi:[0,0,0]
	v_mfma_scale_f32_16x16x128_f8f6f4 v[86:89], v[2:9], v[170:177], v[86:89], v194, v169 op_sel_hi:[0,0,0]
	v_mfma_scale_f32_16x16x128_f8f6f4 v[66:69], v[10:17], v[200:207], v[66:69], v194, v169 op_sel_hi:[0,0,0]
	v_mfma_scale_f32_16x16x128_f8f6f4 v[70:73], v[2:9], v[200:207], v[70:73], v194, v169 op_sel_hi:[0,0,0]
	v_mfma_scale_f32_16x16x128_f8f6f4 v[50:53], v[10:17], v[208:215], v[50:53], v194, v169 op_sel_hi:[0,0,0]
	v_mfma_scale_f32_16x16x128_f8f6f4 v[54:57], v[2:9], v[208:215], v[54:57], v194, v169 op_sel_hi:[0,0,0]
	v_mfma_scale_f32_16x16x128_f8f6f4 v[34:37], v[10:17], v[216:223], v[34:37], v194, v169 op_sel_hi:[0,0,0]
	v_mfma_scale_f32_16x16x128_f8f6f4 v[38:41], v[2:9], v[216:223], v[38:41], v194, v169 op_sel_hi:[0,0,0]
	s_setprio 0
	s_barrier
	s_add_i32 s92, 0, 0x18000
	s_add_i32 s93, 0, 0x1c000
	v_add_u32_e32 v2, s92, v196
	v_add_u32_e32 v6, s93, v196
	ds_read_b128 v[26:29], v2
	ds_read_b128 v[30:33], v2 offset:1024
	ds_read_b128 v[18:21], v2 offset:2048
	ds_read_b128 v[22:25], v2 offset:3072
	ds_read_b128 v[10:13], v6
	ds_read_b128 v[14:17], v6 offset:1024
	ds_read_b128 v[2:5], v6 offset:2048
	ds_read_b128 v[6:9], v6 offset:3072
	s_add_u32 s60, s68, 0x70000
	s_addc_u32 s61, s69, 0
	s_mov_b32 m0, s23
	v_lshl_add_u64 v[232:233], s[60:61], 0, v[162:163]
	ds_read_b128 v[170:173], v198 offset:32768
	ds_read_b128 v[174:177], v198 offset:33792
	ds_read_b128 v[200:203], v198 offset:34816
	ds_read_b128 v[204:207], v198 offset:35840
	ds_read_b128 v[208:211], v198 offset:36864
	ds_read_b128 v[212:215], v198 offset:37888
	ds_read_b128 v[216:219], v198 offset:38912
	ds_read_b128 v[220:223], v198 offset:39936
	global_load_lds_dwordx4 v[232:233], off
	v_lshl_add_u64 v[232:233], s[60:61], 0, v[178:179]
	s_mov_b32 m0, s70
	s_nop 0
	global_load_lds_dwordx4 v[232:233], off
	s_waitcnt vmcnt(8)
	s_waitcnt lgkmcnt(0)
	s_barrier
	s_setprio 1
	s_waitcnt lgkmcnt(0)
	v_mfma_scale_f32_16x16x128_f8f6f4 v[154:157], v[26:33], v[170:177], v[154:157], v194, v169 op_sel_hi:[0,0,0]
	v_mfma_scale_f32_16x16x128_f8f6f4 v[158:161], v[18:25], v[170:177], v[158:161], v194, v169 op_sel_hi:[0,0,0]
	v_mfma_scale_f32_16x16x128_f8f6f4 v[138:141], v[26:33], v[200:207], v[138:141], v194, v169 op_sel_hi:[0,0,0]
	v_mfma_scale_f32_16x16x128_f8f6f4 v[142:145], v[18:25], v[200:207], v[142:145], v194, v169 op_sel_hi:[0,0,0]
	v_mfma_scale_f32_16x16x128_f8f6f4 v[122:125], v[26:33], v[208:215], v[122:125], v194, v169 op_sel_hi:[0,0,0]
	v_mfma_scale_f32_16x16x128_f8f6f4 v[126:129], v[18:25], v[208:215], v[126:129], v194, v169 op_sel_hi:[0,0,0]
	v_mfma_scale_f32_16x16x128_f8f6f4 v[106:109], v[26:33], v[216:223], v[106:109], v194, v169 op_sel_hi:[0,0,0]
	v_mfma_scale_f32_16x16x128_f8f6f4 v[110:113], v[18:25], v[216:223], v[110:113], v194, v169 op_sel_hi:[0,0,0]
	s_setprio 0
	s_setprio 1
	v_mfma_scale_f32_16x16x128_f8f6f4 v[146:149], v[10:17], v[170:177], v[146:149], v194, v169 op_sel_hi:[0,0,0]
	v_mfma_scale_f32_16x16x128_f8f6f4 v[150:153], v[2:9], v[170:177], v[150:153], v194, v169 op_sel_hi:[0,0,0]
	v_mfma_scale_f32_16x16x128_f8f6f4 v[130:133], v[10:17], v[200:207], v[130:133], v194, v169 op_sel_hi:[0,0,0]
	v_mfma_scale_f32_16x16x128_f8f6f4 v[134:137], v[2:9], v[200:207], v[134:137], v194, v169 op_sel_hi:[0,0,0]
	v_mfma_scale_f32_16x16x128_f8f6f4 v[114:117], v[10:17], v[208:215], v[114:117], v194, v169 op_sel_hi:[0,0,0]
	v_mfma_scale_f32_16x16x128_f8f6f4 v[118:121], v[2:9], v[208:215], v[118:121], v194, v169 op_sel_hi:[0,0,0]
	v_mfma_scale_f32_16x16x128_f8f6f4 v[98:101], v[10:17], v[216:223], v[98:101], v194, v169 op_sel_hi:[0,0,0]
	v_mfma_scale_f32_16x16x128_f8f6f4 v[102:105], v[2:9], v[216:223], v[102:105], v194, v169 op_sel_hi:[0,0,0]
	s_setprio 0
	s_barrier
	s_add_i32 s60, s92, s20
	v_lshl_add_u64 v[186:187], v[186:187], 0, s[56:57]
	s_mov_b32 m0, s60
	ds_read_b128 v[170:173], v198 offset:49152
	ds_read_b128 v[174:177], v198 offset:50176
	ds_read_b128 v[200:203], v198 offset:51200
	ds_read_b128 v[204:207], v198 offset:52224
	ds_read_b128 v[208:211], v198 offset:53248
	ds_read_b128 v[212:215], v198 offset:54272
	ds_read_b128 v[216:219], v198 offset:55296
	ds_read_b128 v[220:223], v198 offset:56320
	global_load_lds_dwordx4 v[186:187], off
	s_add_i32 m0, s60, 0x2000
	s_add_u32 s60, s64, 0x70080
	v_lshl_add_u64 v[186:187], v[188:189], 0, s[56:57]
	s_addc_u32 s61, s65, 0
	s_add_i32 s64, s93, s20
	global_load_lds_dwordx4 v[186:187], off
	v_lshl_add_u64 v[186:187], s[60:61], 0, v[164:165]
	s_mov_b32 m0, s64
	s_nop 0
	global_load_lds_dwordx4 v[186:187], off
	v_lshl_add_u64 v[186:187], s[60:61], 0, v[180:181]
	s_add_i32 m0, s64, 0x2000
	s_nop 0
	global_load_lds_dwordx4 v[186:187], off
	v_lshl_add_u64 v[186:187], v[190:191], 0, s[56:57]
	s_mov_b32 m0, s71
	s_nop 0
	global_load_lds_dwordx4 v[186:187], off
	v_lshl_add_u64 v[186:187], v[192:193], 0, s[56:57]
	s_mov_b32 m0, s72
	s_nop 0
	global_load_lds_dwordx4 v[186:187], off
	s_waitcnt vmcnt(8)
	s_waitcnt lgkmcnt(0)
	s_barrier
	s_setprio 1
	s_waitcnt lgkmcnt(0)
	v_mfma_scale_f32_16x16x128_f8f6f4 v[90:93], v[26:33], v[170:177], v[90:93], v194, v169 op_sel_hi:[0,0,0]
	v_mfma_scale_f32_16x16x128_f8f6f4 v[94:97], v[18:25], v[170:177], v[94:97], v194, v169 op_sel_hi:[0,0,0]
	v_mfma_scale_f32_16x16x128_f8f6f4 v[74:77], v[26:33], v[200:207], v[74:77], v194, v169 op_sel_hi:[0,0,0]
	v_mfma_scale_f32_16x16x128_f8f6f4 v[78:81], v[18:25], v[200:207], v[78:81], v194, v169 op_sel_hi:[0,0,0]
	v_mfma_scale_f32_16x16x128_f8f6f4 v[58:61], v[26:33], v[208:215], v[58:61], v194, v169 op_sel_hi:[0,0,0]
	v_mfma_scale_f32_16x16x128_f8f6f4 v[62:65], v[18:25], v[208:215], v[62:65], v194, v169 op_sel_hi:[0,0,0]
	v_mfma_scale_f32_16x16x128_f8f6f4 v[42:45], v[26:33], v[216:223], v[42:45], v194, v169 op_sel_hi:[0,0,0]
	v_mfma_scale_f32_16x16x128_f8f6f4 v[46:49], v[18:25], v[216:223], v[46:49], v194, v169 op_sel_hi:[0,0,0]
	s_setprio 0
	s_setprio 1
	v_mfma_scale_f32_16x16x128_f8f6f4 v[82:85], v[10:17], v[170:177], v[82:85], v194, v169 op_sel_hi:[0,0,0]
	v_mfma_scale_f32_16x16x128_f8f6f4 v[86:89], v[2:9], v[170:177], v[86:89], v194, v169 op_sel_hi:[0,0,0]
	v_mfma_scale_f32_16x16x128_f8f6f4 v[66:69], v[10:17], v[200:207], v[66:69], v194, v169 op_sel_hi:[0,0,0]
	v_mfma_scale_f32_16x16x128_f8f6f4 v[70:73], v[2:9], v[200:207], v[70:73], v194, v169 op_sel_hi:[0,0,0]
	v_mfma_scale_f32_16x16x128_f8f6f4 v[50:53], v[10:17], v[208:215], v[50:53], v194, v169 op_sel_hi:[0,0,0]
	v_mfma_scale_f32_16x16x128_f8f6f4 v[54:57], v[2:9], v[208:215], v[54:57], v194, v169 op_sel_hi:[0,0,0]
	v_mfma_scale_f32_16x16x128_f8f6f4 v[34:37], v[10:17], v[216:223], v[34:37], v194, v169 op_sel_hi:[0,0,0]
	v_mfma_scale_f32_16x16x128_f8f6f4 v[38:41], v[2:9], v[216:223], v[38:41], v194, v169 op_sel_hi:[0,0,0]
	s_setprio 0
	s_add_u32 s51, s51, 0x100
	s_addc_u32 s59, s59, 0
	s_cmp_ge_i32 s91, s8
	s_mov_b64 s[60:61], s[62:63]
	s_mov_b32 s64, s91
	s_cbranch_scc1 .Lrotph16_exitbar
	s_add_i32 s91, s64, 2
	s_add_u32 s62, s60, 0x100
	s_addc_u32 s63, s61, 0
	s_add_i32 s92, 0, 0x10000
	s_cmp_eq_u32 s74, s64
	s_cselect_b32 s69, s53, s63
	s_cselect_b32 s68, s52, s62
	s_cselect_b32 s65, s55, s59
	s_cselect_b32 s64, s54, s51
	s_add_i32 s93, 0, 0x14000
	s_barrier
	s_branch .Lrotph16_body
.Lrotph16_exitbar:
	s_barrier
.Lpeelexitph16:
	s_movk_i32 s93, 0x1000
	v_mov_b32_e32 v209, v1
	s_and_b64 vcc, exec, s[44:45]
	s_cbranch_vccz .LBB0_1780

.Lpeelph18_0:
	s_add_i32 s75, s70, 2
	s_add_u32 s42, s18, 0x100
	s_addc_u32 s43, s19, 0
	s_add_i32 s46, 0, 0x10000
	s_cmp_eq_u32 s14, s70
	s_cselect_b32 vcc_hi, s69, s43
	s_cselect_b32 vcc_lo, s68, s42
	s_cselect_b32 s71, s37, s45
	s_cselect_b32 s70, s36, s35
	s_add_i32 s47, 0, 0x14000
	v_add_u32_e32 v2, s46, v196
	v_add_u32_e32 v6, s47, v196
	ds_read_b128 v[26:29], v2
	ds_read_b128 v[30:33], v2 offset:1024
	ds_read_b128 v[18:21], v2 offset:2048
	ds_read_b128 v[22:25], v2 offset:3072
	ds_read_b128 v[10:13], v6
	ds_read_b128 v[14:17], v6 offset:1024
	ds_read_b128 v[2:5], v6 offset:2048
	ds_read_b128 v[6:9], v6 offset:3072
	v_lshl_add_u64 v[218:219], s[18:19], 0, v[184:185]
	s_add_i32 m0, s73, 0xc000
	ds_read_b128 v[170:173], v201
	ds_read_b128 v[174:177], v201 offset:1024
	ds_read_b128 v[186:189], v201 offset:2048
	ds_read_b128 v[190:193], v201 offset:3072
	ds_read_b128 v[202:205], v201 offset:4096
	ds_read_b128 v[206:209], v201 offset:5120
	ds_read_b128 v[210:213], v201 offset:6144
	ds_read_b128 v[214:217], v201 offset:7168
	global_load_lds_dwordx4 v[218:219], off
	v_lshl_add_u64 v[218:219], s[18:19], 0, v[182:183]
	s_add_i32 m0, s73, 0xe000
	s_nop 0
	global_load_lds_dwordx4 v[218:219], off
	s_waitcnt vmcnt(8)
	s_waitcnt lgkmcnt(0)
	s_barrier
	s_setprio 1
	s_waitcnt lgkmcnt(0)
	v_mfma_scale_f32_16x16x128_f8f6f4 v[158:161], v[26:33], v[170:177], 0, v194, v169 op_sel_hi:[0,0,0]
	v_mfma_scale_f32_16x16x128_f8f6f4 v[154:157], v[18:25], v[170:177], 0, v194, v169 op_sel_hi:[0,0,0]
	v_mfma_scale_f32_16x16x128_f8f6f4 v[142:145], v[26:33], v[186:193], 0, v194, v169 op_sel_hi:[0,0,0]
	v_mfma_scale_f32_16x16x128_f8f6f4 v[138:141], v[18:25], v[186:193], 0, v194, v169 op_sel_hi:[0,0,0]
	v_mfma_scale_f32_16x16x128_f8f6f4 v[126:129], v[26:33], v[202:209], 0, v194, v169 op_sel_hi:[0,0,0]
	v_mfma_scale_f32_16x16x128_f8f6f4 v[122:125], v[18:25], v[202:209], 0, v194, v169 op_sel_hi:[0,0,0]
	v_mfma_scale_f32_16x16x128_f8f6f4 v[110:113], v[26:33], v[210:217], 0, v194, v169 op_sel_hi:[0,0,0]
	v_mfma_scale_f32_16x16x128_f8f6f4 v[106:109], v[18:25], v[210:217], 0, v194, v169 op_sel_hi:[0,0,0]
	s_setprio 0
	s_setprio 1
	v_mfma_scale_f32_16x16x128_f8f6f4 v[150:153], v[10:17], v[170:177], 0, v194, v169 op_sel_hi:[0,0,0]
	v_mfma_scale_f32_16x16x128_f8f6f4 v[146:149], v[2:9], v[170:177], 0, v194, v169 op_sel_hi:[0,0,0]
	v_mfma_scale_f32_16x16x128_f8f6f4 v[134:137], v[10:17], v[186:193], 0, v194, v169 op_sel_hi:[0,0,0]
	v_mfma_scale_f32_16x16x128_f8f6f4 v[130:133], v[2:9], v[186:193], 0, v194, v169 op_sel_hi:[0,0,0]
	v_mfma_scale_f32_16x16x128_f8f6f4 v[118:121], v[10:17], v[202:209], 0, v194, v169 op_sel_hi:[0,0,0]
	v_mfma_scale_f32_16x16x128_f8f6f4 v[114:117], v[2:9], v[202:209], 0, v194, v169 op_sel_hi:[0,0,0]
	v_mfma_scale_f32_16x16x128_f8f6f4 v[102:105], v[10:17], v[210:217], 0, v194, v169 op_sel_hi:[0,0,0]
	v_mfma_scale_f32_16x16x128_f8f6f4 v[98:101], v[2:9], v[210:217], 0, v194, v169 op_sel_hi:[0,0,0]
	s_setprio 0
	s_barrier
	s_add_i32 s18, s46, s95
	v_lshl_add_u64 v[186:187], s[70:71], 0, v[164:165]
	s_mov_b32 m0, s18
	ds_read_b128 v[170:173], v201 offset:16384
	ds_read_b128 v[174:177], v201 offset:17408
	ds_read_b128 v[202:205], v201 offset:18432
	ds_read_b128 v[206:209], v201 offset:19456
	ds_read_b128 v[210:213], v201 offset:20480
	ds_read_b128 v[214:217], v201 offset:21504
	ds_read_b128 v[236:239], v201 offset:22528
	ds_read_b128 v[240:243], v201 offset:23552
	global_load_lds_dwordx4 v[186:187], off
	s_add_i32 m0, s18, 0x2000
	s_add_u32 s18, s70, 0x70000
	v_lshl_add_u64 v[188:189], s[70:71], 0, v[180:181]
	s_addc_u32 s19, s71, 0
	s_add_i32 s46, s47, s95
	global_load_lds_dwordx4 v[188:189], off
	v_lshl_add_u64 v[190:191], s[18:19], 0, v[164:165]
	s_mov_b32 m0, s46
	v_lshl_add_u64 v[192:193], vcc, 0, v[178:179]
	global_load_lds_dwordx4 v[190:191], off
	v_lshl_add_u64 v[190:191], s[18:19], 0, v[180:181]
	s_add_i32 m0, s46, 0x2000
	s_nop 0
	global_load_lds_dwordx4 v[190:191], off
	v_lshl_add_u64 v[190:191], vcc, 0, v[162:163]
	s_mov_b32 m0, s73
	s_nop 0
	global_load_lds_dwordx4 v[190:191], off
	s_mov_b32 m0, s8
	s_nop 0
	global_load_lds_dwordx4 v[192:193], off
	s_waitcnt vmcnt(8)
	s_waitcnt lgkmcnt(0)
	s_barrier
	s_setprio 1
	s_waitcnt lgkmcnt(0)
	v_mfma_scale_f32_16x16x128_f8f6f4 v[94:97], v[26:33], v[170:177], 0, v194, v169 op_sel_hi:[0,0,0]
	v_mfma_scale_f32_16x16x128_f8f6f4 v[90:93], v[18:25], v[170:177], 0, v194, v169 op_sel_hi:[0,0,0]
	v_mfma_scale_f32_16x16x128_f8f6f4 v[78:81], v[26:33], v[202:209], 0, v194, v169 op_sel_hi:[0,0,0]
	v_mfma_scale_f32_16x16x128_f8f6f4 v[74:77], v[18:25], v[202:209], 0, v194, v169 op_sel_hi:[0,0,0]
	v_mfma_scale_f32_16x16x128_f8f6f4 v[62:65], v[26:33], v[210:217], 0, v194, v169 op_sel_hi:[0,0,0]
	v_mfma_scale_f32_16x16x128_f8f6f4 v[58:61], v[18:25], v[210:217], 0, v194, v169 op_sel_hi:[0,0,0]
	v_mfma_scale_f32_16x16x128_f8f6f4 v[46:49], v[26:33], v[236:243], 0, v194, v169 op_sel_hi:[0,0,0]
	v_mfma_scale_f32_16x16x128_f8f6f4 v[42:45], v[18:25], v[236:243], 0, v194, v169 op_sel_hi:[0,0,0]
	s_setprio 0
	s_setprio 1
	v_mfma_scale_f32_16x16x128_f8f6f4 v[86:89], v[10:17], v[170:177], 0, v194, v169 op_sel_hi:[0,0,0]
	v_mfma_scale_f32_16x16x128_f8f6f4 v[82:85], v[2:9], v[170:177], 0, v194, v169 op_sel_hi:[0,0,0]
	v_mfma_scale_f32_16x16x128_f8f6f4 v[70:73], v[10:17], v[202:209], 0, v194, v169 op_sel_hi:[0,0,0]
	v_mfma_scale_f32_16x16x128_f8f6f4 v[66:69], v[2:9], v[202:209], 0, v194, v169 op_sel_hi:[0,0,0]
	v_mfma_scale_f32_16x16x128_f8f6f4 v[54:57], v[10:17], v[210:217], 0, v194, v169 op_sel_hi:[0,0,0]
	v_mfma_scale_f32_16x16x128_f8f6f4 v[50:53], v[2:9], v[210:217], 0, v194, v169 op_sel_hi:[0,0,0]
	v_mfma_scale_f32_16x16x128_f8f6f4 v[38:41], v[10:17], v[236:243], 0, v194, v169 op_sel_hi:[0,0,0]
	v_mfma_scale_f32_16x16x128_f8f6f4 v[34:37], v[2:9], v[236:243], 0, v194, v169 op_sel_hi:[0,0,0]
	s_setprio 0
	s_barrier
	s_add_i32 s46, 0, 0x18000
	s_add_i32 s47, 0, 0x1c000
	v_add_u32_e32 v2, s46, v196
	v_add_u32_e32 v6, s47, v196
	ds_read_b128 v[26:29], v2
	ds_read_b128 v[30:33], v2 offset:1024
	ds_read_b128 v[18:21], v2 offset:2048
	ds_read_b128 v[22:25], v2 offset:3072
	ds_read_b128 v[10:13], v6
	ds_read_b128 v[14:17], v6 offset:1024
	ds_read_b128 v[2:5], v6 offset:2048
	ds_read_b128 v[6:9], v6 offset:3072
	s_add_u32 s18, vcc_lo, 0x70000
	s_addc_u32 s19, vcc_hi, 0
	s_mov_b32 m0, s11
	v_lshl_add_u64 v[218:219], s[18:19], 0, v[162:163]
	ds_read_b128 v[170:173], v201 offset:32768
	ds_read_b128 v[174:177], v201 offset:33792
	ds_read_b128 v[202:205], v201 offset:34816
	ds_read_b128 v[206:209], v201 offset:35840
	ds_read_b128 v[210:213], v201 offset:36864
	ds_read_b128 v[214:217], v201 offset:37888
	ds_read_b128 v[236:239], v201 offset:38912
	ds_read_b128 v[240:243], v201 offset:39936
	global_load_lds_dwordx4 v[218:219], off
	v_lshl_add_u64 v[218:219], s[18:19], 0, v[178:179]
	s_mov_b32 m0, s84
	s_nop 0
	global_load_lds_dwordx4 v[218:219], off
	s_waitcnt vmcnt(8)
	s_waitcnt lgkmcnt(0)
	s_barrier
	s_setprio 1
	s_waitcnt lgkmcnt(0)
	v_mfma_scale_f32_16x16x128_f8f6f4 v[158:161], v[26:33], v[170:177], v[158:161], v194, v169 op_sel_hi:[0,0,0]
	v_mfma_scale_f32_16x16x128_f8f6f4 v[154:157], v[18:25], v[170:177], v[154:157], v194, v169 op_sel_hi:[0,0,0]
	v_mfma_scale_f32_16x16x128_f8f6f4 v[142:145], v[26:33], v[202:209], v[142:145], v194, v169 op_sel_hi:[0,0,0]
	v_mfma_scale_f32_16x16x128_f8f6f4 v[138:141], v[18:25], v[202:209], v[138:141], v194, v169 op_sel_hi:[0,0,0]
	v_mfma_scale_f32_16x16x128_f8f6f4 v[126:129], v[26:33], v[210:217], v[126:129], v194, v169 op_sel_hi:[0,0,0]
	v_mfma_scale_f32_16x16x128_f8f6f4 v[122:125], v[18:25], v[210:217], v[122:125], v194, v169 op_sel_hi:[0,0,0]
	v_mfma_scale_f32_16x16x128_f8f6f4 v[110:113], v[26:33], v[236:243], v[110:113], v194, v169 op_sel_hi:[0,0,0]
	v_mfma_scale_f32_16x16x128_f8f6f4 v[106:109], v[18:25], v[236:243], v[106:109], v194, v169 op_sel_hi:[0,0,0]
	s_setprio 0
	s_setprio 1
	v_mfma_scale_f32_16x16x128_f8f6f4 v[150:153], v[10:17], v[170:177], v[150:153], v194, v169 op_sel_hi:[0,0,0]
	v_mfma_scale_f32_16x16x128_f8f6f4 v[146:149], v[2:9], v[170:177], v[146:149], v194, v169 op_sel_hi:[0,0,0]
	v_mfma_scale_f32_16x16x128_f8f6f4 v[134:137], v[10:17], v[202:209], v[134:137], v194, v169 op_sel_hi:[0,0,0]
	v_mfma_scale_f32_16x16x128_f8f6f4 v[130:133], v[2:9], v[202:209], v[130:133], v194, v169 op_sel_hi:[0,0,0]
	v_mfma_scale_f32_16x16x128_f8f6f4 v[118:121], v[10:17], v[210:217], v[118:121], v194, v169 op_sel_hi:[0,0,0]
	v_mfma_scale_f32_16x16x128_f8f6f4 v[114:117], v[2:9], v[210:217], v[114:117], v194, v169 op_sel_hi:[0,0,0]
	v_mfma_scale_f32_16x16x128_f8f6f4 v[102:105], v[10:17], v[236:243], v[102:105], v194, v169 op_sel_hi:[0,0,0]
	v_mfma_scale_f32_16x16x128_f8f6f4 v[98:101], v[2:9], v[236:243], v[98:101], v194, v169 op_sel_hi:[0,0,0]
	s_setprio 0
	s_barrier
	s_add_i32 s18, s46, s95
	v_lshl_add_u64 v[186:187], v[186:187], 0, s[56:57]
	s_mov_b32 m0, s18
	ds_read_b128 v[170:173], v201 offset:49152
	ds_read_b128 v[174:177], v201 offset:50176
	ds_read_b128 v[202:205], v201 offset:51200
	ds_read_b128 v[206:209], v201 offset:52224
	ds_read_b128 v[210:213], v201 offset:53248
	ds_read_b128 v[214:217], v201 offset:54272
	ds_read_b128 v[236:239], v201 offset:55296
	ds_read_b128 v[240:243], v201 offset:56320
	global_load_lds_dwordx4 v[186:187], off
	s_add_i32 m0, s18, 0x2000
	s_add_u32 s18, s70, 0x70080
	v_lshl_add_u64 v[186:187], v[188:189], 0, s[56:57]
	s_addc_u32 s19, s71, 0
	s_add_i32 s46, s47, s95
	global_load_lds_dwordx4 v[186:187], off
	v_lshl_add_u64 v[186:187], s[18:19], 0, v[164:165]
	s_mov_b32 m0, s46
	s_nop 0
	global_load_lds_dwordx4 v[186:187], off
	v_lshl_add_u64 v[186:187], s[18:19], 0, v[180:181]
	s_add_i32 m0, s46, 0x2000
	s_nop 0
	global_load_lds_dwordx4 v[186:187], off
	v_lshl_add_u64 v[186:187], v[190:191], 0, s[56:57]
	s_mov_b32 m0, s0
	s_nop 0
	global_load_lds_dwordx4 v[186:187], off
	v_lshl_add_u64 v[186:187], v[192:193], 0, s[56:57]
	s_mov_b32 m0, s88
	s_nop 0
	global_load_lds_dwordx4 v[186:187], off
	s_waitcnt vmcnt(8)
	s_waitcnt lgkmcnt(0)
	s_barrier
	s_setprio 1
	s_waitcnt lgkmcnt(0)
	v_mfma_scale_f32_16x16x128_f8f6f4 v[94:97], v[26:33], v[170:177], v[94:97], v194, v169 op_sel_hi:[0,0,0]
	v_mfma_scale_f32_16x16x128_f8f6f4 v[90:93], v[18:25], v[170:177], v[90:93], v194, v169 op_sel_hi:[0,0,0]
	v_mfma_scale_f32_16x16x128_f8f6f4 v[78:81], v[26:33], v[202:209], v[78:81], v194, v169 op_sel_hi:[0,0,0]
	v_mfma_scale_f32_16x16x128_f8f6f4 v[74:77], v[18:25], v[202:209], v[74:77], v194, v169 op_sel_hi:[0,0,0]
	v_mfma_scale_f32_16x16x128_f8f6f4 v[62:65], v[26:33], v[210:217], v[62:65], v194, v169 op_sel_hi:[0,0,0]
	v_mfma_scale_f32_16x16x128_f8f6f4 v[58:61], v[18:25], v[210:217], v[58:61], v194, v169 op_sel_hi:[0,0,0]
	v_mfma_scale_f32_16x16x128_f8f6f4 v[46:49], v[26:33], v[236:243], v[46:49], v194, v169 op_sel_hi:[0,0,0]
	v_mfma_scale_f32_16x16x128_f8f6f4 v[42:45], v[18:25], v[236:243], v[42:45], v194, v169 op_sel_hi:[0,0,0]
	s_setprio 0
	s_setprio 1
	v_mfma_scale_f32_16x16x128_f8f6f4 v[86:89], v[10:17], v[170:177], v[86:89], v194, v169 op_sel_hi:[0,0,0]
	v_mfma_scale_f32_16x16x128_f8f6f4 v[82:85], v[2:9], v[170:177], v[82:85], v194, v169 op_sel_hi:[0,0,0]
	v_mfma_scale_f32_16x16x128_f8f6f4 v[70:73], v[10:17], v[202:209], v[70:73], v194, v169 op_sel_hi:[0,0,0]
	v_mfma_scale_f32_16x16x128_f8f6f4 v[66:69], v[2:9], v[202:209], v[66:69], v194, v169 op_sel_hi:[0,0,0]
	v_mfma_scale_f32_16x16x128_f8f6f4 v[54:57], v[10:17], v[210:217], v[54:57], v194, v169 op_sel_hi:[0,0,0]
	v_mfma_scale_f32_16x16x128_f8f6f4 v[50:53], v[2:9], v[210:217], v[50:53], v194, v169 op_sel_hi:[0,0,0]
	v_mfma_scale_f32_16x16x128_f8f6f4 v[38:41], v[10:17], v[236:243], v[38:41], v194, v169 op_sel_hi:[0,0,0]
	v_mfma_scale_f32_16x16x128_f8f6f4 v[34:37], v[2:9], v[236:243], v[34:37], v194, v169 op_sel_hi:[0,0,0]
	s_setprio 0
	s_add_u32 s35, s35, 0x100
	s_addc_u32 s45, s45, 0
	s_cmp_lt_i32 s75, s16
	s_mov_b64 s[18:19], s[42:43]
	s_mov_b32 s70, s75
	s_cbranch_scc0 .Lrotph18_pexitbar
	s_add_i32 s75, s70, 2
	s_add_u32 s42, s18, 0x100
	s_addc_u32 s43, s19, 0
	s_add_i32 s46, 0, 0x10000
	s_cmp_eq_u32 s14, s70
	s_cselect_b32 vcc_hi, s69, s43
	s_cselect_b32 vcc_lo, s68, s42
	s_cselect_b32 s71, s37, s45
	s_cselect_b32 s70, s36, s35
	s_add_i32 s47, 0, 0x14000
	s_barrier
	s_branch .Lrotph18_body

.Lrotph18_body:
	v_add_u32_e32 v2, s46, v196
	v_add_u32_e32 v6, s47, v196
	ds_read_b128 v[26:29], v2
	ds_read_b128 v[30:33], v2 offset:1024
	ds_read_b128 v[18:21], v2 offset:2048
	ds_read_b128 v[22:25], v2 offset:3072
	ds_read_b128 v[10:13], v6
	ds_read_b128 v[14:17], v6 offset:1024
	ds_read_b128 v[2:5], v6 offset:2048
	ds_read_b128 v[6:9], v6 offset:3072
	v_lshl_add_u64 v[218:219], s[18:19], 0, v[184:185]
	s_add_i32 m0, s73, 0xc000
	ds_read_b128 v[170:173], v201
	ds_read_b128 v[174:177], v201 offset:1024
	ds_read_b128 v[186:189], v201 offset:2048
	ds_read_b128 v[190:193], v201 offset:3072
	ds_read_b128 v[202:205], v201 offset:4096
	ds_read_b128 v[206:209], v201 offset:5120
	ds_read_b128 v[210:213], v201 offset:6144
	ds_read_b128 v[214:217], v201 offset:7168
	global_load_lds_dwordx4 v[218:219], off
	v_lshl_add_u64 v[218:219], s[18:19], 0, v[182:183]
	s_add_i32 m0, s73, 0xe000
	s_nop 0
	global_load_lds_dwordx4 v[218:219], off
	s_waitcnt vmcnt(8)
	s_waitcnt lgkmcnt(0)
	s_barrier
	s_setprio 1
	s_waitcnt lgkmcnt(0)
	v_mfma_scale_f32_16x16x128_f8f6f4 v[158:161], v[26:33], v[170:177], v[158:161], v194, v169 op_sel_hi:[0,0,0]
	v_mfma_scale_f32_16x16x128_f8f6f4 v[154:157], v[18:25], v[170:177], v[154:157], v194, v169 op_sel_hi:[0,0,0]
	v_mfma_scale_f32_16x16x128_f8f6f4 v[142:145], v[26:33], v[186:193], v[142:145], v194, v169 op_sel_hi:[0,0,0]
	v_mfma_scale_f32_16x16x128_f8f6f4 v[138:141], v[18:25], v[186:193], v[138:141], v194, v169 op_sel_hi:[0,0,0]
	v_mfma_scale_f32_16x16x128_f8f6f4 v[126:129], v[26:33], v[202:209], v[126:129], v194, v169 op_sel_hi:[0,0,0]
	v_mfma_scale_f32_16x16x128_f8f6f4 v[122:125], v[18:25], v[202:209], v[122:125], v194, v169 op_sel_hi:[0,0,0]
	v_mfma_scale_f32_16x16x128_f8f6f4 v[110:113], v[26:33], v[210:217], v[110:113], v194, v169 op_sel_hi:[0,0,0]
	v_mfma_scale_f32_16x16x128_f8f6f4 v[106:109], v[18:25], v[210:217], v[106:109], v194, v169 op_sel_hi:[0,0,0]
	s_setprio 0
	s_setprio 1
	v_mfma_scale_f32_16x16x128_f8f6f4 v[150:153], v[10:17], v[170:177], v[150:153], v194, v169 op_sel_hi:[0,0,0]
	v_mfma_scale_f32_16x16x128_f8f6f4 v[146:149], v[2:9], v[170:177], v[146:149], v194, v169 op_sel_hi:[0,0,0]
	v_mfma_scale_f32_16x16x128_f8f6f4 v[134:137], v[10:17], v[186:193], v[134:137], v194, v169 op_sel_hi:[0,0,0]
	v_mfma_scale_f32_16x16x128_f8f6f4 v[130:133], v[2:9], v[186:193], v[130:133], v194, v169 op_sel_hi:[0,0,0]
	v_mfma_scale_f32_16x16x128_f8f6f4 v[118:121], v[10:17], v[202:209], v[118:121], v194, v169 op_sel_hi:[0,0,0]
	v_mfma_scale_f32_16x16x128_f8f6f4 v[114:117], v[2:9], v[202:209], v[114:117], v194, v169 op_sel_hi:[0,0,0]
	v_mfma_scale_f32_16x16x128_f8f6f4 v[102:105], v[10:17], v[210:217], v[102:105], v194, v169 op_sel_hi:[0,0,0]
	v_mfma_scale_f32_16x16x128_f8f6f4 v[98:101], v[2:9], v[210:217], v[98:101], v194, v169 op_sel_hi:[0,0,0]
	s_setprio 0
	s_barrier
	s_add_i32 s18, s46, s95
	v_lshl_add_u64 v[186:187], s[70:71], 0, v[164:165]
	s_mov_b32 m0, s18
	ds_read_b128 v[170:173], v201 offset:16384
	ds_read_b128 v[174:177], v201 offset:17408
	ds_read_b128 v[202:205], v201 offset:18432
	ds_read_b128 v[206:209], v201 offset:19456
	ds_read_b128 v[210:213], v201 offset:20480
	ds_read_b128 v[214:217], v201 offset:21504
	ds_read_b128 v[236:239], v201 offset:22528
	ds_read_b128 v[240:243], v201 offset:23552
	global_load_lds_dwordx4 v[186:187], off
	s_add_i32 m0, s18, 0x2000
	s_add_u32 s18, s70, 0x70000
	v_lshl_add_u64 v[188:189], s[70:71], 0, v[180:181]
	s_addc_u32 s19, s71, 0
	s_add_i32 s46, s47, s95
	global_load_lds_dwordx4 v[188:189], off
	v_lshl_add_u64 v[190:191], s[18:19], 0, v[164:165]
	s_mov_b32 m0, s46
	v_lshl_add_u64 v[192:193], vcc, 0, v[178:179]
	global_load_lds_dwordx4 v[190:191], off
	v_lshl_add_u64 v[190:191], s[18:19], 0, v[180:181]
	s_add_i32 m0, s46, 0x2000
	s_nop 0
	global_load_lds_dwordx4 v[190:191], off
	v_lshl_add_u64 v[190:191], vcc, 0, v[162:163]
	s_mov_b32 m0, s73
	s_nop 0
	global_load_lds_dwordx4 v[190:191], off
	s_mov_b32 m0, s8
	s_nop 0
	global_load_lds_dwordx4 v[192:193], off
	s_waitcnt vmcnt(8)
	s_waitcnt lgkmcnt(0)
	s_barrier
	s_setprio 1
	s_waitcnt lgkmcnt(0)
	v_mfma_scale_f32_16x16x128_f8f6f4 v[94:97], v[26:33], v[170:177], v[94:97], v194, v169 op_sel_hi:[0,0,0]
	v_mfma_scale_f32_16x16x128_f8f6f4 v[90:93], v[18:25], v[170:177], v[90:93], v194, v169 op_sel_hi:[0,0,0]
	v_mfma_scale_f32_16x16x128_f8f6f4 v[78:81], v[26:33], v[202:209], v[78:81], v194, v169 op_sel_hi:[0,0,0]
	v_mfma_scale_f32_16x16x128_f8f6f4 v[74:77], v[18:25], v[202:209], v[74:77], v194, v169 op_sel_hi:[0,0,0]
	v_mfma_scale_f32_16x16x128_f8f6f4 v[62:65], v[26:33], v[210:217], v[62:65], v194, v169 op_sel_hi:[0,0,0]
	v_mfma_scale_f32_16x16x128_f8f6f4 v[58:61], v[18:25], v[210:217], v[58:61], v194, v169 op_sel_hi:[0,0,0]
	v_mfma_scale_f32_16x16x128_f8f6f4 v[46:49], v[26:33], v[236:243], v[46:49], v194, v169 op_sel_hi:[0,0,0]
	v_mfma_scale_f32_16x16x128_f8f6f4 v[42:45], v[18:25], v[236:243], v[42:45], v194, v169 op_sel_hi:[0,0,0]
	s_setprio 0
	s_setprio 1
	v_mfma_scale_f32_16x16x128_f8f6f4 v[86:89], v[10:17], v[170:177], v[86:89], v194, v169 op_sel_hi:[0,0,0]
	v_mfma_scale_f32_16x16x128_f8f6f4 v[82:85], v[2:9], v[170:177], v[82:85], v194, v169 op_sel_hi:[0,0,0]
	v_mfma_scale_f32_16x16x128_f8f6f4 v[70:73], v[10:17], v[202:209], v[70:73], v194, v169 op_sel_hi:[0,0,0]
	v_mfma_scale_f32_16x16x128_f8f6f4 v[66:69], v[2:9], v[202:209], v[66:69], v194, v169 op_sel_hi:[0,0,0]
	v_mfma_scale_f32_16x16x128_f8f6f4 v[54:57], v[10:17], v[210:217], v[54:57], v194, v169 op_sel_hi:[0,0,0]
	v_mfma_scale_f32_16x16x128_f8f6f4 v[50:53], v[2:9], v[210:217], v[50:53], v194, v169 op_sel_hi:[0,0,0]
	v_mfma_scale_f32_16x16x128_f8f6f4 v[38:41], v[10:17], v[236:243], v[38:41], v194, v169 op_sel_hi:[0,0,0]
	v_mfma_scale_f32_16x16x128_f8f6f4 v[34:37], v[2:9], v[236:243], v[34:37], v194, v169 op_sel_hi:[0,0,0]
	s_setprio 0
	s_barrier
	s_add_i32 s46, 0, 0x18000
	s_add_i32 s47, 0, 0x1c000
	v_add_u32_e32 v2, s46, v196
	v_add_u32_e32 v6, s47, v196
	ds_read_b128 v[26:29], v2
	ds_read_b128 v[30:33], v2 offset:1024
	ds_read_b128 v[18:21], v2 offset:2048
	ds_read_b128 v[22:25], v2 offset:3072
	ds_read_b128 v[10:13], v6
	ds_read_b128 v[14:17], v6 offset:1024
	ds_read_b128 v[2:5], v6 offset:2048
	ds_read_b128 v[6:9], v6 offset:3072
	s_add_u32 s18, vcc_lo, 0x70000
	s_addc_u32 s19, vcc_hi, 0
	s_mov_b32 m0, s11
	v_lshl_add_u64 v[218:219], s[18:19], 0, v[162:163]
	ds_read_b128 v[170:173], v201 offset:32768
	ds_read_b128 v[174:177], v201 offset:33792
	ds_read_b128 v[202:205], v201 offset:34816
	ds_read_b128 v[206:209], v201 offset:35840
	ds_read_b128 v[210:213], v201 offset:36864
	ds_read_b128 v[214:217], v201 offset:37888
	ds_read_b128 v[236:239], v201 offset:38912
	ds_read_b128 v[240:243], v201 offset:39936
	global_load_lds_dwordx4 v[218:219], off
	v_lshl_add_u64 v[218:219], s[18:19], 0, v[178:179]
	s_mov_b32 m0, s84
	s_nop 0
	global_load_lds_dwordx4 v[218:219], off
	s_waitcnt vmcnt(8)
	s_waitcnt lgkmcnt(0)
	s_barrier
	s_setprio 1
	s_waitcnt lgkmcnt(0)
	v_mfma_scale_f32_16x16x128_f8f6f4 v[158:161], v[26:33], v[170:177], v[158:161], v194, v169 op_sel_hi:[0,0,0]
	v_mfma_scale_f32_16x16x128_f8f6f4 v[154:157], v[18:25], v[170:177], v[154:157], v194, v169 op_sel_hi:[0,0,0]
	v_mfma_scale_f32_16x16x128_f8f6f4 v[142:145], v[26:33], v[202:209], v[142:145], v194, v169 op_sel_hi:[0,0,0]
	v_mfma_scale_f32_16x16x128_f8f6f4 v[138:141], v[18:25], v[202:209], v[138:141], v194, v169 op_sel_hi:[0,0,0]
	v_mfma_scale_f32_16x16x128_f8f6f4 v[126:129], v[26:33], v[210:217], v[126:129], v194, v169 op_sel_hi:[0,0,0]
	v_mfma_scale_f32_16x16x128_f8f6f4 v[122:125], v[18:25], v[210:217], v[122:125], v194, v169 op_sel_hi:[0,0,0]
	v_mfma_scale_f32_16x16x128_f8f6f4 v[110:113], v[26:33], v[236:243], v[110:113], v194, v169 op_sel_hi:[0,0,0]
	v_mfma_scale_f32_16x16x128_f8f6f4 v[106:109], v[18:25], v[236:243], v[106:109], v194, v169 op_sel_hi:[0,0,0]
	s_setprio 0
	s_setprio 1
	v_mfma_scale_f32_16x16x128_f8f6f4 v[150:153], v[10:17], v[170:177], v[150:153], v194, v169 op_sel_hi:[0,0,0]
	v_mfma_scale_f32_16x16x128_f8f6f4 v[146:149], v[2:9], v[170:177], v[146:149], v194, v169 op_sel_hi:[0,0,0]
	v_mfma_scale_f32_16x16x128_f8f6f4 v[134:137], v[10:17], v[202:209], v[134:137], v194, v169 op_sel_hi:[0,0,0]
	v_mfma_scale_f32_16x16x128_f8f6f4 v[130:133], v[2:9], v[202:209], v[130:133], v194, v169 op_sel_hi:[0,0,0]
	v_mfma_scale_f32_16x16x128_f8f6f4 v[118:121], v[10:17], v[210:217], v[118:121], v194, v169 op_sel_hi:[0,0,0]
	v_mfma_scale_f32_16x16x128_f8f6f4 v[114:117], v[2:9], v[210:217], v[114:117], v194, v169 op_sel_hi:[0,0,0]
	v_mfma_scale_f32_16x16x128_f8f6f4 v[102:105], v[10:17], v[236:243], v[102:105], v194, v169 op_sel_hi:[0,0,0]
	v_mfma_scale_f32_16x16x128_f8f6f4 v[98:101], v[2:9], v[236:243], v[98:101], v194, v169 op_sel_hi:[0,0,0]
	s_setprio 0
	s_barrier
	s_add_i32 s18, s46, s95
	v_lshl_add_u64 v[186:187], v[186:187], 0, s[56:57]
	s_mov_b32 m0, s18
	ds_read_b128 v[170:173], v201 offset:49152
	ds_read_b128 v[174:177], v201 offset:50176
	ds_read_b128 v[202:205], v201 offset:51200
	ds_read_b128 v[206:209], v201 offset:52224
	ds_read_b128 v[210:213], v201 offset:53248
	ds_read_b128 v[214:217], v201 offset:54272
	ds_read_b128 v[236:239], v201 offset:55296
	ds_read_b128 v[240:243], v201 offset:56320
	global_load_lds_dwordx4 v[186:187], off
	s_add_i32 m0, s18, 0x2000
	s_add_u32 s18, s70, 0x70080
	v_lshl_add_u64 v[186:187], v[188:189], 0, s[56:57]
	s_addc_u32 s19, s71, 0
	s_add_i32 s46, s47, s95
	global_load_lds_dwordx4 v[186:187], off
	v_lshl_add_u64 v[186:187], s[18:19], 0, v[164:165]
	s_mov_b32 m0, s46
	s_nop 0
	global_load_lds_dwordx4 v[186:187], off
	v_lshl_add_u64 v[186:187], s[18:19], 0, v[180:181]
	s_add_i32 m0, s46, 0x2000
	s_nop 0
	global_load_lds_dwordx4 v[186:187], off
	v_lshl_add_u64 v[186:187], v[190:191], 0, s[56:57]
	s_mov_b32 m0, s0
	s_nop 0
	global_load_lds_dwordx4 v[186:187], off
	v_lshl_add_u64 v[186:187], v[192:193], 0, s[56:57]
	s_mov_b32 m0, s88
	s_nop 0
	global_load_lds_dwordx4 v[186:187], off
	s_waitcnt vmcnt(8)
	s_waitcnt lgkmcnt(0)
	s_barrier
	s_setprio 1
	s_waitcnt lgkmcnt(0)
	v_mfma_scale_f32_16x16x128_f8f6f4 v[94:97], v[26:33], v[170:177], v[94:97], v194, v169 op_sel_hi:[0,0,0]
	v_mfma_scale_f32_16x16x128_f8f6f4 v[90:93], v[18:25], v[170:177], v[90:93], v194, v169 op_sel_hi:[0,0,0]
	v_mfma_scale_f32_16x16x128_f8f6f4 v[78:81], v[26:33], v[202:209], v[78:81], v194, v169 op_sel_hi:[0,0,0]
	v_mfma_scale_f32_16x16x128_f8f6f4 v[74:77], v[18:25], v[202:209], v[74:77], v194, v169 op_sel_hi:[0,0,0]
	v_mfma_scale_f32_16x16x128_f8f6f4 v[62:65], v[26:33], v[210:217], v[62:65], v194, v169 op_sel_hi:[0,0,0]
	v_mfma_scale_f32_16x16x128_f8f6f4 v[58:61], v[18:25], v[210:217], v[58:61], v194, v169 op_sel_hi:[0,0,0]
	v_mfma_scale_f32_16x16x128_f8f6f4 v[46:49], v[26:33], v[236:243], v[46:49], v194, v169 op_sel_hi:[0,0,0]
	v_mfma_scale_f32_16x16x128_f8f6f4 v[42:45], v[18:25], v[236:243], v[42:45], v194, v169 op_sel_hi:[0,0,0]
	s_setprio 0
	s_setprio 1
	v_mfma_scale_f32_16x16x128_f8f6f4 v[86:89], v[10:17], v[170:177], v[86:89], v194, v169 op_sel_hi:[0,0,0]
	v_mfma_scale_f32_16x16x128_f8f6f4 v[82:85], v[2:9], v[170:177], v[82:85], v194, v169 op_sel_hi:[0,0,0]
	v_mfma_scale_f32_16x16x128_f8f6f4 v[70:73], v[10:17], v[202:209], v[70:73], v194, v169 op_sel_hi:[0,0,0]
	v_mfma_scale_f32_16x16x128_f8f6f4 v[66:69], v[2:9], v[202:209], v[66:69], v194, v169 op_sel_hi:[0,0,0]
	v_mfma_scale_f32_16x16x128_f8f6f4 v[54:57], v[10:17], v[210:217], v[54:57], v194, v169 op_sel_hi:[0,0,0]
	v_mfma_scale_f32_16x16x128_f8f6f4 v[50:53], v[2:9], v[210:217], v[50:53], v194, v169 op_sel_hi:[0,0,0]
	v_mfma_scale_f32_16x16x128_f8f6f4 v[38:41], v[10:17], v[236:243], v[38:41], v194, v169 op_sel_hi:[0,0,0]
	v_mfma_scale_f32_16x16x128_f8f6f4 v[34:37], v[2:9], v[236:243], v[34:37], v194, v169 op_sel_hi:[0,0,0]
	s_setprio 0
	s_add_u32 s35, s35, 0x100
	s_addc_u32 s45, s45, 0
	s_cmp_lt_i32 s75, s16
	s_mov_b64 s[18:19], s[42:43]
	s_mov_b32 s70, s75
	s_cbranch_scc0 .Lrotph18_exitbar
	s_add_i32 s75, s70, 2
	s_add_u32 s42, s18, 0x100
	s_addc_u32 s43, s19, 0
	s_add_i32 s46, 0, 0x10000
	s_cmp_eq_u32 s14, s70
	s_cselect_b32 vcc_hi, s69, s43
	s_cselect_b32 vcc_lo, s68, s42
	s_cselect_b32 s71, s37, s45
	s_cselect_b32 s70, s36, s35
	s_add_i32 s47, 0, 0x14000
	s_barrier
	s_branch .Lrotph18_body
.Lrotph18_exitbar:
	s_barrier
.Lpeelexitph18:
	v_mov_b32_e32 v209, v1
	s_andn2_b64 vcc, exec, s[58:59]
	s_cbranch_vccnz .LBB0_1926
